# v22 + all global stores write-through (sc1), L2 write-back dropped from the grid barrier release
# speedup vs baseline: 1.0524x; 1.0524x over previous
; __device__ __forceinline__ void p0_mod(const Args& a, LAS unsigned char* lds) {
;     ...
;         for (int d0 = dch * 64; d0 < dch * 64 + 64; d0 += 16) {
;             float wv[16];
; #pragma unroll
;             for (int k = 0; k < 16; ++k) wv[k] = __builtin_nontemporal_load(w + (size_t)(d0 + k) * 6144);
; #pragma unroll
;             for (int k = 0; k < 16; ++k)
; #pragma unroll
;                 for (int b = 0; b < 8; ++b) acc[b] += cs[b * D + d0 + k] * wv[k];
;         }
.LBB0_11:
	v_add_co_u32_e32 v144, vcc, 0xfffa6000, v142
	ds_read_b128 v[18:21], v148
	ds_read_b128 v[14:17], v148 offset:16
	ds_read_b128 v[10:13], v148 offset:4096
	ds_read_b128 v[22:25], v148 offset:4112
	ds_read_b128 v[66:69], v148 offset:32
	ds_read_b128 v[54:57], v148 offset:48
	ds_read_b128 v[26:29], v148 offset:4128
	ds_read_b128 v[30:33], v148 offset:4144
	ds_read_b128 v[82:85], v148 offset:8192
	ds_read_b128 v[78:81], v148 offset:8208
	ds_read_b128 v[38:41], v148 offset:12288
	ds_read_b128 v[34:37], v148 offset:12304
	ds_read_b128 v[90:93], v148 offset:8224
	ds_read_b128 v[98:101], v148 offset:8240
	ds_read_b128 v[46:49], v148 offset:12320
	ds_read_b128 v[42:45], v148 offset:12336
	ds_read_b128 v[118:121], v148 offset:16384
	ds_read_b128 v[106:109], v148 offset:16400
	ds_read_b128 v[58:61], v148 offset:20480
	ds_read_b128 v[50:53], v148 offset:20496
	ds_read_b128 v[130:133], v148 offset:24576
	ds_read_b128 v[110:113], v148 offset:24592
	ds_read_b128 v[70:73], v148 offset:28672
	ds_read_b128 v[62:65], v148 offset:28688
	ds_read_b128 v[150:153], v148 offset:16416
	ds_read_b128 v[114:117], v148 offset:16432
	ds_read_b128 v[86:89], v148 offset:20512
	ds_read_b128 v[74:77], v148 offset:20528
	ds_read_b128 v[122:125], v148 offset:24608
	ds_read_b128 v[126:129], v148 offset:24624
	ds_read_b128 v[102:105], v148 offset:28704
	ds_read_b128 v[94:97], v148 offset:28720
	v_addc_co_u32_e32 v145, vcc, -1, v143, vcc
	v_add_co_u32_e32 v154, vcc, 0xfffac000, v142
	s_waitcnt lgkmcnt(0)
	v_mov_b32_e32 v170, v130
	v_addc_co_u32_e32 v155, vcc, -1, v143, vcc
	v_add_co_u32_e32 v156, vcc, 0xfffb2000, v142
	v_mov_b32_e32 v130, v114
	s_nop 0
	v_addc_co_u32_e32 v157, vcc, -1, v143, vcc
	v_add_co_u32_e32 v158, vcc, 0xfffb8000, v142
	v_mov_b32_e32 v171, v70
	s_nop 0
	v_addc_co_u32_e32 v159, vcc, -1, v143, vcc
	v_add_co_u32_e32 v160, vcc, 0xfffbe000, v142
	v_mov_b32_e32 v70, v131
	s_nop 0
	v_addc_co_u32_e32 v161, vcc, -1, v143, vcc
	v_add_co_u32_e32 v162, vcc, 0xfffc4000, v142
	v_mov_b32_e32 v131, v74
	s_nop 0
	v_addc_co_u32_e32 v163, vcc, -1, v143, vcc
	v_add_co_u32_e32 v114, vcc, 0xfffca000, v142
	v_mov_b32_e32 v74, v115
	s_nop 0
	v_addc_co_u32_e32 v115, vcc, -1, v143, vcc
	v_mov_b32_e32 v166, v82
	v_mov_b32_e32 v82, v120
	v_mov_b32_e32 v120, v152
	v_add_co_u32_e32 v152, vcc, 0xfffd0000, v142
	v_mov_b32_e32 v167, v38
	v_mov_b32_e32 v38, v83
	v_mov_b32_e32 v83, v60
	v_mov_b32_e32 v60, v121
	v_mov_b32_e32 v121, v88
	v_mov_b32_e32 v88, v153
	v_addc_co_u32_e32 v153, vcc, -1, v143, vcc
	global_load_dword v144, v[144:145], off nt
	s_nop 0
	global_load_dword v154, v[154:155], off nt
	s_nop 0
	global_load_dword v156, v[156:157], off nt
	s_nop 0
	global_load_dword v158, v[158:159], off nt
	v_mov_b32_e32 v164, v18
	v_mov_b32_e32 v168, v118
	v_mov_b32_e32 v18, v20
	v_mov_b32_e32 v20, v84
	v_mov_b32_e32 v84, v132
	v_mov_b32_e32 v118, v14
	v_mov_b32_e32 v14, v16
	v_mov_b32_e32 v16, v66
	v_mov_b32_e32 v66, v68
	v_mov_b32_e32 v68, v54
	v_mov_b32_e32 v54, v56
	v_mov_b32_e32 v56, v78
	v_mov_b32_e32 v78, v80
	v_mov_b32_e32 v80, v90
	v_mov_b32_e32 v90, v92
	v_mov_b32_e32 v92, v98
	v_mov_b32_e32 v98, v100
	v_mov_b32_e32 v100, v106
	v_mov_b32_e32 v106, v108
	v_mov_b32_e32 v108, v110
	v_mov_b32_e32 v110, v112
	v_mov_b32_e32 v112, v150
	global_load_dword v132, v[160:161], off nt
	global_load_dword v150, v[162:163], off nt
	v_add_co_u32_e32 v160, vcc, 0xfffd6000, v142
	global_load_dword v114, v[114:115], off nt
	s_nop 0
	global_load_dword v152, v[152:153], off nt
	v_addc_co_u32_e32 v161, vcc, -1, v143, vcc
	v_add_co_u32_e32 v162, vcc, 0xfffdc000, v142
	global_load_dword v160, v[160:161], off nt
	s_nop 0
	v_addc_co_u32_e32 v163, vcc, -1, v143, vcc
	v_add_co_u32_e32 v172, vcc, 0xfffe2000, v142
	global_load_dword v162, v[162:163], off nt
	s_nop 0
	v_addc_co_u32_e32 v173, vcc, -1, v143, vcc
	v_add_co_u32_e32 v174, vcc, 0xfffe8000, v142
	v_mov_b32_e32 v165, v10
	s_nop 0
	v_addc_co_u32_e32 v175, vcc, -1, v143, vcc
	v_add_co_u32_e32 v176, vcc, 0xfffee000, v142
	global_load_dword v172, v[172:173], off nt
	s_nop 0
	global_load_dword v174, v[174:175], off nt
	v_addc_co_u32_e32 v177, vcc, -1, v143, vcc
	v_add_co_u32_e32 v178, vcc, 0xffff4000, v142
	global_load_dword v176, v[176:177], off nt
	s_nop 0
	v_addc_co_u32_e32 v179, vcc, -1, v143, vcc
	v_add_co_u32_e32 v180, vcc, 0xffffa000, v142
	global_load_dword v178, v[178:179], off nt
	s_nop 0
	v_addc_co_u32_e32 v181, vcc, -1, v143, vcc
	global_load_dword v180, v[180:181], off nt
	s_nop 0
	global_load_dword v182, v[142:143], off nt
	v_mov_b32_e32 v169, v58
	v_mov_b32_e32 v10, v19
	v_mov_b32_e32 v58, v119
	v_mov_b32_e32 v19, v12
	v_mov_b32_e32 v12, v21
	v_mov_b32_e32 v21, v40
	v_mov_b32_e32 v40, v85
	v_mov_b32_e32 v85, v72
	v_mov_b32_e32 v72, v133
	v_mov_b32_e32 v119, v22
	v_mov_b32_e32 v22, v15
	v_mov_b32_e32 v15, v24
	v_mov_b32_e32 v24, v17
	v_mov_b32_e32 v17, v26
	v_mov_b32_e32 v26, v67
	v_mov_b32_e32 v67, v28
	v_mov_b32_e32 v28, v69
	v_mov_b32_e32 v69, v30
	s_waitcnt vmcnt(15)
	v_pk_fma_f32 v[6:7], v[144:145], v[164:165], v[6:7] op_sel_hi:[0,1,1]
	v_pk_fma_f32 v[8:9], v[144:145], v[166:167], v[8:9] op_sel_hi:[0,1,1]
	v_pk_fma_f32 v[2:3], v[144:145], v[168:169], v[2:3] op_sel_hi:[0,1,1]
	v_pk_fma_f32 v[4:5], v[144:145], v[170:171], v[4:5] op_sel_hi:[0,1,1]
	s_waitcnt vmcnt(14)
	v_pk_fma_f32 v[6:7], v[154:155], v[10:11], v[6:7] op_sel_hi:[0,1,1]
	v_pk_fma_f32 v[8:9], v[154:155], v[38:39], v[8:9] op_sel_hi:[0,1,1]
	v_pk_fma_f32 v[2:3], v[154:155], v[58:59], v[2:3] op_sel_hi:[0,1,1]
	v_pk_fma_f32 v[4:5], v[154:155], v[70:71], v[4:5] op_sel_hi:[0,1,1]
	s_waitcnt vmcnt(13)
; __device__ __forceinline__ void p0_mod(const Args& a, LAS unsigned char* lds) {
;     ...
;         for (int d0 = dch * 64; d0 < dch * 64 + 64; d0 += 16) {
;             float wv[16];
; #pragma unroll
;             for (int k = 0; k < 16; ++k) wv[k] = __builtin_nontemporal_load(w + (size_t)(d0 + k) * 6144);
; #pragma unroll
;             for (int k = 0; k < 16; ++k)
; #pragma unroll
;                 for (int b = 0; b < 8; ++b) acc[b] += cs[b * D + d0 + k] * wv[k];
;         }
	v_pk_fma_f32 v[6:7], v[156:157], v[18:19], v[6:7] op_sel_hi:[0,1,1]
	v_pk_fma_f32 v[8:9], v[156:157], v[20:21], v[8:9] op_sel_hi:[0,1,1]
	v_pk_fma_f32 v[2:3], v[156:157], v[82:83], v[2:3] op_sel_hi:[0,1,1]
	v_pk_fma_f32 v[4:5], v[156:157], v[84:85], v[4:5] op_sel_hi:[0,1,1]
	v_mov_b32_e32 v30, v55
	v_mov_b32_e32 v55, v32
	v_mov_b32_e32 v32, v57
	v_mov_b32_e32 v57, v34
	v_mov_b32_e32 v34, v79
	v_mov_b32_e32 v79, v36
	v_mov_b32_e32 v36, v81
	v_mov_b32_e32 v81, v46
	v_mov_b32_e32 v46, v91
	v_mov_b32_e32 v91, v48
	v_mov_b32_e32 v48, v93
	v_mov_b32_e32 v93, v42
	v_mov_b32_e32 v42, v99
	v_mov_b32_e32 v99, v44
	v_mov_b32_e32 v44, v101
	v_mov_b32_e32 v101, v50
	v_mov_b32_e32 v50, v107
	v_mov_b32_e32 v107, v52
	v_mov_b32_e32 v52, v109
	v_mov_b32_e32 v109, v62
	s_waitcnt vmcnt(12)
	v_pk_fma_f32 v[6:7], v[158:159], v[12:13], v[6:7] op_sel_hi:[0,1,1]
	v_pk_fma_f32 v[8:9], v[158:159], v[40:41], v[8:9] op_sel_hi:[0,1,1]
	v_pk_fma_f32 v[2:3], v[158:159], v[60:61], v[2:3] op_sel_hi:[0,1,1]
	v_pk_fma_f32 v[4:5], v[158:159], v[72:73], v[4:5] op_sel_hi:[0,1,1]
	v_mov_b32_e32 v62, v111
	s_waitcnt vmcnt(11)
	v_pk_fma_f32 v[6:7], v[132:133], v[118:119], v[6:7] op_sel_hi:[0,1,1]
	v_pk_fma_f32 v[8:9], v[132:133], v[56:57], v[8:9] op_sel_hi:[0,1,1]
	v_pk_fma_f32 v[2:3], v[132:133], v[100:101], v[2:3] op_sel_hi:[0,1,1]
	v_pk_fma_f32 v[4:5], v[132:133], v[108:109], v[4:5] op_sel_hi:[0,1,1]
	v_mov_b32_e32 v111, v64
	s_waitcnt vmcnt(10)
	v_pk_fma_f32 v[6:7], v[150:151], v[22:23], v[6:7] op_sel_hi:[0,1,1]
	v_pk_fma_f32 v[8:9], v[150:151], v[34:35], v[8:9] op_sel_hi:[0,1,1]
	v_pk_fma_f32 v[2:3], v[150:151], v[50:51], v[2:3] op_sel_hi:[0,1,1]
	v_pk_fma_f32 v[4:5], v[150:151], v[62:63], v[4:5] op_sel_hi:[0,1,1]
	v_mov_b32_e32 v64, v113
	s_waitcnt vmcnt(9)
	v_pk_fma_f32 v[6:7], v[114:115], v[14:15], v[6:7] op_sel_hi:[0,1,1]
	v_pk_fma_f32 v[8:9], v[114:115], v[78:79], v[8:9] op_sel_hi:[0,1,1]
	v_pk_fma_f32 v[2:3], v[114:115], v[106:107], v[2:3] op_sel_hi:[0,1,1]
	v_pk_fma_f32 v[4:5], v[114:115], v[110:111], v[4:5] op_sel_hi:[0,1,1]
	v_mov_b32_e32 v113, v86
	v_mov_b32_e32 v184, v116
	v_mov_b32_e32 v185, v76
	v_mov_b32_e32 v76, v117
	v_mov_b32_e32 v116, v122
	v_mov_b32_e32 v117, v102
	s_waitcnt vmcnt(8)
	v_pk_fma_f32 v[6:7], v[152:153], v[24:25], v[6:7] op_sel_hi:[0,1,1]
	v_pk_fma_f32 v[8:9], v[152:153], v[36:37], v[8:9] op_sel_hi:[0,1,1]
	v_pk_fma_f32 v[2:3], v[152:153], v[52:53], v[2:3] op_sel_hi:[0,1,1]
	v_pk_fma_f32 v[4:5], v[152:153], v[64:65], v[4:5] op_sel_hi:[0,1,1]
	v_mov_b32_e32 v86, v151
	v_mov_b32_e32 v102, v123
	s_waitcnt vmcnt(7)
	v_pk_fma_f32 v[6:7], v[160:161], v[16:17], v[6:7] op_sel_hi:[0,1,1]
	v_pk_fma_f32 v[8:9], v[160:161], v[80:81], v[8:9] op_sel_hi:[0,1,1]
	v_pk_fma_f32 v[2:3], v[160:161], v[112:113], v[2:3] op_sel_hi:[0,1,1]
	v_pk_fma_f32 v[4:5], v[160:161], v[116:117], v[4:5] op_sel_hi:[0,1,1]
	v_mov_b32_e32 v122, v124
	v_mov_b32_e32 v123, v104
	s_waitcnt vmcnt(6)
	v_pk_fma_f32 v[6:7], v[162:163], v[26:27], v[6:7] op_sel_hi:[0,1,1]
	v_pk_fma_f32 v[8:9], v[162:163], v[46:47], v[8:9] op_sel_hi:[0,1,1]
	v_pk_fma_f32 v[2:3], v[162:163], v[86:87], v[2:3] op_sel_hi:[0,1,1]
	v_pk_fma_f32 v[4:5], v[162:163], v[102:103], v[4:5] op_sel_hi:[0,1,1]
	v_mov_b32_e32 v104, v125
	s_waitcnt vmcnt(5)
	v_pk_fma_f32 v[6:7], v[172:173], v[66:67], v[6:7] op_sel_hi:[0,1,1]
	v_pk_fma_f32 v[8:9], v[172:173], v[90:91], v[8:9] op_sel_hi:[0,1,1]
	v_pk_fma_f32 v[2:3], v[172:173], v[120:121], v[2:3] op_sel_hi:[0,1,1]
	v_pk_fma_f32 v[4:5], v[172:173], v[122:123], v[4:5] op_sel_hi:[0,1,1]
	v_mov_b32_e32 v124, v126
	v_mov_b32_e32 v125, v94
	s_waitcnt vmcnt(4)
	v_pk_fma_f32 v[6:7], v[174:175], v[28:29], v[6:7] op_sel_hi:[0,1,1]
	v_pk_fma_f32 v[8:9], v[174:175], v[48:49], v[8:9] op_sel_hi:[0,1,1]
	v_pk_fma_f32 v[2:3], v[174:175], v[88:89], v[2:3] op_sel_hi:[0,1,1]
	v_pk_fma_f32 v[4:5], v[174:175], v[104:105], v[4:5] op_sel_hi:[0,1,1]
	v_mov_b32_e32 v94, v127
	s_waitcnt vmcnt(3)
	v_pk_fma_f32 v[6:7], v[176:177], v[68:69], v[6:7] op_sel_hi:[0,1,1]
	v_pk_fma_f32 v[8:9], v[176:177], v[92:93], v[8:9] op_sel_hi:[0,1,1]
	v_pk_fma_f32 v[2:3], v[176:177], v[130:131], v[2:3] op_sel_hi:[0,1,1]
	v_pk_fma_f32 v[4:5], v[176:177], v[124:125], v[4:5] op_sel_hi:[0,1,1]
	v_add_u32_e32 v149, 16, v149
	v_mov_b32_e32 v126, v128
	v_mov_b32_e32 v127, v96
	s_waitcnt vmcnt(2)
	v_pk_fma_f32 v[6:7], v[178:179], v[30:31], v[6:7] op_sel_hi:[0,1,1]
	v_pk_fma_f32 v[8:9], v[178:179], v[42:43], v[8:9] op_sel_hi:[0,1,1]
	v_pk_fma_f32 v[2:3], v[178:179], v[74:75], v[2:3] op_sel_hi:[0,1,1]
	v_pk_fma_f32 v[4:5], v[178:179], v[94:95], v[4:5] op_sel_hi:[0,1,1]
	v_cmp_ge_i32_e64 s[6:7], v149, v1
	v_mov_b32_e32 v96, v129
	s_waitcnt vmcnt(1)
	v_pk_fma_f32 v[6:7], v[180:181], v[54:55], v[6:7] op_sel_hi:[0,1,1]
	v_pk_fma_f32 v[8:9], v[180:181], v[98:99], v[8:9] op_sel_hi:[0,1,1]
	v_pk_fma_f32 v[2:3], v[180:181], v[184:185], v[2:3] op_sel_hi:[0,1,1]
	v_pk_fma_f32 v[4:5], v[180:181], v[126:127], v[4:5] op_sel_hi:[0,1,1]
	v_add_u32_e32 v148, 64, v148
	s_or_b64 s[14:15], s[6:7], s[14:15]
	v_lshl_add_u64 v[142:143], v[142:143], 0, s[8:9]
	s_waitcnt vmcnt(0)
	v_pk_fma_f32 v[6:7], v[182:183], v[32:33], v[6:7] op_sel_hi:[0,1,1]
	v_pk_fma_f32 v[8:9], v[182:183], v[44:45], v[8:9] op_sel_hi:[0,1,1]
	v_pk_fma_f32 v[2:3], v[182:183], v[76:77], v[2:3] op_sel_hi:[0,1,1]
	v_pk_fma_f32 v[4:5], v[182:183], v[96:97], v[4:5] op_sel_hi:[0,1,1]
	s_andn2_b64 exec, exec, s[14:15]
	s_cbranch_execnz .LBB0_11
; __device__ __forceinline__ void p0_mod(const Args& a, LAS unsigned char* lds) {
;     ...
;         for (int b = 0; b < 8; ++b) red[(dch * 32 + el) * 8 + b] = acc[b];
;         __syncthreads();
;         if (tid < 256) {
;             const int e2 = tid & 31, b = tid >> 5; float s = 0.f;
;             for (int k = 0; k < 16; ++k) s += red[(k * 32 + e2) * 8 + b];
;             mod[((size_t)l * NB + b) * 6144 + e0 + e2] = s + a.in[I_ADAB][l * 6144 + e0 + e2];
;         }
	s_or_b64 exec, exec, s[14:15]
	ds_write_b128 v146, v[6:9] offset:32768
	ds_write_b128 v146, v[2:5] offset:32784
	s_waitcnt lgkmcnt(0)
	s_barrier
	s_and_saveexec_b64 s[6:7], s[4:5]
	s_cbranch_execz .LBB0_9
	s_mul_i32 s14, s17, 0x1800
	s_add_i32 s14, s14, s12
	v_or_b32_e32 v2, s14, v134
	v_ashrrev_i32_e32 v3, 31, v2
	v_lshl_add_u64 v[2:3], v[2:3], 2, s[10:11]
	global_load_dword v20, v[2:3], off
	ds_read2st64_b32 v[2:3], v147 offset0:128 offset1:132
	ds_read2st64_b32 v[4:5], v147 offset0:136 offset1:140
	ds_read2st64_b32 v[6:7], v147 offset0:144 offset1:148
	ds_read2st64_b32 v[8:9], v147 offset0:152 offset1:156
	ds_read2st64_b32 v[10:11], v147 offset0:160 offset1:164
	ds_read2st64_b32 v[12:13], v147 offset0:168 offset1:172
	ds_read2st64_b32 v[14:15], v147 offset0:176 offset1:180
	ds_read2st64_b32 v[16:17], v147 offset0:184 offset1:188
	s_waitcnt lgkmcnt(7)
	v_add_f32_e32 v2, 0, v2
	v_add_f32_e32 v2, v2, v3
	s_waitcnt lgkmcnt(6)
	v_add_f32_e32 v2, v2, v4
	v_add_f32_e32 v2, v2, v5
	s_waitcnt lgkmcnt(5)
	v_add_f32_e32 v2, v2, v6
	v_add_f32_e32 v2, v2, v7
	s_waitcnt lgkmcnt(4)
	v_add_f32_e32 v2, v2, v8
	v_add_f32_e32 v2, v2, v9
	s_waitcnt lgkmcnt(3)
	v_add_f32_e32 v2, v2, v10
	v_add_f32_e32 v2, v2, v11
	s_waitcnt lgkmcnt(2)
	v_add_f32_e32 v2, v2, v12
	v_add_f32_e32 v2, v2, v13
	s_waitcnt lgkmcnt(1)
	v_add_f32_e32 v2, v2, v14
	v_lshl_add_u32 v21, s17, 3, v136
	v_mov_b64_e32 v[18:19], s[0:1]
	v_add_f32_e32 v2, v2, v15
	v_mad_i64_i32 v[18:19], s[14:15], v21, s3, v[18:19]
	s_waitcnt lgkmcnt(0)
	v_add_f32_e32 v2, v2, v16
	v_lshl_add_u64 v[18:19], s[12:13], 2, v[18:19]
	v_add_f32_e32 v2, v2, v17
	s_waitcnt vmcnt(0)
	v_add_f32_e32 v4, v2, v20
	v_lshl_add_u64 v[2:3], v[18:19], 0, v[138:139]
	global_store_dword v[2:3], v4, off sc1
	s_branch .LBB0_9

; #define LAS __attribute__((address_space(3)))
; __device__ __forceinline__ unsigned pk2(float lo, float hi) { pk2_f32x2 v = {lo, hi}; pk2_bf16x2 b = __builtin_convertvector(v, pk2_bf16x2); return __builtin_bit_cast(unsigned, b); }
;     ...
;         for (int i = 0; i < 32; ++i) scr[(2 * i + (lane >> 5)) * 33 + (lane & 31)] = tv[i];
;         if (it + ngw < I_E) { const PrepItem q = prep_decode(a, l, it + ngw);
; #pragma unroll
;             for (int i = 0; i < 32; ++i) tv[i] = __builtin_nontemporal_load(q.src + (size_t)(2 * i + (lane >> 5)) * q.ldw + (lane & 31)); }
;         asm volatile("s_waitcnt lgkmcnt(0)" ::: "memory");
;         const int c = lane & 7;
; #pragma unroll
;         for (int j = 0; j < 4; ++j) { const int n = (lane >> 3) + 8 * j; const LAS float* sp = scr + (8 * c) * 33 + n;
;             u32x4 o; o.x = pk2(sp[0 * 33], sp[1 * 33]); o.y = pk2(sp[2 * 33], sp[3 * 33]); o.z = pk2(sp[4 * 33], sp[5 * 33]); o.w = pk2(sp[6 * 33], sp[7 * 33]);
;             *(u32x4*)(p.dst + (size_t)n * p.K + 8 * c) = o; }
;         asm volatile("s_waitcnt lgkmcnt(0)" ::: "memory");
.LBB0_30:
	s_or_b64 exec, exec, s[24:25]
	s_waitcnt lgkmcnt(0)
	v_add_u32_e32 v41, 0xc000, v77
	ds_read2_b32 v[96:97], v41 offset0:33 offset1:41
	ds_read2_b32 v[98:99], v41 offset1:8
	ds_read2_b32 v[100:101], v41 offset0:66 offset1:74
	ds_read2_b32 v[102:103], v41 offset0:99 offset1:107
	ds_read2_b32 v[104:105], v41 offset0:132 offset1:140
	ds_read2_b32 v[106:107], v41 offset0:165 offset1:173
	ds_read2_b32 v[108:109], v41 offset0:198 offset1:206
	ds_read2_b32 v[110:111], v41 offset0:231 offset1:239
	v_mov_b32_e32 v39, v35
	v_lshl_add_u64 v[42:43], v[42:43], 0, v[38:39]
	v_mul_u32_u24_e32 v39, v40, v76
	v_lshlrev_b32_e32 v112, 1, v39
	v_mov_b32_e32 v113, v35
	s_waitcnt lgkmcnt(6)
	v_cvt_pk_bf16_f32 v92, v98, v96
	s_waitcnt lgkmcnt(4)
	v_cvt_pk_bf16_f32 v93, v100, v102
	s_waitcnt lgkmcnt(2)
	v_cvt_pk_bf16_f32 v94, v104, v106
	s_waitcnt lgkmcnt(0)
	v_cvt_pk_bf16_f32 v95, v108, v110
	v_lshl_add_u64 v[112:113], v[42:43], 0, v[112:113]
	global_store_dwordx4 v[112:113], v[92:95], off sc1
	v_mul_u32_u24_e32 v39, v40, v78
	v_lshlrev_b32_e32 v96, 1, v39
	v_cvt_pk_bf16_f32 v92, v99, v97
	v_cvt_pk_bf16_f32 v93, v101, v103
	v_cvt_pk_bf16_f32 v94, v105, v107
	v_cvt_pk_bf16_f32 v95, v109, v111
	ds_read2_b32 v[98:99], v41 offset0:16 offset1:24
	ds_read2_b32 v[100:101], v41 offset0:49 offset1:57
	ds_read2_b32 v[102:103], v41 offset0:82 offset1:90
	ds_read2_b32 v[104:105], v41 offset0:115 offset1:123
	ds_read2_b32 v[106:107], v41 offset0:148 offset1:156
	ds_read2_b32 v[108:109], v41 offset0:181 offset1:189
	ds_read2_b32 v[110:111], v41 offset0:214 offset1:222
	ds_read2_b32 v[112:113], v41 offset0:247 offset1:255
	v_mov_b32_e32 v97, v35
	v_lshl_add_u64 v[96:97], v[42:43], 0, v[96:97]
	v_mul_u32_u24_e32 v39, v40, v79
	global_store_dwordx4 v[96:97], v[92:95], off sc1
	v_lshlrev_b32_e32 v96, 1, v39
	v_mov_b32_e32 v97, v35
	v_mul_u32_u24_e32 v39, v40, v80
	s_waitcnt lgkmcnt(6)
	v_cvt_pk_bf16_f32 v92, v98, v100
	s_waitcnt lgkmcnt(4)
	v_cvt_pk_bf16_f32 v93, v102, v104
	s_waitcnt lgkmcnt(2)
	v_cvt_pk_bf16_f32 v94, v106, v108
	s_waitcnt lgkmcnt(0)
	v_cvt_pk_bf16_f32 v95, v110, v112
	v_lshl_add_u64 v[96:97], v[42:43], 0, v[96:97]
	v_lshlrev_b32_e32 v40, 1, v39
	v_mov_b32_e32 v41, v35
	global_store_dwordx4 v[96:97], v[92:95], off sc1
	v_lshl_add_u64 v[40:41], v[42:43], 0, v[40:41]
	s_and_b64 s[4:5], exec, vcc
	v_cvt_pk_bf16_f32 v92, v99, v101
	v_cvt_pk_bf16_f32 v93, v103, v105
	v_cvt_pk_bf16_f32 v94, v107, v109
	v_cvt_pk_bf16_f32 v95, v111, v113
	global_store_dwordx4 v[40:41], v[92:95], off sc1
	s_waitcnt lgkmcnt(0)
	s_or_b64 s[20:21], s[4:5], s[20:21]
	v_add_u32_e32 v36, s2, v36
	v_add_u32_e32 v81, s3, v81
	v_add_u32_e32 v82, s34, v82
	v_add_u32_e32 v83, s35, v83
	v_add_u32_e32 v84, s38, v84
	v_add_u32_e32 v85, s39, v85
	v_add_u32_e32 v86, s40, v86
	v_add_u32_e32 v87, s41, v87
	v_mov_b32_e32 v39, v44
	s_andn2_b64 exec, exec, s[20:21]
	s_cbranch_execz .LBB0_56

; __device__ __forceinline__ unsigned xb_add(unsigned* p, unsigned v) { return __hip_atomic_fetch_add(p, v, __ATOMIC_RELAXED, __HIP_MEMORY_SCOPE_AGENT); }
; __device__ __forceinline__ void xcd_barrier(const XcdBarrier& b) {
;     ...
;         if (old + 1u == (gen + 1u) * nloc) {
;             __builtin_amdgcn_fence(__ATOMIC_RELEASE, "agent");
;             asm volatile("s_waitcnt vmcnt(0)" ::: "memory");
;             const unsigned og = xb_add(&bar[XB_TOP], 1u);
.LBB0_85:
	s_andn2_saveexec_b64 s[4:5], s[4:5]
	s_cbranch_execz .LBB0_101
	v_mov_b32_e32 v1, s38
	v_add_co_u32_e32 v4, vcc, 0x3000, v1
	v_mov_b32_e32 v1, s39
	s_waitcnt vmcnt(0)
	v_addc_co_u32_e32 v5, vcc, 0, v1, vcc
	v_mov_b32_e32 v1, 1
	flat_atomic_add v1, v[4:5], v1 offset:1024 sc0
	v_cvt_f32_u32_e32 v3, v2
	v_sub_u32_e32 v4, 0, v2
	s_add_u32 s4, s38, 0x3500
	s_addc_u32 s5, s39, 0
	v_rcp_iflag_f32_e32 v3, v3
	s_mov_b64 s[8:9], -1
	v_mul_f32_e32 v3, 0x4f7ffffe, v3
	v_cvt_u32_f32_e32 v3, v3
	v_mul_lo_u32 v4, v4, v3
	v_mul_hi_u32 v4, v3, v4
	v_add_u32_e32 v3, v3, v4
	s_waitcnt vmcnt(0) lgkmcnt(0)
	v_mul_hi_u32 v3, v1, v3
	v_mul_lo_u32 v5, v3, v2
	v_add_u32_e32 v4, 1, v1
	v_sub_u32_e32 v1, v1, v5
	v_add_u32_e32 v6, 1, v3
	v_cmp_ge_u32_e32 vcc, v1, v2
	v_sub_u32_e32 v5, v1, v2
	s_nop 0
	v_cndmask_b32_e32 v3, v3, v6, vcc
	v_cndmask_b32_e32 v1, v1, v5, vcc
	v_add_u32_e32 v5, 1, v3
	v_cmp_ge_u32_e32 vcc, v1, v2
	s_nop 1
	v_cndmask_b32_e32 v1, v3, v5, vcc
	v_mad_u64_u32 v[2:3], s[6:7], v2, v1, v[2:3]
	v_cmp_ne_u32_e32 vcc, v4, v2
	v_mov_b64_e32 v[2:3], s[4:5]
	s_and_saveexec_b64 s[6:7], vcc
	s_cbranch_execz .LBB0_98
	v_mov_b64_e32 v[2:3], s[4:5]
	flat_load_dword v2, v[2:3] sc1
	s_mov_b64 s[12:13], 0
	s_waitcnt vmcnt(0) lgkmcnt(0)
	v_cmp_eq_u32_e32 vcc, v2, v1
	s_and_saveexec_b64 s[10:11], vcc
	s_cbranch_execz .LBB0_97
	s_add_u32 s8, s38, 0x200
	s_addc_u32 s9, s39, 0
	s_mov_b32 s3, 1
	s_branch .LBB0_90

; __device__ __forceinline__ unsigned pk2(float lo, float hi) { pk2_f32x2 v = {lo, hi}; pk2_bf16x2 b = __builtin_convertvector(v, pk2_bf16x2); return __builtin_bit_cast(unsigned, b); }
; __device__ __forceinline__ void n1_norm(const Args& a, LAS unsigned char* lds, int layer, bool dry = false) {
;     ...
; #pragma unroll
;             for (int q2 = 0; q2 < 2; ++q2) {
;                 const int row = row0 + i + q2;
;                 if (layer > 0 && !dry) {
;                     bf16_t* xb = (bf16_t*)(a.ws + WS_XB) + (size_t)row * D;
; #pragma unroll
;                     for (int jp = 0; jp < 2; ++jp) { u32x4 xo; xo.x = pk2(v[q2][2 * jp].x, v[q2][2 * jp].y); xo.y = pk2(v[q2][2 * jp].z, v[q2][2 * jp].w); xo.z = pk2(v[q2][2 * jp + 1].x, v[q2][2 * jp + 1].y); xo.w = pk2(v[q2][2 * jp + 1].z, v[q2][2 * jp + 1].w);
;                         *(u32x4*)(xb + 8 * lane + 512 * jp) = xo; }
;                 }
;                 ss[q2] = 0.f;
; #pragma unroll
;                 for (int j = 0; j < 4; ++j) ss[q2] += v[q2][j].x * v[q2][j].x + v[q2][j].y * v[q2][j].y + v[q2][j].z * v[q2][j].z + v[q2][j].w * v[q2][j].w;
;             }
; #pragma unroll
;             for (int o2 = 1; o2 < 64; o2 <<= 1) { ss[0] += __shfl_xor(ss[0], o2); ss[1] += __shfl_xor(ss[1], o2); }
; #pragma unroll
;             for (int q2 = 0; q2 < 2; ++q2) {
;                 const int row = row0 + i + q2;
;                 const float rstd = rsqrtf(ss[q2] * (1.f / D) + RMS_EPS);
; #pragma unroll
;                 for (int q = 0; q < 4; ++q) fl[q2][q] = 0.f;
; #pragma unroll
;                 for (int jp = 0; jp < 2; ++jp) {
;                     f32x4 h[2];
; #pragma unroll
;                     for (int k = 0; k < 2; ++k) {
;                         const int col = 8 * lane + 512 * jp + 4 * k;
;                         h[k] = v[q2][2 * jp + k] * rstd * ga[2 * jp + k] + s0v[2 * jp + k];
; #pragma unroll
;                         for (int q = 0; q < 4; ++q) fl[q2][q] += h[k].x * wf[(col + 0) * 4 + q] + h[k].y * wf[(col + 1) * 4 + q] + h[k].z * wf[(col + 2) * 4 + q] + h[k].w * wf[(col + 3) * 4 + q];
;                     }
;                     u32x4 o; o.x = pk2(h[0].x, h[0].y); o.y = pk2(h[0].z, h[0].w); o.z = pk2(h[1].x, h[1].y); o.w = pk2(h[1].z, h[1].w);
;                     *(u32x4*)(act + (size_t)row * D + 8 * lane + 512 * jp) = o;
;                 }
;             }
.LBB0_133:
	v_lshlrev_b64 v[148:149], 11, v[226:227]
	v_lshl_add_u64 v[152:153], v[204:205], 0, v[148:149]
	v_cvt_pk_bf16_f32 v148, v184, v185
	v_cvt_pk_bf16_f32 v149, v186, v187
	v_cvt_pk_bf16_f32 v150, v180, v181
	v_cvt_pk_bf16_f32 v151, v182, v183
	global_store_dwordx4 v[152:153], v[148:151], off sc1
	s_nop 1
	v_cvt_pk_bf16_f32 v148, v168, v169
	v_cvt_pk_bf16_f32 v149, v170, v171
	v_cvt_pk_bf16_f32 v150, v164, v165
	v_cvt_pk_bf16_f32 v151, v166, v167
	global_store_dwordx4 v[152:153], v[148:151], off offset:1024 sc1
.LBB0_134:
	s_nop 1
	v_add_u32_e32 v148, 1, v226
	v_ashrrev_i32_e32 v149, 31, v148
	s_and_b64 vcc, exec, s[10:11]
	v_lshlrev_b64 v[148:149], 11, v[148:149]
	s_cbranch_vccnz .LBB0_136
	v_lshl_add_u64 v[154:155], v[204:205], 0, v[148:149]
	v_cvt_pk_bf16_f32 v150, v172, v173
	v_cvt_pk_bf16_f32 v151, v174, v175
	v_cvt_pk_bf16_f32 v152, v176, v177
	v_cvt_pk_bf16_f32 v153, v178, v179
	global_store_dwordx4 v[154:155], v[150:153], off sc1
	s_nop 1
	v_cvt_pk_bf16_f32 v150, v156, v157
	v_cvt_pk_bf16_f32 v151, v158, v159
	v_cvt_pk_bf16_f32 v152, v160, v161
	v_cvt_pk_bf16_f32 v153, v162, v163
	global_store_dwordx4 v[154:155], v[150:153], off offset:1024 sc1
.LBB0_136:
	v_mul_f32_e32 v34, v185, v185
	s_nop 0
	v_mul_f32_e32 v150, v181, v181
	v_fmac_f32_e32 v34, v184, v184
	v_fmac_f32_e32 v150, v180, v180
	v_fmac_f32_e32 v34, v186, v186
	v_fmac_f32_e32 v150, v182, v182
	v_fmac_f32_e32 v34, v187, v187
	v_fmac_f32_e32 v150, v183, v183
	v_add_f32_e32 v34, v150, v34
	v_mul_f32_e32 v150, v169, v169
	v_fmac_f32_e32 v150, v168, v168
	v_fmac_f32_e32 v150, v170, v170
	v_fmac_f32_e32 v150, v171, v171
	v_add_f32_e32 v34, v150, v34
	v_mul_f32_e32 v150, v165, v165
	v_fmac_f32_e32 v150, v164, v164
	v_fmac_f32_e32 v150, v166, v166
	v_fmac_f32_e32 v150, v167, v167
	v_mov_b32_e32 v152, v177
	v_mov_b32_e32 v153, v173
	v_add_f32_e32 v34, v150, v34
	v_mov_b32_e32 v150, v176
	v_mov_b32_e32 v151, v172
	v_pk_mul_f32 v[152:153], v[152:153], v[152:153]
	v_mov_b32_e32 v154, v161
	v_pk_fma_f32 v[150:151], v[150:151], v[150:151], v[152:153]
	v_mov_b32_e32 v152, v178
	v_mov_b32_e32 v153, v174
	v_pk_fma_f32 v[150:151], v[152:153], v[152:153], v[150:151]
	v_mov_b32_e32 v152, v179
	v_mov_b32_e32 v153, v175
	v_mov_b32_e32 v155, v157
	v_pk_fma_f32 v[150:151], v[152:153], v[152:153], v[150:151]
	v_mov_b32_e32 v152, v160
	v_mov_b32_e32 v153, v156
	v_pk_mul_f32 v[154:155], v[154:155], v[154:155]
	v_pk_add_f32 v[150:151], v[150:151], v[150:151] op_sel:[0,1] op_sel_hi:[1,0]
	v_pk_fma_f32 v[152:153], v[152:153], v[152:153], v[154:155]
	v_mov_b32_e32 v154, v162
	v_mov_b32_e32 v155, v158
	v_pk_fma_f32 v[152:153], v[154:155], v[154:155], v[152:153]
	v_mov_b32_e32 v154, v163
	v_mov_b32_e32 v155, v159
	v_pk_fma_f32 v[152:153], v[154:155], v[154:155], v[152:153]
	s_mov_b32 s20, 0x3a800000
	v_pk_add_f32 v[150:151], v[152:153], v[150:151] op_sel:[1,0] op_sel_hi:[0,1]
	v_pk_add_f32 v[150:151], v[152:153], v[150:151]
	ds_bpermute_b32 v153, v200, v34
	ds_bpermute_b32 v152, v200, v150
	v_mov_b32_e32 v151, v34
	v_lshl_add_u64 v[148:149], v[190:191], 0, v[148:149]
	s_waitcnt lgkmcnt(0)
	v_pk_add_f32 v[150:151], v[150:151], v[152:153]
	ds_bpermute_b32 v153, v243, v151
	ds_bpermute_b32 v152, v243, v150
	s_waitcnt lgkmcnt(0)
	v_pk_add_f32 v[150:151], v[150:151], v[152:153]
	ds_bpermute_b32 v153, v244, v151
	ds_bpermute_b32 v152, v244, v150
	s_waitcnt lgkmcnt(0)
	v_pk_add_f32 v[150:151], v[150:151], v[152:153]
	ds_bpermute_b32 v153, v245, v151
	ds_bpermute_b32 v152, v245, v150
	s_waitcnt lgkmcnt(0)
	v_pk_add_f32 v[150:151], v[150:151], v[152:153]
	ds_bpermute_b32 v153, v246, v151
	ds_bpermute_b32 v152, v246, v150
	s_waitcnt lgkmcnt(0)
	v_pk_add_f32 v[150:151], v[150:151], v[152:153]
	ds_bpermute_b32 v153, v247, v151
	ds_bpermute_b32 v152, v247, v150
	s_waitcnt lgkmcnt(0)
	v_pk_add_f32 v[150:151], v[150:151], v[152:153]
	s_nop 0
	v_pk_fma_f32 v[154:155], v[150:151], s[20:21], v[198:199] op_sel_hi:[1,0,0]
	v_lshlrev_b64 v[150:151], 11, v[226:227]
	v_mul_f32_e32 v34, 0x4b800000, v155
	v_cmp_gt_f32_e32 vcc, s76, v155
	v_lshl_add_u64 v[226:227], v[190:191], 0, v[150:151]
	s_nop 0
	v_cndmask_b32_e32 v34, v155, v34, vcc
	v_rsq_f32_e32 v34, v34
	s_nop 0
	v_mul_f32_e32 v150, 0x45800000, v34
	v_cndmask_b32_e32 v34, v34, v150, vcc
	v_pk_mul_f32 v[150:151], v[184:185], v[34:35] op_sel_hi:[1,0]
	v_pk_mul_f32 v[180:181], v[180:181], v[34:35] op_sel_hi:[1,0]
	v_pk_fma_f32 v[150:151], v[212:213], v[150:151], v[72:73]
	v_pk_mul_f32 v[152:153], v[186:187], v[34:35] op_sel_hi:[1,0]
	v_mul_f32_e32 v155, v6, v151
	v_pk_fma_f32 v[180:181], v[216:217], v[180:181], v[68:69]
	v_pk_fma_f32 v[152:153], v[210:211], v[152:153], v[74:75]
	v_fmac_f32_e32 v155, v2, v150
	v_pk_mul_f32 v[182:183], v[182:183], v[34:35] op_sel_hi:[1,0]
	v_mul_f32_e32 v187, v181, v22
	v_fmac_f32_e32 v155, v10, v152
	v_pk_fma_f32 v[182:183], v[214:215], v[182:183], v[70:71]
	v_fmac_f32_e32 v187, v180, v18
	v_fmac_f32_e32 v155, v14, v153
	v_mul_f32_e32 v184, v7, v151
	v_mul_f32_e32 v185, v8, v151
	v_mul_f32_e32 v186, v151, v9
	v_fmac_f32_e32 v187, v182, v26
	v_add_f32_e32 v155, 0, v155
	v_fmac_f32_e32 v184, v3, v150
	v_fmac_f32_e32 v185, v4, v150
	v_fmac_f32_e32 v186, v5, v150
	v_fmac_f32_e32 v187, v183, v30
	v_fmac_f32_e32 v184, v11, v152
	v_fmac_f32_e32 v185, v12, v152
	v_fmac_f32_e32 v186, v152, v13
	v_add_f32_e32 v155, v155, v187
	v_mul_f32_e32 v187, v181, v23
	v_fmac_f32_e32 v184, v15, v153
	v_fmac_f32_e32 v185, v16, v153
	v_fmac_f32_e32 v186, v153, v17
	v_fmac_f32_e32 v187, v180, v19
	v_cvt_pk_bf16_f32 v150, v150, v151
	v_cvt_pk_bf16_f32 v151, v152, v153
	v_cvt_pk_bf16_f32 v152, v180, v181
	v_cvt_pk_bf16_f32 v153, v182, v183
; __device__ __forceinline__ unsigned pk2(float lo, float hi) { pk2_f32x2 v = {lo, hi}; pk2_bf16x2 b = __builtin_convertvector(v, pk2_bf16x2); return __builtin_bit_cast(unsigned, b); }
; __device__ __forceinline__ void n1_norm(const Args& a, LAS unsigned char* lds, int layer, bool dry = false) {
;     ...
;             for (int q2 = 0; q2 < 2; ++q2) {
;                 const int row = row0 + i + q2;
;                 const float rstd = rsqrtf(ss[q2] * (1.f / D) + RMS_EPS);
; #pragma unroll
;                 for (int q = 0; q < 4; ++q) fl[q2][q] = 0.f;
; #pragma unroll
;                 for (int jp = 0; jp < 2; ++jp) {
;                     f32x4 h[2];
; #pragma unroll
;                     for (int k = 0; k < 2; ++k) {
;                         const int col = 8 * lane + 512 * jp + 4 * k;
;                         h[k] = v[q2][2 * jp + k] * rstd * ga[2 * jp + k] + s0v[2 * jp + k];
; #pragma unroll
;                         for (int q = 0; q < 4; ++q) fl[q2][q] += h[k].x * wf[(col + 0) * 4 + q] + h[k].y * wf[(col + 1) * 4 + q] + h[k].z * wf[(col + 2) * 4 + q] + h[k].w * wf[(col + 3) * 4 + q];
;                     }
;                     u32x4 o; o.x = pk2(h[0].x, h[0].y); o.y = pk2(h[0].z, h[0].w); o.z = pk2(h[1].x, h[1].y); o.w = pk2(h[1].z, h[1].w);
;                     *(u32x4*)(act + (size_t)row * D + 8 * lane + 512 * jp) = o;
;                 }
;             }
	v_fmac_f32_e32 v187, v182, v27
	global_store_dwordx4 v[226:227], v[150:153], off sc1
	v_add_f32_e32 v184, 0, v184
	v_fmac_f32_e32 v187, v183, v31
	v_pk_mul_f32 v[150:151], v[168:169], v[34:35] op_sel_hi:[1,0]
	v_pk_mul_f32 v[164:165], v[164:165], v[34:35] op_sel_hi:[1,0]
	v_pk_fma_f32 v[150:151], v[220:221], v[150:151], v[88:89]
	v_add_f32_e32 v184, v184, v187
	v_mul_f32_e32 v187, v181, v24
	v_pk_mul_f32 v[152:153], v[170:171], v[34:35] op_sel_hi:[1,0]
	v_mul_f32_e32 v168, v151, v40
	v_pk_fma_f32 v[164:165], v[224:225], v[164:165], v[84:85]
	v_fmac_f32_e32 v187, v180, v20
	v_pk_fma_f32 v[152:153], v[218:219], v[152:153], v[90:91]
	v_fmac_f32_e32 v168, v150, v36
	v_pk_mul_f32 v[166:167], v[166:167], v[34:35] op_sel_hi:[1,0]
	v_mul_f32_e32 v34, v165, v56
	v_fmac_f32_e32 v187, v182, v28
	v_fmac_f32_e32 v168, v152, v44
	v_pk_fma_f32 v[166:167], v[222:223], v[166:167], v[86:87]
	v_fmac_f32_e32 v34, v164, v52
	v_add_f32_e32 v185, 0, v185
	v_fmac_f32_e32 v187, v183, v32
	v_fmac_f32_e32 v168, v153, v48
	v_fmac_f32_e32 v34, v166, v60
	v_add_f32_e32 v185, v185, v187
	v_mul_f32_e32 v187, v181, v25
	v_add_f32_e32 v155, v155, v168
	v_mul_f32_e32 v168, v151, v41
	v_fmac_f32_e32 v34, v167, v64
	v_fmac_f32_e32 v187, v180, v21
	v_fmac_f32_e32 v168, v150, v37
	v_add_f32_e32 v180, v155, v34
	v_mul_f32_e32 v34, v165, v57
	v_fmac_f32_e32 v168, v152, v45
	v_fmac_f32_e32 v34, v164, v53
	v_fmac_f32_e32 v168, v153, v49
	v_fmac_f32_e32 v34, v166, v61
	v_add_f32_e32 v168, v184, v168
	v_mul_f32_e32 v169, v151, v42
	v_fmac_f32_e32 v34, v167, v65
	v_fmac_f32_e32 v169, v150, v38
	v_add_f32_e32 v181, v168, v34
	v_mul_f32_e32 v34, v165, v58
	v_fmac_f32_e32 v169, v152, v46
	v_fmac_f32_e32 v34, v164, v54
	v_fmac_f32_e32 v169, v153, v50
	v_fmac_f32_e32 v34, v166, v62
	v_add_f32_e32 v169, v185, v169
	v_mul_f32_e32 v170, v151, v43
	v_fmac_f32_e32 v34, v167, v66
	v_fmac_f32_e32 v187, v182, v29
	v_fmac_f32_e32 v170, v150, v39
	v_add_f32_e32 v182, v169, v34
	v_mul_f32_e32 v34, v165, v59
	v_add_f32_e32 v186, 0, v186
	v_fmac_f32_e32 v187, v183, v33
	v_fmac_f32_e32 v170, v152, v47
	v_fmac_f32_e32 v34, v164, v55
	v_add_f32_e32 v186, v186, v187
	v_fmac_f32_e32 v170, v153, v51
	v_fmac_f32_e32 v34, v166, v63
	v_add_f32_e32 v170, v186, v170
	v_fmac_f32_e32 v34, v167, v67
	v_add_f32_e32 v183, v170, v34
	v_mul_f32_e32 v34, 0x4b800000, v154
	v_cmp_gt_f32_e32 vcc, s76, v154
	v_cvt_pk_bf16_f32 v150, v150, v151
	v_cvt_pk_bf16_f32 v151, v152, v153
	v_cndmask_b32_e32 v34, v154, v34, vcc
	v_rsq_f32_e32 v34, v34
	v_cvt_pk_bf16_f32 v152, v164, v165
	v_cvt_pk_bf16_f32 v153, v166, v167
	global_store_dwordx4 v[226:227], v[150:153], off offset:1024 sc1
	s_nop 1
	v_mul_f32_e32 v150, 0x45800000, v34
	v_cndmask_b32_e32 v34, v34, v150, vcc
	v_pk_mul_f32 v[150:151], v[172:173], v[34:35] op_sel_hi:[1,0]
	v_pk_mul_f32 v[152:153], v[174:175], v[34:35] op_sel_hi:[1,0]
	v_pk_fma_f32 v[150:151], v[212:213], v[150:151], v[72:73]
	v_pk_fma_f32 v[152:153], v[210:211], v[152:153], v[74:75]
	v_mul_f32_e32 v154, v151, v6
	v_fmac_f32_e32 v154, v150, v2
	v_fmac_f32_e32 v154, v152, v10
	v_fmac_f32_e32 v154, v153, v14
	v_add_f32_e32 v166, 0, v154
	v_mul_f32_e32 v154, v151, v7
	v_fmac_f32_e32 v154, v150, v3
	v_fmac_f32_e32 v154, v152, v11
	v_fmac_f32_e32 v154, v153, v15
	v_add_f32_e32 v167, 0, v154
	v_mul_f32_e32 v154, v151, v8
	v_fmac_f32_e32 v154, v150, v4
	v_fmac_f32_e32 v154, v152, v12
	v_fmac_f32_e32 v154, v153, v16
	v_add_f32_e32 v168, 0, v154
	v_mul_f32_e32 v154, v151, v9
	v_fmac_f32_e32 v154, v150, v5
	v_fmac_f32_e32 v154, v152, v13
	v_fmac_f32_e32 v154, v153, v17
	v_add_f32_e32 v169, 0, v154
	v_pk_mul_f32 v[154:155], v[176:177], v[34:35] op_sel_hi:[1,0]
	v_pk_mul_f32 v[164:165], v[178:179], v[34:35] op_sel_hi:[1,0]
	v_pk_fma_f32 v[154:155], v[216:217], v[154:155], v[68:69]
	v_pk_fma_f32 v[164:165], v[214:215], v[164:165], v[70:71]
	v_mul_f32_e32 v170, v155, v22
	v_fmac_f32_e32 v170, v154, v18
	v_fmac_f32_e32 v170, v164, v26
	v_fmac_f32_e32 v170, v165, v30
	v_add_f32_e32 v166, v166, v170
	v_mul_f32_e32 v170, v155, v23
	v_fmac_f32_e32 v170, v154, v19
	v_fmac_f32_e32 v170, v164, v27
	v_fmac_f32_e32 v170, v165, v31
	v_add_f32_e32 v167, v167, v170
	v_mul_f32_e32 v170, v155, v24
	v_fmac_f32_e32 v170, v154, v20
	v_fmac_f32_e32 v170, v164, v28
	v_fmac_f32_e32 v170, v165, v32
	v_add_f32_e32 v170, v168, v170
	v_mul_f32_e32 v168, v155, v25
	v_fmac_f32_e32 v168, v154, v21
	v_cvt_pk_bf16_f32 v150, v150, v151
	v_cvt_pk_bf16_f32 v151, v152, v153
	v_cvt_pk_bf16_f32 v152, v154, v155
	v_cvt_pk_bf16_f32 v153, v164, v165
	v_fmac_f32_e32 v168, v164, v29
	global_store_dwordx4 v[148:149], v[150:153], off sc1
	v_fmac_f32_e32 v168, v165, v33
	v_add_f32_e32 v171, v169, v168
	v_pk_mul_f32 v[150:151], v[156:157], v[34:35] op_sel_hi:[1,0]
	v_pk_mul_f32 v[152:153], v[158:159], v[34:35] op_sel_hi:[1,0]
	v_pk_fma_f32 v[150:151], v[220:221], v[150:151], v[88:89]
	v_pk_fma_f32 v[168:169], v[218:219], v[152:153], v[90:91]
	v_mul_f32_e32 v152, v151, v40
	v_fmac_f32_e32 v152, v150, v36
	v_fmac_f32_e32 v152, v168, v44
	v_fmac_f32_e32 v152, v169, v48
	v_add_f32_e32 v156, v166, v152
	v_mul_f32_e32 v152, v151, v41
	v_fmac_f32_e32 v152, v150, v37
	v_fmac_f32_e32 v152, v168, v45
	v_fmac_f32_e32 v152, v169, v49
	v_add_f32_e32 v157, v167, v152
	v_mul_f32_e32 v152, v151, v42
	v_fmac_f32_e32 v152, v150, v38
	v_fmac_f32_e32 v152, v168, v46
	v_fmac_f32_e32 v152, v169, v50
	v_add_f32_e32 v158, v170, v152
	v_mul_f32_e32 v152, v151, v43
	v_fmac_f32_e32 v152, v150, v39
	v_fmac_f32_e32 v152, v168, v47
	v_fmac_f32_e32 v152, v169, v51
	v_add_f32_e32 v159, v171, v152
	v_pk_mul_f32 v[152:153], v[160:161], v[34:35] op_sel_hi:[1,0]
	v_pk_mul_f32 v[154:155], v[162:163], v[34:35] op_sel_hi:[1,0]
	v_pk_fma_f32 v[172:173], v[224:225], v[152:153], v[84:85]
	v_pk_fma_f32 v[170:171], v[222:223], v[154:155], v[86:87]
	v_mul_f32_e32 v34, v173, v56
	v_mul_f32_e32 v152, v173, v57
	v_fmac_f32_e32 v34, v172, v52
	v_fmac_f32_e32 v152, v172, v53
	v_fmac_f32_e32 v34, v170, v60
	v_fmac_f32_e32 v152, v170, v61
	v_fmac_f32_e32 v34, v171, v64
	v_fmac_f32_e32 v152, v171, v65
	v_add_f32_e32 v34, v156, v34
	v_add_f32_e32 v152, v157, v152
	v_mul_f32_e32 v153, v173, v58
	v_mul_f32_e32 v154, v173, v59
	v_cvt_pk_bf16_f32 v166, v150, v151
	ds_bpermute_b32 v151, v200, v34
	ds_bpermute_b32 v155, v200, v181
	ds_bpermute_b32 v156, v200, v152
	ds_bpermute_b32 v157, v200, v182
	v_fmac_f32_e32 v153, v172, v54
	v_fmac_f32_e32 v154, v172, v55
	ds_bpermute_b32 v150, v200, v180
	v_fmac_f32_e32 v153, v170, v62
	v_fmac_f32_e32 v154, v170, v63
	v_fmac_f32_e32 v153, v171, v66
	v_fmac_f32_e32 v154, v171, v67
	v_add_f32_e32 v153, v158, v153
	v_add_f32_e32 v154, v159, v154
	s_waitcnt lgkmcnt(4)
; __device__ __forceinline__ float log_sigmoid_f(float v) { return fminf(v, 0.f) - log1pf(expf(-fabsf(v))); }
; __device__ __forceinline__ void n1_norm(const Args& a, LAS unsigned char* lds, int layer, bool dry = false) {
;     ...
; #pragma unroll
;             for (int o2 = 1; o2 < 64; o2 <<= 1) {
; #pragma unroll
;                 for (int q = 0; q < 4; ++q) { fl[0][q] += __shfl_xor(fl[0][q], o2); fl[1][q] += __shfl_xor(fl[1][q], o2); }
;             }
;             if (lane < 8) {
;                 const int q2 = lane >> 2, q = lane & 3;
;                 const float f = q2 == 0 ? (q == 0 ? fl[0][0] : q == 1 ? fl[0][1] : q == 2 ? fl[0][2] : fl[0][3]) : (q == 0 ? fl[1][0] : q == 1 ? fl[1][1] : q == 2 ? fl[1][2] : fl[1][3]);
;                 flog[(size_t)(row0 + i + q2) * 4 + q] = log_sigmoid_f(f + a.in[I_BFORGET][layer * 4 + q]);
	v_add_f32_e32 v34, v34, v151
	s_waitcnt lgkmcnt(3)
	v_add_f32_e32 v151, v181, v155
	s_waitcnt lgkmcnt(2)
	v_add_f32_e32 v152, v152, v156
	s_waitcnt lgkmcnt(1)
	v_add_f32_e32 v155, v182, v157
	ds_bpermute_b32 v156, v200, v153
	ds_bpermute_b32 v157, v200, v183
	ds_bpermute_b32 v158, v200, v154
	s_waitcnt lgkmcnt(3)
	v_add_f32_e32 v150, v180, v150
	ds_bpermute_b32 v160, v243, v34
	ds_bpermute_b32 v159, v243, v150
	s_waitcnt lgkmcnt(4)
	v_add_f32_e32 v153, v153, v156
	s_waitcnt lgkmcnt(3)
	v_add_f32_e32 v156, v183, v157
	s_waitcnt lgkmcnt(2)
	v_add_f32_e32 v154, v154, v158
	ds_bpermute_b32 v157, v243, v151
	ds_bpermute_b32 v158, v243, v152
	s_waitcnt lgkmcnt(3)
	v_add_f32_e32 v34, v34, v160
	ds_bpermute_b32 v160, v243, v153
	ds_bpermute_b32 v161, v243, v156
	s_waitcnt lgkmcnt(4)
	v_add_f32_e32 v150, v150, v159
	ds_bpermute_b32 v159, v243, v155
	s_waitcnt lgkmcnt(4)
	v_add_f32_e32 v151, v151, v157
	s_waitcnt lgkmcnt(3)
	v_add_f32_e32 v152, v152, v158
	ds_bpermute_b32 v157, v243, v154
	ds_bpermute_b32 v158, v244, v150
	s_waitcnt lgkmcnt(4)
	v_add_f32_e32 v153, v153, v160
	s_waitcnt lgkmcnt(3)
	v_add_f32_e32 v156, v156, v161
	ds_bpermute_b32 v160, v244, v151
	ds_bpermute_b32 v161, v244, v152
	s_waitcnt lgkmcnt(4)
	v_add_f32_e32 v155, v155, v159
	ds_bpermute_b32 v159, v244, v34
	s_waitcnt lgkmcnt(4)
	v_add_f32_e32 v154, v154, v157
	s_waitcnt lgkmcnt(3)
	v_add_f32_e32 v150, v150, v158
	ds_bpermute_b32 v157, v244, v155
	ds_bpermute_b32 v158, v244, v153
	s_waitcnt lgkmcnt(4)
	v_add_f32_e32 v151, v151, v160
	s_waitcnt lgkmcnt(3)
	v_add_f32_e32 v152, v152, v161
	ds_bpermute_b32 v160, v244, v154
	ds_bpermute_b32 v161, v245, v150
	s_waitcnt lgkmcnt(4)
	v_add_f32_e32 v34, v34, v159
	ds_bpermute_b32 v159, v244, v156
	s_waitcnt lgkmcnt(4)
	v_add_f32_e32 v155, v155, v157
	s_waitcnt lgkmcnt(3)
	v_add_f32_e32 v153, v153, v158
	s_waitcnt lgkmcnt(2)
	v_add_f32_e32 v154, v154, v160
	s_waitcnt lgkmcnt(1)
	v_add_f32_e32 v150, v150, v161
	ds_bpermute_b32 v157, v245, v34
	ds_bpermute_b32 v158, v245, v151
	ds_bpermute_b32 v160, v245, v155
	ds_bpermute_b32 v161, v245, v153
	s_waitcnt lgkmcnt(4)
	v_add_f32_e32 v156, v156, v159
	ds_bpermute_b32 v159, v245, v152
	s_waitcnt lgkmcnt(4)
	v_add_f32_e32 v34, v34, v157
	s_waitcnt lgkmcnt(3)
	v_add_f32_e32 v151, v151, v158
	s_waitcnt lgkmcnt(2)
	v_add_f32_e32 v157, v155, v160
	s_waitcnt lgkmcnt(1)
	v_add_f32_e32 v158, v153, v161
	ds_bpermute_b32 v153, v245, v156
	ds_bpermute_b32 v155, v245, v154
	s_waitcnt lgkmcnt(2)
	v_add_f32_e32 v152, v152, v159
	ds_bpermute_b32 v159, v246, v150
	ds_bpermute_b32 v160, v246, v34
	ds_bpermute_b32 v161, v246, v151
	s_waitcnt lgkmcnt(4)
	v_add_f32_e32 v156, v156, v153
	s_waitcnt lgkmcnt(3)
	v_add_f32_e32 v163, v154, v155
	s_waitcnt lgkmcnt(2)
	v_add_f32_e32 v153, v150, v159
	s_waitcnt lgkmcnt(1)
	v_add_f32_e32 v162, v34, v160
	s_waitcnt lgkmcnt(0)
	v_add_f32_e32 v150, v151, v161
	ds_bpermute_b32 v34, v246, v152
	ds_bpermute_b32 v151, v246, v157
	ds_bpermute_b32 v154, v246, v158
	ds_bpermute_b32 v159, v246, v156
	ds_bpermute_b32 v161, v246, v163
	s_waitcnt lgkmcnt(4)
	v_add_f32_e32 v155, v152, v34
	s_waitcnt lgkmcnt(3)
	v_add_f32_e32 v152, v157, v151
	s_waitcnt lgkmcnt(2)
	v_add_f32_e32 v160, v158, v154
	s_waitcnt lgkmcnt(1)
	v_add_f32_e32 v154, v156, v159
	s_waitcnt lgkmcnt(0)
	v_add_f32_e32 v161, v163, v161
	ds_bpermute_b32 v159, v247, v153
	ds_bpermute_b32 v165, v247, v162
	ds_bpermute_b32 v151, v247, v150
	ds_bpermute_b32 v158, v247, v155
	ds_bpermute_b32 v156, v247, v152
	ds_bpermute_b32 v163, v247, v160
	ds_bpermute_b32 v157, v247, v154
	ds_bpermute_b32 v164, v247, v161
	v_cvt_pk_bf16_f32 v167, v168, v169
	v_cvt_pk_bf16_f32 v168, v172, v173
	v_cvt_pk_bf16_f32 v169, v170, v171
	global_store_dwordx4 v[148:149], v[166:169], off offset:1024 sc1
	s_and_saveexec_b64 s[20:21], s[4:5]
	s_cbranch_execz .LBB0_154
	s_and_saveexec_b64 s[22:23], s[6:7]
	s_xor_b64 s[22:23], exec, s[22:23]
	s_cbranch_execz .LBB0_145
	s_waitcnt lgkmcnt(6)
	v_add_f32_e32 v34, v162, v165
	v_cmp_lt_i32_e32 vcc, 0, v1
	s_and_saveexec_b64 s[24:25], vcc
	s_cbranch_execz .LBB0_144
	v_cmp_ne_u32_e32 vcc, 1, v1
	s_and_saveexec_b64 s[26:27], vcc
	s_xor_b64 s[26:27], exec, s[26:27]
	s_cbranch_execz .LBB0_141
	s_waitcnt lgkmcnt(2)
	v_add_f32_e32 v34, v160, v163
	s_waitcnt lgkmcnt(0)
	v_add_f32_e32 v148, v161, v164
	v_cndmask_b32_e64 v34, v148, v34, s[8:9]

; __device__ __forceinline__ float log_sigmoid_f(float v) { return fminf(v, 0.f) - log1pf(expf(-fabsf(v))); }
; __device__ __forceinline__ void n1_norm(const Args& a, LAS unsigned char* lds, int layer, bool dry = false) {
;     ...
;             if (lane < 8) {
;                 const int q2 = lane >> 2, q = lane & 3;
;                 const float f = q2 == 0 ? (q == 0 ? fl[0][0] : q == 1 ? fl[0][1] : q == 2 ? fl[0][2] : fl[0][3]) : (q == 0 ? fl[1][0] : q == 1 ? fl[1][1] : q == 2 ? fl[1][2] : fl[1][3]);
;                 flog[(size_t)(row0 + i + q2) * 4 + q] = log_sigmoid_f(f + a.in[I_BFORGET][layer * 4 + q]);
.LBB0_153:
	s_or_b64 exec, exec, s[22:23]
	global_load_dword v148, v[206:207], off
	s_mov_b32 s22, 0xb2a5705f
	s_waitcnt vmcnt(0)
	v_add_f32_e32 v34, v34, v148
	v_mul_f32_e64 v148, |v34|, s60
	v_fma_f32 v149, |v34|, s60, -v148
	v_rndne_f32_e32 v150, v148
	v_fma_f32 v149, |v34|, s22, v149
	v_sub_f32_e32 v148, v148, v150
	v_add_f32_e32 v148, v148, v149
	v_exp_f32_e32 v148, v148
	v_cvt_i32_f32_e32 v149, v150
	s_mov_b32 s22, 0x42ce8ed0
	v_cmp_ngt_f32_e64 vcc, |v34|, s22
	s_mov_b32 s22, 0xc2b17218
	v_ldexp_f32 v148, v148, v149
	v_cndmask_b32_e32 v148, 0, v148, vcc
	v_cmp_nlt_f32_e64 vcc, |v34|, s22
	v_min_f32_e32 v162, 0, v34
	s_mov_b32 s22, 0x3f2aaaab
	v_cndmask_b32_e32 v34, v239, v148, vcc
	v_add_f32_e32 v150, 1.0, v34
	v_add_f32_e32 v148, -1.0, v150
	v_sub_f32_e32 v149, v148, v150
	v_add_f32_e32 v149, 1.0, v149
	v_sub_f32_e32 v148, v34, v148
	s_waitcnt lgkmcnt(5)
	v_add_f32_e32 v151, v148, v149
	v_frexp_mant_f32_e32 v148, v150
	v_cmp_gt_f32_e32 vcc, s22, v148
	v_cvt_f64_f32_e32 v[148:149], v150
	v_frexp_exp_i32_f64_e32 v148, v[148:149]
	s_waitcnt lgkmcnt(3)
	v_subbrev_co_u32_e32 v156, vcc, 0, v148, vcc
	v_sub_u32_e32 v148, 0, v156
	v_ldexp_f32 v149, v150, v148
	v_add_f32_e32 v150, -1.0, v149
	v_add_f32_e32 v152, 1.0, v149
	v_ldexp_f32 v148, v151, v148
	v_add_f32_e32 v151, 1.0, v150
	v_add_f32_e32 v153, -1.0, v152
	v_sub_f32_e32 v151, v149, v151
	v_sub_f32_e32 v149, v149, v153
	v_add_f32_e32 v151, v148, v151
	v_add_f32_e32 v148, v148, v149
	s_waitcnt lgkmcnt(1)
	v_add_f32_e32 v157, v152, v148
	v_rcp_f32_e32 v159, v157
	v_sub_f32_e32 v149, v152, v157
	v_add_f32_e32 v158, v148, v149
	v_add_f32_e32 v149, v150, v151
	v_mul_f32_e32 v161, v149, v159
	v_sub_f32_e32 v148, v150, v149
	v_mul_f32_e32 v150, v157, v161
	v_fma_f32 v152, v161, v157, -v150
	v_fmac_f32_e32 v152, v161, v158
	v_add_f32_e32 v160, v151, v148
	v_add_f32_e32 v148, v150, v152
	v_sub_f32_e32 v151, v149, v148
	v_pk_add_f32 v[154:155], v[148:149], v[150:151] neg_lo:[0,1] neg_hi:[0,1]
	v_mov_b32_e32 v153, v148
	v_pk_add_f32 v[148:149], v[154:155], v[152:153] neg_lo:[0,1] neg_hi:[0,1]
	s_mov_b32 s22, 0x3f317218
	v_add_f32_e32 v149, v160, v149
	v_add_f32_e32 v148, v148, v149
	v_add_f32_e32 v149, v151, v148
	v_mul_f32_e32 v160, v159, v149
	v_mul_f32_e32 v150, v157, v160
	v_fma_f32 v152, v160, v157, -v150
	v_fmac_f32_e32 v152, v160, v158
	v_sub_f32_e32 v151, v151, v149
	v_add_f32_e32 v157, v148, v151
	v_add_f32_e32 v148, v150, v152
	v_sub_f32_e32 v151, v149, v148
	v_pk_add_f32 v[154:155], v[148:149], v[150:151] neg_lo:[0,1] neg_hi:[0,1]
	v_mov_b32_e32 v153, v148
	v_pk_add_f32 v[148:149], v[154:155], v[152:153] neg_lo:[0,1] neg_hi:[0,1]
	s_nop 0
	v_add_f32_e32 v149, v157, v149
	v_add_f32_e32 v148, v148, v149
	v_add_f32_e32 v149, v161, v160
	v_add_f32_e32 v148, v151, v148
	v_sub_f32_e32 v150, v149, v161
	v_mul_f32_e32 v148, v159, v148
	v_sub_f32_e32 v150, v160, v150
	v_add_f32_e32 v150, v150, v148
	v_add_f32_e32 v152, v149, v150
	v_mul_f32_e32 v153, v152, v152
	v_mov_b32_e32 v148, 0x3ecc95a3
	v_fmamk_f32 v148, v153, 0x3e9b6dac, v148
	v_fmaak_f32 v203, v153, v148, 0x3f2aaada
	v_cvt_f32_i32_e32 v148, v156
	v_sub_f32_e32 v149, v152, v149
	v_sub_f32_e32 v149, v150, v149
	v_ldexp_f32 v154, v149, 1
	v_mul_f32_e32 v149, v152, v153
	v_ldexp_f32 v151, v152, 1
	v_pk_mul_f32 v[152:153], v[148:149], v[202:203]
	s_nop 0
	v_fma_f32 v150, v148, s22, -v152
	v_fmac_f32_e32 v150, 0xb102e308, v148
	v_pk_add_f32 v[148:149], v[152:153], v[150:151]
	s_mov_b32 s22, 0x7f800000
	v_sub_f32_e32 v151, v149, v151
	v_sub_f32_e32 v151, v153, v151
	v_add_f32_e32 v155, v154, v151
	v_mov_b32_e32 v154, v152
	v_pk_add_f32 v[152:153], v[148:149], v[152:153] neg_lo:[0,1] neg_hi:[0,1]
	v_pk_add_f32 v[156:157], v[148:149], v[154:155]
	v_mov_b32_e32 v151, v148
	v_mov_b32_e32 v153, v157
	v_pk_add_f32 v[158:159], v[150:151], v[152:153] neg_lo:[0,1] neg_hi:[0,1]
	v_pk_add_f32 v[150:151], v[150:151], v[152:153]
	v_mov_b32_e32 v154, v155
	v_pk_add_f32 v[152:153], v[150:151], v[148:149] op_sel:[1,0] op_sel_hi:[0,1] neg_lo:[0,1] neg_hi:[0,1]
	v_pk_add_f32 v[160:161], v[156:157], v[152:153] op_sel_hi:[1,0] neg_lo:[0,1] neg_hi:[0,1]
	v_mov_b32_e32 v156, v157
	v_mov_b32_e32 v157, v151
	v_pk_mov_b32 v[152:153], v[148:149], v[152:153] op_sel:[1,0]
	v_mov_b32_e32 v155, v148
	v_pk_add_f32 v[152:153], v[156:157], v[152:153] neg_lo:[0,1] neg_hi:[0,1]
	v_mov_b32_e32 v160, v158
	v_pk_add_f32 v[148:149], v[154:155], v[152:153] neg_lo:[0,1] neg_hi:[0,1]
	v_mov_b32_e32 v159, v151
	v_pk_add_f32 v[152:153], v[160:161], v[148:149]
	v_cmp_neq_f32_e32 vcc, s22, v34
	v_pk_add_f32 v[154:155], v[152:153], v[152:153] op_sel:[0,1] op_sel_hi:[1,0]
	s_mov_b32 s22, 0x33800000
	v_pk_add_f32 v[150:151], v[150:151], v[154:155] op_sel:[1,0] op_sel_hi:[0,1]
	v_mov_b32_e32 v153, v150
	v_pk_add_f32 v[156:157], v[152:153], v[158:159] neg_lo:[0,1] neg_hi:[0,1]
	v_mov_b32_e32 v149, v154
	v_sub_f32_e32 v151, v152, v156
	v_pk_add_f32 v[148:149], v[148:149], v[156:157] neg_lo:[0,1] neg_hi:[0,1]
	v_sub_f32_e32 v151, v158, v151
	v_add_f32_e32 v148, v148, v151
	v_add_f32_e32 v148, v148, v149
	v_add_f32_e32 v148, v150, v148
	v_cndmask_b32_e32 v148, v239, v148, vcc
	v_cmp_lt_f32_e64 vcc, |v34|, s22
	s_nop 1
	v_cndmask_b32_e32 v34, v148, v34, vcc
	v_add_u32_e32 v148, s2, v249
	v_ashrrev_i32_e32 v149, 31, v148
	v_sub_f32_e32 v34, v162, v34
	v_lshl_add_u64 v[148:149], v[148:149], 4, v[192:193]
	global_store_dword v[148:149], v34, off sc1

; __device__ __forceinline__ unsigned xb_ld(unsigned* p)              { return __hip_atomic_load(p, __ATOMIC_RELAXED, __HIP_MEMORY_SCOPE_AGENT); }
; __device__ __forceinline__ unsigned xb_add(unsigned* p, unsigned v) { return __hip_atomic_fetch_add(p, v, __ATOMIC_RELAXED, __HIP_MEMORY_SCOPE_AGENT); }
; #define XB_SPIN(cond, bar) do { unsigned _sp = 0; while (cond) { __builtin_amdgcn_s_sleep(1); \
;     if ((++_sp & 255u) == 0u) { if (xb_ld(&(bar)[XB_TMO])) break; if (_sp > XB_SPIN_CAP) { atomicAdd(&(bar)[XB_TMO], 1u); break; } } } } while (0)
; __device__ __forceinline__ void xcd_barrier(const XcdBarrier& b) {
;     ...
;         const unsigned old = xb_add(&bar[XB_XSUB(bx)], 1u);
;         const unsigned gen = old / nloc;
;         if (old + 1u == (gen + 1u) * nloc) {
;             __builtin_amdgcn_fence(__ATOMIC_RELEASE, "agent");
;             asm volatile("s_waitcnt vmcnt(0)" ::: "memory");
;             const unsigned og = xb_add(&bar[XB_TOP], 1u);
;             const unsigned tg = og / nx;
;             if (og + 1u == (tg + 1u) * nx) xb_add(&bar[XB_TOPGEN], 1u);
;             else XB_SPIN(xb_ld(&bar[XB_TOPGEN]) == tg, bar);
.LBB0_184:
	s_andn2_saveexec_b64 s[4:5], s[4:5]
	s_cbranch_execz .LBB0_200
	v_mov_b32_e32 v1, s40
	v_add_co_u32_e32 v4, vcc, 0x3000, v1
	v_mov_b32_e32 v1, s41
	s_waitcnt vmcnt(0)
	v_addc_co_u32_e32 v5, vcc, 0, v1, vcc
	flat_atomic_add v3, v[4:5], v238 offset:1024 sc0
	v_cvt_f32_u32_e32 v1, v2
	v_sub_u32_e32 v4, 0, v2
	s_mov_b64 s[8:9], -1
	v_rcp_iflag_f32_e32 v1, v1
	s_nop 0
	v_mul_f32_e32 v1, 0x4f7ffffe, v1
	v_cvt_u32_f32_e32 v1, v1
	v_mul_lo_u32 v4, v4, v1
	v_mul_hi_u32 v4, v1, v4
	v_add_u32_e32 v1, v1, v4
	s_waitcnt vmcnt(0) lgkmcnt(0)
	v_mul_hi_u32 v1, v3, v1
	v_mul_lo_u32 v4, v1, v2
	v_sub_u32_e32 v4, v3, v4
	v_cmp_ge_u32_e32 vcc, v4, v2
	v_add_u32_e32 v5, 1, v1
	s_nop 0
	v_cndmask_b32_e32 v1, v1, v5, vcc
	v_sub_u32_e32 v5, v4, v2
	v_cndmask_b32_e32 v4, v4, v5, vcc
	v_cmp_ge_u32_e32 vcc, v4, v2
	v_add_u32_e32 v4, 1, v1
	s_nop 0
	v_cndmask_b32_e32 v1, v1, v4, vcc
	v_add_u32_e32 v4, 1, v3
	v_mad_u64_u32 v[2:3], s[4:5], v2, v1, v[2:3]
	s_add_u32 s4, s40, 0x3500
	s_addc_u32 s5, s41, 0
	v_cmp_ne_u32_e32 vcc, v4, v2
	v_mov_b64_e32 v[2:3], s[4:5]
	s_and_saveexec_b64 s[6:7], vcc
	s_cbranch_execz .LBB0_197
	v_mov_b64_e32 v[2:3], s[4:5]
	flat_load_dword v2, v[2:3] sc1
	s_mov_b64 s[12:13], 0
	s_waitcnt vmcnt(0) lgkmcnt(0)
	v_cmp_eq_u32_e32 vcc, v2, v1
	s_and_saveexec_b64 s[10:11], vcc
	s_cbranch_execz .LBB0_196
	s_add_u32 s8, s40, 0x200
	s_addc_u32 s9, s41, 0
	s_mov_b32 s24, 1
	s_branch .LBB0_189

; __device__ __forceinline__ unsigned cvt_pk_bf16(float lo, float hi) { unsigned r; asm volatile("v_cvt_pk_bf16_f32 %0, %1, %2" : "=v"(r) : "v"(lo), "v"(hi)); return r; }
;     __device__ __forceinline__ void operator()(const f32x4 (&acc)[2][2][4][2], const pg8::Unit& u, int wr, int wc, int fr, int fq) const {
;     ...
;                 float rstd = 1.f;
;                 if (nrm) {
;                     float ss = 0.f;
; #pragma unroll
;                     for (int bj = 0; bj < 2; ++bj)
; #pragma unroll
;                         for (int n = 0; n < 2; ++n) ss += (v[bj][n][0] * v[bj][n][0] + v[bj][n][1] * v[bj][n][1]) + (v[bj][n][2] * v[bj][n][2] + v[bj][n][3] * v[bj][n][3]);
;                     ss += __shfl_xor(ss, 16); ss += __shfl_xor(ss, 32);
;                     rstd = rsqrtf(ss * (1.f / 64.f) + RMS_EPS);
;                 }
;                 if (st == ST_G) {
; #pragma unroll
;                     for (int bj = 0; bj < 2; ++bj)
; #pragma unroll
;                         for (int n = 0; n < 2; ++n)
; #pragma unroll
;                             for (int j = 0; j < 4; ++j) v[bj][n][j] = __builtin_amdgcn_rcpf(1.f + __expf(-v[bj][n][j]));
;                 }
;                 bf16_t* rowp = base + (size_t)(ai * 128 + m * 16) * 64;
; #pragma unroll
;                 for (int bj = 0; bj < 2; ++bj) {
;                     const f32x4 v0 = v[bj][0] * rstd * g[bj][0], v1 = v[bj][1] * rstd * g[bj][1];
;                     u32x4 w; w.x = pg8::cvt_pk_bf16(v0[0], v0[1]); w.y = pg8::cvt_pk_bf16(v0[2], v0[3]); w.z = pg8::cvt_pk_bf16(v1[0], v1[1]); w.w = pg8::cvt_pk_bf16(v1[2], v1[3]);
;                     *(u32x4*)(rowp + 32 * bj) = w;
.LBB0_240:
	s_ashr_i32 s23, s22, 31
	s_ashr_i32 s9, s8, 31
	s_lshl_b64 s[22:23], s[22:23], 22
	s_lshl_b64 s[8:9], s[8:9], 15
	s_add_u32 s15, s96, s22
	s_addc_u32 s17, s97, s23
	s_add_u32 s8, s15, s8
	s_addc_u32 s9, s17, s9
	v_lshl_add_u64 v[162:163], s[8:9], 0, v[150:151]
	v_pk_mul_f32 v[140:141], v[164:165], v[140:141] op_sel_hi:[0,1]
	v_pk_mul_f32 v[138:139], v[164:165], v[138:139] op_sel_hi:[0,1]
	v_pk_mul_f32 v[136:137], v[164:165], v[136:137] op_sel_hi:[0,1]
	v_pk_mul_f32 v[134:135], v[164:165], v[134:135] op_sel_hi:[0,1]
	v_lshl_add_u64 v[162:163], v[162:163], 0, v[34:35]
	v_pk_mul_f32 v[140:141], v[156:157], v[140:141]
	v_pk_mul_f32 v[138:139], v[62:63], v[138:139]
	v_pk_mul_f32 v[168:169], v[158:159], v[136:137]
	v_pk_mul_f32 v[136:137], v[64:65], v[134:135]
	v_cvt_pk_bf16_f32 v134, v138, v139
	v_cvt_pk_bf16_f32 v135, v140, v141
	v_pk_mul_f32 v[130:131], v[164:165], v[130:131] op_sel_hi:[0,1]
	v_pk_mul_f32 v[128:129], v[164:165], v[128:129] op_sel_hi:[0,1]
	v_pk_mul_f32 v[126:127], v[164:165], v[126:127] op_sel_hi:[0,1]
	v_cvt_pk_bf16_f32 v136, v136, v137
	v_cvt_pk_bf16_f32 v137, v168, v169
	global_store_dwordx4 v[162:163], v[134:137], off sc1
	v_pk_mul_f32 v[132:133], v[164:165], v[132:133] op_sel_hi:[0,1]
	v_pk_mul_f32 v[130:131], v[66:67], v[130:131]
	v_pk_mul_f32 v[134:135], v[160:161], v[128:129]
	v_pk_mul_f32 v[128:129], v[52:53], v[126:127]
	v_cvt_pk_bf16_f32 v126, v130, v131
	v_pk_mul_f32 v[132:133], v[68:69], v[132:133]
	s_and_b64 vcc, exec, s[6:7]
	v_cvt_pk_bf16_f32 v127, v132, v133
	v_cvt_pk_bf16_f32 v128, v128, v129
	v_cvt_pk_bf16_f32 v129, v134, v135
	global_store_dwordx4 v[162:163], v[126:129], off offset:64 sc1
	s_nop 1
	v_mov_b32_e32 v126, 1.0
	s_cbranch_vccnz .LBB0_242
	v_pk_mul_f32 v[126:127], v[124:125], v[124:125]
	v_pk_mul_f32 v[128:129], v[122:123], v[122:123]
	v_cmp_lt_i32_e32 vcc, v236, v241
	v_pk_mov_b32 v[130:131], v[128:129], v[126:127] op_sel:[1,0]
	v_mov_b32_e32 v129, v127
	v_pk_add_f32 v[126:127], v[130:131], v[128:129]
	v_pk_mul_f32 v[128:129], v[120:121], v[120:121]
	v_pk_mul_f32 v[130:131], v[118:119], v[118:119]
	v_pk_add_f32 v[126:127], v[126:127], v[126:127] op_sel:[0,1] op_sel_hi:[1,0]
	v_pk_mov_b32 v[132:133], v[130:131], v[128:129] op_sel:[1,0]
	v_mov_b32_e32 v131, v129
	v_pk_add_f32 v[128:129], v[132:133], v[130:131]
	v_mul_f32_e32 v130, v110, v110
	v_mul_f32_e32 v131, v111, v111
	v_pk_add_f32 v[128:129], v[128:129], v[128:129] op_sel:[0,1] op_sel_hi:[1,0]
	v_mov_b32_e32 v127, v130
	v_mov_b32_e32 v129, v131
	v_pk_add_f32 v[126:127], v[126:127], v[128:129]
	v_mul_f32_e32 v128, v115, v115
	v_mul_f32_e32 v130, v117, v117
	v_mul_f32_e32 v132, v112, v112
	v_mul_f32_e32 v133, v113, v113
	v_pk_fma_f32 v[128:129], v[114:115], v[114:115], v[128:129] op_sel_hi:[1,1,0]
	v_pk_fma_f32 v[130:131], v[116:117], v[116:117], v[130:131] op_sel_hi:[1,1,0]
	v_mov_b32_e32 v129, v132
	v_mov_b32_e32 v131, v133
	v_pk_add_f32 v[128:129], v[128:129], v[130:131]
	s_nop 0
	v_pk_add_f32 v[126:127], v[126:127], v[128:129]
	s_nop 0
	v_add_f32_e32 v126, v126, v127
	v_cndmask_b32_e32 v127, v199, v236, vcc
	v_lshlrev_b32_e32 v127, 2, v127
	ds_bpermute_b32 v127, v127, v126
	v_cmp_lt_i32_e32 vcc, v237, v241
	s_waitcnt lgkmcnt(0)
	v_add_f32_e32 v126, v126, v127
	v_cndmask_b32_e32 v127, v199, v237, vcc
	v_lshlrev_b32_e32 v127, 2, v127
	ds_bpermute_b32 v127, v127, v126
	s_waitcnt lgkmcnt(0)
	v_add_f32_e32 v126, v126, v127
	v_fmamk_f32 v126, v126, 0x3c800000, v198
	v_mul_f32_e32 v127, 0x4b800000, v126
	v_cmp_gt_f32_e32 vcc, s76, v126
	s_nop 1
	v_cndmask_b32_e32 v126, v126, v127, vcc
	v_rsq_f32_e32 v126, v126
	s_nop 0
	v_mul_f32_e32 v127, 0x45800000, v126
	v_cndmask_b32_e32 v126, v126, v127, vcc

; __device__ __forceinline__ unsigned cvt_pk_bf16(float lo, float hi) { unsigned r; asm volatile("v_cvt_pk_bf16_f32 %0, %1, %2" : "=v"(r) : "v"(lo), "v"(hi)); return r; }
;     __device__ __forceinline__ void operator()(const f32x4 (&acc)[2][2][4][2], const pg8::Unit& u, int wr, int wc, int fr, int fq) const {
;     ...
;                 bf16_t* rowp = base + (size_t)(ai * 128 + m * 16) * 64;
; #pragma unroll
;                 for (int bj = 0; bj < 2; ++bj) {
;                     const f32x4 v0 = v[bj][0] * rstd * g[bj][0], v1 = v[bj][1] * rstd * g[bj][1];
;                     u32x4 w; w.x = pg8::cvt_pk_bf16(v0[0], v0[1]); w.y = pg8::cvt_pk_bf16(v0[2], v0[3]); w.z = pg8::cvt_pk_bf16(v1[0], v1[1]); w.w = pg8::cvt_pk_bf16(v1[2], v1[3]);
;                     *(u32x4*)(rowp + 32 * bj) = w;
;                 }
.LBB0_246:
	v_pk_mul_f32 v[124:125], v[126:127], v[124:125] op_sel_hi:[0,1]
	v_pk_mul_f32 v[122:123], v[126:127], v[122:123] op_sel_hi:[0,1]
	v_pk_mul_f32 v[120:121], v[126:127], v[120:121] op_sel_hi:[0,1]
	v_pk_mul_f32 v[118:119], v[126:127], v[118:119] op_sel_hi:[0,1]
	v_pk_mul_f32 v[124:125], v[156:157], v[124:125]
	v_pk_mul_f32 v[122:123], v[62:63], v[122:123]
	v_pk_mul_f32 v[128:129], v[158:159], v[120:121]
	v_pk_mul_f32 v[120:121], v[64:65], v[118:119]
	v_cvt_pk_bf16_f32 v118, v122, v123
	v_cvt_pk_bf16_f32 v119, v124, v125
	v_pk_mul_f32 v[114:115], v[126:127], v[114:115] op_sel_hi:[0,1]
	v_pk_mul_f32 v[112:113], v[126:127], v[112:113] op_sel_hi:[0,1]
	v_pk_mul_f32 v[110:111], v[126:127], v[110:111] op_sel_hi:[0,1]
	v_cvt_pk_bf16_f32 v120, v120, v121
	v_cvt_pk_bf16_f32 v121, v128, v129
	global_store_dwordx4 v[162:163], v[118:121], off offset:2048 sc1
	v_pk_mul_f32 v[116:117], v[126:127], v[116:117] op_sel_hi:[0,1]
	v_pk_mul_f32 v[114:115], v[66:67], v[114:115]
	v_pk_mul_f32 v[118:119], v[160:161], v[112:113]
	v_pk_mul_f32 v[112:113], v[52:53], v[110:111]
	v_cvt_pk_bf16_f32 v110, v114, v115
	v_pk_mul_f32 v[116:117], v[68:69], v[116:117]
	s_and_b64 vcc, exec, s[6:7]
	v_cvt_pk_bf16_f32 v111, v116, v117
	v_cvt_pk_bf16_f32 v112, v112, v113
	v_cvt_pk_bf16_f32 v113, v118, v119
	global_store_dwordx4 v[162:163], v[110:113], off offset:2112 sc1
	s_nop 1
	v_mov_b32_e32 v110, 1.0
	s_cbranch_vccz .LBB0_251
	s_and_b64 vcc, exec, s[8:9]
	s_mov_b64 s[22:23], -1
	s_cbranch_vccnz .LBB0_252

; __device__ __forceinline__ unsigned cvt_pk_bf16(float lo, float hi) { unsigned r; asm volatile("v_cvt_pk_bf16_f32 %0, %1, %2" : "=v"(r) : "v"(lo), "v"(hi)); return r; }
;     __device__ __forceinline__ void operator()(const f32x4 (&acc)[2][2][4][2], const pg8::Unit& u, int wr, int wc, int fr, int fq) const {
;     ...
;                 bf16_t* rowp = base + (size_t)(ai * 128 + m * 16) * 64;
; #pragma unroll
;                 for (int bj = 0; bj < 2; ++bj) {
;                     const f32x4 v0 = v[bj][0] * rstd * g[bj][0], v1 = v[bj][1] * rstd * g[bj][1];
;                     u32x4 w; w.x = pg8::cvt_pk_bf16(v0[0], v0[1]); w.y = pg8::cvt_pk_bf16(v0[2], v0[3]); w.z = pg8::cvt_pk_bf16(v1[0], v1[1]); w.w = pg8::cvt_pk_bf16(v1[2], v1[3]);
;                     *(u32x4*)(rowp + 32 * bj) = w;
;                 }
.LBB0_254:
	v_pk_mul_f32 v[106:107], v[110:111], v[106:107] op_sel_hi:[0,1]
	v_pk_mul_f32 v[102:103], v[110:111], v[102:103] op_sel_hi:[0,1]
	v_pk_mul_f32 v[108:109], v[110:111], v[108:109] op_sel_hi:[0,1]
	v_pk_mul_f32 v[106:107], v[62:63], v[106:107]
	v_pk_mul_f32 v[104:105], v[110:111], v[104:105] op_sel_hi:[0,1]
	v_pk_mul_f32 v[102:103], v[64:65], v[102:103]
	v_pk_mul_f32 v[108:109], v[156:157], v[108:109]
	v_pk_mul_f32 v[112:113], v[158:159], v[104:105]
	v_cvt_pk_bf16_f32 v104, v106, v107
	v_cvt_pk_bf16_f32 v105, v108, v109
	v_cvt_pk_bf16_f32 v106, v102, v103
	v_add_co_u32_e32 v102, vcc, s33, v162
	v_pk_mul_f32 v[98:99], v[110:111], v[98:99] op_sel_hi:[0,1]
	s_nop 0
	v_addc_co_u32_e32 v103, vcc, 0, v163, vcc
	v_pk_mul_f32 v[96:97], v[110:111], v[96:97] op_sel_hi:[0,1]
	v_pk_mul_f32 v[94:95], v[110:111], v[94:95] op_sel_hi:[0,1]
	v_cvt_pk_bf16_f32 v107, v112, v113
	global_store_dwordx4 v[102:103], v[104:107], off sc1
	v_pk_mul_f32 v[100:101], v[110:111], v[100:101] op_sel_hi:[0,1]
	v_pk_mul_f32 v[98:99], v[66:67], v[98:99]
	v_pk_mul_f32 v[104:105], v[160:161], v[96:97]
	v_pk_mul_f32 v[96:97], v[52:53], v[94:95]
	v_cvt_pk_bf16_f32 v94, v98, v99
	v_pk_mul_f32 v[100:101], v[68:69], v[100:101]
	s_and_b64 vcc, exec, s[6:7]
	v_cvt_pk_bf16_f32 v95, v100, v101
	v_cvt_pk_bf16_f32 v96, v96, v97
	v_cvt_pk_bf16_f32 v97, v104, v105
	global_store_dwordx4 v[102:103], v[94:97], off offset:64 sc1
	s_nop 1
	v_mov_b32_e32 v94, 1.0
	s_cbranch_vccz .LBB0_257
	s_and_b64 vcc, exec, s[8:9]
	s_mov_b64 s[22:23], -1
	s_cbranch_vccnz .LBB0_258

; __device__ __forceinline__ unsigned cvt_pk_bf16(float lo, float hi) { unsigned r; asm volatile("v_cvt_pk_bf16_f32 %0, %1, %2" : "=v"(r) : "v"(lo), "v"(hi)); return r; }
;     __device__ __forceinline__ void operator()(const f32x4 (&acc)[2][2][4][2], const pg8::Unit& u, int wr, int wc, int fr, int fq) const {
;     ...
;                 bf16_t* rowp = base + (size_t)(ai * 128 + m * 16) * 64;
; #pragma unroll
;                 for (int bj = 0; bj < 2; ++bj) {
;                     const f32x4 v0 = v[bj][0] * rstd * g[bj][0], v1 = v[bj][1] * rstd * g[bj][1];
;                     u32x4 w; w.x = pg8::cvt_pk_bf16(v0[0], v0[1]); w.y = pg8::cvt_pk_bf16(v0[2], v0[3]); w.z = pg8::cvt_pk_bf16(v1[0], v1[1]); w.w = pg8::cvt_pk_bf16(v1[2], v1[3]);
;                     *(u32x4*)(rowp + 32 * bj) = w;
;                 }
.LBB0_260:
	v_pk_mul_f32 v[92:93], v[94:95], v[92:93] op_sel_hi:[0,1]
	v_pk_mul_f32 v[90:91], v[94:95], v[90:91] op_sel_hi:[0,1]
	v_pk_mul_f32 v[88:89], v[94:95], v[88:89] op_sel_hi:[0,1]
	v_pk_mul_f32 v[86:87], v[94:95], v[86:87] op_sel_hi:[0,1]
	v_pk_mul_f32 v[92:93], v[156:157], v[92:93]
	v_pk_mul_f32 v[90:91], v[62:63], v[90:91]
	v_pk_mul_f32 v[96:97], v[158:159], v[88:89]
	v_pk_mul_f32 v[88:89], v[64:65], v[86:87]
	v_cvt_pk_bf16_f32 v86, v90, v91
	v_cvt_pk_bf16_f32 v87, v92, v93
	v_pk_mul_f32 v[82:83], v[94:95], v[82:83] op_sel_hi:[0,1]
	v_pk_mul_f32 v[80:81], v[94:95], v[80:81] op_sel_hi:[0,1]
	v_pk_mul_f32 v[78:79], v[94:95], v[78:79] op_sel_hi:[0,1]
	v_cvt_pk_bf16_f32 v88, v88, v89
	v_cvt_pk_bf16_f32 v89, v96, v97
	global_store_dwordx4 v[102:103], v[86:89], off offset:2048 sc1
	v_pk_mul_f32 v[84:85], v[94:95], v[84:85] op_sel_hi:[0,1]
	v_pk_mul_f32 v[82:83], v[66:67], v[82:83]
	v_pk_mul_f32 v[86:87], v[160:161], v[80:81]
	v_pk_mul_f32 v[80:81], v[52:53], v[78:79]
	v_cvt_pk_bf16_f32 v78, v82, v83
	v_pk_mul_f32 v[84:85], v[68:69], v[84:85]
	s_and_b64 vcc, exec, s[6:7]
	v_cvt_pk_bf16_f32 v79, v84, v85
	v_cvt_pk_bf16_f32 v80, v80, v81
	v_cvt_pk_bf16_f32 v81, v86, v87
	global_store_dwordx4 v[102:103], v[78:81], off offset:2112 sc1
	s_nop 1
	v_mov_b32_e32 v78, 1.0
	s_cbranch_vccz .LBB0_263
	s_and_b64 vcc, exec, s[8:9]
	s_mov_b64 s[22:23], -1
	s_cbranch_vccnz .LBB0_264

; __device__ __forceinline__ unsigned cvt_pk_bf16(float lo, float hi) { unsigned r; asm volatile("v_cvt_pk_bf16_f32 %0, %1, %2" : "=v"(r) : "v"(lo), "v"(hi)); return r; }
;     __device__ __forceinline__ void operator()(const f32x4 (&acc)[2][2][4][2], const pg8::Unit& u, int wr, int wc, int fr, int fq) const {
;     ...
;                 bf16_t* rowp = base + (size_t)(ai * 128 + m * 16) * 64;
; #pragma unroll
;                 for (int bj = 0; bj < 2; ++bj) {
;                     const f32x4 v0 = v[bj][0] * rstd * g[bj][0], v1 = v[bj][1] * rstd * g[bj][1];
;                     u32x4 w; w.x = pg8::cvt_pk_bf16(v0[0], v0[1]); w.y = pg8::cvt_pk_bf16(v0[2], v0[3]); w.z = pg8::cvt_pk_bf16(v1[0], v1[1]); w.w = pg8::cvt_pk_bf16(v1[2], v1[3]);
;                     *(u32x4*)(rowp + 32 * bj) = w;
;                 }
.LBB0_266:
	v_pk_mul_f32 v[74:75], v[78:79], v[74:75] op_sel_hi:[0,1]
	v_pk_mul_f32 v[70:71], v[78:79], v[70:71] op_sel_hi:[0,1]
	v_pk_mul_f32 v[76:77], v[78:79], v[76:77] op_sel_hi:[0,1]
	v_pk_mul_f32 v[74:75], v[62:63], v[74:75]
	v_pk_mul_f32 v[72:73], v[78:79], v[72:73] op_sel_hi:[0,1]
	v_pk_mul_f32 v[70:71], v[64:65], v[70:71]
	s_movk_i32 s15, 0x4000
	v_pk_mul_f32 v[76:77], v[156:157], v[76:77]
	v_pk_mul_f32 v[80:81], v[158:159], v[72:73]
	v_cvt_pk_bf16_f32 v72, v74, v75
	v_cvt_pk_bf16_f32 v73, v76, v77
	v_cvt_pk_bf16_f32 v74, v70, v71
	v_add_co_u32_e32 v70, vcc, s15, v162
	v_pk_mul_f32 v[58:59], v[78:79], v[58:59] op_sel_hi:[0,1]
	s_nop 0
	v_addc_co_u32_e32 v71, vcc, 0, v163, vcc
	v_pk_mul_f32 v[56:57], v[78:79], v[56:57] op_sel_hi:[0,1]
	v_pk_mul_f32 v[54:55], v[78:79], v[54:55] op_sel_hi:[0,1]
	v_cvt_pk_bf16_f32 v75, v80, v81
	global_store_dwordx4 v[70:71], v[72:75], off sc1
	v_pk_mul_f32 v[60:61], v[78:79], v[60:61] op_sel_hi:[0,1]
	v_pk_mul_f32 v[58:59], v[66:67], v[58:59]
	v_pk_mul_f32 v[72:73], v[160:161], v[56:57]
	v_pk_mul_f32 v[56:57], v[52:53], v[54:55]
	v_cvt_pk_bf16_f32 v54, v58, v59
	v_pk_mul_f32 v[60:61], v[68:69], v[60:61]
	s_and_b64 vcc, exec, s[6:7]
	v_cvt_pk_bf16_f32 v55, v60, v61
	v_cvt_pk_bf16_f32 v56, v56, v57
	v_cvt_pk_bf16_f32 v57, v72, v73
	global_store_dwordx4 v[70:71], v[54:57], off offset:64 sc1
	s_nop 1
	v_mov_b32_e32 v54, 1.0
	s_cbranch_vccz .LBB0_269
	s_and_b64 vcc, exec, s[8:9]
	s_mov_b64 s[22:23], -1
	s_cbranch_vccnz .LBB0_270

; __device__ __forceinline__ unsigned cvt_pk_bf16(float lo, float hi) { unsigned r; asm volatile("v_cvt_pk_bf16_f32 %0, %1, %2" : "=v"(r) : "v"(lo), "v"(hi)); return r; }
;     __device__ __forceinline__ void operator()(const f32x4 (&acc)[2][2][4][2], const pg8::Unit& u, int wr, int wc, int fr, int fq) const {
;     ...
;                 bf16_t* rowp = base + (size_t)(ai * 128 + m * 16) * 64;
; #pragma unroll
;                 for (int bj = 0; bj < 2; ++bj) {
;                     const f32x4 v0 = v[bj][0] * rstd * g[bj][0], v1 = v[bj][1] * rstd * g[bj][1];
;                     u32x4 w; w.x = pg8::cvt_pk_bf16(v0[0], v0[1]); w.y = pg8::cvt_pk_bf16(v0[2], v0[3]); w.z = pg8::cvt_pk_bf16(v1[0], v1[1]); w.w = pg8::cvt_pk_bf16(v1[2], v1[3]);
;                     *(u32x4*)(rowp + 32 * bj) = w;
;                 }
.LBB0_272:
	v_pk_mul_f32 v[50:51], v[54:55], v[50:51] op_sel_hi:[0,1]
	v_pk_mul_f32 v[48:49], v[54:55], v[48:49] op_sel_hi:[0,1]
	v_pk_mul_f32 v[46:47], v[54:55], v[46:47] op_sel_hi:[0,1]
	v_pk_mul_f32 v[44:45], v[54:55], v[44:45] op_sel_hi:[0,1]
	v_pk_mul_f32 v[50:51], v[156:157], v[50:51]
	v_pk_mul_f32 v[48:49], v[62:63], v[48:49]
	v_pk_mul_f32 v[56:57], v[158:159], v[46:47]
	v_pk_mul_f32 v[46:47], v[64:65], v[44:45]
	v_cvt_pk_bf16_f32 v44, v48, v49
	v_cvt_pk_bf16_f32 v45, v50, v51
	v_pk_mul_f32 v[40:41], v[54:55], v[40:41] op_sel_hi:[0,1]
	v_pk_mul_f32 v[38:39], v[54:55], v[38:39] op_sel_hi:[0,1]
	v_pk_mul_f32 v[36:37], v[54:55], v[36:37] op_sel_hi:[0,1]
	v_cvt_pk_bf16_f32 v46, v46, v47
	v_cvt_pk_bf16_f32 v47, v56, v57
	global_store_dwordx4 v[70:71], v[44:47], off offset:2048 sc1
	v_pk_mul_f32 v[42:43], v[54:55], v[42:43] op_sel_hi:[0,1]
	v_pk_mul_f32 v[40:41], v[66:67], v[40:41]
	v_pk_mul_f32 v[44:45], v[160:161], v[38:39]
	v_pk_mul_f32 v[38:39], v[52:53], v[36:37]
	v_cvt_pk_bf16_f32 v36, v40, v41
	v_pk_mul_f32 v[42:43], v[68:69], v[42:43]
	s_and_b64 vcc, exec, s[6:7]
	v_cvt_pk_bf16_f32 v37, v42, v43
	v_cvt_pk_bf16_f32 v38, v38, v39
	v_cvt_pk_bf16_f32 v39, v44, v45
	global_store_dwordx4 v[70:71], v[36:39], off offset:2112 sc1
	s_nop 1
	v_mov_b32_e32 v36, 1.0
	s_cbranch_vccz .LBB0_275
	s_and_b64 vcc, exec, s[8:9]
	s_mov_b64 s[22:23], -1
	s_cbranch_vccnz .LBB0_276

; __device__ __forceinline__ unsigned cvt_pk_bf16(float lo, float hi) { unsigned r; asm volatile("v_cvt_pk_bf16_f32 %0, %1, %2" : "=v"(r) : "v"(lo), "v"(hi)); return r; }
;     __device__ __forceinline__ void operator()(const f32x4 (&acc)[2][2][4][2], const pg8::Unit& u, int wr, int wc, int fr, int fq) const {
;     ...
;                 bf16_t* rowp = base + (size_t)(ai * 128 + m * 16) * 64;
; #pragma unroll
;                 for (int bj = 0; bj < 2; ++bj) {
;                     const f32x4 v0 = v[bj][0] * rstd * g[bj][0], v1 = v[bj][1] * rstd * g[bj][1];
;                     u32x4 w; w.x = pg8::cvt_pk_bf16(v0[0], v0[1]); w.y = pg8::cvt_pk_bf16(v0[2], v0[3]); w.z = pg8::cvt_pk_bf16(v1[0], v1[1]); w.w = pg8::cvt_pk_bf16(v1[2], v1[3]);
;                     *(u32x4*)(rowp + 32 * bj) = w;
;                 }
.LBB0_278:
	v_pk_mul_f32 v[30:31], v[36:37], v[30:31] op_sel_hi:[0,1]
	v_pk_mul_f32 v[26:27], v[36:37], v[26:27] op_sel_hi:[0,1]
	v_pk_mul_f32 v[32:33], v[36:37], v[32:33] op_sel_hi:[0,1]
	v_pk_mul_f32 v[30:31], v[62:63], v[30:31]
	v_pk_mul_f32 v[28:29], v[36:37], v[28:29] op_sel_hi:[0,1]
	v_pk_mul_f32 v[26:27], v[64:65], v[26:27]
	s_movk_i32 s15, 0x5000
	v_pk_mul_f32 v[32:33], v[156:157], v[32:33]
	v_pk_mul_f32 v[38:39], v[158:159], v[28:29]
	v_cvt_pk_bf16_f32 v28, v30, v31
	v_cvt_pk_bf16_f32 v29, v32, v33
	v_cvt_pk_bf16_f32 v30, v26, v27
	v_add_co_u32_e32 v26, vcc, s15, v162
	v_pk_mul_f32 v[22:23], v[36:37], v[22:23] op_sel_hi:[0,1]
	s_nop 0
	v_addc_co_u32_e32 v27, vcc, 0, v163, vcc
	v_pk_mul_f32 v[20:21], v[36:37], v[20:21] op_sel_hi:[0,1]
	v_pk_mul_f32 v[18:19], v[36:37], v[18:19] op_sel_hi:[0,1]
	v_cvt_pk_bf16_f32 v31, v38, v39
	global_store_dwordx4 v[26:27], v[28:31], off sc1
	v_pk_mul_f32 v[24:25], v[36:37], v[24:25] op_sel_hi:[0,1]
	v_pk_mul_f32 v[22:23], v[66:67], v[22:23]
	v_pk_mul_f32 v[28:29], v[160:161], v[20:21]
	v_pk_mul_f32 v[20:21], v[52:53], v[18:19]
	v_cvt_pk_bf16_f32 v18, v22, v23
	v_pk_mul_f32 v[24:25], v[68:69], v[24:25]
	s_and_b64 vcc, exec, s[6:7]
	v_cvt_pk_bf16_f32 v19, v24, v25
	v_cvt_pk_bf16_f32 v20, v20, v21
	v_cvt_pk_bf16_f32 v21, v28, v29
	global_store_dwordx4 v[26:27], v[18:21], off offset:64 sc1
	s_nop 1
	v_mov_b32_e32 v18, 1.0
	s_cbranch_vccz .LBB0_281
	s_and_b64 vcc, exec, s[8:9]
	s_mov_b64 s[6:7], -1
	s_cbranch_vccnz .LBB0_282

; __device__ __forceinline__ unsigned cvt_pk_bf16(float lo, float hi) { unsigned r; asm volatile("v_cvt_pk_bf16_f32 %0, %1, %2" : "=v"(r) : "v"(lo), "v"(hi)); return r; }
;     __device__ __forceinline__ void operator()(const f32x4 (&acc)[2][2][4][2], const pg8::Unit& u, int wr, int wc, int fr, int fq) const {
;     ...
;                 bf16_t* rowp = base + (size_t)(ai * 128 + m * 16) * 64;
; #pragma unroll
;                 for (int bj = 0; bj < 2; ++bj) {
;                     const f32x4 v0 = v[bj][0] * rstd * g[bj][0], v1 = v[bj][1] * rstd * g[bj][1];
;                     u32x4 w; w.x = pg8::cvt_pk_bf16(v0[0], v0[1]); w.y = pg8::cvt_pk_bf16(v0[2], v0[3]); w.z = pg8::cvt_pk_bf16(v1[0], v1[1]); w.w = pg8::cvt_pk_bf16(v1[2], v1[3]);
;                     *(u32x4*)(rowp + 32 * bj) = w;
;                 }
.LBB0_284:
	v_pk_mul_f32 v[16:17], v[18:19], v[16:17] op_sel_hi:[0,1]
	v_pk_mul_f32 v[14:15], v[18:19], v[14:15] op_sel_hi:[0,1]
	v_pk_mul_f32 v[12:13], v[18:19], v[12:13] op_sel_hi:[0,1]
	v_pk_mul_f32 v[10:11], v[18:19], v[10:11] op_sel_hi:[0,1]
	v_pk_mul_f32 v[16:17], v[156:157], v[16:17]
	v_pk_mul_f32 v[14:15], v[62:63], v[14:15]
	v_pk_mul_f32 v[20:21], v[158:159], v[12:13]
	v_pk_mul_f32 v[12:13], v[64:65], v[10:11]
	v_cvt_pk_bf16_f32 v10, v14, v15
	v_cvt_pk_bf16_f32 v11, v16, v17
	v_pk_mul_f32 v[4:5], v[18:19], v[4:5] op_sel_hi:[0,1]
	v_pk_mul_f32 v[2:3], v[18:19], v[2:3] op_sel_hi:[0,1]
	v_cvt_pk_bf16_f32 v12, v12, v13
	v_cvt_pk_bf16_f32 v13, v20, v21
	global_store_dwordx4 v[26:27], v[10:13], off offset:2048 sc1
	v_pk_mul_f32 v[8:9], v[18:19], v[8:9] op_sel_hi:[0,1]
	v_pk_mul_f32 v[6:7], v[18:19], v[6:7] op_sel_hi:[0,1]
	v_pk_mul_f32 v[10:11], v[160:161], v[4:5]
	v_pk_mul_f32 v[4:5], v[52:53], v[2:3]
	s_andn2_b64 vcc, exec, s[4:5]
	s_mov_b64 s[4:5], -1
	v_pk_mul_f32 v[8:9], v[68:69], v[8:9]
	v_pk_mul_f32 v[6:7], v[66:67], v[6:7]
	s_nop 0
	v_cvt_pk_bf16_f32 v2, v6, v7
	v_cvt_pk_bf16_f32 v3, v8, v9
	v_cvt_pk_bf16_f32 v4, v4, v5
	v_cvt_pk_bf16_f32 v5, v10, v11
	global_store_dwordx4 v[26:27], v[2:5], off offset:2112 sc1
	s_cbranch_vccnz .LBB0_209
	s_andn2_b64 vcc, exec, s[10:11]
	s_cbranch_vccnz .LBB0_208
	s_barrier
	s_branch .LBB0_208

; __device__ __forceinline__ void cumsum_unit(const Args& a, LAS unsigned char* lds, int bh) {
;     ...
;     double base = incl - run;
;     for (int w = 0; w < (tid >> 6); ++w) base += sd[w];
; #pragma unroll
;     for (int j = 0; j < 8; ++j) cum[tid * 8 + j] = (float)(base + loc[j]);
;     __syncthreads();
.LBB0_301:
	s_or_b64 exec, exec, s[4:5]
	v_readlane_b32 s4, v252, 34
	v_readlane_b32 s5, v252, 35
	v_add_f64 v[22:23], v[16:17], v[20:21]
	v_add_f64 v[16:17], v[18:19], v[20:21]
	v_lshl_add_u64 v[24:25], v[2:3], 2, s[4:5]
	v_add_f64 v[2:3], v[12:13], v[20:21]
	v_cvt_f32_f64_e32 v18, v[2:3]
	v_add_f64 v[4:5], v[4:5], v[20:21]
	v_add_f64 v[2:3], v[6:7], v[20:21]
	v_add_f64 v[12:13], v[14:15], v[20:21]
	v_cvt_f32_f64_e32 v3, v[2:3]
	v_cvt_f32_f64_e32 v2, v[4:5]
	v_add_f64 v[6:7], v[8:9], v[20:21]
	v_add_f64 v[4:5], v[10:11], v[20:21]
	v_cvt_f32_f64_e32 v17, v[16:17]
	v_cvt_f32_f64_e32 v16, v[22:23]
	v_cvt_f32_f64_e32 v19, v[12:13]
	v_cvt_f32_f64_e32 v5, v[4:5]
	v_cvt_f32_f64_e32 v4, v[6:7]
	global_store_dwordx4 v[24:25], v[16:19], off sc1
	global_store_dwordx4 v[24:25], v[2:5], off offset:16 sc1
	s_barrier

; #define LAS __attribute__((address_space(3)))
; __device__ __forceinline__ unsigned pk2(float lo, float hi) { pk2_f32x2 v = {lo, hi}; pk2_bf16x2 b = __builtin_convertvector(v, pk2_bf16x2); return __builtin_bit_cast(unsigned, b); }
;     ...
;         const int c = lane & 7;
; #pragma unroll
;         for (int j = 0; j < 4; ++j) { const int n = (lane >> 3) + 8 * j; const LAS float* sp = scr + (8 * c) * 33 + n;
;             u32x4 o; o.x = pk2(sp[0 * 33], sp[1 * 33]); o.y = pk2(sp[2 * 33], sp[3 * 33]); o.z = pk2(sp[4 * 33], sp[5 * 33]); o.w = pk2(sp[6 * 33], sp[7 * 33]);
;             *(u32x4*)(p.dst + (size_t)n * p.K + 8 * c) = o; }
;         asm volatile("s_waitcnt lgkmcnt(0)" ::: "memory");
.LBB0_319:
	s_or_b64 exec, exec, s[10:11]
	v_mov_b32_e32 v37, v35
	s_waitcnt lgkmcnt(0)
	v_lshl_add_u64 v[46:47], v[42:43], 0, v[36:37]
	v_add_u32_e32 v37, 0xc000, v80
	ds_read2_b32 v[94:95], v37 offset0:33 offset1:41
	ds_read2_b32 v[96:97], v37 offset1:8
	ds_read2_b32 v[98:99], v37 offset0:66 offset1:74
	ds_read2_b32 v[100:101], v37 offset0:99 offset1:107
	ds_read2_b32 v[102:103], v37 offset0:132 offset1:140
	ds_read2_b32 v[104:105], v37 offset0:165 offset1:173
	ds_read2_b32 v[106:107], v37 offset0:198 offset1:206
	ds_read2_b32 v[108:109], v37 offset0:231 offset1:239
	v_mul_u32_u24_e32 v39, v38, v79
	v_lshlrev_b32_e32 v110, 1, v39
	v_mov_b32_e32 v111, v35
	s_waitcnt lgkmcnt(6)
	v_cvt_pk_bf16_f32 v42, v96, v94
	s_waitcnt lgkmcnt(4)
	v_cvt_pk_bf16_f32 v43, v98, v100
	s_waitcnt lgkmcnt(2)
	v_cvt_pk_bf16_f32 v44, v102, v104
	s_waitcnt lgkmcnt(0)
	v_cvt_pk_bf16_f32 v45, v106, v108
	v_lshl_add_u64 v[110:111], v[46:47], 0, v[110:111]
	v_mul_u32_u24_e32 v39, v38, v81
	global_store_dwordx4 v[110:111], v[42:45], off sc1
	v_lshlrev_b32_e32 v94, 1, v39
	v_mov_b32_e32 v111, v35
	v_cvt_pk_bf16_f32 v42, v97, v95
	v_mov_b32_e32 v95, v35
	v_cvt_pk_bf16_f32 v43, v99, v101
	v_cvt_pk_bf16_f32 v44, v103, v105
	v_cvt_pk_bf16_f32 v45, v107, v109
	v_lshl_add_u64 v[94:95], v[46:47], 0, v[94:95]
	global_store_dwordx4 v[94:95], v[42:45], off sc1
	ds_read2_b32 v[94:95], v37 offset0:16 offset1:24
	ds_read2_b32 v[96:97], v37 offset0:49 offset1:57
	ds_read2_b32 v[98:99], v37 offset0:82 offset1:90
	ds_read2_b32 v[100:101], v37 offset0:115 offset1:123
	ds_read2_b32 v[102:103], v37 offset0:148 offset1:156
	ds_read2_b32 v[104:105], v37 offset0:181 offset1:189
	ds_read2_b32 v[106:107], v37 offset0:214 offset1:222
	ds_read2_b32 v[108:109], v37 offset0:247 offset1:255
	v_mul_u32_u24_e32 v37, v38, v82
	v_lshlrev_b32_e32 v110, 1, v37
	v_mul_u32_u24_e32 v37, v38, v83
	s_waitcnt lgkmcnt(6)
	v_cvt_pk_bf16_f32 v42, v94, v96
	s_waitcnt lgkmcnt(4)
	v_cvt_pk_bf16_f32 v43, v98, v100
	s_waitcnt lgkmcnt(2)
	v_cvt_pk_bf16_f32 v44, v102, v104
	s_waitcnt lgkmcnt(0)
	v_cvt_pk_bf16_f32 v45, v106, v108
	v_lshl_add_u64 v[110:111], v[46:47], 0, v[110:111]
	v_lshlrev_b32_e32 v38, 1, v37
	v_mov_b32_e32 v39, v35
	global_store_dwordx4 v[110:111], v[42:45], off sc1
	v_lshl_add_u64 v[38:39], v[46:47], 0, v[38:39]
	s_and_b64 s[4:5], exec, vcc
	v_cvt_pk_bf16_f32 v42, v95, v97
	v_cvt_pk_bf16_f32 v43, v99, v101
	v_cvt_pk_bf16_f32 v44, v103, v105
	v_cvt_pk_bf16_f32 v45, v107, v109
	global_store_dwordx4 v[38:39], v[42:45], off sc1
	s_waitcnt lgkmcnt(0)
	s_or_b64 s[8:9], s[4:5], s[8:9]
	v_add_u32_e32 v84, s2, v84
	v_add_u32_e32 v85, s18, v85
	v_add_u32_e32 v86, s19, v86
	v_add_u32_e32 v87, s20, v87
	v_add_u32_e32 v88, s21, v88
	v_add_u32_e32 v89, s22, v89
	v_add_u32_e32 v90, s23, v90
	v_add_u32_e32 v91, s24, v91
	v_mov_b32_e32 v37, v40
	s_andn2_b64 exec, exec, s[8:9]
	s_cbranch_execz .LBB0_345

; #define LAS __attribute__((address_space(3)))
; __device__ __forceinline__ unsigned cvtpk(float lo, float hi) { f32x2_t v = {lo, hi}; bf16x2_t b = __builtin_convertvector(v, bf16x2_t); return __builtin_bit_cast(unsigned, b); }
; template <class RowPtr, class GatePtr>
; __device__ __forceinline__ void store_o(const f32x16 (&o)[2], float scale, LAS unsigned char* lds, int wid, int lane, const RowPtr& rowp, const GatePtr& gatep, bool has_gate) {
;     ...
; #pragma unroll
;     for (int d0 = 0; d0 < 2; ++d0)
; #pragma unroll
;         for (int g = 0; g < 4; ++g) {
;             u32x2 w; w.x = cvtpk(o[d0][4 * g] * scale, o[d0][4 * g + 1] * scale); w.y = cvtpk(o[d0][4 * g + 2] * scale, o[d0][4 * g + 3] * scale);
;             *(LAS u32x2*)(stg + r32 * OST_PITCH + (32 * d0 + 8 * g + 4 * hi) * 2) = w;
;         }
;     asm volatile("s_waitcnt lgkmcnt(0)" ::: "memory");
; #pragma unroll
;     for (int i = 0; i < 4; ++i) {
;         const int row = i * 8 + (lane >> 3), ch = lane & 7;
;         u32x4 v = *(const LAS u32x4*)(stg + row * OST_PITCH + ch * 16);
;         if (has_gate) {
; #pragma unroll
;             for (int k = 0; k < 4; ++k) {
;                 const float a0 = __uint_as_float(v[k] << 16) * __uint_as_float(gv[i][k] << 16), a1 = __uint_as_float(v[k] & 0xffff0000u) * __uint_as_float(gv[i][k] & 0xffff0000u);
;                 v[k] = cvtpk(a0, a1);
;             }
;         }
;         *(u32x4*)(rowp(row) + ch * 8) = v;
;     }
;     ...
;                 const int v2 = u - AT_NFOX - AT_NDIL, qb = 15 - v2 / 48, bh = v2 % 48, b = bh / 6, h = bh % 6, tw = qb * 256 + 32 * wid;
;                 const size_t rb = (size_t)b * S;
;                 bf16_t* O = mix + ((size_t)(10 + h) * NTOK + rb + tw) * 64;
;                 store_o(o, 1.f, lds, wid, lane, [&](int row) { return O + (size_t)row * 64; }, [&](int row) { return (const bf16_t*)nullptr; }, false);
.LBB0_515:
	s_cmpk_gt_u32 s73, 0xaff
	s_cbranch_scc0 .LBB0_517
	s_add_i32 s4, s73, 0xfffff500
	s_mul_hi_u32 s5, s4, 0xaaaaaaab
	s_lshr_b32 s5, s5, 5
	s_mul_i32 s12, s5, 48
	s_sub_i32 s4, s4, s12
	s_mul_i32 s12, s4, 0xab
	s_bfe_u32 s12, s12, 0x6000a
	s_mul_i32 s13, s12, 6
	s_sub_i32 s13, s4, s13
	s_lshl_b32 s4, s5, 8
	s_sub_i32 s4, s48, s4
	s_ashr_i32 s5, s4, 31
	s_and_b32 s13, s13, 0xff
	v_ashrrev_i32_e32 v54, 2, v148
	s_lshl_b32 s12, s12, 19
	s_lshl_b32 s13, s13, 22
	s_lshl_b64 s[4:5], s[4:5], 7
	v_mul_u32_u24_e32 v34, 0x90, v169
	v_and_b32_e32 v54, -8, v54
	s_add_u32 s12, s80, s12
	v_cvt_pk_bf16_f32 v52, v36, v37
	v_cvt_pk_bf16_f32 v53, v38, v39
	v_add3_u32 v34, s49, v34, v54
	v_cvt_pk_bf16_f32 v54, v40, v41
	v_cvt_pk_bf16_f32 v55, v42, v43
	s_addc_u32 s14, s81, 0
	ds_write2_b64 v34, v[52:53], v[54:55] offset1:2
	v_cvt_pk_bf16_f32 v52, v44, v45
	v_cvt_pk_bf16_f32 v53, v46, v47
	v_cvt_pk_bf16_f32 v54, v48, v49
	v_cvt_pk_bf16_f32 v55, v50, v51
	s_add_u32 s12, s12, s13
	ds_write2_b64 v34, v[52:53], v[54:55] offset0:4 offset1:6
	v_cvt_pk_bf16_f32 v52, v18, v19
	v_cvt_pk_bf16_f32 v53, v20, v21
	v_cvt_pk_bf16_f32 v54, v22, v23
	v_cvt_pk_bf16_f32 v55, v24, v25
	s_addc_u32 s13, s14, 0
	ds_write2_b64 v34, v[52:53], v[54:55] offset0:8 offset1:10
	v_cvt_pk_bf16_f32 v52, v26, v27
	v_cvt_pk_bf16_f32 v53, v28, v29
	v_cvt_pk_bf16_f32 v54, v30, v31
	v_cvt_pk_bf16_f32 v55, v32, v33
	s_add_u32 s4, s12, s4
	ds_write2_b64 v34, v[52:53], v[54:55] offset0:12 offset1:14
	v_ashrrev_i32_e32 v58, 3, v148
	v_lshlrev_b32_e32 v34, 4, v148
	s_movk_i32 s12, 0x90
	v_and_b32_e32 v34, 0x70, v34
	v_mul_lo_u32 v52, v58, s12
	s_waitcnt lgkmcnt(0)
	v_add3_u32 v57, s49, v34, v52
	v_ashrrev_i32_e32 v59, 31, v58
	s_addc_u32 s5, s13, s5
	ds_read_b128 v[52:55], v57
	v_lshlrev_b64 v[58:59], 7, v[58:59]
	v_lshl_add_u64 v[58:59], s[4:5], 0, v[58:59]
	v_lshl_add_u64 v[58:59], v[58:59], 0, v[34:35]
	s_mov_b64 s[4:5], 0x2800000
	v_lshl_add_u64 v[60:61], v[58:59], 0, s[4:5]
	v_add_co_u32_e32 v58, vcc, 0x2800000, v58
	s_mov_b64 s[20:21], 0
	s_nop 0
	v_addc_co_u32_e32 v59, vcc, 0, v59, vcc
	s_waitcnt lgkmcnt(0)
	global_store_dwordx4 v[58:59], v[52:55], off sc1
	ds_read_b128 v[52:55], v57 offset:1152
	s_waitcnt lgkmcnt(0)
	global_store_dwordx4 v[60:61], v[52:55], off offset:1024 sc1
	ds_read_b128 v[52:55], v57 offset:2304
	s_waitcnt lgkmcnt(0)
	global_store_dwordx4 v[60:61], v[52:55], off offset:2048 sc1
	ds_read_b128 v[52:55], v57 offset:3456
	s_waitcnt lgkmcnt(0)
	global_store_dwordx4 v[60:61], v[52:55], off offset:3072 sc1
	s_waitcnt lgkmcnt(0)
; #define LAS __attribute__((address_space(3)))
; __device__ __forceinline__ unsigned cvtpk(float lo, float hi) { f32x2_t v = {lo, hi}; bf16x2_t b = __builtin_convertvector(v, bf16x2_t); return __builtin_bit_cast(unsigned, b); }
; template <class RowPtr, class GatePtr>
; __device__ __forceinline__ void store_o(const f32x16 (&o)[2], float scale, LAS unsigned char* lds, int wid, int lane, const RowPtr& rowp, const GatePtr& gatep, bool has_gate) {
;     ...
; #pragma unroll
;     for (int d0 = 0; d0 < 2; ++d0)
; #pragma unroll
;         for (int g = 0; g < 4; ++g) {
;             u32x2 w; w.x = cvtpk(o[d0][4 * g] * scale, o[d0][4 * g + 1] * scale); w.y = cvtpk(o[d0][4 * g + 2] * scale, o[d0][4 * g + 3] * scale);
;             *(LAS u32x2*)(stg + r32 * OST_PITCH + (32 * d0 + 8 * g + 4 * hi) * 2) = w;
;         }
;     asm volatile("s_waitcnt lgkmcnt(0)" ::: "memory");
; #pragma unroll
;     for (int i = 0; i < 4; ++i) {
;         const int row = i * 8 + (lane >> 3), ch = lane & 7;
;         u32x4 v = *(const LAS u32x4*)(stg + row * OST_PITCH + ch * 16);
;         if (has_gate) {
; #pragma unroll
;             for (int k = 0; k < 4; ++k) {
;                 const float a0 = __uint_as_float(v[k] << 16) * __uint_as_float(gv[i][k] << 16), a1 = __uint_as_float(v[k] & 0xffff0000u) * __uint_as_float(gv[i][k] & 0xffff0000u);
;                 v[k] = cvtpk(a0, a1);
;             }
;         }
;         *(u32x4*)(rowp(row) + ch * 8) = v;
;     }
;     ...
;                 const int v2 = u - AT_NFOX, bh = v2 % 48, rest = v2 / 48, b = bh / 6, h = bh % 6, p = rest >> 4, x = rest & 15;
;                 const int dil = p == 0 ? 1 : p == 1 ? 4 : 16, res = x % dil, nb2 = x / dil;
;                 const size_t rb = (size_t)b * S;
;                 const int mw = 256 * nb2 + 32 * wid;
;                 bf16_t* O = dilo + (((size_t)p * 6 + h) * NTOK + rb) * 64;
;                 const size_t mw_row = (size_t)mw * dil + res;
;                 store_o(o, oscale, lds, wid, lane, [&](int row) { return O + (mw_row + (size_t)row * dil) * 64; }, [&](int row) { return (const bf16_t*)nullptr; }, false);
;                 if (hi == 0) dill[((size_t)p * 6 + h) * NTOK + rb + (size_t)(mw + r32) * dil + res] = lse;
.LBB0_517:
	s_andn2_b64 vcc, exec, s[20:21]
	s_cbranch_vccnz .LBB0_521
	s_add_i32 s4, s73, 0xfffffe00
	s_and_b32 s5, s4, 0xffff
	s_mul_i32 s5, s5, 0xaaab
	s_lshr_b32 s12, s5, 21
	s_mul_i32 s13, s12, 48
	s_sub_i32 s13, s4, s13
	s_mul_i32 s14, s13, 0xab
	s_bfe_u32 s16, s14, 0x6000a
	s_mul_i32 s14, s16, 6
	s_sub_i32 s13, s13, s14
	s_and_b32 s13, s13, 0xff
	s_lshr_b32 s17, s5, 25
	s_bfe_u32 s20, s5, 0x40015
	s_cmpk_lt_u32 s4, 0x300
	v_pk_mul_f32 v[52:53], v[36:37], v[56:57] op_sel_hi:[1,0]
	v_pk_mul_f32 v[54:55], v[38:39], v[56:57] op_sel_hi:[1,0]
	s_cselect_b64 s[4:5], -1, 0
	s_cmp_eq_u32 s17, 1
	v_cvt_pk_bf16_f32 v52, v52, v53
	v_cvt_pk_bf16_f32 v53, v54, v55
	v_ashrrev_i32_e32 v54, 2, v148
	s_cselect_b32 s21, 3, 15
	s_cselect_b32 s25, 2, 4
	s_and_b64 s[14:15], s[4:5], exec
	v_mul_u32_u24_e32 v34, 0x90, v169
	v_and_b32_e32 v54, -8, v54
	s_cselect_b32 s14, 0, s21
	v_add3_u32 v34, s49, v34, v54
	v_pk_mul_f32 v[54:55], v[40:41], v[56:57] op_sel_hi:[1,0]
	v_pk_mul_f32 v[58:59], v[42:43], v[56:57] op_sel_hi:[1,0]
	s_and_b32 s34, s14, s12
	v_cvt_pk_bf16_f32 v54, v54, v55
	v_cvt_pk_bf16_f32 v55, v58, v59
	s_and_b64 s[4:5], s[4:5], exec
	ds_write2_b64 v34, v[52:53], v[54:55] offset1:2
	v_pk_mul_f32 v[52:53], v[44:45], v[56:57] op_sel_hi:[1,0]
	v_pk_mul_f32 v[54:55], v[46:47], v[56:57] op_sel_hi:[1,0]
	s_cselect_b32 s35, 0, s25
	v_cvt_pk_bf16_f32 v52, v52, v53
	v_cvt_pk_bf16_f32 v53, v54, v55
	v_pk_mul_f32 v[54:55], v[48:49], v[56:57] op_sel_hi:[1,0]
	v_pk_mul_f32 v[58:59], v[50:51], v[56:57] op_sel_hi:[1,0]
	s_lshr_b32 s4, s20, s35
	v_cvt_pk_bf16_f32 v54, v54, v55
	v_cvt_pk_bf16_f32 v55, v58, v59
	s_lshl_b32 s4, s4, 8
	ds_write2_b64 v34, v[52:53], v[54:55] offset0:4 offset1:6
	v_pk_mul_f32 v[52:53], v[18:19], v[56:57] op_sel_hi:[1,0]
	v_pk_mul_f32 v[54:55], v[20:21], v[56:57] op_sel_hi:[1,0]
	s_add_i32 s20, s4, s2
	s_mul_i32 s4, s17, 6
	v_cvt_pk_bf16_f32 v52, v52, v53
	v_cvt_pk_bf16_f32 v53, v54, v55
	v_pk_mul_f32 v[54:55], v[22:23], v[56:57] op_sel_hi:[1,0]
	v_pk_mul_f32 v[58:59], v[24:25], v[56:57] op_sel_hi:[1,0]
	s_add_i32 s4, s4, s13
	v_cvt_pk_bf16_f32 v54, v54, v55
	v_cvt_pk_bf16_f32 v55, v58, v59
	s_lshl_b32 s5, s16, 12
	s_lshl_b32 s4, s4, 15
	ds_write2_b64 v34, v[52:53], v[54:55] offset0:8 offset1:10
	v_pk_mul_f32 v[52:53], v[26:27], v[56:57] op_sel_hi:[1,0]
	v_pk_mul_f32 v[54:55], v[28:29], v[56:57] op_sel_hi:[1,0]
	s_add_i32 s66, s5, s4
	v_readlane_b32 s12, v252, 8
	v_cvt_pk_bf16_f32 v52, v52, v53
	v_cvt_pk_bf16_f32 v53, v54, v55
	v_pk_mul_f32 v[54:55], v[30:31], v[56:57] op_sel_hi:[1,0]
	v_pk_mul_f32 v[58:59], v[32:33], v[56:57] op_sel_hi:[1,0]
	s_lshl_b64 s[4:5], s[66:67], 7
	v_readlane_b32 s14, v252, 10
	v_cvt_pk_bf16_f32 v54, v54, v55
	v_cvt_pk_bf16_f32 v55, v58, v59
	v_readlane_b32 s15, v252, 11
	s_add_u32 s28, s14, s4
	ds_write2_b64 v34, v[52:53], v[54:55] offset0:12 offset1:14
	v_ashrrev_i32_e32 v58, 3, v148
	v_lshlrev_b32_e32 v34, 4, v148
	s_movk_i32 s4, 0x90
	s_addc_u32 s29, s15, s5
	s_ashr_i32 s21, s20, 31
	v_and_b32_e32 v34, 0x70, v34
	v_mul_lo_u32 v52, v58, s4
	s_lshl_b64 s[30:31], s[20:21], s35
	s_waitcnt lgkmcnt(0)
	v_add3_u32 v57, s49, v34, v52
	v_ashrrev_i32_e32 v59, 31, v58
	s_or_b32 s30, s30, s34
	ds_read_b128 v[52:55], v57
	v_lshlrev_b64 v[60:61], s35, v[58:59]
	v_lshl_add_u64 v[60:61], v[60:61], 0, s[30:31]
	v_lshlrev_b64 v[60:61], 7, v[60:61]
	v_lshl_add_u64 v[60:61], s[28:29], 0, v[60:61]
	v_lshl_add_u64 v[60:61], v[60:61], 0, v[34:35]
	s_waitcnt lgkmcnt(0)
	global_store_dwordx4 v[60:61], v[52:55], off sc1
	v_add_u32_e32 v60, 8, v58
	v_ashrrev_i32_e32 v61, 31, v60
	ds_read_b128 v[52:55], v57 offset:1152
	v_lshlrev_b64 v[60:61], s35, v[60:61]
	v_lshl_add_u64 v[60:61], v[60:61], 0, s[30:31]
	v_lshlrev_b64 v[60:61], 7, v[60:61]
	v_lshl_add_u64 v[60:61], s[28:29], 0, v[60:61]
	v_lshl_add_u64 v[60:61], v[60:61], 0, v[34:35]
	s_waitcnt lgkmcnt(0)
	global_store_dwordx4 v[60:61], v[52:55], off sc1
	v_add_u32_e32 v60, 16, v58
	v_ashrrev_i32_e32 v61, 31, v60
	ds_read_b128 v[52:55], v57 offset:2304
	v_lshlrev_b64 v[60:61], s35, v[60:61]
	v_lshl_add_u64 v[60:61], v[60:61], 0, s[30:31]
	v_lshlrev_b64 v[60:61], 7, v[60:61]
	v_lshl_add_u64 v[60:61], s[28:29], 0, v[60:61]
	v_add_u32_e32 v58, 24, v58
	v_lshl_add_u64 v[60:61], v[60:61], 0, v[34:35]
	v_ashrrev_i32_e32 v59, 31, v58
	s_waitcnt lgkmcnt(0)
	global_store_dwordx4 v[60:61], v[52:55], off sc1
	ds_read_b128 v[52:55], v57 offset:3456
	v_lshlrev_b64 v[58:59], s35, v[58:59]
	v_lshl_add_u64 v[58:59], v[58:59], 0, s[30:31]
	v_lshlrev_b64 v[58:59], 7, v[58:59]
	v_lshl_add_u64 v[58:59], s[28:29], 0, v[58:59]
	v_lshl_add_u64 v[58:59], v[58:59], 0, v[34:35]
	s_waitcnt lgkmcnt(0)
	global_store_dwordx4 v[58:59], v[52:55], off sc1
	s_waitcnt lgkmcnt(0)
	v_cmp_gt_u32_e32 vcc, 32, v148
	v_readlane_b32 s13, v252, 9
	s_and_saveexec_b64 s[28:29], vcc
	s_cbranch_execz .LBB0_520
	s_lshl_b32 s4, s66, 2
	v_or_b32_e32 v52, s20, v148
	s_add_u32 s4, s82, s4
	v_ashrrev_i32_e32 v53, 31, v52
	s_addc_u32 s5, s83, 0
	v_lshlrev_b64 v[52:53], s35, v[52:53]
	v_lshl_add_u64 v[52:53], v[52:53], 2, s[4:5]
	s_lshl_b32 s66, s34, 2
	v_lshl_add_u64 v[52:53], v[52:53], 0, s[66:67]
	global_store_dword v[52:53], v1, off sc1

; #define LAS __attribute__((address_space(3)))
; __device__ __forceinline__ unsigned cvtpk(float lo, float hi) { f32x2_t v = {lo, hi}; bf16x2_t b = __builtin_convertvector(v, bf16x2_t); return __builtin_bit_cast(unsigned, b); }
; template <class RowPtr, class GatePtr>
; __device__ __forceinline__ void store_o(const f32x16 (&o)[2], float scale, LAS unsigned char* lds, int wid, int lane, const RowPtr& rowp, const GatePtr& gatep, bool has_gate) {
;     ...
;     u32x4 gv[4];
;     if (has_gate) {
; #pragma unroll
;         for (int i = 0; i < 4; ++i) gv[i] = *(const u32x4*)(gatep(i * 8 + (lane >> 3)) + (lane & 7) * 8);
;     }
; #pragma unroll
;     for (int d0 = 0; d0 < 2; ++d0)
; #pragma unroll
;         for (int g = 0; g < 4; ++g) {
;             u32x2 w; w.x = cvtpk(o[d0][4 * g] * scale, o[d0][4 * g + 1] * scale); w.y = cvtpk(o[d0][4 * g + 2] * scale, o[d0][4 * g + 3] * scale);
;             *(LAS u32x2*)(stg + r32 * OST_PITCH + (32 * d0 + 8 * g + 4 * hi) * 2) = w;
;         }
;     asm volatile("s_waitcnt lgkmcnt(0)" ::: "memory");
; #pragma unroll
;     for (int i = 0; i < 4; ++i) {
;         const int row = i * 8 + (lane >> 3), ch = lane & 7;
;         u32x4 v = *(const LAS u32x4*)(stg + row * OST_PITCH + ch * 16);
;     ...
;                 const int qb = 15 - (u >> 5), bh = u & 31, b = bh >> 2, h = bh & 3, tw = qb * 256 + 32 * wid;
;                 const size_t rb = (size_t)b * S;
;                 const bf16_t* G = proj + ((size_t)(12 + h) * NTOK + rb + tw) * 64;
;                 bf16_t* O = mix + ((size_t)h * NTOK + rb + tw) * 64;
;                 store_o(o, oscale, lds, wid, lane, [&](int row) { return O + (size_t)row * 64; }, [&](int row) { return G + (size_t)row * 64; }, true);
.LBB0_522:
	s_lshl_b32 s4, s73, 3
	s_and_b32 s4, s4, 0xffffff00
	s_sub_i32 s20, s48, s4
	s_lshl_b32 s4, s73, 10
	s_lshl_b32 s5, s73, 15
	s_and_b32 s4, s4, 0x7000
	s_and_b32 s5, s5, 0x18000
	s_or_b32 s21, s5, s4
	s_or_b32 s4, s21, 0x60000
	s_ashr_i32 s28, s20, 31
	s_add_u32 s4, s4, s20
	s_addc_u32 s5, 0, s28
	s_lshl_b64 s[4:5], s[4:5], 7
	s_add_u32 s4, s96, s4
	v_ashrrev_i32_e32 v60, 3, v148
	v_lshlrev_b32_e32 v1, 4, v148
	s_addc_u32 s5, s97, s5
	v_and_b32_e32 v34, 0x70, v1
	v_ashrrev_i32_e32 v61, 31, v60
	v_lshl_add_u64 v[62:63], s[4:5], 0, v[34:35]
	v_lshlrev_b64 v[58:59], 7, v[60:61]
	v_lshl_add_u64 v[52:53], v[62:63], 0, v[58:59]
	global_load_dwordx4 v[52:55], v[52:53], off
	s_mov_b64 s[4:5], 0x400
	v_pk_mul_f32 v[68:69], v[40:41], v[56:57] op_sel_hi:[1,0]
	v_lshl_add_u64 v[40:41], v[58:59], 0, s[4:5]
	v_pk_mul_f32 v[64:65], v[36:37], v[56:57] op_sel_hi:[1,0]
	v_lshl_add_u64 v[36:37], v[62:63], 0, v[40:41]
	v_pk_mul_f32 v[66:67], v[38:39], v[56:57] op_sel_hi:[1,0]
	global_load_dwordx4 v[36:39], v[36:37], off
	v_pk_mul_f32 v[42:43], v[42:43], v[56:57] op_sel_hi:[1,0]
	v_pk_mul_f32 v[44:45], v[44:45], v[56:57] op_sel_hi:[1,0]
	v_pk_mul_f32 v[48:49], v[48:49], v[56:57] op_sel_hi:[1,0]
	v_pk_mul_f32 v[22:23], v[22:23], v[56:57] op_sel_hi:[1,0]
	v_pk_mul_f32 v[46:47], v[46:47], v[56:57] op_sel_hi:[1,0]
	v_pk_mul_f32 v[50:51], v[50:51], v[56:57] op_sel_hi:[1,0]
	v_pk_mul_f32 v[18:19], v[18:19], v[56:57] op_sel_hi:[1,0]
	v_pk_mul_f32 v[20:21], v[20:21], v[56:57] op_sel_hi:[1,0]
	v_pk_mul_f32 v[24:25], v[24:25], v[56:57] op_sel_hi:[1,0]
	v_pk_mul_f32 v[26:27], v[26:27], v[56:57] op_sel_hi:[1,0]
	v_pk_mul_f32 v[28:29], v[28:29], v[56:57] op_sel_hi:[1,0]
	v_pk_mul_f32 v[30:31], v[30:31], v[56:57] op_sel_hi:[1,0]
	v_pk_mul_f32 v[32:33], v[32:33], v[56:57] op_sel_hi:[1,0]
	v_cvt_pk_bf16_f32 v56, v64, v65
	v_cvt_pk_bf16_f32 v65, v42, v43
	v_cvt_pk_bf16_f32 v42, v44, v45
	v_cvt_pk_bf16_f32 v44, v48, v49
	v_cvt_pk_bf16_f32 v48, v22, v23
	v_lshl_add_u64 v[22:23], v[58:59], 0, s[86:87]
	v_cvt_pk_bf16_f32 v43, v46, v47
	v_cvt_pk_bf16_f32 v46, v18, v19
	v_lshl_add_u64 v[18:19], v[62:63], 0, v[22:23]
	v_cvt_pk_bf16_f32 v47, v20, v21
	global_load_dwordx4 v[18:21], v[18:19], off
	v_ashrrev_i32_e32 v61, 2, v148
	s_movk_i32 s4, 0x90
	v_mul_u32_u24_e32 v1, 0x90, v169
	v_and_b32_e32 v61, -8, v61
	v_cvt_pk_bf16_f32 v49, v24, v25
	v_mul_lo_u32 v24, v60, s4
	s_mov_b64 s[4:5], 0xc00
	v_cvt_pk_bf16_f32 v57, v66, v67
	v_cvt_pk_bf16_f32 v64, v68, v69
	v_cvt_pk_bf16_f32 v26, v26, v27
	v_cvt_pk_bf16_f32 v27, v28, v29
	v_add3_u32 v1, s49, v1, v61
	v_add3_u32 v60, s49, v34, v24
	v_lshl_add_u64 v[24:25], v[58:59], 0, s[4:5]
	v_cvt_pk_bf16_f32 v45, v50, v51
	v_cvt_pk_bf16_f32 v28, v30, v31
	v_cvt_pk_bf16_f32 v29, v32, v33
	ds_write2_b64 v1, v[56:57], v[64:65] offset1:2
	ds_write2_b64 v1, v[42:43], v[44:45] offset0:4 offset1:6
	ds_write2_b64 v1, v[46:47], v[48:49] offset0:8 offset1:10
	ds_write2_b64 v1, v[26:27], v[28:29] offset0:12 offset1:14
	v_lshl_add_u64 v[26:27], v[62:63], 0, v[24:25]
	global_load_dwordx4 v[26:29], v[26:27], off
	s_waitcnt lgkmcnt(0)
	ds_read_b128 v[30:33], v60
	ds_read_b128 v[42:45], v60 offset:1152
	s_add_u32 s4, s21, s20
	s_addc_u32 s5, 0, s28
	s_lshl_b64 s[4:5], s[4:5], 7
	s_waitcnt lgkmcnt(1)
	v_lshlrev_b32_e32 v46, 16, v30
	v_and_b32_e32 v47, 0xffff0000, v30
	v_lshlrev_b32_e32 v30, 16, v31
	v_and_b32_e32 v31, 0xffff0000, v31
	s_add_u32 s20, s80, s4
	s_addc_u32 s21, s81, s5
	v_lshl_add_u64 v[40:41], s[20:21], 0, v[40:41]
	v_lshl_add_u64 v[40:41], v[40:41], 0, v[34:35]
	v_lshl_add_u64 v[22:23], s[20:21], 0, v[22:23]
	v_lshl_add_u64 v[22:23], v[22:23], 0, v[34:35]
	s_waitcnt vmcnt(3)
; #define LAS __attribute__((address_space(3)))
; __device__ __forceinline__ unsigned cvtpk(float lo, float hi) { f32x2_t v = {lo, hi}; bf16x2_t b = __builtin_convertvector(v, bf16x2_t); return __builtin_bit_cast(unsigned, b); }
; template <class RowPtr, class GatePtr>
; __device__ __forceinline__ void store_o(const f32x16 (&o)[2], float scale, LAS unsigned char* lds, int wid, int lane, const RowPtr& rowp, const GatePtr& gatep, bool has_gate) {
;     ...
;     for (int i = 0; i < 4; ++i) {
;         const int row = i * 8 + (lane >> 3), ch = lane & 7;
;         u32x4 v = *(const LAS u32x4*)(stg + row * OST_PITCH + ch * 16);
;         if (has_gate) {
; #pragma unroll
;             for (int k = 0; k < 4; ++k) {
;                 const float a0 = __uint_as_float(v[k] << 16) * __uint_as_float(gv[i][k] << 16), a1 = __uint_as_float(v[k] & 0xffff0000u) * __uint_as_float(gv[i][k] & 0xffff0000u);
;                 v[k] = cvtpk(a0, a1);
;             }
;         }
;         *(u32x4*)(rowp(row) + ch * 8) = v;
;     }
	v_lshlrev_b32_e32 v48, 16, v52
	v_and_b32_e32 v49, 0xffff0000, v52
	v_lshlrev_b32_e32 v50, 16, v53
	v_and_b32_e32 v51, 0xffff0000, v53
	v_pk_mul_f32 v[46:47], v[48:49], v[46:47]
	v_pk_mul_f32 v[48:49], v[50:51], v[30:31]
	v_cvt_pk_bf16_f32 v30, v46, v47
	v_cvt_pk_bf16_f32 v31, v48, v49
	v_lshlrev_b32_e32 v46, 16, v32
	v_and_b32_e32 v47, 0xffff0000, v32
	v_lshlrev_b32_e32 v48, 16, v54
	v_and_b32_e32 v49, 0xffff0000, v54
	v_pk_mul_f32 v[46:47], v[48:49], v[46:47]
	v_lshlrev_b32_e32 v48, 16, v55
	v_cvt_pk_bf16_f32 v32, v46, v47
	v_lshlrev_b32_e32 v46, 16, v33
	v_and_b32_e32 v47, 0xffff0000, v33
	v_and_b32_e32 v49, 0xffff0000, v55
	v_pk_mul_f32 v[46:47], v[48:49], v[46:47]
	s_nop 0
	v_cvt_pk_bf16_f32 v33, v46, v47
	v_lshl_add_u64 v[46:47], s[20:21], 0, v[58:59]
	v_lshl_add_u64 v[46:47], v[46:47], 0, v[34:35]
	global_store_dwordx4 v[46:47], v[30:33], off sc1
	s_waitcnt lgkmcnt(0)
	s_nop 0
	v_lshlrev_b32_e32 v30, 16, v42
	v_and_b32_e32 v31, 0xffff0000, v42
	s_waitcnt vmcnt(3)
	v_lshlrev_b32_e32 v32, 16, v36
	v_and_b32_e32 v33, 0xffff0000, v36
	v_pk_mul_f32 v[30:31], v[32:33], v[30:31]
	v_lshlrev_b32_e32 v32, 16, v43
	v_and_b32_e32 v33, 0xffff0000, v43
	v_lshlrev_b32_e32 v36, 16, v37
	v_and_b32_e32 v37, 0xffff0000, v37
	v_pk_mul_f32 v[32:33], v[36:37], v[32:33]
	v_cvt_pk_bf16_f32 v30, v30, v31
	v_cvt_pk_bf16_f32 v31, v32, v33
	v_lshlrev_b32_e32 v32, 16, v44
	v_and_b32_e32 v33, 0xffff0000, v44
	v_lshlrev_b32_e32 v36, 16, v38
	v_and_b32_e32 v37, 0xffff0000, v38
	v_pk_mul_f32 v[32:33], v[36:37], v[32:33]
	v_lshlrev_b32_e32 v36, 16, v45
	v_and_b32_e32 v37, 0xffff0000, v45
	v_lshlrev_b32_e32 v38, 16, v39
	v_and_b32_e32 v39, 0xffff0000, v39
	v_pk_mul_f32 v[36:37], v[38:39], v[36:37]
	v_cvt_pk_bf16_f32 v32, v32, v33
	v_cvt_pk_bf16_f32 v33, v36, v37
	ds_read_b128 v[36:39], v60 offset:2304
	global_store_dwordx4 v[40:41], v[30:33], off sc1
	ds_read_b128 v[30:33], v60 offset:3456
	s_waitcnt vmcnt(3)
	v_lshlrev_b32_e32 v42, 16, v18
	v_and_b32_e32 v43, 0xffff0000, v18
	s_waitcnt lgkmcnt(1)
	v_lshlrev_b32_e32 v40, 16, v36
	v_and_b32_e32 v41, 0xffff0000, v36
	v_pk_mul_f32 v[40:41], v[42:43], v[40:41]
	v_lshlrev_b32_e32 v36, 16, v37
	v_cvt_pk_bf16_f32 v18, v40, v41
	v_and_b32_e32 v37, 0xffff0000, v37
	v_lshlrev_b32_e32 v40, 16, v19
	v_and_b32_e32 v41, 0xffff0000, v19
	v_pk_mul_f32 v[36:37], v[40:41], v[36:37]
	v_lshlrev_b32_e32 v40, 16, v20
	v_cvt_pk_bf16_f32 v19, v36, v37
	v_lshlrev_b32_e32 v36, 16, v38
	v_and_b32_e32 v37, 0xffff0000, v38
	v_and_b32_e32 v41, 0xffff0000, v20
	v_pk_mul_f32 v[36:37], v[40:41], v[36:37]
	v_lshlrev_b32_e32 v38, 16, v21
	v_cvt_pk_bf16_f32 v20, v36, v37
	v_lshlrev_b32_e32 v36, 16, v39
	v_and_b32_e32 v37, 0xffff0000, v39
	v_and_b32_e32 v39, 0xffff0000, v21
	v_pk_mul_f32 v[36:37], v[38:39], v[36:37]
	s_nop 0
	v_cvt_pk_bf16_f32 v21, v36, v37
	global_store_dwordx4 v[22:23], v[18:21], off sc1
	s_waitcnt vmcnt(3)
	v_lshlrev_b32_e32 v22, 16, v27
	v_and_b32_e32 v23, 0xffff0000, v27
	s_waitcnt lgkmcnt(0)
	v_lshlrev_b32_e32 v18, 16, v30
	v_and_b32_e32 v19, 0xffff0000, v30
	v_lshlrev_b32_e32 v20, 16, v26
	v_and_b32_e32 v21, 0xffff0000, v26
	v_pk_mul_f32 v[18:19], v[20:21], v[18:19]
	v_lshlrev_b32_e32 v20, 16, v31
	v_and_b32_e32 v21, 0xffff0000, v31
	v_pk_mul_f32 v[20:21], v[22:23], v[20:21]
	v_cvt_pk_bf16_f32 v18, v18, v19
	v_cvt_pk_bf16_f32 v19, v20, v21
	v_lshlrev_b32_e32 v20, 16, v32
	v_and_b32_e32 v21, 0xffff0000, v32
	v_lshlrev_b32_e32 v22, 16, v28
	v_and_b32_e32 v23, 0xffff0000, v28
	v_pk_mul_f32 v[20:21], v[22:23], v[20:21]
	v_lshlrev_b32_e32 v22, 16, v33
	v_and_b32_e32 v23, 0xffff0000, v33
	v_lshlrev_b32_e32 v26, 16, v29
	v_and_b32_e32 v27, 0xffff0000, v29
	v_pk_mul_f32 v[22:23], v[26:27], v[22:23]
	v_cvt_pk_bf16_f32 v20, v20, v21
	v_cvt_pk_bf16_f32 v21, v22, v23
	v_lshl_add_u64 v[22:23], s[20:21], 0, v[24:25]
	v_lshl_add_u64 v[22:23], v[22:23], 0, v[34:35]
	global_store_dwordx4 v[22:23], v[18:21], off sc1
	s_waitcnt lgkmcnt(0)
	s_branch .LBB0_414

; __device__ __forceinline__ void at_dil(const Args& a, LAS unsigned char* lds, int layer) {
;     ...
;         const float l_run = other_half_sum(l_part);
;         const float oscale = 1.f / l_run, lse = ((dil_fixed ? m_dil : m_run) + __builtin_amdgcn_logf(l_run)) * LN2;
;         asm volatile("s_waitcnt lgkmcnt(0)\n\ts_barrier" ::: "memory");
;         {
;             const size_t rb = (size_t)b * S;
;             const int mw = 256 * nb2 + 32 * wid;
;             bf16_t* O = dilo + (((size_t)p * 6 + h) * NTOK + rb) * 64;
;             const size_t mw_row = (size_t)mw * dil + res;
;             store_o(o, oscale, lds, wid, lane, [&](int row) { return O + (mw_row + (size_t)row * dil) * 64; }, [&](int row) { return (const bf16_t*)nullptr; }, false);
;             if (hi == 0) dill[((size_t)p * 6 + h) * NTOK + rb + (size_t)(mw + r32) * dil + res] = lse;
.LBB0_598:
	v_mov_b32_e32 v34, v138
	s_nop 1
	v_permlane32_swap_b32_e32 v138, v34
	v_add_f32_e32 v54, v138, v34
	v_div_scale_f32 v34, s[24:25], v54, v54, 1.0
	v_rcp_f32_e32 v53, v34
	s_and_b64 s[24:25], s[20:21], exec
	s_cselect_b32 s27, 3, 15
	s_and_b64 s[24:25], s[16:17], exec
	v_fma_f32 v55, -v34, v53, 1.0
	v_fmac_f32_e32 v53, v55, v53
	v_div_scale_f32 v55, vcc, 1.0, v54, 1.0
	v_mul_f32_e32 v56, v55, v53
	v_fma_f32 v57, -v34, v56, v55
	v_fmac_f32_e32 v56, v57, v53
	s_sext_i32_i8 s26, s79
	v_fma_f32 v34, -v34, v56, v55
	s_mul_i32 s25, s94, 6
	s_cselect_b32 s24, 0, s27
	v_div_fmas_f32 v34, v34, v53, v56
	s_add_i32 s26, s25, s26
	s_and_b32 s28, s24, s78
	v_div_fixup_f32 v34, v34, v54, 1.0
	s_lshl_b32 s24, s95, 8
	s_ashr_i32 s27, s26, 31
	s_lshl_b64 s[18:19], s[18:19], 12
	s_add_i32 s24, s24, s43
	s_lshl_b64 s[26:27], s[26:27], 15
	v_pk_mul_f32 v[36:37], v[36:37], v[34:35] op_sel_hi:[1,0]
	v_pk_mul_f32 v[38:39], v[38:39], v[34:35] op_sel_hi:[1,0]
	s_add_u32 s18, s26, s18
	v_cvt_pk_bf16_f32 v36, v36, v37
	v_cvt_pk_bf16_f32 v37, v38, v39
	v_ashrrev_i32_e32 v38, 2, v135
	v_pk_mul_f32 v[18:19], v[18:19], v[34:35] op_sel_hi:[1,0]
	v_pk_mul_f32 v[20:21], v[20:21], v[34:35] op_sel_hi:[1,0]
	s_addc_u32 s19, s27, s19
	v_readlane_b32 s56, v252, 8
	v_mul_u32_u24_e32 v53, 0x90, v136
	v_and_b32_e32 v38, -8, v38
	v_cvt_pk_bf16_f32 v18, v18, v19
	v_cvt_pk_bf16_f32 v19, v20, v21
	v_pk_mul_f32 v[20:21], v[22:23], v[34:35] op_sel_hi:[1,0]
	v_pk_mul_f32 v[22:23], v[24:25], v[34:35] op_sel_hi:[1,0]
	s_lshl_b64 s[26:27], s[18:19], 7
	v_readlane_b32 s58, v252, 10
	v_add3_u32 v53, s45, v53, v38
	v_pk_mul_f32 v[38:39], v[40:41], v[34:35] op_sel_hi:[1,0]
	v_pk_mul_f32 v[40:41], v[42:43], v[34:35] op_sel_hi:[1,0]
	v_cvt_pk_bf16_f32 v20, v20, v21
	v_cvt_pk_bf16_f32 v21, v22, v23
	s_waitcnt lgkmcnt(0)
	s_barrier
	v_readlane_b32 s59, v252, 11
	s_add_u32 s26, s58, s26
	v_cvt_pk_bf16_f32 v38, v38, v39
	v_cvt_pk_bf16_f32 v39, v40, v41
	ds_write2_b64 v53, v[18:19], v[20:21] offset0:8 offset1:10
	v_pk_mul_f32 v[18:19], v[26:27], v[34:35] op_sel_hi:[1,0]
	v_pk_mul_f32 v[20:21], v[28:29], v[34:35] op_sel_hi:[1,0]
	s_addc_u32 s27, s59, s27
	s_ashr_i32 s25, s24, 31
	ds_write2_b64 v53, v[36:37], v[38:39] offset1:2
	v_pk_mul_f32 v[36:37], v[44:45], v[34:35] op_sel_hi:[1,0]
	v_pk_mul_f32 v[38:39], v[46:47], v[34:35] op_sel_hi:[1,0]
	v_cvt_pk_bf16_f32 v18, v18, v19
	v_cvt_pk_bf16_f32 v19, v20, v21
	v_pk_mul_f32 v[20:21], v[30:31], v[34:35] op_sel_hi:[1,0]
	v_pk_mul_f32 v[22:23], v[32:33], v[34:35] op_sel_hi:[1,0]
	s_and_b64 s[20:21], s[20:21], exec
	v_cvt_pk_bf16_f32 v36, v36, v37
	v_cvt_pk_bf16_f32 v37, v38, v39
	v_pk_mul_f32 v[38:39], v[48:49], v[34:35] op_sel_hi:[1,0]
	v_pk_mul_f32 v[40:41], v[50:51], v[34:35] op_sel_hi:[1,0]
	v_cvt_pk_bf16_f32 v20, v20, v21
	v_cvt_pk_bf16_f32 v21, v22, v23
	s_cselect_b32 s20, 2, 4
	s_and_b64 s[16:17], s[16:17], exec
	v_cvt_pk_bf16_f32 v38, v38, v39
	v_cvt_pk_bf16_f32 v39, v40, v41
	ds_write2_b64 v53, v[18:19], v[20:21] offset0:12 offset1:14
	v_lshlrev_b32_e32 v18, 4, v135
	s_movk_i32 s10, 0x90
	s_cselect_b32 s20, 0, s20
	ds_write2_b64 v53, v[36:37], v[38:39] offset0:4 offset1:6
	v_and_b32_e32 v34, 0x70, v18
	v_mul_lo_u32 v18, v52, s10
	s_lshl_b64 s[16:17], s[24:25], s20
	s_waitcnt lgkmcnt(0)
	v_add3_u32 v28, s45, v34, v18
	v_ashrrev_i32_e32 v53, 31, v52
	s_or_b32 s16, s16, s28
	ds_read_b128 v[18:21], v28
	v_lshlrev_b64 v[22:23], s20, v[52:53]
	v_lshl_add_u64 v[22:23], v[22:23], 0, s[16:17]
	v_lshlrev_b64 v[22:23], 7, v[22:23]
	v_lshl_add_u64 v[22:23], s[26:27], 0, v[22:23]
	v_lshl_add_u64 v[26:27], v[22:23], 0, v[34:35]
	ds_read_b128 v[22:25], v28 offset:1152
	s_waitcnt lgkmcnt(1)
	global_store_dwordx4 v[26:27], v[18:21], off sc1
	v_cmp_gt_u32_e32 vcc, 32, v135
	v_readlane_b32 s57, v252, 9
	v_add_u32_e32 v18, 8, v52
	v_ashrrev_i32_e32 v19, 31, v18
	v_lshlrev_b64 v[18:19], s20, v[18:19]
	v_lshl_add_u64 v[18:19], v[18:19], 0, s[16:17]
	v_lshlrev_b64 v[18:19], 7, v[18:19]
	v_lshl_add_u64 v[18:19], s[26:27], 0, v[18:19]
	v_lshl_add_u64 v[18:19], v[18:19], 0, v[34:35]
	s_waitcnt lgkmcnt(0)
	global_store_dwordx4 v[18:19], v[22:25], off sc1
	ds_read_b128 v[18:21], v28 offset:2304
	s_nop 0
	v_add_u32_e32 v22, 16, v52
	v_ashrrev_i32_e32 v23, 31, v22
	v_lshlrev_b64 v[22:23], s20, v[22:23]
	v_lshl_add_u64 v[22:23], v[22:23], 0, s[16:17]
	v_lshlrev_b64 v[22:23], 7, v[22:23]
	v_lshl_add_u64 v[22:23], s[26:27], 0, v[22:23]
	v_lshl_add_u64 v[26:27], v[22:23], 0, v[34:35]
	ds_read_b128 v[22:25], v28 offset:3456
	s_waitcnt lgkmcnt(1)
	global_store_dwordx4 v[26:27], v[18:21], off sc1
	s_nop 1
	v_add_u32_e32 v18, 24, v52
	v_ashrrev_i32_e32 v19, 31, v18
	v_lshlrev_b64 v[18:19], s20, v[18:19]
	v_lshl_add_u64 v[18:19], v[18:19], 0, s[16:17]
	v_lshlrev_b64 v[18:19], 7, v[18:19]
	v_lshl_add_u64 v[18:19], s[26:27], 0, v[18:19]
	v_lshl_add_u64 v[18:19], v[18:19], 0, v[34:35]
	s_waitcnt lgkmcnt(0)
	global_store_dwordx4 v[18:19], v[22:25], off sc1
	s_waitcnt lgkmcnt(0)
	s_and_saveexec_b64 s[16:17], vcc
	s_cbranch_execz .LBB0_546
	v_log_f32_e32 v18, v54
	s_lshl_b64 s[18:19], s[18:19], 2
	s_add_u32 s18, s82, s18
	s_addc_u32 s19, s83, s19
	v_add_f32_e32 v18, v137, v18
	v_mul_f32_e32 v20, 0x3f317218, v18
	v_or_b32_e32 v18, s24, v135
	v_ashrrev_i32_e32 v19, 31, v18
	v_lshlrev_b64 v[18:19], s20, v[18:19]
	v_lshl_add_u64 v[18:19], v[18:19], 2, s[18:19]
	s_lshl_b32 s66, s28, 2
	v_lshl_add_u64 v[18:19], v[18:19], 0, s[66:67]
	global_store_dword v[18:19], v20, off sc1
	s_branch .LBB0_546

; __device__ __forceinline__ unsigned pk2(float lo, float hi) { pk2_f32x2 v = {lo, hi}; pk2_bf16x2 b = __builtin_convertvector(v, pk2_bf16x2); return __builtin_bit_cast(unsigned, b); }
; __device__ __forceinline__ void mg_merge(const Args& a) {
;     ...
;         for (int q = 0; q < 4; ++q) { const size_t i = i0 + q * step; if (i < total) { const size_t ht = i >> 3; const int c = (int)(i & 7);
;             const float mx = fmaxf(l0[q], fmaxf(l1[q], l2[q]));
;             float w0 = __expf(l0[q] - mx), w1 = __expf(l1[q] - mx), w2 = __expf(l2[q] - mx);
;             const float inv = 1.f / (w0 + w1 + w2); w0 *= inv; w1 *= inv; w2 *= inv;
;             u32x4 r;
; #pragma unroll
;             for (int k = 0; k < 4; ++k) {
;                 const float x0 = w0 * __uint_as_float(a0[q][k] << 16) + w1 * __uint_as_float(a1[q][k] << 16) + w2 * __uint_as_float(a2[q][k] << 16);
;                 const float x1 = w0 * __uint_as_float(a0[q][k] & 0xffff0000u) + w1 * __uint_as_float(a1[q][k] & 0xffff0000u) + w2 * __uint_as_float(a2[q][k] & 0xffff0000u);
;                 r[k] = pk2(x0, x1);
;             }
;             *(u32x4*)(mix + ((size_t)4 * NTOK + ht) * 64 + c * 8) = r; } }
.LBB0_654:
	s_or_b64 exec, exec, s[14:15]
	s_waitcnt vmcnt(0)
	v_max3_f32 v56, v72, v70, v71
	v_sub_f32_e32 v57, v72, v56
	v_mul_f32_e32 v57, 0x3fb8aa3b, v57
	v_exp_f32_e32 v58, v57
	v_sub_f32_e32 v57, v70, v56
	v_mul_f32_e32 v57, 0x3fb8aa3b, v57
	v_sub_f32_e32 v56, v71, v56
	v_exp_f32_e32 v59, v57
	v_mul_f32_e32 v56, 0x3fb8aa3b, v56
	v_exp_f32_e32 v60, v56
	v_lshlrev_b32_e32 v74, 16, v48
	v_add_f32_e32 v56, v58, v59
	v_and_b32_e32 v75, 0xffff0000, v48
	v_add_f32_e32 v61, v60, v56
	v_div_scale_f32 v70, s[14:15], v61, v61, 1.0
	v_rcp_f32_e32 v71, v70
	v_readlane_b32 s14, v253, 17
	v_readlane_b32 s15, v253, 18
	v_lshlrev_b32_e32 v48, 16, v49
	v_and_b32_e32 v49, 0xffff0000, v49
	v_lshl_add_u64 v[56:57], s[14:15], 0, v[34:35]
	v_fma_f32 v34, -v70, v71, 1.0
	v_fmac_f32_e32 v71, v34, v71
	v_div_scale_f32 v34, vcc, 1.0, v61, 1.0
	v_mul_f32_e32 v72, v34, v71
	v_fma_f32 v73, -v70, v72, v34
	v_fmac_f32_e32 v72, v73, v71
	v_fma_f32 v34, -v70, v72, v34
	v_div_fmas_f32 v34, v34, v71, v72
	v_div_fixup_f32 v34, v34, v61, 1.0
	v_pk_mul_f32 v[58:59], v[58:59], v[34:35] op_sel_hi:[1,0]
	v_lshlrev_b32_e32 v70, 16, v40
	v_and_b32_e32 v71, 0xffff0000, v44
	v_lshlrev_b32_e32 v72, 16, v44
	v_and_b32_e32 v73, 0xffff0000, v40
	v_pk_mul_f32 v[70:71], v[58:59], v[70:71] op_sel:[1,0] op_sel_hi:[0,1]
	v_mul_f32_e32 v60, v60, v34
	v_pk_fma_f32 v[70:71], v[58:59], v[72:73], v[70:71]
	v_lshlrev_b32_e32 v44, 16, v45
	v_pk_fma_f32 v[70:71], v[60:61], v[74:75], v[70:71] op_sel_hi:[0,1,1]
	v_cvt_pk_bf16_f32 v40, v70, v71
	v_lshlrev_b32_e32 v70, 16, v41
	v_and_b32_e32 v71, 0xffff0000, v45
	v_and_b32_e32 v45, 0xffff0000, v41
	v_pk_mul_f32 v[70:71], v[58:59], v[70:71] op_sel:[1,0] op_sel_hi:[0,1]
	v_pk_fma_f32 v[44:45], v[58:59], v[44:45], v[70:71]
	v_lshlrev_b32_e32 v70, 16, v50
	v_pk_fma_f32 v[44:45], v[60:61], v[48:49], v[44:45] op_sel_hi:[0,1,1]
	v_cvt_pk_bf16_f32 v41, v44, v45
	v_lshlrev_b32_e32 v44, 16, v42
	v_and_b32_e32 v45, 0xffff0000, v46
	v_lshlrev_b32_e32 v48, 16, v46
	v_and_b32_e32 v49, 0xffff0000, v42
	v_pk_mul_f32 v[44:45], v[58:59], v[44:45] op_sel:[1,0] op_sel_hi:[0,1]
	v_and_b32_e32 v71, 0xffff0000, v50
	v_pk_fma_f32 v[44:45], v[58:59], v[48:49], v[44:45]
	v_lshlrev_b32_e32 v46, 16, v47
	v_pk_fma_f32 v[44:45], v[60:61], v[70:71], v[44:45] op_sel_hi:[0,1,1]
	v_cvt_pk_bf16_f32 v42, v44, v45
	v_lshlrev_b32_e32 v44, 16, v43
	v_and_b32_e32 v45, 0xffff0000, v47
	v_pk_mul_f32 v[44:45], v[58:59], v[44:45] op_sel:[1,0] op_sel_hi:[0,1]
	v_and_b32_e32 v47, 0xffff0000, v43
	v_pk_fma_f32 v[44:45], v[58:59], v[46:47], v[44:45]
	v_lshlrev_b32_e32 v46, 16, v51
	v_and_b32_e32 v47, 0xffff0000, v51
	v_and_b32_e32 v34, 0xffffc0, v52
	v_pk_fma_f32 v[44:45], v[60:61], v[46:47], v[44:45] op_sel_hi:[0,1,1]
	v_lshlrev_b32_e32 v34, 1, v34
	v_cvt_pk_bf16_f32 v43, v44, v45
	v_lshl_add_u64 v[44:45], v[56:57], 0, v[34:35]
	global_store_dwordx4 v[44:45], v[40:43], off sc1
	s_and_saveexec_b64 s[14:15], s[4:5]
	s_cbranch_execz .LBB0_657
	v_max3_f32 v34, v63, v66, v69
	v_sub_f32_e32 v40, v63, v34
	v_sub_f32_e32 v41, v66, v34
	v_mul_f32_e32 v40, 0x3fb8aa3b, v40
	v_mul_f32_e32 v41, 0x3fb8aa3b, v41
	v_sub_f32_e32 v34, v69, v34
	v_exp_f32_e32 v40, v40
	v_exp_f32_e32 v41, v41
	v_mul_f32_e32 v34, 0x3fb8aa3b, v34
	v_exp_f32_e32 v42, v34
	v_lshlrev_b32_e32 v48, 16, v14
	v_add_f32_e32 v34, v40, v41
	v_and_b32_e32 v49, 0xffff0000, v14
	v_add_f32_e32 v34, v42, v34
	v_div_scale_f32 v43, s[4:5], v34, v34, 1.0
	v_rcp_f32_e32 v44, v43
	v_lshlrev_b32_e32 v50, 16, v15
	v_and_b32_e32 v51, 0xffff0000, v15
	v_readlane_b32 s4, v254, 12
	v_fma_f32 v45, -v43, v44, 1.0
	v_fmac_f32_e32 v44, v45, v44
	v_div_scale_f32 v45, vcc, 1.0, v34, 1.0
	v_mul_f32_e32 v46, v45, v44
	v_fma_f32 v47, -v43, v46, v45
	v_fmac_f32_e32 v46, v47, v44
	v_fma_f32 v43, -v43, v46, v45
	v_div_fmas_f32 v43, v43, v44, v46
	v_div_fixup_f32 v34, v43, v34, 1.0
	v_pk_mul_f32 v[46:47], v[40:41], v[34:35] op_sel_hi:[1,0]
	v_lshlrev_b32_e32 v40, 16, v26
	v_and_b32_e32 v41, 0xffff0000, v2
	v_mul_f32_e32 v44, v42, v34
	v_lshlrev_b32_e32 v42, 16, v2
	v_and_b32_e32 v43, 0xffff0000, v26
	v_pk_mul_f32 v[40:41], v[46:47], v[40:41] op_sel:[1,0] op_sel_hi:[0,1]
	v_pk_fma_f32 v[40:41], v[46:47], v[42:43], v[40:41]
	v_lshlrev_b32_e32 v42, 16, v27
	v_and_b32_e32 v43, 0xffff0000, v3
	v_pk_fma_f32 v[40:41], v[44:45], v[48:49], v[40:41] op_sel_hi:[0,1,1]
	v_lshlrev_b32_e32 v48, 16, v3
	v_and_b32_e32 v49, 0xffff0000, v27
	v_pk_mul_f32 v[42:43], v[46:47], v[42:43] op_sel:[1,0] op_sel_hi:[0,1]
	v_pk_fma_f32 v[42:43], v[46:47], v[48:49], v[42:43]
	v_cvt_pk_bf16_f32 v40, v40, v41
	v_pk_fma_f32 v[42:43], v[44:45], v[50:51], v[42:43] op_sel_hi:[0,1,1]
	v_cvt_pk_bf16_f32 v41, v42, v43
	v_lshlrev_b32_e32 v42, 16, v28
	v_and_b32_e32 v43, 0xffff0000, v4
	v_lshlrev_b32_e32 v48, 16, v4
	v_and_b32_e32 v49, 0xffff0000, v28
	v_pk_mul_f32 v[42:43], v[46:47], v[42:43] op_sel:[1,0] op_sel_hi:[0,1]
	v_lshlrev_b32_e32 v50, 16, v16
	v_and_b32_e32 v51, 0xffff0000, v16
	v_pk_fma_f32 v[42:43], v[46:47], v[48:49], v[42:43]
	v_lshlrev_b32_e32 v48, 16, v29
	v_and_b32_e32 v49, 0xffff0000, v5
	v_pk_fma_f32 v[42:43], v[44:45], v[50:51], v[42:43] op_sel_hi:[0,1,1]
	v_pk_mul_f32 v[48:49], v[46:47], v[48:49] op_sel:[1,0] op_sel_hi:[0,1]
	v_lshlrev_b32_e32 v50, 16, v5
	v_and_b32_e32 v51, 0xffff0000, v29
	v_add_u32_e32 v34, s4, v52
	v_pk_fma_f32 v[46:47], v[46:47], v[50:51], v[48:49]
	v_lshlrev_b32_e32 v48, 16, v17
	v_and_b32_e32 v49, 0xffff0000, v17
	v_and_b32_e32 v34, 0xffffc0, v34
	v_pk_fma_f32 v[44:45], v[44:45], v[48:49], v[46:47] op_sel_hi:[0,1,1]
	v_lshlrev_b32_e32 v34, 1, v34
	v_cvt_pk_bf16_f32 v42, v42, v43
	v_cvt_pk_bf16_f32 v43, v44, v45
	v_lshl_add_u64 v[44:45], v[56:57], 0, v[34:35]
	v_readlane_b32 s5, v254, 13
	global_store_dwordx4 v[44:45], v[40:43], off sc1
	s_or_b64 exec, exec, s[14:15]
	s_and_saveexec_b64 s[4:5], s[6:7]
	s_cbranch_execnz .LBB0_658

; __device__ __forceinline__ unsigned pk2(float lo, float hi) { pk2_f32x2 v = {lo, hi}; pk2_bf16x2 b = __builtin_convertvector(v, pk2_bf16x2); return __builtin_bit_cast(unsigned, b); }
; __device__ __forceinline__ void mg_merge(const Args& a) {
;     ...
;         for (int q = 0; q < 4; ++q) { const size_t i = i0 + q * step; if (i < total) { const size_t ht = i >> 3; const int c = (int)(i & 7);
;             const float mx = fmaxf(l0[q], fmaxf(l1[q], l2[q]));
;             float w0 = __expf(l0[q] - mx), w1 = __expf(l1[q] - mx), w2 = __expf(l2[q] - mx);
;             const float inv = 1.f / (w0 + w1 + w2); w0 *= inv; w1 *= inv; w2 *= inv;
;             u32x4 r;
; #pragma unroll
;             for (int k = 0; k < 4; ++k) {
;                 const float x0 = w0 * __uint_as_float(a0[q][k] << 16) + w1 * __uint_as_float(a1[q][k] << 16) + w2 * __uint_as_float(a2[q][k] << 16);
;                 const float x1 = w0 * __uint_as_float(a0[q][k] & 0xffff0000u) + w1 * __uint_as_float(a1[q][k] & 0xffff0000u) + w2 * __uint_as_float(a2[q][k] & 0xffff0000u);
;                 r[k] = pk2(x0, x1);
;             }
;             *(u32x4*)(mix + ((size_t)4 * NTOK + ht) * 64 + c * 8) = r; } }
.LBB0_658:
	v_max3_f32 v34, v62, v65, v68
	v_sub_f32_e32 v40, v62, v34
	v_sub_f32_e32 v41, v65, v34
	v_mul_f32_e32 v40, 0x3fb8aa3b, v40
	v_mul_f32_e32 v41, 0x3fb8aa3b, v41
	v_sub_f32_e32 v34, v68, v34
	v_exp_f32_e32 v40, v40
	v_exp_f32_e32 v41, v41
	v_mul_f32_e32 v34, 0x3fb8aa3b, v34
	v_exp_f32_e32 v42, v34
	v_lshlrev_b32_e32 v48, 16, v10
	v_add_f32_e32 v34, v40, v41
	v_and_b32_e32 v49, 0xffff0000, v10
	v_add_f32_e32 v34, v42, v34
	v_div_scale_f32 v43, s[6:7], v34, v34, 1.0
	v_rcp_f32_e32 v44, v43
	v_lshlrev_b32_e32 v50, 16, v11
	v_and_b32_e32 v51, 0xffff0000, v11
	v_readlane_b32 s6, v254, 2
	v_fma_f32 v45, -v43, v44, 1.0
	v_fmac_f32_e32 v44, v45, v44
	v_div_scale_f32 v45, vcc, 1.0, v34, 1.0
	v_mul_f32_e32 v46, v45, v44
	v_fma_f32 v47, -v43, v46, v45
	v_fmac_f32_e32 v46, v47, v44
	v_fma_f32 v43, -v43, v46, v45
	v_div_fmas_f32 v43, v43, v44, v46
	v_div_fixup_f32 v34, v43, v34, 1.0
	v_pk_mul_f32 v[46:47], v[40:41], v[34:35] op_sel_hi:[1,0]
	v_lshlrev_b32_e32 v40, 16, v30
	v_and_b32_e32 v41, 0xffff0000, v18
	v_mul_f32_e32 v44, v42, v34
	v_lshlrev_b32_e32 v42, 16, v18
	v_and_b32_e32 v43, 0xffff0000, v30
	v_pk_mul_f32 v[40:41], v[46:47], v[40:41] op_sel:[1,0] op_sel_hi:[0,1]
	v_pk_fma_f32 v[40:41], v[46:47], v[42:43], v[40:41]
	v_lshlrev_b32_e32 v42, 16, v31
	v_and_b32_e32 v43, 0xffff0000, v19
	v_pk_fma_f32 v[40:41], v[44:45], v[48:49], v[40:41] op_sel_hi:[0,1,1]
	v_lshlrev_b32_e32 v48, 16, v19
	v_and_b32_e32 v49, 0xffff0000, v31
	v_pk_mul_f32 v[42:43], v[46:47], v[42:43] op_sel:[1,0] op_sel_hi:[0,1]
	v_pk_fma_f32 v[42:43], v[46:47], v[48:49], v[42:43]
	v_cvt_pk_bf16_f32 v40, v40, v41
	v_pk_fma_f32 v[42:43], v[44:45], v[50:51], v[42:43] op_sel_hi:[0,1,1]
	v_cvt_pk_bf16_f32 v41, v42, v43
	v_lshlrev_b32_e32 v42, 16, v32
	v_and_b32_e32 v43, 0xffff0000, v20
	v_lshlrev_b32_e32 v48, 16, v20
	v_and_b32_e32 v49, 0xffff0000, v32
	v_pk_mul_f32 v[42:43], v[46:47], v[42:43] op_sel:[1,0] op_sel_hi:[0,1]
	v_lshlrev_b32_e32 v50, 16, v12
	v_and_b32_e32 v51, 0xffff0000, v12
	v_pk_fma_f32 v[42:43], v[46:47], v[48:49], v[42:43]
	v_lshlrev_b32_e32 v48, 16, v33
	v_and_b32_e32 v49, 0xffff0000, v21
	v_pk_fma_f32 v[42:43], v[44:45], v[50:51], v[42:43] op_sel_hi:[0,1,1]
	v_pk_mul_f32 v[48:49], v[46:47], v[48:49] op_sel:[1,0] op_sel_hi:[0,1]
	v_lshlrev_b32_e32 v50, 16, v21
	v_and_b32_e32 v51, 0xffff0000, v33
	v_add_u32_e32 v34, s6, v52
	v_pk_fma_f32 v[46:47], v[46:47], v[50:51], v[48:49]
	v_lshlrev_b32_e32 v48, 16, v13
	v_and_b32_e32 v49, 0xffff0000, v13
	v_and_b32_e32 v34, 0xffffc0, v34
	v_pk_fma_f32 v[44:45], v[44:45], v[48:49], v[46:47] op_sel_hi:[0,1,1]
	v_lshlrev_b32_e32 v34, 1, v34
	v_cvt_pk_bf16_f32 v42, v42, v43
	v_cvt_pk_bf16_f32 v43, v44, v45
	v_lshl_add_u64 v[44:45], v[56:57], 0, v[34:35]
	v_readlane_b32 s7, v254, 3
	global_store_dwordx4 v[44:45], v[40:43], off sc1
	s_or_b64 exec, exec, s[4:5]
	s_and_saveexec_b64 s[4:5], s[8:9]
	s_cbranch_execz .LBB0_647
.LBB0_659:
	v_max3_f32 v34, v1, v64, v67
	v_sub_f32_e32 v40, v1, v34
	v_mul_f32_e32 v40, 0x3fb8aa3b, v40
	v_exp_f32_e32 v41, v40
	v_sub_f32_e32 v40, v64, v34
	v_mul_f32_e32 v40, 0x3fb8aa3b, v40
	v_sub_f32_e32 v34, v67, v34
	v_exp_f32_e32 v40, v40
	v_mul_f32_e32 v34, 0x3fb8aa3b, v34
	v_exp_f32_e32 v42, v34
	v_lshlrev_b32_e32 v48, 16, v6
	v_add_f32_e32 v34, v41, v40
	v_and_b32_e32 v49, 0xffff0000, v6
	v_add_f32_e32 v34, v42, v34
	v_div_scale_f32 v43, s[6:7], v34, v34, 1.0
	v_rcp_f32_e32 v44, v43
	v_lshlrev_b32_e32 v50, 16, v7
	v_and_b32_e32 v51, 0xffff0000, v7
	v_readlane_b32 s2, v253, 49
	v_fma_f32 v45, -v43, v44, 1.0
	v_fmac_f32_e32 v44, v45, v44
	v_div_scale_f32 v45, vcc, 1.0, v34, 1.0
	v_mul_f32_e32 v46, v45, v44
	v_fma_f32 v47, -v43, v46, v45
	v_fmac_f32_e32 v46, v47, v44
	v_fma_f32 v43, -v43, v46, v45
	v_div_fmas_f32 v43, v43, v44, v46
	v_div_fixup_f32 v34, v43, v34, 1.0
	v_mul_f32_e32 v44, v42, v34
	v_pk_mul_f32 v[46:47], v[40:41], v[34:35] op_sel_hi:[1,0]
	v_lshlrev_b32_e32 v42, 16, v22
	v_and_b32_e32 v43, 0xffff0000, v36
	v_lshlrev_b32_e32 v40, 16, v36
	v_and_b32_e32 v41, 0xffff0000, v22
	v_pk_mul_f32 v[42:43], v[46:47], v[42:43] op_sel:[1,0] op_sel_hi:[0,1]
	v_pk_fma_f32 v[40:41], v[46:47], v[40:41], v[42:43]
	v_lshlrev_b32_e32 v42, 16, v37
	v_pk_fma_f32 v[40:41], v[44:45], v[48:49], v[40:41] op_sel_hi:[0,1,1]
	v_lshlrev_b32_e32 v48, 16, v23
	v_and_b32_e32 v49, 0xffff0000, v37
	v_and_b32_e32 v43, 0xffff0000, v23
	v_pk_mul_f32 v[48:49], v[46:47], v[48:49] op_sel:[1,0] op_sel_hi:[0,1]
	v_pk_fma_f32 v[42:43], v[46:47], v[42:43], v[48:49]
	v_lshlrev_b32_e32 v48, 16, v24
	v_pk_fma_f32 v[42:43], v[44:45], v[50:51], v[42:43] op_sel_hi:[0,1,1]
	v_and_b32_e32 v49, 0xffff0000, v38
	v_cvt_pk_bf16_f32 v40, v40, v41
	v_cvt_pk_bf16_f32 v41, v42, v43
	v_lshlrev_b32_e32 v42, 16, v38
	v_and_b32_e32 v43, 0xffff0000, v24
	v_pk_mul_f32 v[48:49], v[46:47], v[48:49] op_sel:[1,0] op_sel_hi:[0,1]
	v_lshlrev_b32_e32 v50, 16, v8
	v_and_b32_e32 v51, 0xffff0000, v8
	v_pk_fma_f32 v[42:43], v[46:47], v[42:43], v[48:49]
	v_lshlrev_b32_e32 v48, 16, v39
	v_pk_fma_f32 v[42:43], v[44:45], v[50:51], v[42:43] op_sel_hi:[0,1,1]
	v_lshlrev_b32_e32 v50, 16, v25
	v_and_b32_e32 v51, 0xffff0000, v39
	v_and_b32_e32 v49, 0xffff0000, v25
	v_pk_mul_f32 v[50:51], v[46:47], v[50:51] op_sel:[1,0] op_sel_hi:[0,1]
	v_add_u32_e32 v34, s2, v52
	v_pk_fma_f32 v[46:47], v[46:47], v[48:49], v[50:51]
	v_lshlrev_b32_e32 v48, 16, v9
	v_and_b32_e32 v49, 0xffff0000, v9
	v_and_b32_e32 v34, 0xffffc0, v34
	v_pk_fma_f32 v[44:45], v[44:45], v[48:49], v[46:47] op_sel_hi:[0,1,1]
	v_lshlrev_b32_e32 v34, 1, v34
	v_cvt_pk_bf16_f32 v42, v42, v43
	v_cvt_pk_bf16_f32 v43, v44, v45
	v_lshl_add_u64 v[44:45], v[56:57], 0, v[34:35]
	global_store_dwordx4 v[44:45], v[40:43], off sc1
	s_branch .LBB0_647

; __device__ __forceinline__ unsigned cvt_pk_bf16(float lo, float hi) { unsigned r; asm volatile("v_cvt_pk_bf16_f32 %0, %1, %2" : "=v"(r) : "v"(lo), "v"(hi)); return r; }
;     __device__ __forceinline__ void operator()(const f32x4 (&acc)[2][2][4][2], const pg8::Unit& u, int wr, int wc, int fr, int fq) const {
;         const int row0 = u.pm * 256 + wr * 64 + fr, col0 = u.pn * 256 + wc * 32 + 8 * fq, b = (u.pm * 256) / S;
;         f32x4 gv[2][2];
; #pragma unroll
;         for (int bj = 0; bj < 2; ++bj)
; #pragma unroll
;             for (int n = 0; n < 2; ++n) gv[bj][n] = *(const f32x4*)(gm + (size_t)b * 6144 + col0 + bj * 128 + n * 4);
;     ...
;         constexpr int PF = 4;
;         if (xin32) {
;             f32x4 xq[PF][2];
; #pragma unroll
;             for (int it = 0; it < PF; ++it) { xq[it][0] = __builtin_nontemporal_load((const f32x4*)(xin32 + EO_OFF(it))); xq[it][1] = __builtin_nontemporal_load((const f32x4*)(xin32 + EO_OFF(it) + 4)); }
; #pragma unroll
;             for (int it = 0; it < 16; ++it) {
;                 const int ai = it >> 3, m = (it >> 1) & 3, bj = it & 1;
;                 const f32x4 x0 = xq[it % PF][0], x1 = xq[it % PF][1];
;                 if (it + PF < 16) { xq[it % PF][0] = __builtin_nontemporal_load((const f32x4*)(xin32 + EO_OFF(it + PF))); xq[it % PF][1] = __builtin_nontemporal_load((const f32x4*)(xin32 + EO_OFF(it + PF) + 4)); }
;                 const f32x4 v0 = x0 + gv[bj][0] * acc[ai][bj][m][0], v1 = x1 + gv[bj][1] * acc[ai][bj][m][1];
;                 u32x4 w; w.x = pg8::cvt_pk_bf16(v0[0], v0[1]); w.y = pg8::cvt_pk_bf16(v0[2], v0[3]); w.z = pg8::cvt_pk_bf16(v1[0], v1[1]); w.w = pg8::cvt_pk_bf16(v1[2], v1[3]);
;                 *(u32x4*)(out + EO_OFF(it)) = w;
;             }
.LBB0_720:
	s_ashr_i32 s15, s43, 31
	s_lshr_b32 s15, s15, 28
	s_add_i32 s15, s43, s15
	s_ashr_i32 s15, s15, 4
	s_mul_hi_i32 s17, s15, 0x6000
	s_mulk_i32 s15, 0x6000
	v_lshl_or_b32 v204, s44, 8, v248
	s_add_u32 s22, s36, s15
	s_addc_u32 s23, s37, s17
	v_ashrrev_i32_e32 v205, 31, v204
	v_lshl_add_u64 v[56:57], v[204:205], 2, s[22:23]
	global_load_dwordx4 v[60:63], v[56:57], off offset:16
	global_load_dwordx4 v[64:67], v[56:57], off
	global_load_dwordx4 v[52:55], v[56:57], off offset:528
	s_nop 0
	global_load_dwordx4 v[56:59], v[56:57], off offset:512
	v_lshl_add_u32 v226, s43, 8, v1
	v_or_b32_e32 v148, 16, v226
	v_ashrrev_i32_e32 v227, 31, v226
	v_ashrrev_i32_e32 v149, 31, v148
	v_lshlrev_b64 v[222:223], 11, v[226:227]
	v_lshlrev_b64 v[220:221], 11, v[148:149]
	s_andn2_b64 vcc, exec, s[12:13]
	v_lshlrev_b64 v[206:207], 1, v[204:205]
	v_or_b32_e32 v218, 32, v226
	v_lshl_add_u64 v[216:217], s[50:51], 0, v[222:223]
	v_or_b32_e32 v214, 48, v226
	v_lshl_add_u64 v[212:213], s[50:51], 0, v[220:221]
	v_add_u32_e32 v210, 0xa0, v226
	v_add_u32_e32 v208, 0xb0, v226
	s_cbranch_vccnz .LBB0_726
	v_lshlrev_b64 v[224:225], 2, v[204:205]
	v_lshl_add_u64 v[154:155], s[8:9], 0, v[224:225]
	v_lshlrev_b64 v[150:151], 12, v[226:227]
	v_lshl_add_u64 v[156:157], v[154:155], 0, v[150:151]
	global_load_dwordx4 v[150:153], v[156:157], off offset:16 nt
	global_load_dwordx4 v[172:175], v[156:157], off nt
	global_load_dwordx4 v[176:179], v[156:157], off offset:528 nt
	global_load_dwordx4 v[232:235], v[156:157], off offset:512 nt
	v_lshlrev_b64 v[148:149], 12, v[148:149]
	v_lshl_add_u64 v[148:149], v[154:155], 0, v[148:149]
	global_load_dwordx4 v[244:247], v[148:149], off offset:16 nt
	global_load_dwordx4 v[228:231], v[148:149], off nt
	global_load_dwordx4 v[156:159], v[148:149], off offset:528 nt
	global_load_dwordx4 v[160:163], v[148:149], off offset:512 nt
	v_ashrrev_i32_e32 v219, 31, v218
	v_lshlrev_b64 v[148:149], 12, v[218:219]
	v_lshl_add_u64 v[148:149], s[8:9], 0, v[148:149]
	v_lshl_add_u64 v[154:155], v[148:149], 0, v[224:225]
	global_load_dwordx4 v[164:167], v[154:155], off offset:16 nt
	global_load_dwordx4 v[168:171], v[154:155], off nt
	v_ashrrev_i32_e32 v215, 31, v214
	v_ashrrev_i32_e32 v211, 31, v210
	v_ashrrev_i32_e32 v209, 31, v208
	s_waitcnt vmcnt(0)
	v_pk_fma_f32 v[152:153], v[142:143], v[62:63], v[152:153]
	v_pk_fma_f32 v[148:149], v[144:145], v[64:65], v[172:173]
	v_pk_fma_f32 v[150:151], v[140:141], v[60:61], v[150:151]
	v_pk_fma_f32 v[174:175], v[146:147], v[66:67], v[174:175]
	v_cvt_pk_bf16_f32 v148, v148, v149
	v_pk_fma_f32 v[172:173], v[132:133], v[52:53], v[176:177]
	v_cvt_pk_bf16_f32 v149, v174, v175
	v_cvt_pk_bf16_f32 v150, v150, v151
	v_cvt_pk_bf16_f32 v151, v152, v153
	v_lshl_add_u64 v[152:153], v[216:217], 0, v[206:207]
	global_store_dwordx4 v[152:153], v[148:151], off sc1
	global_load_dwordx4 v[180:183], v[154:155], off offset:528 nt
	global_load_dwordx4 v[184:187], v[154:155], off offset:512 nt
	v_pk_fma_f32 v[148:149], v[136:137], v[56:57], v[232:233]
	v_pk_fma_f32 v[150:151], v[138:139], v[58:59], v[234:235]
	v_cvt_pk_bf16_f32 v148, v148, v149
	v_pk_fma_f32 v[154:155], v[134:135], v[54:55], v[178:179]
	v_cvt_pk_bf16_f32 v149, v150, v151
	v_cvt_pk_bf16_f32 v150, v172, v173
	v_pk_fma_f32 v[174:175], v[130:131], v[66:67], v[230:231]
	v_cvt_pk_bf16_f32 v151, v154, v155
	global_store_dwordx4 v[152:153], v[148:151], off offset:256 sc1
	v_pk_fma_f32 v[172:173], v[128:129], v[64:65], v[228:229]
	v_pk_fma_f32 v[228:229], v[124:125], v[60:61], v[244:245]
	v_lshlrev_b64 v[148:149], 12, v[214:215]
	v_lshl_add_u64 v[148:149], s[8:9], 0, v[148:149]
	v_lshl_add_u64 v[176:177], v[148:149], 0, v[224:225]
	global_load_dwordx4 v[148:151], v[176:177], off offset:16 nt
	global_load_dwordx4 v[152:155], v[176:177], off nt
	v_cvt_pk_bf16_f32 v172, v172, v173
	v_cvt_pk_bf16_f32 v173, v174, v175
	v_cvt_pk_bf16_f32 v174, v228, v229
	v_lshl_add_u64 v[228:229], v[212:213], 0, v[206:207]
	v_pk_fma_f32 v[178:179], v[126:127], v[62:63], v[246:247]
	v_pk_fma_f32 v[230:231], v[118:119], v[54:55], v[158:159]
	v_cvt_pk_bf16_f32 v175, v178, v179
	global_store_dwordx4 v[228:229], v[172:175], off sc1
	v_pk_fma_f32 v[158:159], v[116:117], v[52:53], v[156:157]
	global_load_dwordx4 v[172:175], v[176:177], off offset:528 nt
	s_nop 0
	global_load_dwordx4 v[176:179], v[176:177], off offset:512 nt
	v_pk_fma_f32 v[162:163], v[122:123], v[58:59], v[162:163]
	v_pk_fma_f32 v[160:161], v[120:121], v[56:57], v[160:161]
	v_pk_fma_f32 v[168:169], v[112:113], v[64:65], v[168:169]
	v_cvt_pk_bf16_f32 v156, v160, v161
	v_cvt_pk_bf16_f32 v157, v162, v163
	v_cvt_pk_bf16_f32 v158, v158, v159
	v_cvt_pk_bf16_f32 v159, v230, v231
	global_store_dwordx4 v[228:229], v[156:159], off offset:256 sc1
	v_add_u32_e32 v228, 0x80, v226
	v_ashrrev_i32_e32 v229, 31, v228
	v_lshlrev_b64 v[156:157], 12, v[228:229]
	v_lshl_add_u64 v[156:157], s[8:9], 0, v[156:157]
	v_lshl_add_u64 v[230:231], v[156:157], 0, v[224:225]
	global_load_dwordx4 v[156:159], v[230:231], off offset:16 nt
	global_load_dwordx4 v[160:163], v[230:231], off nt
	v_pk_fma_f32 v[232:233], v[110:111], v[62:63], v[166:167]
	v_pk_fma_f32 v[166:167], v[108:109], v[60:61], v[164:165]
	v_cvt_pk_bf16_f32 v164, v168, v169
	v_lshlrev_b64 v[168:169], 11, v[218:219]
	v_lshl_add_u64 v[168:169], s[50:51], 0, v[168:169]
	v_pk_fma_f32 v[170:171], v[114:115], v[66:67], v[170:171]
	v_add_u32_e32 v226, 0x90, v226
	v_cvt_pk_bf16_f32 v165, v170, v171
	v_cvt_pk_bf16_f32 v166, v166, v167
	v_cvt_pk_bf16_f32 v167, v232, v233
	v_lshl_add_u64 v[232:233], v[168:169], 0, v[206:207]
	global_store_dwordx4 v[232:233], v[164:167], off sc1
	global_load_dwordx4 v[164:167], v[230:231], off offset:528 nt
	s_nop 0
	global_load_dwordx4 v[168:171], v[230:231], off offset:512 nt
	v_ashrrev_i32_e32 v227, 31, v226
	s_waitcnt vmcnt(13)
; __device__ __forceinline__ unsigned cvt_pk_bf16(float lo, float hi) { unsigned r; asm volatile("v_cvt_pk_bf16_f32 %0, %1, %2" : "=v"(r) : "v"(lo), "v"(hi)); return r; }
;     __device__ __forceinline__ void operator()(const f32x4 (&acc)[2][2][4][2], const pg8::Unit& u, int wr, int wc, int fr, int fq) const {
;     ...
;             for (int it = 0; it < 16; ++it) {
;                 const int ai = it >> 3, m = (it >> 1) & 3, bj = it & 1;
;                 const f32x4 x0 = xq[it % PF][0], x1 = xq[it % PF][1];
;                 if (it + PF < 16) { xq[it % PF][0] = __builtin_nontemporal_load((const f32x4*)(xin32 + EO_OFF(it + PF))); xq[it % PF][1] = __builtin_nontemporal_load((const f32x4*)(xin32 + EO_OFF(it + PF) + 4)); }
;                 const f32x4 v0 = x0 + gv[bj][0] * acc[ai][bj][m][0], v1 = x1 + gv[bj][1] * acc[ai][bj][m][1];
;                 u32x4 w; w.x = pg8::cvt_pk_bf16(v0[0], v0[1]); w.y = pg8::cvt_pk_bf16(v0[2], v0[3]); w.z = pg8::cvt_pk_bf16(v1[0], v1[1]); w.w = pg8::cvt_pk_bf16(v1[2], v1[3]);
;                 *(u32x4*)(out + EO_OFF(it)) = w;
;             }
	v_pk_fma_f32 v[230:231], v[102:103], v[54:55], v[182:183]
	s_waitcnt vmcnt(12)
	v_pk_fma_f32 v[186:187], v[106:107], v[58:59], v[186:187]
	v_pk_fma_f32 v[184:185], v[104:105], v[56:57], v[184:185]
	v_pk_fma_f32 v[182:183], v[100:101], v[52:53], v[180:181]
	v_cvt_pk_bf16_f32 v180, v184, v185
	v_cvt_pk_bf16_f32 v181, v186, v187
	s_waitcnt vmcnt(9)
	v_pk_fma_f32 v[152:153], v[96:97], v[64:65], v[152:153]
	v_cvt_pk_bf16_f32 v182, v182, v183
	v_cvt_pk_bf16_f32 v183, v230, v231
	global_store_dwordx4 v[232:233], v[180:183], off offset:256 sc1
	v_pk_fma_f32 v[232:233], v[94:95], v[62:63], v[150:151]
	v_pk_fma_f32 v[150:151], v[92:93], v[60:61], v[148:149]
	v_lshlrev_b64 v[180:181], 12, v[226:227]
	v_lshl_add_u64 v[180:181], s[8:9], 0, v[180:181]
	v_lshl_add_u64 v[230:231], v[180:181], 0, v[224:225]
	global_load_dwordx4 v[180:183], v[230:231], off offset:16 nt
	global_load_dwordx4 v[184:187], v[230:231], off nt
	v_cvt_pk_bf16_f32 v148, v152, v153
	v_lshlrev_b64 v[152:153], 11, v[214:215]
	v_lshl_add_u64 v[152:153], s[50:51], 0, v[152:153]
	v_pk_fma_f32 v[154:155], v[98:99], v[66:67], v[154:155]
	s_waitcnt vmcnt(9)
	v_pk_fma_f32 v[178:179], v[90:91], v[58:59], v[178:179]
	v_cvt_pk_bf16_f32 v149, v154, v155
	v_cvt_pk_bf16_f32 v150, v150, v151
	v_cvt_pk_bf16_f32 v151, v232, v233
	v_lshl_add_u64 v[232:233], v[152:153], 0, v[206:207]
	global_store_dwordx4 v[232:233], v[148:151], off sc1
	global_load_dwordx4 v[148:151], v[230:231], off offset:528 nt
	s_nop 0
	global_load_dwordx4 v[152:155], v[230:231], off offset:512 nt
	v_pk_fma_f32 v[176:177], v[88:89], v[56:57], v[176:177]
	v_pk_fma_f32 v[230:231], v[86:87], v[54:55], v[174:175]
	v_pk_fma_f32 v[174:175], v[84:85], v[52:53], v[172:173]
	v_cvt_pk_bf16_f32 v172, v176, v177
	v_cvt_pk_bf16_f32 v173, v178, v179
	s_waitcnt vmcnt(9)
	v_pk_fma_f32 v[160:161], v[80:81], v[64:65], v[160:161]
	v_cvt_pk_bf16_f32 v174, v174, v175
	v_cvt_pk_bf16_f32 v175, v230, v231
	global_store_dwordx4 v[232:233], v[172:175], off offset:256 sc1
	v_pk_fma_f32 v[232:233], v[78:79], v[62:63], v[158:159]
	v_pk_fma_f32 v[158:159], v[76:77], v[60:61], v[156:157]
	v_lshlrev_b64 v[172:173], 12, v[210:211]
	v_lshl_add_u64 v[172:173], s[8:9], 0, v[172:173]
	v_lshl_add_u64 v[230:231], v[172:173], 0, v[224:225]
	global_load_dwordx4 v[172:175], v[230:231], off offset:16 nt
	global_load_dwordx4 v[176:179], v[230:231], off nt
	v_cvt_pk_bf16_f32 v156, v160, v161
	v_lshlrev_b64 v[160:161], 11, v[228:229]
	v_lshl_add_u64 v[160:161], s[50:51], 0, v[160:161]
	v_lshl_add_u64 v[228:229], v[160:161], 0, v[206:207]
	v_pk_fma_f32 v[162:163], v[82:83], v[66:67], v[162:163]
	s_waitcnt vmcnt(9)
	v_pk_fma_f32 v[170:171], v[74:75], v[58:59], v[170:171]
	v_cvt_pk_bf16_f32 v157, v162, v163
	v_cvt_pk_bf16_f32 v158, v158, v159
	v_cvt_pk_bf16_f32 v159, v232, v233
	global_store_dwordx4 v[228:229], v[156:159], off sc1
	global_load_dwordx4 v[156:159], v[230:231], off offset:528 nt
	s_nop 0
	global_load_dwordx4 v[160:163], v[230:231], off offset:512 nt
	v_pk_fma_f32 v[168:169], v[72:73], v[56:57], v[168:169]
	v_pk_fma_f32 v[230:231], v[70:71], v[54:55], v[166:167]
	v_pk_fma_f32 v[166:167], v[68:69], v[52:53], v[164:165]
	v_cvt_pk_bf16_f32 v164, v168, v169
	v_cvt_pk_bf16_f32 v165, v170, v171
	s_waitcnt vmcnt(9)
	v_pk_fma_f32 v[184:185], v[48:49], v[64:65], v[184:185]
	v_cvt_pk_bf16_f32 v166, v166, v167
	v_cvt_pk_bf16_f32 v167, v230, v231
	global_store_dwordx4 v[228:229], v[164:167], off offset:256 sc1
	v_pk_fma_f32 v[228:229], v[46:47], v[62:63], v[182:183]
	v_pk_fma_f32 v[182:183], v[44:45], v[60:61], v[180:181]
	v_lshlrev_b64 v[164:165], 12, v[208:209]
	v_lshl_add_u64 v[164:165], s[8:9], 0, v[164:165]
	v_lshl_add_u64 v[224:225], v[164:165], 0, v[224:225]
	global_load_dwordx4 v[164:167], v[224:225], off offset:16 nt
	global_load_dwordx4 v[168:171], v[224:225], off nt
	v_cvt_pk_bf16_f32 v180, v184, v185
	v_lshlrev_b64 v[184:185], 11, v[226:227]
	v_lshl_add_u64 v[184:185], s[50:51], 0, v[184:185]
	v_lshl_add_u64 v[226:227], v[184:185], 0, v[206:207]
	v_pk_fma_f32 v[186:187], v[50:51], v[66:67], v[186:187]
	s_waitcnt vmcnt(9)
	v_pk_fma_f32 v[154:155], v[42:43], v[58:59], v[154:155]
	v_cvt_pk_bf16_f32 v181, v186, v187
	v_cvt_pk_bf16_f32 v182, v182, v183
	v_cvt_pk_bf16_f32 v183, v228, v229
	global_store_dwordx4 v[226:227], v[180:183], off sc1
	global_load_dwordx4 v[180:183], v[224:225], off offset:528 nt
	s_nop 0
	global_load_dwordx4 v[184:187], v[224:225], off offset:512 nt
	v_pk_fma_f32 v[224:225], v[38:39], v[54:55], v[150:151]
	v_pk_fma_f32 v[150:151], v[36:37], v[52:53], v[148:149]
	v_pk_fma_f32 v[152:153], v[40:41], v[56:57], v[152:153]
	s_waitcnt vmcnt(7)
	v_pk_fma_f32 v[156:157], v[18:19], v[52:53], v[156:157]
	v_cvt_pk_bf16_f32 v148, v152, v153
	v_cvt_pk_bf16_f32 v149, v154, v155
	v_cvt_pk_bf16_f32 v150, v150, v151
	v_cvt_pk_bf16_f32 v151, v224, v225
	global_store_dwordx4 v[226:227], v[148:151], off offset:256 sc1
	v_pk_fma_f32 v[152:153], v[28:29], v[62:63], v[174:175]
	v_pk_fma_f32 v[154:155], v[26:27], v[60:61], v[172:173]
	v_pk_fma_f32 v[150:151], v[32:33], v[66:67], v[178:179]
	v_pk_fma_f32 v[148:149], v[30:31], v[64:65], v[176:177]
	s_nop 0
	v_cvt_pk_bf16_f32 v148, v148, v149
	v_cvt_pk_bf16_f32 v149, v150, v151
	v_cvt_pk_bf16_f32 v150, v154, v155
	v_cvt_pk_bf16_f32 v151, v152, v153
	v_lshlrev_b64 v[152:153], 11, v[210:211]
	v_lshl_add_u64 v[152:153], s[50:51], 0, v[152:153]
	v_lshl_add_u64 v[152:153], v[152:153], 0, v[206:207]
	global_store_dwordx4 v[152:153], v[148:151], off sc1
	v_pk_fma_f32 v[154:155], v[20:21], v[54:55], v[158:159]
	s_waitcnt vmcnt(8)
	v_pk_fma_f32 v[150:151], v[24:25], v[58:59], v[162:163]
	v_pk_fma_f32 v[148:149], v[22:23], v[56:57], v[160:161]
	s_nop 0
	v_cvt_pk_bf16_f32 v148, v148, v149
	v_cvt_pk_bf16_f32 v149, v150, v151
	v_cvt_pk_bf16_f32 v150, v156, v157
	v_cvt_pk_bf16_f32 v151, v154, v155
	global_store_dwordx4 v[152:153], v[148:151], off offset:256 sc1
	s_waitcnt vmcnt(7)
	v_pk_fma_f32 v[152:153], v[12:13], v[62:63], v[166:167]
	s_waitcnt vmcnt(6)
	v_pk_fma_f32 v[150:151], v[16:17], v[66:67], v[170:171]
	v_pk_fma_f32 v[148:149], v[14:15], v[64:65], v[168:169]
	v_pk_fma_f32 v[154:155], v[10:11], v[60:61], v[164:165]
	v_cvt_pk_bf16_f32 v148, v148, v149
	v_cvt_pk_bf16_f32 v149, v150, v151
	s_waitcnt vmcnt(4)
	v_pk_fma_f32 v[156:157], v[2:3], v[52:53], v[180:181]
	v_cvt_pk_bf16_f32 v150, v154, v155
	v_cvt_pk_bf16_f32 v151, v152, v153
	v_lshlrev_b64 v[152:153], 11, v[208:209]
	v_lshl_add_u64 v[154:155], s[50:51], 0, v[152:153]
	v_lshl_add_u64 v[154:155], v[154:155], 0, v[206:207]
	global_store_dwordx4 v[154:155], v[148:151], off sc1
	v_pk_fma_f32 v[154:155], v[4:5], v[54:55], v[182:183]
	s_waitcnt vmcnt(4)
	v_pk_fma_f32 v[150:151], v[8:9], v[58:59], v[186:187]
	v_pk_fma_f32 v[148:149], v[6:7], v[56:57], v[184:185]
	s_nop 0
	v_cvt_pk_bf16_f32 v148, v148, v149
	v_cvt_pk_bf16_f32 v149, v150, v151
	v_cvt_pk_bf16_f32 v150, v156, v157
	v_cvt_pk_bf16_f32 v151, v154, v155
	s_cbranch_execnz .LBB0_723
; __device__ __forceinline__ unsigned cvt_pk_bf16(float lo, float hi) { unsigned r; asm volatile("v_cvt_pk_bf16_f32 %0, %1, %2" : "=v"(r) : "v"(lo), "v"(hi)); return r; }
;     __device__ __forceinline__ void operator()(const f32x4 (&acc)[2][2][4][2], const pg8::Unit& u, int wr, int wc, int fr, int fq) const {
;     ...
;             u32x4 xq[PF];
; #pragma unroll
;             for (int it = 0; it < PF; ++it) xq[it] = __builtin_nontemporal_load((const u32x4*)(xin16 + EO_OFF(it)));
; #pragma unroll
;             for (int it = 0; it < 16; ++it) {
;                 const int ai = it >> 3, m = (it >> 1) & 3, bj = it & 1;
;                 const u32x4 xv = xq[it % PF];
;                 if (it + PF < 16) xq[it % PF] = __builtin_nontemporal_load((const u32x4*)(xin16 + EO_OFF(it + PF)));
;                 const f32x4 x0 = (f32x4){__uint_as_float(xv.x << 16), __uint_as_float(xv.x & 0xffff0000u), __uint_as_float(xv.y << 16), __uint_as_float(xv.y & 0xffff0000u)};
;                 const f32x4 x1 = (f32x4){__uint_as_float(xv.z << 16), __uint_as_float(xv.z & 0xffff0000u), __uint_as_float(xv.w << 16), __uint_as_float(xv.w & 0xffff0000u)};
;                 const f32x4 v0 = x0 + gv[bj][0] * acc[ai][bj][m][0], v1 = x1 + gv[bj][1] * acc[ai][bj][m][1];
;                 u32x4 w; w.x = pg8::cvt_pk_bf16(v0[0], v0[1]); w.y = pg8::cvt_pk_bf16(v0[2], v0[3]); w.z = pg8::cvt_pk_bf16(v1[0], v1[1]); w.w = pg8::cvt_pk_bf16(v1[2], v1[3]);
;                 *(u32x4*)(out + EO_OFF(it)) = w;
;             }
.LBB0_722:
	v_lshl_add_u64 v[148:149], s[50:51], 0, v[206:207]
	v_lshl_add_u64 v[150:151], v[148:149], 0, v[222:223]
	global_load_dwordx4 v[162:165], v[150:151], off nt
	global_load_dwordx4 v[166:169], v[150:151], off offset:256 nt
	v_lshl_add_u64 v[148:149], v[148:149], 0, v[220:221]
	global_load_dwordx4 v[156:159], v[148:149], off nt
	global_load_dwordx4 v[152:155], v[148:149], off offset:256 nt
	v_ashrrev_i32_e32 v219, 31, v218
	v_lshlrev_b64 v[148:149], 11, v[218:219]
	v_lshl_add_u64 v[148:149], s[50:51], 0, v[148:149]
	v_lshl_add_u64 v[160:161], v[148:149], 0, v[206:207]
	global_load_dwordx4 v[148:151], v[160:161], off nt
	v_ashrrev_i32_e32 v215, 31, v214
	s_mov_b32 s15, 0x40000
	s_mov_b64 s[22:23], 0x40000
	v_ashrrev_i32_e32 v211, 31, v210
	v_ashrrev_i32_e32 v209, 31, v208
	s_waitcnt vmcnt(0)
	v_lshlrev_b32_e32 v170, 16, v162
	v_and_b32_e32 v171, 0xffff0000, v162
	v_lshlrev_b32_e32 v162, 16, v163
	v_and_b32_e32 v163, 0xffff0000, v163
	v_lshlrev_b32_e32 v172, 16, v164
	v_and_b32_e32 v173, 0xffff0000, v164
	v_lshlrev_b32_e32 v164, 16, v165
	v_and_b32_e32 v165, 0xffff0000, v165
	v_pk_fma_f32 v[146:147], v[146:147], v[66:67], v[162:163]
	v_pk_fma_f32 v[144:145], v[144:145], v[64:65], v[170:171]
	v_pk_fma_f32 v[162:163], v[142:143], v[62:63], v[164:165]
	v_pk_fma_f32 v[142:143], v[140:141], v[60:61], v[172:173]
	v_cvt_pk_bf16_f32 v140, v144, v145
	v_cvt_pk_bf16_f32 v141, v146, v147
	v_lshl_add_u64 v[144:145], v[216:217], 0, v[206:207]
	v_cvt_pk_bf16_f32 v142, v142, v143
	v_cvt_pk_bf16_f32 v143, v162, v163
	global_store_dwordx4 v[144:145], v[140:143], off sc1
	global_load_dwordx4 v[140:143], v[160:161], off offset:256 nt
	v_lshlrev_b32_e32 v146, 16, v166
	v_and_b32_e32 v147, 0xffff0000, v166
	v_lshlrev_b32_e32 v162, 16, v167
	v_and_b32_e32 v163, 0xffff0000, v167
	v_lshlrev_b32_e32 v164, 16, v168
	v_and_b32_e32 v165, 0xffff0000, v168
	v_lshlrev_b32_e32 v166, 16, v169
	v_and_b32_e32 v167, 0xffff0000, v169
	v_pk_fma_f32 v[138:139], v[138:139], v[58:59], v[162:163]
	v_pk_fma_f32 v[136:137], v[136:137], v[56:57], v[146:147]
	v_pk_fma_f32 v[146:147], v[134:135], v[54:55], v[166:167]
	v_pk_fma_f32 v[134:135], v[132:133], v[52:53], v[164:165]
	v_cvt_pk_bf16_f32 v132, v136, v137
	v_cvt_pk_bf16_f32 v133, v138, v139
	v_lshlrev_b32_e32 v138, 16, v156
	v_cvt_pk_bf16_f32 v134, v134, v135
	v_cvt_pk_bf16_f32 v135, v146, v147
	global_store_dwordx4 v[144:145], v[132:135], off offset:256 sc1
	v_and_b32_e32 v139, 0xffff0000, v156
	v_lshlrev_b32_e32 v146, 16, v157
	v_lshlrev_b64 v[132:133], 11, v[214:215]
	v_lshl_add_u64 v[132:133], s[50:51], 0, v[132:133]
	v_lshl_add_u64 v[136:137], v[132:133], 0, v[206:207]
	v_and_b32_e32 v147, 0xffff0000, v157
	v_lshlrev_b32_e32 v156, 16, v158
	v_and_b32_e32 v157, 0xffff0000, v158
	v_lshlrev_b32_e32 v158, 16, v159
	v_and_b32_e32 v159, 0xffff0000, v159
	global_load_dwordx4 v[132:135], v[136:137], off nt
	v_pk_fma_f32 v[128:129], v[128:129], v[64:65], v[138:139]
	v_pk_fma_f32 v[138:139], v[126:127], v[62:63], v[158:159]
	v_pk_fma_f32 v[126:127], v[124:125], v[60:61], v[156:157]
	v_pk_fma_f32 v[130:131], v[130:131], v[66:67], v[146:147]
	v_cvt_pk_bf16_f32 v124, v128, v129
	v_lshl_add_u64 v[128:129], v[212:213], 0, v[206:207]
	v_cvt_pk_bf16_f32 v125, v130, v131
	v_cvt_pk_bf16_f32 v126, v126, v127
	v_cvt_pk_bf16_f32 v127, v138, v139
	global_store_dwordx4 v[128:129], v[124:127], off sc1
	global_load_dwordx4 v[124:127], v[136:137], off offset:256 nt
	v_lshlrev_b32_e32 v138, 16, v153
	v_and_b32_e32 v139, 0xffff0000, v153
	v_lshlrev_b32_e32 v130, 16, v152
	v_and_b32_e32 v131, 0xffff0000, v152
	v_lshlrev_b32_e32 v146, 16, v154
	v_and_b32_e32 v147, 0xffff0000, v154
	v_lshlrev_b32_e32 v152, 16, v155
	v_and_b32_e32 v153, 0xffff0000, v155
	v_pk_fma_f32 v[122:123], v[122:123], v[58:59], v[138:139]
	v_pk_fma_f32 v[120:121], v[120:121], v[56:57], v[130:131]
	v_pk_fma_f32 v[130:131], v[118:119], v[54:55], v[152:153]
	v_pk_fma_f32 v[118:119], v[116:117], v[52:53], v[146:147]
	v_cvt_pk_bf16_f32 v116, v120, v121
	v_cvt_pk_bf16_f32 v117, v122, v123
	v_add_co_u32_e32 v122, vcc, s15, v144
	v_cvt_pk_bf16_f32 v118, v118, v119
	v_cvt_pk_bf16_f32 v119, v130, v131
	global_store_dwordx4 v[128:129], v[116:119], off offset:256 sc1
	s_nop 0
	v_addc_co_u32_e32 v123, vcc, 0, v145, vcc
	v_lshlrev_b32_e32 v128, 16, v148
	v_and_b32_e32 v129, 0xffff0000, v148
	v_lshlrev_b32_e32 v138, 16, v150
	v_and_b32_e32 v139, 0xffff0000, v150
	v_lshlrev_b32_e32 v146, 16, v151
	v_and_b32_e32 v147, 0xffff0000, v151
	global_load_dwordx4 v[116:119], v[122:123], off nt
	v_lshlrev_b32_e32 v130, 16, v149
	v_and_b32_e32 v131, 0xffff0000, v149
	v_pk_fma_f32 v[112:113], v[112:113], v[64:65], v[128:129]
	v_pk_fma_f32 v[128:129], v[110:111], v[62:63], v[146:147]
	v_pk_fma_f32 v[110:111], v[108:109], v[60:61], v[138:139]
	v_lshl_add_u64 v[120:121], v[144:145], 0, s[22:23]
	v_pk_fma_f32 v[114:115], v[114:115], v[66:67], v[130:131]
	v_cvt_pk_bf16_f32 v108, v112, v113
	s_mov_b32 s15, 0x48000
	v_cvt_pk_bf16_f32 v109, v114, v115
	v_cvt_pk_bf16_f32 v110, v110, v111
	v_cvt_pk_bf16_f32 v111, v128, v129
	global_store_dwordx4 v[160:161], v[108:111], off sc1
	global_load_dwordx4 v[108:111], v[120:121], off offset:256 nt
	s_waitcnt vmcnt(8)
; __device__ __forceinline__ unsigned cvt_pk_bf16(float lo, float hi) { unsigned r; asm volatile("v_cvt_pk_bf16_f32 %0, %1, %2" : "=v"(r) : "v"(lo), "v"(hi)); return r; }
;     __device__ __forceinline__ void operator()(const f32x4 (&acc)[2][2][4][2], const pg8::Unit& u, int wr, int wc, int fr, int fq) const {
;     ...
;             u32x4 xq[PF];
; #pragma unroll
;             for (int it = 0; it < PF; ++it) xq[it] = __builtin_nontemporal_load((const u32x4*)(xin16 + EO_OFF(it)));
; #pragma unroll
;             for (int it = 0; it < 16; ++it) {
;                 const int ai = it >> 3, m = (it >> 1) & 3, bj = it & 1;
;                 const u32x4 xv = xq[it % PF];
;                 if (it + PF < 16) xq[it % PF] = __builtin_nontemporal_load((const u32x4*)(xin16 + EO_OFF(it + PF)));
;                 const f32x4 x0 = (f32x4){__uint_as_float(xv.x << 16), __uint_as_float(xv.x & 0xffff0000u), __uint_as_float(xv.y << 16), __uint_as_float(xv.y & 0xffff0000u)};
;                 const f32x4 x1 = (f32x4){__uint_as_float(xv.z << 16), __uint_as_float(xv.z & 0xffff0000u), __uint_as_float(xv.w << 16), __uint_as_float(xv.w & 0xffff0000u)};
;                 const f32x4 v0 = x0 + gv[bj][0] * acc[ai][bj][m][0], v1 = x1 + gv[bj][1] * acc[ai][bj][m][1];
;                 u32x4 w; w.x = pg8::cvt_pk_bf16(v0[0], v0[1]); w.y = pg8::cvt_pk_bf16(v0[2], v0[3]); w.z = pg8::cvt_pk_bf16(v1[0], v1[1]); w.w = pg8::cvt_pk_bf16(v1[2], v1[3]);
;                 *(u32x4*)(out + EO_OFF(it)) = w;
;             }
	v_lshlrev_b32_e32 v114, 16, v141
	v_and_b32_e32 v115, 0xffff0000, v141
	v_lshlrev_b32_e32 v112, 16, v140
	v_and_b32_e32 v113, 0xffff0000, v140
	v_lshlrev_b32_e32 v128, 16, v142
	v_and_b32_e32 v129, 0xffff0000, v142
	v_lshlrev_b32_e32 v130, 16, v143
	v_and_b32_e32 v131, 0xffff0000, v143
	v_pk_fma_f32 v[106:107], v[106:107], v[58:59], v[114:115]
	v_pk_fma_f32 v[104:105], v[104:105], v[56:57], v[112:113]
	v_pk_fma_f32 v[112:113], v[102:103], v[54:55], v[130:131]
	v_pk_fma_f32 v[102:103], v[100:101], v[52:53], v[128:129]
	v_cvt_pk_bf16_f32 v100, v104, v105
	v_cvt_pk_bf16_f32 v101, v106, v107
	v_add_co_u32_e32 v106, vcc, s15, v144
	v_cvt_pk_bf16_f32 v102, v102, v103
	v_cvt_pk_bf16_f32 v103, v112, v113
	global_store_dwordx4 v[160:161], v[100:103], off offset:256 sc1
	s_nop 0
	v_addc_co_u32_e32 v107, vcc, 0, v145, vcc
	global_load_dwordx4 v[100:103], v[106:107], off nt
	s_mov_b64 s[22:23], 0x48000
	v_lshl_add_u64 v[104:105], v[144:145], 0, s[22:23]
	v_lshlrev_b64 v[152:153], 11, v[208:209]
	s_waitcnt vmcnt(8)
	v_lshlrev_b32_e32 v112, 16, v132
	v_and_b32_e32 v113, 0xffff0000, v132
	v_lshlrev_b32_e32 v114, 16, v133
	v_and_b32_e32 v115, 0xffff0000, v133
	v_lshlrev_b32_e32 v128, 16, v134
	v_and_b32_e32 v129, 0xffff0000, v134
	v_lshlrev_b32_e32 v130, 16, v135
	v_and_b32_e32 v131, 0xffff0000, v135
	v_pk_fma_f32 v[98:99], v[98:99], v[66:67], v[114:115]
	v_pk_fma_f32 v[96:97], v[96:97], v[64:65], v[112:113]
	v_pk_fma_f32 v[112:113], v[94:95], v[62:63], v[130:131]
	v_pk_fma_f32 v[94:95], v[92:93], v[60:61], v[128:129]
	v_cvt_pk_bf16_f32 v92, v96, v97
	v_cvt_pk_bf16_f32 v93, v98, v99
	s_waitcnt vmcnt(6)
	v_lshlrev_b32_e32 v96, 16, v124
	v_cvt_pk_bf16_f32 v94, v94, v95
	v_cvt_pk_bf16_f32 v95, v112, v113
	v_and_b32_e32 v97, 0xffff0000, v124
	v_lshlrev_b32_e32 v98, 16, v125
	v_and_b32_e32 v99, 0xffff0000, v125
	v_lshlrev_b32_e32 v112, 16, v126
	v_and_b32_e32 v113, 0xffff0000, v126
	v_lshlrev_b32_e32 v114, 16, v127
	v_and_b32_e32 v115, 0xffff0000, v127
	global_store_dwordx4 v[136:137], v[92:95], off sc1
	global_load_dwordx4 v[92:95], v[104:105], off offset:256 nt
	v_pk_fma_f32 v[90:91], v[90:91], v[58:59], v[98:99]
	v_pk_fma_f32 v[88:89], v[88:89], v[56:57], v[96:97]
	v_pk_fma_f32 v[96:97], v[86:87], v[54:55], v[114:115]
	v_pk_fma_f32 v[86:87], v[84:85], v[52:53], v[112:113]
	v_cvt_pk_bf16_f32 v84, v88, v89
	v_cvt_pk_bf16_f32 v85, v90, v91
	s_waitcnt vmcnt(6)
	v_lshlrev_b32_e32 v90, 16, v116
	v_cvt_pk_bf16_f32 v86, v86, v87
	v_cvt_pk_bf16_f32 v87, v96, v97
	global_store_dwordx4 v[136:137], v[84:87], off offset:256 sc1
	v_and_b32_e32 v91, 0xffff0000, v116
	v_lshlrev_b32_e32 v96, 16, v117
	v_lshlrev_b64 v[84:85], 11, v[210:211]
	v_lshl_add_u64 v[84:85], s[50:51], 0, v[84:85]
	v_lshl_add_u64 v[88:89], v[84:85], 0, v[206:207]
	v_and_b32_e32 v97, 0xffff0000, v117
	v_lshlrev_b32_e32 v98, 16, v118
	v_and_b32_e32 v99, 0xffff0000, v118
	v_lshlrev_b32_e32 v112, 16, v119
	v_and_b32_e32 v113, 0xffff0000, v119
	global_load_dwordx4 v[84:87], v[88:89], off nt
	v_pk_fma_f32 v[82:83], v[82:83], v[66:67], v[96:97]
	v_pk_fma_f32 v[80:81], v[80:81], v[64:65], v[90:91]
	v_pk_fma_f32 v[90:91], v[78:79], v[62:63], v[112:113]
	v_pk_fma_f32 v[78:79], v[76:77], v[60:61], v[98:99]
	v_cvt_pk_bf16_f32 v76, v80, v81
	v_cvt_pk_bf16_f32 v77, v82, v83
	s_waitcnt vmcnt(6)
	v_lshlrev_b32_e32 v80, 16, v108
	v_cvt_pk_bf16_f32 v78, v78, v79
	v_cvt_pk_bf16_f32 v79, v90, v91
	v_and_b32_e32 v81, 0xffff0000, v108
	v_lshlrev_b32_e32 v82, 16, v109
	v_and_b32_e32 v83, 0xffff0000, v109
	v_lshlrev_b32_e32 v90, 16, v110
	v_and_b32_e32 v91, 0xffff0000, v110
	v_lshlrev_b32_e32 v96, 16, v111
	v_and_b32_e32 v97, 0xffff0000, v111
	global_store_dwordx4 v[122:123], v[76:79], off sc1
	global_load_dwordx4 v[76:79], v[88:89], off offset:256 nt
	v_pk_fma_f32 v[74:75], v[74:75], v[58:59], v[82:83]
	v_pk_fma_f32 v[72:73], v[72:73], v[56:57], v[80:81]
	v_pk_fma_f32 v[80:81], v[70:71], v[54:55], v[96:97]
	v_pk_fma_f32 v[70:71], v[68:69], v[52:53], v[90:91]
	v_cvt_pk_bf16_f32 v68, v72, v73
	v_cvt_pk_bf16_f32 v69, v74, v75
	s_waitcnt vmcnt(6)
; __device__ __forceinline__ unsigned cvt_pk_bf16(float lo, float hi) { unsigned r; asm volatile("v_cvt_pk_bf16_f32 %0, %1, %2" : "=v"(r) : "v"(lo), "v"(hi)); return r; }
;     __device__ __forceinline__ void operator()(const f32x4 (&acc)[2][2][4][2], const pg8::Unit& u, int wr, int wc, int fr, int fq) const {
;     ...
;             u32x4 xq[PF];
; #pragma unroll
;             for (int it = 0; it < PF; ++it) xq[it] = __builtin_nontemporal_load((const u32x4*)(xin16 + EO_OFF(it)));
; #pragma unroll
;             for (int it = 0; it < 16; ++it) {
;                 const int ai = it >> 3, m = (it >> 1) & 3, bj = it & 1;
;                 const u32x4 xv = xq[it % PF];
;                 if (it + PF < 16) xq[it % PF] = __builtin_nontemporal_load((const u32x4*)(xin16 + EO_OFF(it + PF)));
;                 const f32x4 x0 = (f32x4){__uint_as_float(xv.x << 16), __uint_as_float(xv.x & 0xffff0000u), __uint_as_float(xv.y << 16), __uint_as_float(xv.y & 0xffff0000u)};
;                 const f32x4 x1 = (f32x4){__uint_as_float(xv.z << 16), __uint_as_float(xv.z & 0xffff0000u), __uint_as_float(xv.w << 16), __uint_as_float(xv.w & 0xffff0000u)};
;                 const f32x4 v0 = x0 + gv[bj][0] * acc[ai][bj][m][0], v1 = x1 + gv[bj][1] * acc[ai][bj][m][1];
;                 u32x4 w; w.x = pg8::cvt_pk_bf16(v0[0], v0[1]); w.y = pg8::cvt_pk_bf16(v0[2], v0[3]); w.z = pg8::cvt_pk_bf16(v1[0], v1[1]); w.w = pg8::cvt_pk_bf16(v1[2], v1[3]);
;                 *(u32x4*)(out + EO_OFF(it)) = w;
;             }
	v_lshlrev_b32_e32 v74, 16, v100
	v_cvt_pk_bf16_f32 v70, v70, v71
	v_cvt_pk_bf16_f32 v71, v80, v81
	global_store_dwordx4 v[120:121], v[68:71], off offset:256 sc1
	v_and_b32_e32 v75, 0xffff0000, v100
	v_lshlrev_b32_e32 v82, 16, v102
	v_lshl_add_u64 v[68:69], s[50:51], 0, v[152:153]
	v_lshl_add_u64 v[72:73], v[68:69], 0, v[206:207]
	global_load_dwordx4 v[68:71], v[72:73], off nt
	v_and_b32_e32 v83, 0xffff0000, v102
	v_lshlrev_b32_e32 v90, 16, v103
	v_and_b32_e32 v91, 0xffff0000, v103
	v_lshlrev_b32_e32 v80, 16, v101
	v_and_b32_e32 v81, 0xffff0000, v101
	v_pk_fma_f32 v[48:49], v[48:49], v[64:65], v[74:75]
	v_pk_fma_f32 v[74:75], v[46:47], v[62:63], v[90:91]
	v_pk_fma_f32 v[46:47], v[44:45], v[60:61], v[82:83]
	v_pk_fma_f32 v[50:51], v[50:51], v[66:67], v[80:81]
	v_cvt_pk_bf16_f32 v44, v48, v49
	s_waitcnt vmcnt(6)
	v_lshlrev_b32_e32 v48, 16, v92
	v_cvt_pk_bf16_f32 v45, v50, v51
	v_cvt_pk_bf16_f32 v46, v46, v47
	v_cvt_pk_bf16_f32 v47, v74, v75
	global_store_dwordx4 v[106:107], v[44:47], off sc1
	global_load_dwordx4 v[44:47], v[72:73], off offset:256 nt
	v_and_b32_e32 v49, 0xffff0000, v92
	v_lshlrev_b32_e32 v50, 16, v93
	v_and_b32_e32 v51, 0xffff0000, v93
	v_lshlrev_b32_e32 v74, 16, v94
	v_and_b32_e32 v75, 0xffff0000, v94
	v_lshlrev_b32_e32 v80, 16, v95
	v_and_b32_e32 v81, 0xffff0000, v95
	v_pk_fma_f32 v[42:43], v[42:43], v[58:59], v[50:51]
	v_pk_fma_f32 v[40:41], v[40:41], v[56:57], v[48:49]
	v_pk_fma_f32 v[48:49], v[38:39], v[54:55], v[80:81]
	v_pk_fma_f32 v[38:39], v[36:37], v[52:53], v[74:75]
	v_cvt_pk_bf16_f32 v36, v40, v41
	v_cvt_pk_bf16_f32 v37, v42, v43
	s_waitcnt vmcnt(6)
	v_lshlrev_b32_e32 v40, 16, v86
	v_cvt_pk_bf16_f32 v38, v38, v39
	v_cvt_pk_bf16_f32 v39, v48, v49
	global_store_dwordx4 v[104:105], v[36:39], off offset:256 sc1
	v_and_b32_e32 v41, 0xffff0000, v86
	v_lshlrev_b32_e32 v42, 16, v87
	v_lshlrev_b32_e32 v36, 16, v84
	v_and_b32_e32 v37, 0xffff0000, v84
	v_and_b32_e32 v43, 0xffff0000, v87
	v_lshlrev_b32_e32 v38, 16, v85
	v_and_b32_e32 v39, 0xffff0000, v85
	v_pk_fma_f32 v[30:31], v[30:31], v[64:65], v[36:37]
	v_pk_fma_f32 v[36:37], v[28:29], v[62:63], v[42:43]
	v_pk_fma_f32 v[28:29], v[26:27], v[60:61], v[40:41]
	v_pk_fma_f32 v[32:33], v[32:33], v[66:67], v[38:39]
	v_cvt_pk_bf16_f32 v26, v30, v31
	s_waitcnt vmcnt(5)
	v_lshlrev_b32_e32 v30, 16, v78
	v_cvt_pk_bf16_f32 v27, v32, v33
	v_cvt_pk_bf16_f32 v28, v28, v29
	v_cvt_pk_bf16_f32 v29, v36, v37
	global_store_dwordx4 v[88:89], v[26:29], off sc1
	v_and_b32_e32 v31, 0xffff0000, v78
	v_lshlrev_b32_e32 v32, 16, v79
	v_lshlrev_b32_e32 v26, 16, v76
	v_and_b32_e32 v27, 0xffff0000, v76
	v_lshlrev_b32_e32 v28, 16, v77
	v_and_b32_e32 v29, 0xffff0000, v77
	v_and_b32_e32 v33, 0xffff0000, v79
	v_pk_fma_f32 v[24:25], v[24:25], v[58:59], v[28:29]
	v_pk_fma_f32 v[22:23], v[22:23], v[56:57], v[26:27]
	v_pk_fma_f32 v[26:27], v[20:21], v[54:55], v[32:33]
	v_pk_fma_f32 v[20:21], v[18:19], v[52:53], v[30:31]
	v_cvt_pk_bf16_f32 v18, v22, v23
	v_cvt_pk_bf16_f32 v19, v24, v25
	s_waitcnt vmcnt(4)
	v_lshlrev_b32_e32 v22, 16, v70
	v_cvt_pk_bf16_f32 v20, v20, v21
	v_cvt_pk_bf16_f32 v21, v26, v27
	global_store_dwordx4 v[88:89], v[18:21], off offset:256 sc1
	v_and_b32_e32 v23, 0xffff0000, v70
	v_lshlrev_b32_e32 v24, 16, v71
	v_lshlrev_b32_e32 v18, 16, v68
	v_and_b32_e32 v19, 0xffff0000, v68
	v_and_b32_e32 v25, 0xffff0000, v71
	v_lshlrev_b32_e32 v20, 16, v69
	v_and_b32_e32 v21, 0xffff0000, v69
	v_pk_fma_f32 v[14:15], v[14:15], v[64:65], v[18:19]
	v_pk_fma_f32 v[18:19], v[12:13], v[62:63], v[24:25]
	v_pk_fma_f32 v[12:13], v[10:11], v[60:61], v[22:23]
	v_pk_fma_f32 v[16:17], v[16:17], v[66:67], v[20:21]
	v_cvt_pk_bf16_f32 v10, v14, v15
	s_waitcnt vmcnt(3)
	v_lshlrev_b32_e32 v14, 16, v46
	v_cvt_pk_bf16_f32 v11, v16, v17
	v_cvt_pk_bf16_f32 v12, v12, v13
	v_cvt_pk_bf16_f32 v13, v18, v19
	global_store_dwordx4 v[72:73], v[10:13], off sc1
	v_and_b32_e32 v15, 0xffff0000, v46
	v_lshlrev_b32_e32 v16, 16, v47
	v_lshlrev_b32_e32 v10, 16, v44
	v_and_b32_e32 v11, 0xffff0000, v44
	v_lshlrev_b32_e32 v12, 16, v45
	v_and_b32_e32 v13, 0xffff0000, v45
	v_and_b32_e32 v17, 0xffff0000, v47
	v_pk_fma_f32 v[8:9], v[8:9], v[58:59], v[12:13]
	v_pk_fma_f32 v[6:7], v[6:7], v[56:57], v[10:11]
	v_pk_fma_f32 v[4:5], v[4:5], v[54:55], v[16:17]
	v_pk_fma_f32 v[2:3], v[2:3], v[52:53], v[14:15]
	v_cvt_pk_bf16_f32 v148, v6, v7
	v_cvt_pk_bf16_f32 v149, v8, v9
	s_nop 0
	v_cvt_pk_bf16_f32 v150, v2, v3
	v_cvt_pk_bf16_f32 v151, v4, v5
.LBB0_723:
	v_lshl_add_u64 v[2:3], s[50:51], 0, v[152:153]
	v_lshl_add_u64 v[2:3], v[204:205], 1, v[2:3]
	s_andn2_b64 vcc, exec, s[4:5]
	s_mov_b64 s[4:5], -1
	global_store_dwordx4 v[2:3], v[148:151], off offset:256 sc1
	s_cbranch_vccnz .LBB0_709
	s_andn2_b64 vcc, exec, s[6:7]
	s_cbranch_vccnz .LBB0_708
	s_barrier
	s_branch .LBB0_708

; __device__ __forceinline__ unsigned xb_ld(unsigned* p)              { return __hip_atomic_load(p, __ATOMIC_RELAXED, __HIP_MEMORY_SCOPE_AGENT); }
; __device__ __forceinline__ unsigned xb_add(unsigned* p, unsigned v) { return __hip_atomic_fetch_add(p, v, __ATOMIC_RELAXED, __HIP_MEMORY_SCOPE_AGENT); }
; #define XB_SPIN(cond, bar) do { unsigned _sp = 0; while (cond) { __builtin_amdgcn_s_sleep(1); \
;     if ((++_sp & 255u) == 0u) { if (xb_ld(&(bar)[XB_TMO])) break; if (_sp > XB_SPIN_CAP) { atomicAdd(&(bar)[XB_TMO], 1u); break; } } } } while (0)
; __device__ __forceinline__ void xcd_barrier(const XcdBarrier& b) {
;     ...
;         const unsigned old = xb_add(&bar[XB_XSUB(bx)], 1u);
;         const unsigned gen = old / nloc;
;         if (old + 1u == (gen + 1u) * nloc) {
;             __builtin_amdgcn_fence(__ATOMIC_RELEASE, "agent");
;             asm volatile("s_waitcnt vmcnt(0)" ::: "memory");
;             const unsigned og = xb_add(&bar[XB_TOP], 1u);
;             const unsigned tg = og / nx;
;             if (og + 1u == (tg + 1u) * nx) xb_add(&bar[XB_TOPGEN], 1u);
;             else XB_SPIN(xb_ld(&bar[XB_TOPGEN]) == tg, bar);
.LBB0_756:
	s_andn2_saveexec_b64 s[4:5], s[4:5]
	s_cbranch_execz .LBB0_772
	v_mov_b32_e32 v1, s38
	v_add_co_u32_e32 v4, vcc, 0x3000, v1
	v_mov_b32_e32 v1, s39
	s_waitcnt vmcnt(0)
	v_addc_co_u32_e32 v5, vcc, 0, v1, vcc
	flat_atomic_add v3, v[4:5], v238 offset:1024 sc0
	v_cvt_f32_u32_e32 v1, v2
	v_sub_u32_e32 v4, 0, v2
	s_mov_b64 s[8:9], -1
	v_rcp_iflag_f32_e32 v1, v1
	s_nop 0
	v_mul_f32_e32 v1, 0x4f7ffffe, v1
	v_cvt_u32_f32_e32 v1, v1
	v_mul_lo_u32 v4, v4, v1
	v_mul_hi_u32 v4, v1, v4
	v_add_u32_e32 v1, v1, v4
	s_waitcnt vmcnt(0) lgkmcnt(0)
	v_mul_hi_u32 v1, v3, v1
	v_mul_lo_u32 v4, v1, v2
	v_sub_u32_e32 v4, v3, v4
	v_cmp_ge_u32_e32 vcc, v4, v2
	v_add_u32_e32 v5, 1, v1
	s_nop 0
	v_cndmask_b32_e32 v1, v1, v5, vcc
	v_sub_u32_e32 v5, v4, v2
	v_cndmask_b32_e32 v4, v4, v5, vcc
	v_cmp_ge_u32_e32 vcc, v4, v2
	v_add_u32_e32 v4, 1, v1
	s_nop 0
	v_cndmask_b32_e32 v1, v1, v4, vcc
	v_add_u32_e32 v4, 1, v3
	v_mad_u64_u32 v[2:3], s[4:5], v2, v1, v[2:3]
	s_add_u32 s4, s38, 0x3500
	s_addc_u32 s5, s39, 0
	v_cmp_ne_u32_e32 vcc, v4, v2
	v_mov_b64_e32 v[2:3], s[4:5]
	s_and_saveexec_b64 s[6:7], vcc
	s_cbranch_execz .LBB0_769
	v_mov_b64_e32 v[2:3], s[4:5]
	flat_load_dword v2, v[2:3] sc1
	s_mov_b64 s[12:13], 0
	s_waitcnt vmcnt(0) lgkmcnt(0)
	v_cmp_eq_u32_e32 vcc, v2, v1
	s_and_saveexec_b64 s[10:11], vcc
	s_cbranch_execz .LBB0_768
	s_add_u32 s8, s38, 0x200
	s_addc_u32 s9, s39, 0
	s_mov_b32 s24, 1
	s_branch .LBB0_761

; #define LAS __attribute__((address_space(3)))
; __device__ __forceinline__ void n2_mfma(const Args& a, LAS unsigned char* lds, int layer) {
;     ...
;         const LAS unsigned char* rdb = lds + N2_BUF + wave * 6144 + r * 128;
;         const int sw = (r >> 1) & 7;
;         const int sl0 = 16 * (g ^ sw), sl1 = 16 * ((g + 4) ^ sw);
;         u32x4 xs[32];
;         f32x4 acc0 = (f32x4){0.f, 0.f, 0.f, 0.f}, acc1 = (f32x4){0.f, 0.f, 0.f, 0.f};
;         float ss = 0.f;
; #pragma unroll
;         for (int c = 0; c < 16; ++c) {
;             asm volatile("s_waitcnt lgkmcnt(0)" ::: "memory");
;             if (c + 2 < 16) { N2_DMA(c + 2); asm volatile("s_waitcnt vmcnt(4)" ::: "memory"); }
;             else if (c + 1 < 16) asm volatile("s_waitcnt vmcnt(2)" ::: "memory");
;             else asm volatile("s_waitcnt vmcnt(0)" ::: "memory");
;             const LAS unsigned char* cb = rdb + (c % 3) * 2048;
;             xs[2 * c] = *(const LAS u32x4*)(cb + sl0);
;             xs[2 * c + 1] = *(const LAS u32x4*)(cb + sl1);
;             const LAS f32x4* wq = (const LAS f32x4*)(WgL + ((c * 4) * 4 * 16) * 4) + (g * 4) * 16 + r;
;             f32x4 w0 = wq[0], w1 = wq[16], w2 = wq[32], w3 = wq[48];
; #pragma unroll
;             for (int k = 0; k < 4; ++k) {
;                 const unsigned v0 = xs[2 * c][k], v1 = xs[2 * c + 1][k];
;                 const float x00 = __uint_as_float(v0 << 16), x01 = __uint_as_float(v0 & 0xffff0000u);
;                 const float x10 = __uint_as_float(v1 << 16), x11 = __uint_as_float(v1 & 0xffff0000u);
;                 ss += x00 * x00 + x01 * x01; ss += x10 * x10 + x11 * x11;
;                 const float wa = (k < 2 ? w0 : w1)[2 * (k & 1)], wb = (k < 2 ? w0 : w1)[2 * (k & 1) + 1];
;                 const float wc = (k < 2 ? w2 : w3)[2 * (k & 1)], wd = (k < 2 ? w2 : w3)[2 * (k & 1) + 1];
;                 acc0 = __builtin_amdgcn_mfma_f32_16x16x4f32(wa, x00, acc0, 0, 0, 0);
;                 acc1 = __builtin_amdgcn_mfma_f32_16x16x4f32(wc, x10, acc1, 0, 0, 0);
;                 acc0 = __builtin_amdgcn_mfma_f32_16x16x4f32(wb, x01, acc0, 0, 0, 0);
;                 acc1 = __builtin_amdgcn_mfma_f32_16x16x4f32(wd, x11, acc1, 0, 0, 0);
;             }
;             __builtin_amdgcn_sched_barrier(0);
;         }
.LBB0_787:
	s_or_b64 exec, exec, s[14:15]
	v_and_b32_e32 v2, 15, v30
	v_ashrrev_i32_e32 v4, 4, v30
	s_waitcnt lgkmcnt(0)
	s_barrier
	v_lshl_add_u32 v5, v2, 7, s75
	v_lshlrev_b32_e32 v3, 10, v4
	v_lshlrev_b32_e32 v2, 4, v2
	s_waitcnt lgkmcnt(0)
	v_add3_u32 v34, 0, v3, v2
	s_add_i32 s14, s11, 0x16c00
	v_lshl_add_u64 v[2:3], v[108:109], 0, s[94:95]
	s_mov_b32 s15, m0
	s_mov_b32 m0, s14
	s_nop 0
	global_load_lds_dwordx4 v[2:3], off
	s_mov_b32 m0, s15
	v_lshrrev_b32_e32 v14, 1, v30
	v_lshl_add_u64 v[2:3], v[110:111], 0, s[94:95]
	s_add_i32 s15, s11, 0x17000
	s_mov_b32 s16, m0
	s_mov_b32 m0, s15
	s_nop 0
	global_load_lds_dwordx4 v[2:3], off
	s_mov_b32 m0, s16
	s_waitcnt vmcnt(4)
	v_bitop3_b32 v2, v14, v4, 7 bitop3:0x6c
	ds_read_b128 v[10:13], v34
	ds_read_b128 v[18:21], v34 offset:512
	v_lshl_add_u32 v125, v2, 4, v5
	v_add_u32_e32 v2, 4, v4
	v_bitop3_b32 v2, v2, v14, 7 bitop3:0x78
	v_lshl_add_u32 v124, v2, 4, v5
	ds_read_b128 v[6:9], v125
	ds_read_b128 v[2:5], v124
	s_waitcnt lgkmcnt(1)
	v_lshlrev_b32_e32 v26, 16, v6
	s_waitcnt lgkmcnt(0)
	v_lshlrev_b32_e32 v27, 16, v2
	v_mfma_f32_16x16x4_f32 v[14:17], v10, v26, 0
	v_and_b32_e32 v28, 0xffff0000, v6
	v_and_b32_e32 v29, 0xffff0000, v2
	v_lshlrev_b32_e32 v30, 16, v7
	v_lshlrev_b32_e32 v31, 16, v3
	v_and_b32_e32 v32, 0xffff0000, v7
	v_and_b32_e32 v33, 0xffff0000, v3
	v_lshlrev_b32_e32 v36, 16, v8
	v_mfma_f32_16x16x4_f32 v[22:25], v18, v27, 0
	v_mfma_f32_16x16x4_f32 v[14:17], v11, v28, v[14:17]
	v_mfma_f32_16x16x4_f32 v[22:25], v19, v29, v[22:25]
	v_mfma_f32_16x16x4_f32 v[14:17], v12, v30, v[14:17]
	v_mfma_f32_16x16x4_f32 v[22:25], v20, v31, v[22:25]
	v_mfma_f32_16x16x4_f32 v[10:13], v13, v32, v[14:17]
	v_mfma_f32_16x16x4_f32 v[14:17], v21, v33, v[22:25]
	ds_read_b128 v[18:21], v34 offset:256
	s_nop 6
	ds_read_b128 v[22:25], v34 offset:768
	s_waitcnt lgkmcnt(1)
	v_mfma_f32_16x16x4_f32 v[10:13], v18, v36, v[10:13]
	v_lshlrev_b32_e32 v18, 16, v4
	s_waitcnt lgkmcnt(0)
	s_nop 0
	v_mfma_f32_16x16x4_f32 v[14:17], v22, v18, v[14:17]
	v_and_b32_e32 v22, 0xffff0000, v8
	s_nop 1
	v_mfma_f32_16x16x4_f32 v[10:13], v19, v22, v[10:13]
	v_and_b32_e32 v19, 0xffff0000, v4
	v_mul_f32_e32 v22, v22, v22
	v_fmac_f32_e32 v22, v36, v36
	v_mfma_f32_16x16x4_f32 v[14:17], v23, v19, v[14:17]
	v_mul_f32_e32 v23, v28, v28
	v_fmac_f32_e32 v23, v26, v26
	v_mul_f32_e32 v26, v29, v29
	v_fmac_f32_e32 v26, v27, v27
	v_add_f32_e32 v23, v23, v26
	v_lshlrev_b32_e32 v26, 16, v9
	v_mul_f32_e32 v19, v19, v19
	v_fmac_f32_e32 v19, v18, v18
	v_mfma_f32_16x16x4_f32 v[10:13], v20, v26, v[10:13]
	v_mul_f32_e32 v20, v32, v32
	v_fmac_f32_e32 v20, v30, v30
	v_add_f32_e32 v20, v20, v23
	v_mul_f32_e32 v23, v33, v33
	v_fmac_f32_e32 v23, v31, v31
	v_add_f32_e32 v20, v23, v20
	v_lshlrev_b32_e32 v23, 16, v5
	v_add_f32_e32 v20, v22, v20
	v_add_f32_e32 v22, v19, v20
	v_mfma_f32_16x16x4_f32 v[14:17], v24, v23, v[14:17]
	v_and_b32_e32 v24, 0xffff0000, v9
	s_nop 1
	v_mfma_f32_16x16x4_f32 v[18:21], v21, v24, v[10:13]
	v_and_b32_e32 v10, 0xffff0000, v5
	v_mul_f32_e32 v11, v24, v24
	v_fmac_f32_e32 v11, v26, v26
	v_mul_f32_e32 v12, v10, v10
	v_add_f32_e32 v11, v11, v22
	v_fmac_f32_e32 v12, v23, v23
	v_add_f32_e32 v36, v12, v11
	v_mfma_f32_16x16x4_f32 v[22:25], v25, v10, v[14:17]
	s_waitcnt lgkmcnt(0)
	s_mov_b64 s[18:19], 0x180
	v_lshl_add_u64 v[10:11], v[108:109], 0, s[18:19]
	s_mov_b32 s16, m0
	s_mov_b32 m0, s75
	s_nop 0
	global_load_lds_dwordx4 v[10:11], off
	s_mov_b32 m0, s16
	v_lshl_add_u64 v[10:11], v[110:111], 0, s[18:19]
	s_mov_b32 s16, m0
	s_mov_b32 m0, s13
	s_nop 0
	global_load_lds_dwordx4 v[10:11], off
	s_mov_b32 m0, s16
	s_waitcnt vmcnt(4)
	ds_read_b128 v[26:29], v34 offset:4096
	ds_read_b128 v[14:17], v125 offset:2048
	ds_read_b128 v[10:13], v124 offset:2048
	ds_read_b128 v[30:33], v34 offset:4608
	s_waitcnt lgkmcnt(2)
	v_lshlrev_b32_e32 v37, 16, v14
	s_nop 1
	v_mfma_f32_16x16x4_f32 v[18:21], v26, v37, v[18:21]
	v_and_b32_e32 v39, 0xffff0000, v14
	v_lshlrev_b32_e32 v41, 16, v15
	s_waitcnt lgkmcnt(1)
	v_lshlrev_b32_e32 v38, 16, v10
	v_and_b32_e32 v43, 0xffff0000, v15
	v_and_b32_e32 v40, 0xffff0000, v10
	v_lshlrev_b32_e32 v42, 16, v11
	v_and_b32_e32 v44, 0xffff0000, v11
	v_mfma_f32_16x16x4_f32 v[18:21], v27, v39, v[18:21]
	v_lshlrev_b32_e32 v45, 16, v16
	v_mfma_f32_16x16x4_f32 v[18:21], v28, v41, v[18:21]
	v_mfma_f32_16x16x4_f32 v[18:21], v29, v43, v[18:21]
	ds_read_b128 v[26:29], v34 offset:4352
	s_waitcnt lgkmcnt(1)
	v_mfma_f32_16x16x4_f32 v[22:25], v30, v38, v[22:25]
	v_mfma_f32_16x16x4_f32 v[22:25], v31, v40, v[22:25]
	v_mfma_f32_16x16x4_f32 v[22:25], v32, v42, v[22:25]
	v_mfma_f32_16x16x4_f32 v[22:25], v33, v44, v[22:25]
	ds_read_b128 v[30:33], v34 offset:4864
	s_waitcnt lgkmcnt(1)
	v_mfma_f32_16x16x4_f32 v[18:21], v26, v45, v[18:21]
	v_lshlrev_b32_e32 v26, 16, v12
	s_waitcnt lgkmcnt(0)
	s_nop 0
	v_mfma_f32_16x16x4_f32 v[22:25], v30, v26, v[22:25]
	v_and_b32_e32 v30, 0xffff0000, v16
	s_nop 1
	v_mfma_f32_16x16x4_f32 v[18:21], v27, v30, v[18:21]
	v_and_b32_e32 v27, 0xffff0000, v12
	v_mul_f32_e32 v30, v30, v30
	v_fmac_f32_e32 v30, v45, v45
	v_mfma_f32_16x16x4_f32 v[22:25], v31, v27, v[22:25]
	v_mul_f32_e32 v31, v39, v39
	v_fmac_f32_e32 v31, v37, v37
	v_add_f32_e32 v31, v36, v31
	v_mul_f32_e32 v36, v40, v40
	v_fmac_f32_e32 v36, v38, v38
	v_add_f32_e32 v31, v36, v31
	v_lshlrev_b32_e32 v36, 16, v17
	v_mul_f32_e32 v27, v27, v27
	v_fmac_f32_e32 v27, v26, v26
	v_mfma_f32_16x16x4_f32 v[18:21], v28, v36, v[18:21]
	v_mul_f32_e32 v28, v43, v43
	v_fmac_f32_e32 v28, v41, v41
	v_add_f32_e32 v28, v28, v31
	v_mul_f32_e32 v31, v44, v44
	v_fmac_f32_e32 v31, v42, v42
	v_add_f32_e32 v28, v31, v28
	v_lshlrev_b32_e32 v31, 16, v13
	v_add_f32_e32 v28, v30, v28
	v_add_f32_e32 v30, v27, v28
	v_mfma_f32_16x16x4_f32 v[22:25], v32, v31, v[22:25]
	v_and_b32_e32 v32, 0xffff0000, v17
	s_nop 1
	v_mfma_f32_16x16x4_f32 v[26:29], v29, v32, v[18:21]
	v_and_b32_e32 v18, 0xffff0000, v13
	v_mul_f32_e32 v19, v32, v32
	v_fmac_f32_e32 v19, v36, v36
	v_mul_f32_e32 v20, v18, v18
	v_add_f32_e32 v19, v19, v30
	v_fmac_f32_e32 v20, v31, v31
	v_add_f32_e32 v44, v20, v19
	v_mfma_f32_16x16x4_f32 v[30:33], v33, v18, v[22:25]
	s_waitcnt lgkmcnt(0)
; #define LAS __attribute__((address_space(3)))
; #define N2_DMA(c) do { const unsigned d_ = (unsigned)__builtin_amdgcn_readfirstlane(bufw + ((c) % 3) * 2048); n2_glds16(src0 + (c) * 64, d_); n2_glds16(src1 + (c) * 64, d_ + 1024); } while (0)
; __device__ __forceinline__ void n2_mfma(const Args& a, LAS unsigned char* lds, int layer) {
;     ...
;         for (int c = 0; c < 16; ++c) {
;             asm volatile("s_waitcnt lgkmcnt(0)" ::: "memory");
;             if (c + 2 < 16) { N2_DMA(c + 2); asm volatile("s_waitcnt vmcnt(4)" ::: "memory"); }
;             else if (c + 1 < 16) asm volatile("s_waitcnt vmcnt(2)" ::: "memory");
;             else asm volatile("s_waitcnt vmcnt(0)" ::: "memory");
;             const LAS unsigned char* cb = rdb + (c % 3) * 2048;
;             xs[2 * c] = *(const LAS u32x4*)(cb + sl0);
;             xs[2 * c + 1] = *(const LAS u32x4*)(cb + sl1);
;             const LAS f32x4* wq = (const LAS f32x4*)(WgL + ((c * 4) * 4 * 16) * 4) + (g * 4) * 16 + r;
;             f32x4 w0 = wq[0], w1 = wq[16], w2 = wq[32], w3 = wq[48];
; #pragma unroll
;             for (int k = 0; k < 4; ++k) {
;                 const unsigned v0 = xs[2 * c][k], v1 = xs[2 * c + 1][k];
;                 const float x00 = __uint_as_float(v0 << 16), x01 = __uint_as_float(v0 & 0xffff0000u);
;                 const float x10 = __uint_as_float(v1 << 16), x11 = __uint_as_float(v1 & 0xffff0000u);
;                 ss += x00 * x00 + x01 * x01; ss += x10 * x10 + x11 * x11;
;                 const float wa = (k < 2 ? w0 : w1)[2 * (k & 1)], wb = (k < 2 ? w0 : w1)[2 * (k & 1) + 1];
;                 const float wc = (k < 2 ? w2 : w3)[2 * (k & 1)], wd = (k < 2 ? w2 : w3)[2 * (k & 1) + 1];
;                 acc0 = __builtin_amdgcn_mfma_f32_16x16x4f32(wa, x00, acc0, 0, 0, 0);
;                 acc1 = __builtin_amdgcn_mfma_f32_16x16x4f32(wc, x10, acc1, 0, 0, 0);
;                 acc0 = __builtin_amdgcn_mfma_f32_16x16x4f32(wb, x01, acc0, 0, 0, 0);
;                 acc1 = __builtin_amdgcn_mfma_f32_16x16x4f32(wd, x11, acc1, 0, 0, 0);
;             }
;             __builtin_amdgcn_sched_barrier(0);
;         }
	s_mov_b64 s[18:19], 0x200
	v_lshl_add_u64 v[18:19], v[108:109], 0, s[18:19]
	s_mov_b32 s16, m0
	s_mov_b32 m0, s26
	s_nop 0
	global_load_lds_dwordx4 v[18:19], off
	s_mov_b32 m0, s16
	v_lshl_add_u64 v[18:19], v[110:111], 0, s[18:19]
	s_mov_b32 s16, m0
	s_mov_b32 m0, s27
	s_nop 0
	global_load_lds_dwordx4 v[18:19], off
	s_mov_b32 m0, s16
	s_waitcnt vmcnt(4)
	ds_read_b128 v[36:39], v34 offset:8192
	ds_read_b128 v[22:25], v125 offset:4096
	ds_read_b128 v[18:21], v124 offset:4096
	ds_read_b128 v[40:43], v34 offset:8704
	s_waitcnt lgkmcnt(2)
	v_lshlrev_b32_e32 v45, 16, v22
	s_nop 1
	v_mfma_f32_16x16x4_f32 v[26:29], v36, v45, v[26:29]
	v_and_b32_e32 v47, 0xffff0000, v22
	v_lshlrev_b32_e32 v49, 16, v23
	s_waitcnt lgkmcnt(1)
	v_lshlrev_b32_e32 v46, 16, v18
	v_and_b32_e32 v51, 0xffff0000, v23
	v_and_b32_e32 v48, 0xffff0000, v18
	v_lshlrev_b32_e32 v50, 16, v19
	v_and_b32_e32 v52, 0xffff0000, v19
	v_mfma_f32_16x16x4_f32 v[26:29], v37, v47, v[26:29]
	v_lshlrev_b32_e32 v53, 16, v24
	v_mfma_f32_16x16x4_f32 v[26:29], v38, v49, v[26:29]
	v_mfma_f32_16x16x4_f32 v[26:29], v39, v51, v[26:29]
	ds_read_b128 v[36:39], v34 offset:8448
	s_waitcnt lgkmcnt(1)
	v_mfma_f32_16x16x4_f32 v[30:33], v40, v46, v[30:33]
	v_mfma_f32_16x16x4_f32 v[30:33], v41, v48, v[30:33]
	v_mfma_f32_16x16x4_f32 v[30:33], v42, v50, v[30:33]
	v_mfma_f32_16x16x4_f32 v[30:33], v43, v52, v[30:33]
	ds_read_b128 v[40:43], v34 offset:8960
	s_waitcnt lgkmcnt(1)
	v_mfma_f32_16x16x4_f32 v[26:29], v36, v53, v[26:29]
	v_lshlrev_b32_e32 v36, 16, v20
	s_waitcnt lgkmcnt(0)
	s_nop 0
	v_mfma_f32_16x16x4_f32 v[30:33], v40, v36, v[30:33]
	v_and_b32_e32 v40, 0xffff0000, v24
	s_nop 1
	v_mfma_f32_16x16x4_f32 v[26:29], v37, v40, v[26:29]
	v_and_b32_e32 v37, 0xffff0000, v20
	v_mul_f32_e32 v40, v40, v40
	v_fmac_f32_e32 v40, v53, v53
	v_mfma_f32_16x16x4_f32 v[30:33], v41, v37, v[30:33]
	v_mul_f32_e32 v41, v47, v47
	v_fmac_f32_e32 v41, v45, v45
	v_add_f32_e32 v41, v44, v41
	v_mul_f32_e32 v44, v48, v48
	v_fmac_f32_e32 v44, v46, v46
	v_add_f32_e32 v41, v44, v41
	v_lshlrev_b32_e32 v44, 16, v25
	v_mul_f32_e32 v37, v37, v37
	v_fmac_f32_e32 v37, v36, v36
	v_mfma_f32_16x16x4_f32 v[26:29], v38, v44, v[26:29]
	v_mul_f32_e32 v38, v51, v51
	v_fmac_f32_e32 v38, v49, v49
	v_add_f32_e32 v38, v38, v41
	v_mul_f32_e32 v41, v52, v52
	v_fmac_f32_e32 v41, v50, v50
	v_add_f32_e32 v38, v41, v38
	v_lshlrev_b32_e32 v41, 16, v21
	v_add_f32_e32 v38, v40, v38
	v_add_f32_e32 v40, v37, v38
	v_mfma_f32_16x16x4_f32 v[30:33], v42, v41, v[30:33]
	v_and_b32_e32 v42, 0xffff0000, v25
	s_nop 1
	v_mfma_f32_16x16x4_f32 v[36:39], v39, v42, v[26:29]
	v_and_b32_e32 v26, 0xffff0000, v21
	v_mul_f32_e32 v27, v42, v42
	v_fmac_f32_e32 v27, v44, v44
	v_mul_f32_e32 v28, v26, v26
	v_add_f32_e32 v27, v27, v40
	v_fmac_f32_e32 v28, v41, v41
	v_add_f32_e32 v52, v28, v27
	v_mfma_f32_16x16x4_f32 v[40:43], v43, v26, v[30:33]
	s_waitcnt lgkmcnt(0)
	s_mov_b64 s[18:19], 0x280
	v_lshl_add_u64 v[26:27], v[108:109], 0, s[18:19]
	s_mov_b32 s16, m0
	s_mov_b32 m0, s14
	s_nop 0
	global_load_lds_dwordx4 v[26:27], off
	s_mov_b32 m0, s16
	v_lshl_add_u64 v[26:27], v[110:111], 0, s[18:19]
	s_mov_b32 s16, m0
	s_mov_b32 m0, s15
	s_nop 0
	global_load_lds_dwordx4 v[26:27], off
	s_mov_b32 m0, s16
	s_waitcnt vmcnt(4)
	ds_read_b128 v[44:47], v34 offset:12288
	ds_read_b128 v[30:33], v125
	ds_read_b128 v[26:29], v124
	ds_read_b128 v[48:51], v34 offset:12800
	s_waitcnt lgkmcnt(2)
	v_lshlrev_b32_e32 v53, 16, v30
	s_nop 1
	v_mfma_f32_16x16x4_f32 v[36:39], v44, v53, v[36:39]
	v_and_b32_e32 v55, 0xffff0000, v30
	v_lshlrev_b32_e32 v57, 16, v31
	s_waitcnt lgkmcnt(1)
	v_lshlrev_b32_e32 v54, 16, v26
	v_and_b32_e32 v59, 0xffff0000, v31
	v_and_b32_e32 v56, 0xffff0000, v26
	v_lshlrev_b32_e32 v58, 16, v27
	v_and_b32_e32 v60, 0xffff0000, v27
	v_mfma_f32_16x16x4_f32 v[36:39], v45, v55, v[36:39]
	v_lshlrev_b32_e32 v61, 16, v32
	v_mfma_f32_16x16x4_f32 v[36:39], v46, v57, v[36:39]
	v_mfma_f32_16x16x4_f32 v[36:39], v47, v59, v[36:39]
	ds_read_b128 v[44:47], v34 offset:12544
	s_waitcnt lgkmcnt(1)
	v_mfma_f32_16x16x4_f32 v[40:43], v48, v54, v[40:43]
	v_mfma_f32_16x16x4_f32 v[40:43], v49, v56, v[40:43]
	v_mfma_f32_16x16x4_f32 v[40:43], v50, v58, v[40:43]
	v_mfma_f32_16x16x4_f32 v[40:43], v51, v60, v[40:43]
	ds_read_b128 v[48:51], v34 offset:13056
	s_waitcnt lgkmcnt(1)
	v_mfma_f32_16x16x4_f32 v[36:39], v44, v61, v[36:39]
	v_lshlrev_b32_e32 v44, 16, v28
	s_waitcnt lgkmcnt(0)
	s_nop 0
	v_mfma_f32_16x16x4_f32 v[40:43], v48, v44, v[40:43]
	v_and_b32_e32 v48, 0xffff0000, v32
	s_nop 1
	v_mfma_f32_16x16x4_f32 v[36:39], v45, v48, v[36:39]
	v_and_b32_e32 v45, 0xffff0000, v28
	v_mul_f32_e32 v48, v48, v48
	v_fmac_f32_e32 v48, v61, v61
	v_mfma_f32_16x16x4_f32 v[40:43], v49, v45, v[40:43]
	v_mul_f32_e32 v49, v55, v55
	v_fmac_f32_e32 v49, v53, v53
	v_add_f32_e32 v49, v52, v49
	v_mul_f32_e32 v52, v56, v56
	v_fmac_f32_e32 v52, v54, v54
	v_add_f32_e32 v49, v52, v49
	v_lshlrev_b32_e32 v52, 16, v33
	v_mul_f32_e32 v45, v45, v45
	v_fmac_f32_e32 v45, v44, v44
	v_mfma_f32_16x16x4_f32 v[36:39], v46, v52, v[36:39]
	v_mul_f32_e32 v46, v59, v59
	v_fmac_f32_e32 v46, v57, v57
	v_add_f32_e32 v46, v46, v49
	v_mul_f32_e32 v49, v60, v60
	v_fmac_f32_e32 v49, v58, v58
	v_add_f32_e32 v46, v49, v46
	v_lshlrev_b32_e32 v49, 16, v29
	v_add_f32_e32 v46, v48, v46
	v_add_f32_e32 v48, v45, v46
	v_mfma_f32_16x16x4_f32 v[40:43], v50, v49, v[40:43]
	v_and_b32_e32 v50, 0xffff0000, v33
	s_nop 1
	v_mfma_f32_16x16x4_f32 v[44:47], v47, v50, v[36:39]
	v_and_b32_e32 v36, 0xffff0000, v29
	v_mul_f32_e32 v37, v50, v50
	v_fmac_f32_e32 v37, v52, v52
	v_mul_f32_e32 v38, v36, v36
	v_add_f32_e32 v37, v37, v48
	v_fmac_f32_e32 v38, v49, v49
	v_add_f32_e32 v60, v38, v37
	v_mfma_f32_16x16x4_f32 v[48:51], v51, v36, v[40:43]
	s_waitcnt lgkmcnt(0)
; #define LAS __attribute__((address_space(3)))
; #define N2_DMA(c) do { const unsigned d_ = (unsigned)__builtin_amdgcn_readfirstlane(bufw + ((c) % 3) * 2048); n2_glds16(src0 + (c) * 64, d_); n2_glds16(src1 + (c) * 64, d_ + 1024); } while (0)
; __device__ __forceinline__ void n2_mfma(const Args& a, LAS unsigned char* lds, int layer) {
;     ...
;         for (int c = 0; c < 16; ++c) {
;             asm volatile("s_waitcnt lgkmcnt(0)" ::: "memory");
;             if (c + 2 < 16) { N2_DMA(c + 2); asm volatile("s_waitcnt vmcnt(4)" ::: "memory"); }
;             else if (c + 1 < 16) asm volatile("s_waitcnt vmcnt(2)" ::: "memory");
;             else asm volatile("s_waitcnt vmcnt(0)" ::: "memory");
;             const LAS unsigned char* cb = rdb + (c % 3) * 2048;
;             xs[2 * c] = *(const LAS u32x4*)(cb + sl0);
;             xs[2 * c + 1] = *(const LAS u32x4*)(cb + sl1);
;             const LAS f32x4* wq = (const LAS f32x4*)(WgL + ((c * 4) * 4 * 16) * 4) + (g * 4) * 16 + r;
;             f32x4 w0 = wq[0], w1 = wq[16], w2 = wq[32], w3 = wq[48];
; #pragma unroll
;             for (int k = 0; k < 4; ++k) {
;                 const unsigned v0 = xs[2 * c][k], v1 = xs[2 * c + 1][k];
;                 const float x00 = __uint_as_float(v0 << 16), x01 = __uint_as_float(v0 & 0xffff0000u);
;                 const float x10 = __uint_as_float(v1 << 16), x11 = __uint_as_float(v1 & 0xffff0000u);
;                 ss += x00 * x00 + x01 * x01; ss += x10 * x10 + x11 * x11;
;                 const float wa = (k < 2 ? w0 : w1)[2 * (k & 1)], wb = (k < 2 ? w0 : w1)[2 * (k & 1) + 1];
;                 const float wc = (k < 2 ? w2 : w3)[2 * (k & 1)], wd = (k < 2 ? w2 : w3)[2 * (k & 1) + 1];
;                 acc0 = __builtin_amdgcn_mfma_f32_16x16x4f32(wa, x00, acc0, 0, 0, 0);
;                 acc1 = __builtin_amdgcn_mfma_f32_16x16x4f32(wc, x10, acc1, 0, 0, 0);
;                 acc0 = __builtin_amdgcn_mfma_f32_16x16x4f32(wb, x01, acc0, 0, 0, 0);
;                 acc1 = __builtin_amdgcn_mfma_f32_16x16x4f32(wd, x11, acc1, 0, 0, 0);
;             }
;             __builtin_amdgcn_sched_barrier(0);
;         }
	s_mov_b64 s[18:19], 0x300
	v_lshl_add_u64 v[36:37], v[108:109], 0, s[18:19]
	s_mov_b32 s16, m0
	s_mov_b32 m0, s75
	s_nop 0
	global_load_lds_dwordx4 v[36:37], off
	s_mov_b32 m0, s16
	v_lshl_add_u64 v[36:37], v[110:111], 0, s[18:19]
	s_mov_b32 s16, m0
	s_mov_b32 m0, s13
	s_nop 0
	global_load_lds_dwordx4 v[36:37], off
	s_mov_b32 m0, s16
	s_waitcnt vmcnt(4)
	ds_read_b128 v[52:55], v34 offset:16384
	ds_read_b128 v[40:43], v125 offset:2048
	ds_read_b128 v[36:39], v124 offset:2048
	ds_read_b128 v[56:59], v34 offset:16896
	s_waitcnt lgkmcnt(2)
	v_lshlrev_b32_e32 v61, 16, v40
	s_nop 1
	v_mfma_f32_16x16x4_f32 v[44:47], v52, v61, v[44:47]
	v_and_b32_e32 v63, 0xffff0000, v40
	v_lshlrev_b32_e32 v65, 16, v41
	s_waitcnt lgkmcnt(1)
	v_lshlrev_b32_e32 v62, 16, v36
	v_and_b32_e32 v67, 0xffff0000, v41
	v_and_b32_e32 v64, 0xffff0000, v36
	v_lshlrev_b32_e32 v66, 16, v37
	v_and_b32_e32 v68, 0xffff0000, v37
	v_mfma_f32_16x16x4_f32 v[44:47], v53, v63, v[44:47]
	v_lshlrev_b32_e32 v69, 16, v42
	v_mfma_f32_16x16x4_f32 v[44:47], v54, v65, v[44:47]
	v_mfma_f32_16x16x4_f32 v[44:47], v55, v67, v[44:47]
	ds_read_b128 v[52:55], v34 offset:16640
	s_waitcnt lgkmcnt(1)
	v_mfma_f32_16x16x4_f32 v[48:51], v56, v62, v[48:51]
	v_mfma_f32_16x16x4_f32 v[48:51], v57, v64, v[48:51]
	v_mfma_f32_16x16x4_f32 v[48:51], v58, v66, v[48:51]
	v_mfma_f32_16x16x4_f32 v[48:51], v59, v68, v[48:51]
	ds_read_b128 v[56:59], v34 offset:17152
	s_waitcnt lgkmcnt(1)
	v_mfma_f32_16x16x4_f32 v[44:47], v52, v69, v[44:47]
	v_lshlrev_b32_e32 v52, 16, v38
	s_waitcnt lgkmcnt(0)
	s_nop 0
	v_mfma_f32_16x16x4_f32 v[48:51], v56, v52, v[48:51]
	v_and_b32_e32 v56, 0xffff0000, v42
	s_nop 1
	v_mfma_f32_16x16x4_f32 v[44:47], v53, v56, v[44:47]
	v_and_b32_e32 v53, 0xffff0000, v38
	v_mul_f32_e32 v56, v56, v56
	v_fmac_f32_e32 v56, v69, v69
	v_mfma_f32_16x16x4_f32 v[48:51], v57, v53, v[48:51]
	v_mul_f32_e32 v57, v63, v63
	v_fmac_f32_e32 v57, v61, v61
	v_add_f32_e32 v57, v60, v57
	v_mul_f32_e32 v60, v64, v64
	v_fmac_f32_e32 v60, v62, v62
	v_add_f32_e32 v57, v60, v57
	v_lshlrev_b32_e32 v60, 16, v43
	v_mul_f32_e32 v53, v53, v53
	v_fmac_f32_e32 v53, v52, v52
	v_mfma_f32_16x16x4_f32 v[44:47], v54, v60, v[44:47]
	v_mul_f32_e32 v54, v67, v67
	v_fmac_f32_e32 v54, v65, v65
	v_add_f32_e32 v54, v54, v57
	v_mul_f32_e32 v57, v68, v68
	v_fmac_f32_e32 v57, v66, v66
	v_add_f32_e32 v54, v57, v54
	v_lshlrev_b32_e32 v57, 16, v39
	v_add_f32_e32 v54, v56, v54
	v_add_f32_e32 v56, v53, v54
	v_mfma_f32_16x16x4_f32 v[48:51], v58, v57, v[48:51]
	v_and_b32_e32 v58, 0xffff0000, v43
	s_nop 1
	v_mfma_f32_16x16x4_f32 v[52:55], v55, v58, v[44:47]
	v_and_b32_e32 v44, 0xffff0000, v39
	v_mul_f32_e32 v45, v58, v58
	v_fmac_f32_e32 v45, v60, v60
	v_mul_f32_e32 v46, v44, v44
	v_add_f32_e32 v45, v45, v56
	v_fmac_f32_e32 v46, v57, v57
	v_add_f32_e32 v68, v46, v45
	v_mfma_f32_16x16x4_f32 v[56:59], v59, v44, v[48:51]
	s_waitcnt lgkmcnt(0)
	s_mov_b64 s[18:19], 0x380
	v_lshl_add_u64 v[44:45], v[108:109], 0, s[18:19]
	s_mov_b32 s16, m0
	s_mov_b32 m0, s26
	s_nop 0
	global_load_lds_dwordx4 v[44:45], off
	s_mov_b32 m0, s16
	v_lshl_add_u64 v[44:45], v[110:111], 0, s[18:19]
	s_mov_b32 s16, m0
	s_mov_b32 m0, s27
	s_nop 0
	global_load_lds_dwordx4 v[44:45], off
	s_mov_b32 m0, s16
	s_waitcnt vmcnt(4)
	ds_read_b128 v[60:63], v34 offset:20480
	ds_read_b128 v[48:51], v125 offset:4096
	ds_read_b128 v[44:47], v124 offset:4096
	ds_read_b128 v[64:67], v34 offset:20992
	s_waitcnt lgkmcnt(2)
	v_lshlrev_b32_e32 v69, 16, v48
	s_nop 1
	v_mfma_f32_16x16x4_f32 v[52:55], v60, v69, v[52:55]
	v_and_b32_e32 v71, 0xffff0000, v48
	v_lshlrev_b32_e32 v73, 16, v49
	s_waitcnt lgkmcnt(1)
	v_lshlrev_b32_e32 v70, 16, v44
	v_and_b32_e32 v75, 0xffff0000, v49
	v_and_b32_e32 v72, 0xffff0000, v44
	v_lshlrev_b32_e32 v74, 16, v45
	v_and_b32_e32 v76, 0xffff0000, v45
	v_mfma_f32_16x16x4_f32 v[52:55], v61, v71, v[52:55]
	v_lshlrev_b32_e32 v77, 16, v50
	v_mfma_f32_16x16x4_f32 v[52:55], v62, v73, v[52:55]
	v_mfma_f32_16x16x4_f32 v[52:55], v63, v75, v[52:55]
	ds_read_b128 v[60:63], v34 offset:20736
	s_waitcnt lgkmcnt(1)
	v_mfma_f32_16x16x4_f32 v[56:59], v64, v70, v[56:59]
	v_mfma_f32_16x16x4_f32 v[56:59], v65, v72, v[56:59]
	v_mfma_f32_16x16x4_f32 v[56:59], v66, v74, v[56:59]
	v_mfma_f32_16x16x4_f32 v[56:59], v67, v76, v[56:59]
	ds_read_b128 v[64:67], v34 offset:21248
	s_waitcnt lgkmcnt(1)
	v_mfma_f32_16x16x4_f32 v[52:55], v60, v77, v[52:55]
	v_lshlrev_b32_e32 v60, 16, v46
	s_waitcnt lgkmcnt(0)
	s_nop 0
	v_mfma_f32_16x16x4_f32 v[56:59], v64, v60, v[56:59]
	v_and_b32_e32 v64, 0xffff0000, v50
	s_nop 1
	v_mfma_f32_16x16x4_f32 v[52:55], v61, v64, v[52:55]
	v_and_b32_e32 v61, 0xffff0000, v46
	v_mul_f32_e32 v64, v64, v64
	v_fmac_f32_e32 v64, v77, v77
	v_mfma_f32_16x16x4_f32 v[56:59], v65, v61, v[56:59]
	v_mul_f32_e32 v65, v71, v71
	v_fmac_f32_e32 v65, v69, v69
	v_add_f32_e32 v65, v68, v65
	v_mul_f32_e32 v68, v72, v72
	v_fmac_f32_e32 v68, v70, v70
	v_add_f32_e32 v65, v68, v65
	v_lshlrev_b32_e32 v68, 16, v51
	v_mul_f32_e32 v61, v61, v61
	v_fmac_f32_e32 v61, v60, v60
	v_mfma_f32_16x16x4_f32 v[52:55], v62, v68, v[52:55]
	v_mul_f32_e32 v62, v75, v75
	v_fmac_f32_e32 v62, v73, v73
	v_add_f32_e32 v62, v62, v65
	v_mul_f32_e32 v65, v76, v76
	v_fmac_f32_e32 v65, v74, v74
	v_add_f32_e32 v62, v65, v62
	v_lshlrev_b32_e32 v65, 16, v47
	v_add_f32_e32 v62, v64, v62
	v_add_f32_e32 v64, v61, v62
	v_mfma_f32_16x16x4_f32 v[56:59], v66, v65, v[56:59]
	v_and_b32_e32 v66, 0xffff0000, v51
	s_nop 1
	v_mfma_f32_16x16x4_f32 v[60:63], v63, v66, v[52:55]
	v_and_b32_e32 v52, 0xffff0000, v47
	v_mul_f32_e32 v53, v66, v66
	v_fmac_f32_e32 v53, v68, v68
	v_mul_f32_e32 v54, v52, v52
	v_add_f32_e32 v53, v53, v64
	v_fmac_f32_e32 v54, v65, v65
	v_add_f32_e32 v76, v54, v53
	v_mfma_f32_16x16x4_f32 v[64:67], v67, v52, v[56:59]
	s_waitcnt lgkmcnt(0)
; #define LAS __attribute__((address_space(3)))
; #define N2_DMA(c) do { const unsigned d_ = (unsigned)__builtin_amdgcn_readfirstlane(bufw + ((c) % 3) * 2048); n2_glds16(src0 + (c) * 64, d_); n2_glds16(src1 + (c) * 64, d_ + 1024); } while (0)
; __device__ __forceinline__ void n2_mfma(const Args& a, LAS unsigned char* lds, int layer) {
;     ...
;         for (int c = 0; c < 16; ++c) {
;             asm volatile("s_waitcnt lgkmcnt(0)" ::: "memory");
;             if (c + 2 < 16) { N2_DMA(c + 2); asm volatile("s_waitcnt vmcnt(4)" ::: "memory"); }
;             else if (c + 1 < 16) asm volatile("s_waitcnt vmcnt(2)" ::: "memory");
;             else asm volatile("s_waitcnt vmcnt(0)" ::: "memory");
;             const LAS unsigned char* cb = rdb + (c % 3) * 2048;
;             xs[2 * c] = *(const LAS u32x4*)(cb + sl0);
;             xs[2 * c + 1] = *(const LAS u32x4*)(cb + sl1);
;             const LAS f32x4* wq = (const LAS f32x4*)(WgL + ((c * 4) * 4 * 16) * 4) + (g * 4) * 16 + r;
;             f32x4 w0 = wq[0], w1 = wq[16], w2 = wq[32], w3 = wq[48];
; #pragma unroll
;             for (int k = 0; k < 4; ++k) {
;                 const unsigned v0 = xs[2 * c][k], v1 = xs[2 * c + 1][k];
;                 const float x00 = __uint_as_float(v0 << 16), x01 = __uint_as_float(v0 & 0xffff0000u);
;                 const float x10 = __uint_as_float(v1 << 16), x11 = __uint_as_float(v1 & 0xffff0000u);
;                 ss += x00 * x00 + x01 * x01; ss += x10 * x10 + x11 * x11;
;                 const float wa = (k < 2 ? w0 : w1)[2 * (k & 1)], wb = (k < 2 ? w0 : w1)[2 * (k & 1) + 1];
;                 const float wc = (k < 2 ? w2 : w3)[2 * (k & 1)], wd = (k < 2 ? w2 : w3)[2 * (k & 1) + 1];
;                 acc0 = __builtin_amdgcn_mfma_f32_16x16x4f32(wa, x00, acc0, 0, 0, 0);
;                 acc1 = __builtin_amdgcn_mfma_f32_16x16x4f32(wc, x10, acc1, 0, 0, 0);
;                 acc0 = __builtin_amdgcn_mfma_f32_16x16x4f32(wb, x01, acc0, 0, 0, 0);
;                 acc1 = __builtin_amdgcn_mfma_f32_16x16x4f32(wd, x11, acc1, 0, 0, 0);
;             }
;             __builtin_amdgcn_sched_barrier(0);
;         }
	s_mov_b64 s[18:19], 0x400
	v_lshl_add_u64 v[52:53], v[108:109], 0, s[18:19]
	s_mov_b32 s16, m0
	s_mov_b32 m0, s14
	s_nop 0
	global_load_lds_dwordx4 v[52:53], off
	s_mov_b32 m0, s16
	v_lshl_add_u64 v[52:53], v[110:111], 0, s[18:19]
	s_mov_b32 s16, m0
	s_mov_b32 m0, s15
	s_nop 0
	global_load_lds_dwordx4 v[52:53], off
	s_mov_b32 m0, s16
	s_waitcnt vmcnt(4)
	ds_read_b128 v[68:71], v34 offset:24576
	ds_read_b128 v[56:59], v125
	ds_read_b128 v[52:55], v124
	ds_read_b128 v[72:75], v34 offset:25088
	s_waitcnt lgkmcnt(2)
	v_lshlrev_b32_e32 v77, 16, v56
	s_nop 1
	v_mfma_f32_16x16x4_f32 v[60:63], v68, v77, v[60:63]
	v_and_b32_e32 v79, 0xffff0000, v56
	v_lshlrev_b32_e32 v81, 16, v57
	s_waitcnt lgkmcnt(1)
	v_lshlrev_b32_e32 v78, 16, v52
	v_and_b32_e32 v83, 0xffff0000, v57
	v_and_b32_e32 v80, 0xffff0000, v52
	v_lshlrev_b32_e32 v82, 16, v53
	v_and_b32_e32 v84, 0xffff0000, v53
	v_mfma_f32_16x16x4_f32 v[60:63], v69, v79, v[60:63]
	v_lshlrev_b32_e32 v85, 16, v58
	v_mfma_f32_16x16x4_f32 v[60:63], v70, v81, v[60:63]
	v_mfma_f32_16x16x4_f32 v[60:63], v71, v83, v[60:63]
	ds_read_b128 v[68:71], v34 offset:24832
	s_waitcnt lgkmcnt(1)
	v_mfma_f32_16x16x4_f32 v[64:67], v72, v78, v[64:67]
	v_mfma_f32_16x16x4_f32 v[64:67], v73, v80, v[64:67]
	v_mfma_f32_16x16x4_f32 v[64:67], v74, v82, v[64:67]
	v_mfma_f32_16x16x4_f32 v[64:67], v75, v84, v[64:67]
	ds_read_b128 v[72:75], v34 offset:25344
	s_waitcnt lgkmcnt(1)
	v_mfma_f32_16x16x4_f32 v[60:63], v68, v85, v[60:63]
	v_lshlrev_b32_e32 v68, 16, v54
	s_waitcnt lgkmcnt(0)
	s_nop 0
	v_mfma_f32_16x16x4_f32 v[64:67], v72, v68, v[64:67]
	v_and_b32_e32 v72, 0xffff0000, v58
	s_nop 1
	v_mfma_f32_16x16x4_f32 v[60:63], v69, v72, v[60:63]
	v_and_b32_e32 v69, 0xffff0000, v54
	v_mul_f32_e32 v72, v72, v72
	v_fmac_f32_e32 v72, v85, v85
	v_mfma_f32_16x16x4_f32 v[64:67], v73, v69, v[64:67]
	v_mul_f32_e32 v73, v79, v79
	v_fmac_f32_e32 v73, v77, v77
	v_add_f32_e32 v73, v76, v73
	v_mul_f32_e32 v76, v80, v80
	v_fmac_f32_e32 v76, v78, v78
	v_add_f32_e32 v73, v76, v73
	v_lshlrev_b32_e32 v76, 16, v59
	v_mul_f32_e32 v69, v69, v69
	v_fmac_f32_e32 v69, v68, v68
	v_mfma_f32_16x16x4_f32 v[60:63], v70, v76, v[60:63]
	v_mul_f32_e32 v70, v83, v83
	v_fmac_f32_e32 v70, v81, v81
	v_add_f32_e32 v70, v70, v73
	v_mul_f32_e32 v73, v84, v84
	v_fmac_f32_e32 v73, v82, v82
	v_add_f32_e32 v70, v73, v70
	v_lshlrev_b32_e32 v73, 16, v55
	v_add_f32_e32 v70, v72, v70
	v_add_f32_e32 v72, v69, v70
	v_mfma_f32_16x16x4_f32 v[64:67], v74, v73, v[64:67]
	v_and_b32_e32 v74, 0xffff0000, v59
	s_nop 1
	v_mfma_f32_16x16x4_f32 v[68:71], v71, v74, v[60:63]
	v_and_b32_e32 v60, 0xffff0000, v55
	v_mul_f32_e32 v61, v74, v74
	v_fmac_f32_e32 v61, v76, v76
	v_mul_f32_e32 v62, v60, v60
	v_add_f32_e32 v61, v61, v72
	v_fmac_f32_e32 v62, v73, v73
	v_add_f32_e32 v84, v62, v61
	v_mfma_f32_16x16x4_f32 v[72:75], v75, v60, v[64:67]
	s_waitcnt lgkmcnt(0)
	s_mov_b64 s[18:19], 0x480
	v_lshl_add_u64 v[60:61], v[108:109], 0, s[18:19]
	s_mov_b32 s16, m0
	s_mov_b32 m0, s75
	s_nop 0
	global_load_lds_dwordx4 v[60:61], off
	s_mov_b32 m0, s16
	v_lshl_add_u64 v[60:61], v[110:111], 0, s[18:19]
	s_mov_b32 s16, m0
	s_mov_b32 m0, s13
	s_nop 0
	global_load_lds_dwordx4 v[60:61], off
	s_mov_b32 m0, s16
	s_waitcnt vmcnt(4)
	ds_read_b128 v[76:79], v34 offset:28672
	ds_read_b128 v[64:67], v125 offset:2048
	ds_read_b128 v[60:63], v124 offset:2048
	ds_read_b128 v[80:83], v34 offset:29184
	s_waitcnt lgkmcnt(2)
	v_lshlrev_b32_e32 v85, 16, v64
	s_nop 1
	v_mfma_f32_16x16x4_f32 v[68:71], v76, v85, v[68:71]
	v_and_b32_e32 v87, 0xffff0000, v64
	v_lshlrev_b32_e32 v89, 16, v65
	s_waitcnt lgkmcnt(1)
	v_lshlrev_b32_e32 v86, 16, v60
	v_and_b32_e32 v91, 0xffff0000, v65
	v_and_b32_e32 v88, 0xffff0000, v60
	v_lshlrev_b32_e32 v90, 16, v61
	v_and_b32_e32 v92, 0xffff0000, v61
	v_mfma_f32_16x16x4_f32 v[68:71], v77, v87, v[68:71]
	v_lshlrev_b32_e32 v93, 16, v66
	v_mfma_f32_16x16x4_f32 v[68:71], v78, v89, v[68:71]
	v_mfma_f32_16x16x4_f32 v[68:71], v79, v91, v[68:71]
	ds_read_b128 v[76:79], v34 offset:28928
	s_waitcnt lgkmcnt(1)
	v_mfma_f32_16x16x4_f32 v[72:75], v80, v86, v[72:75]
	v_mfma_f32_16x16x4_f32 v[72:75], v81, v88, v[72:75]
	v_mfma_f32_16x16x4_f32 v[72:75], v82, v90, v[72:75]
	v_mfma_f32_16x16x4_f32 v[72:75], v83, v92, v[72:75]
	ds_read_b128 v[80:83], v34 offset:29440
	s_waitcnt lgkmcnt(1)
	v_mfma_f32_16x16x4_f32 v[68:71], v76, v93, v[68:71]
	v_lshlrev_b32_e32 v76, 16, v62
	s_waitcnt lgkmcnt(0)
	s_nop 0
	v_mfma_f32_16x16x4_f32 v[72:75], v80, v76, v[72:75]
	v_and_b32_e32 v80, 0xffff0000, v66
	s_nop 1
	v_mfma_f32_16x16x4_f32 v[68:71], v77, v80, v[68:71]
	v_and_b32_e32 v77, 0xffff0000, v62
	v_mul_f32_e32 v80, v80, v80
	v_fmac_f32_e32 v80, v93, v93
	v_mfma_f32_16x16x4_f32 v[72:75], v81, v77, v[72:75]
	v_mul_f32_e32 v81, v87, v87
	v_fmac_f32_e32 v81, v85, v85
	v_add_f32_e32 v81, v84, v81
	v_mul_f32_e32 v84, v88, v88
	v_fmac_f32_e32 v84, v86, v86
	v_add_f32_e32 v81, v84, v81
	v_lshlrev_b32_e32 v84, 16, v67
	v_mul_f32_e32 v77, v77, v77
	v_fmac_f32_e32 v77, v76, v76
	v_mfma_f32_16x16x4_f32 v[68:71], v78, v84, v[68:71]
	v_mul_f32_e32 v78, v91, v91
	v_fmac_f32_e32 v78, v89, v89
	v_add_f32_e32 v78, v78, v81
	v_mul_f32_e32 v81, v92, v92
	v_fmac_f32_e32 v81, v90, v90
	v_add_f32_e32 v78, v81, v78
	v_lshlrev_b32_e32 v81, 16, v63
	v_add_f32_e32 v78, v80, v78
	v_add_f32_e32 v80, v77, v78
	v_mfma_f32_16x16x4_f32 v[72:75], v82, v81, v[72:75]
	v_and_b32_e32 v82, 0xffff0000, v67
	s_nop 1
	v_mfma_f32_16x16x4_f32 v[76:79], v79, v82, v[68:71]
	v_and_b32_e32 v68, 0xffff0000, v63
	v_mul_f32_e32 v69, v82, v82
	v_fmac_f32_e32 v69, v84, v84
	v_mul_f32_e32 v70, v68, v68
	v_add_f32_e32 v69, v69, v80
	v_fmac_f32_e32 v70, v81, v81
	v_add_f32_e32 v92, v70, v69
	v_mfma_f32_16x16x4_f32 v[80:83], v83, v68, v[72:75]
	s_waitcnt lgkmcnt(0)
; #define LAS __attribute__((address_space(3)))
; #define N2_DMA(c) do { const unsigned d_ = (unsigned)__builtin_amdgcn_readfirstlane(bufw + ((c) % 3) * 2048); n2_glds16(src0 + (c) * 64, d_); n2_glds16(src1 + (c) * 64, d_ + 1024); } while (0)
; __device__ __forceinline__ void n2_mfma(const Args& a, LAS unsigned char* lds, int layer) {
;     ...
;         for (int c = 0; c < 16; ++c) {
;             asm volatile("s_waitcnt lgkmcnt(0)" ::: "memory");
;             if (c + 2 < 16) { N2_DMA(c + 2); asm volatile("s_waitcnt vmcnt(4)" ::: "memory"); }
;             else if (c + 1 < 16) asm volatile("s_waitcnt vmcnt(2)" ::: "memory");
;             else asm volatile("s_waitcnt vmcnt(0)" ::: "memory");
;             const LAS unsigned char* cb = rdb + (c % 3) * 2048;
;             xs[2 * c] = *(const LAS u32x4*)(cb + sl0);
;             xs[2 * c + 1] = *(const LAS u32x4*)(cb + sl1);
;             const LAS f32x4* wq = (const LAS f32x4*)(WgL + ((c * 4) * 4 * 16) * 4) + (g * 4) * 16 + r;
;             f32x4 w0 = wq[0], w1 = wq[16], w2 = wq[32], w3 = wq[48];
; #pragma unroll
;             for (int k = 0; k < 4; ++k) {
;                 const unsigned v0 = xs[2 * c][k], v1 = xs[2 * c + 1][k];
;                 const float x00 = __uint_as_float(v0 << 16), x01 = __uint_as_float(v0 & 0xffff0000u);
;                 const float x10 = __uint_as_float(v1 << 16), x11 = __uint_as_float(v1 & 0xffff0000u);
;                 ss += x00 * x00 + x01 * x01; ss += x10 * x10 + x11 * x11;
;                 const float wa = (k < 2 ? w0 : w1)[2 * (k & 1)], wb = (k < 2 ? w0 : w1)[2 * (k & 1) + 1];
;                 const float wc = (k < 2 ? w2 : w3)[2 * (k & 1)], wd = (k < 2 ? w2 : w3)[2 * (k & 1) + 1];
;                 acc0 = __builtin_amdgcn_mfma_f32_16x16x4f32(wa, x00, acc0, 0, 0, 0);
;                 acc1 = __builtin_amdgcn_mfma_f32_16x16x4f32(wc, x10, acc1, 0, 0, 0);
;                 acc0 = __builtin_amdgcn_mfma_f32_16x16x4f32(wb, x01, acc0, 0, 0, 0);
;                 acc1 = __builtin_amdgcn_mfma_f32_16x16x4f32(wd, x11, acc1, 0, 0, 0);
;             }
;             __builtin_amdgcn_sched_barrier(0);
;         }
	s_mov_b64 s[18:19], 0x500
	v_lshl_add_u64 v[68:69], v[108:109], 0, s[18:19]
	s_mov_b32 s16, m0
	s_mov_b32 m0, s26
	s_nop 0
	global_load_lds_dwordx4 v[68:69], off
	s_mov_b32 m0, s16
	v_lshl_add_u64 v[68:69], v[110:111], 0, s[18:19]
	s_mov_b32 s16, m0
	s_mov_b32 m0, s27
	s_nop 0
	global_load_lds_dwordx4 v[68:69], off
	s_mov_b32 m0, s16
	s_waitcnt vmcnt(4)
	ds_read_b128 v[84:87], v34 offset:32768
	ds_read_b128 v[72:75], v125 offset:4096
	ds_read_b128 v[68:71], v124 offset:4096
	ds_read_b128 v[88:91], v34 offset:33280
	s_waitcnt lgkmcnt(2)
	v_lshlrev_b32_e32 v93, 16, v72
	s_nop 1
	v_mfma_f32_16x16x4_f32 v[76:79], v84, v93, v[76:79]
	v_and_b32_e32 v95, 0xffff0000, v72
	v_lshlrev_b32_e32 v97, 16, v73
	s_waitcnt lgkmcnt(1)
	v_lshlrev_b32_e32 v94, 16, v68
	v_and_b32_e32 v99, 0xffff0000, v73
	v_and_b32_e32 v96, 0xffff0000, v68
	v_lshlrev_b32_e32 v98, 16, v69
	v_and_b32_e32 v100, 0xffff0000, v69
	v_mfma_f32_16x16x4_f32 v[76:79], v85, v95, v[76:79]
	v_lshlrev_b32_e32 v101, 16, v74
	v_mfma_f32_16x16x4_f32 v[76:79], v86, v97, v[76:79]
	v_mfma_f32_16x16x4_f32 v[76:79], v87, v99, v[76:79]
	ds_read_b128 v[84:87], v34 offset:33024
	s_waitcnt lgkmcnt(1)
	v_mfma_f32_16x16x4_f32 v[80:83], v88, v94, v[80:83]
	v_mfma_f32_16x16x4_f32 v[80:83], v89, v96, v[80:83]
	v_mfma_f32_16x16x4_f32 v[80:83], v90, v98, v[80:83]
	v_mfma_f32_16x16x4_f32 v[80:83], v91, v100, v[80:83]
	ds_read_b128 v[88:91], v34 offset:33536
	s_waitcnt lgkmcnt(1)
	v_mfma_f32_16x16x4_f32 v[76:79], v84, v101, v[76:79]
	v_lshlrev_b32_e32 v84, 16, v70
	s_waitcnt lgkmcnt(0)
	s_nop 0
	v_mfma_f32_16x16x4_f32 v[80:83], v88, v84, v[80:83]
	v_and_b32_e32 v88, 0xffff0000, v74
	s_nop 1
	v_mfma_f32_16x16x4_f32 v[76:79], v85, v88, v[76:79]
	v_and_b32_e32 v85, 0xffff0000, v70
	v_mul_f32_e32 v88, v88, v88
	v_fmac_f32_e32 v88, v101, v101
	v_mfma_f32_16x16x4_f32 v[80:83], v89, v85, v[80:83]
	v_mul_f32_e32 v89, v95, v95
	v_fmac_f32_e32 v89, v93, v93
	v_add_f32_e32 v89, v92, v89
	v_mul_f32_e32 v92, v96, v96
	v_fmac_f32_e32 v92, v94, v94
	v_add_f32_e32 v89, v92, v89
	v_lshlrev_b32_e32 v92, 16, v75
	v_mul_f32_e32 v85, v85, v85
	v_fmac_f32_e32 v85, v84, v84
	v_mfma_f32_16x16x4_f32 v[76:79], v86, v92, v[76:79]
	v_mul_f32_e32 v86, v99, v99
	v_fmac_f32_e32 v86, v97, v97
	v_add_f32_e32 v86, v86, v89
	v_mul_f32_e32 v89, v100, v100
	v_fmac_f32_e32 v89, v98, v98
	v_add_f32_e32 v86, v89, v86
	v_lshlrev_b32_e32 v89, 16, v71
	v_add_f32_e32 v86, v88, v86
	v_add_f32_e32 v88, v85, v86
	v_mfma_f32_16x16x4_f32 v[80:83], v90, v89, v[80:83]
	v_and_b32_e32 v90, 0xffff0000, v75
	s_nop 1
	v_mfma_f32_16x16x4_f32 v[84:87], v87, v90, v[76:79]
	v_and_b32_e32 v76, 0xffff0000, v71
	v_mul_f32_e32 v77, v90, v90
	v_fmac_f32_e32 v77, v92, v92
	v_mul_f32_e32 v78, v76, v76
	v_add_f32_e32 v77, v77, v88
	v_fmac_f32_e32 v78, v89, v89
	v_add_f32_e32 v100, v78, v77
	v_mfma_f32_16x16x4_f32 v[88:91], v91, v76, v[80:83]
	s_waitcnt lgkmcnt(0)
	s_mov_b64 s[18:19], 0x580
	v_lshl_add_u64 v[76:77], v[108:109], 0, s[18:19]
	s_mov_b32 s16, m0
	s_mov_b32 m0, s14
	s_nop 0
	global_load_lds_dwordx4 v[76:77], off
	s_mov_b32 m0, s16
	v_lshl_add_u64 v[76:77], v[110:111], 0, s[18:19]
	s_mov_b32 s16, m0
	s_mov_b32 m0, s15
	s_nop 0
	global_load_lds_dwordx4 v[76:77], off
	s_mov_b32 m0, s16
	s_waitcnt vmcnt(4)
	ds_read_b128 v[92:95], v34 offset:36864
	ds_read_b128 v[80:83], v125
	ds_read_b128 v[76:79], v124
	ds_read_b128 v[96:99], v34 offset:37376
	s_waitcnt lgkmcnt(2)
	v_lshlrev_b32_e32 v101, 16, v80
	s_nop 1
	v_mfma_f32_16x16x4_f32 v[84:87], v92, v101, v[84:87]
	v_and_b32_e32 v103, 0xffff0000, v80
	v_lshlrev_b32_e32 v105, 16, v81
	s_waitcnt lgkmcnt(1)
	v_lshlrev_b32_e32 v102, 16, v76
	v_and_b32_e32 v107, 0xffff0000, v81
	v_and_b32_e32 v104, 0xffff0000, v76
	v_lshlrev_b32_e32 v106, 16, v77
	v_and_b32_e32 v112, 0xffff0000, v77
	v_mfma_f32_16x16x4_f32 v[84:87], v93, v103, v[84:87]
	v_lshlrev_b32_e32 v113, 16, v82
	v_mfma_f32_16x16x4_f32 v[84:87], v94, v105, v[84:87]
	v_mfma_f32_16x16x4_f32 v[84:87], v95, v107, v[84:87]
	ds_read_b128 v[92:95], v34 offset:37120
	s_waitcnt lgkmcnt(1)
	v_mfma_f32_16x16x4_f32 v[88:91], v96, v102, v[88:91]
	v_mfma_f32_16x16x4_f32 v[88:91], v97, v104, v[88:91]
	v_mfma_f32_16x16x4_f32 v[88:91], v98, v106, v[88:91]
	v_mfma_f32_16x16x4_f32 v[88:91], v99, v112, v[88:91]
	ds_read_b128 v[96:99], v34 offset:37632
	s_waitcnt lgkmcnt(1)
	v_mfma_f32_16x16x4_f32 v[84:87], v92, v113, v[84:87]
	v_lshlrev_b32_e32 v92, 16, v78
	s_waitcnt lgkmcnt(0)
	s_nop 0
	v_mfma_f32_16x16x4_f32 v[88:91], v96, v92, v[88:91]
	v_and_b32_e32 v96, 0xffff0000, v82
	s_nop 1
	v_mfma_f32_16x16x4_f32 v[84:87], v93, v96, v[84:87]
	v_and_b32_e32 v93, 0xffff0000, v78
	v_mul_f32_e32 v96, v96, v96
	v_fmac_f32_e32 v96, v113, v113
	v_mfma_f32_16x16x4_f32 v[88:91], v97, v93, v[88:91]
	v_mul_f32_e32 v97, v103, v103
	v_fmac_f32_e32 v97, v101, v101
	v_add_f32_e32 v97, v100, v97
	v_mul_f32_e32 v100, v104, v104
	v_fmac_f32_e32 v100, v102, v102
	v_add_f32_e32 v97, v100, v97
	v_lshlrev_b32_e32 v100, 16, v83
	v_mul_f32_e32 v93, v93, v93
	v_fmac_f32_e32 v93, v92, v92
	v_mfma_f32_16x16x4_f32 v[84:87], v94, v100, v[84:87]
	v_mul_f32_e32 v94, v107, v107
	v_fmac_f32_e32 v94, v105, v105
	v_add_f32_e32 v94, v94, v97
	v_mul_f32_e32 v97, v112, v112
	v_fmac_f32_e32 v97, v106, v106
	v_add_f32_e32 v94, v97, v94
	v_lshlrev_b32_e32 v97, 16, v79
	v_add_f32_e32 v94, v96, v94
	v_add_f32_e32 v96, v93, v94
	v_mfma_f32_16x16x4_f32 v[88:91], v98, v97, v[88:91]
	v_and_b32_e32 v98, 0xffff0000, v83
	s_nop 1
	v_mfma_f32_16x16x4_f32 v[92:95], v95, v98, v[84:87]
	v_and_b32_e32 v84, 0xffff0000, v79
	v_mul_f32_e32 v85, v98, v98
	v_fmac_f32_e32 v85, v100, v100
	v_mul_f32_e32 v86, v84, v84
	v_add_f32_e32 v85, v85, v96
	v_fmac_f32_e32 v86, v97, v97
	v_add_f32_e32 v112, v86, v85
	v_mfma_f32_16x16x4_f32 v[96:99], v99, v84, v[88:91]
	s_waitcnt lgkmcnt(0)
; #define LAS __attribute__((address_space(3)))
; #define N2_DMA(c) do { const unsigned d_ = (unsigned)__builtin_amdgcn_readfirstlane(bufw + ((c) % 3) * 2048); n2_glds16(src0 + (c) * 64, d_); n2_glds16(src1 + (c) * 64, d_ + 1024); } while (0)
; __device__ __forceinline__ void n2_mfma(const Args& a, LAS unsigned char* lds, int layer) {
;     ...
;         for (int c = 0; c < 16; ++c) {
;             asm volatile("s_waitcnt lgkmcnt(0)" ::: "memory");
;             if (c + 2 < 16) { N2_DMA(c + 2); asm volatile("s_waitcnt vmcnt(4)" ::: "memory"); }
;             else if (c + 1 < 16) asm volatile("s_waitcnt vmcnt(2)" ::: "memory");
;             else asm volatile("s_waitcnt vmcnt(0)" ::: "memory");
;             const LAS unsigned char* cb = rdb + (c % 3) * 2048;
;             xs[2 * c] = *(const LAS u32x4*)(cb + sl0);
;             xs[2 * c + 1] = *(const LAS u32x4*)(cb + sl1);
;             const LAS f32x4* wq = (const LAS f32x4*)(WgL + ((c * 4) * 4 * 16) * 4) + (g * 4) * 16 + r;
;             f32x4 w0 = wq[0], w1 = wq[16], w2 = wq[32], w3 = wq[48];
; #pragma unroll
;             for (int k = 0; k < 4; ++k) {
;                 const unsigned v0 = xs[2 * c][k], v1 = xs[2 * c + 1][k];
;                 const float x00 = __uint_as_float(v0 << 16), x01 = __uint_as_float(v0 & 0xffff0000u);
;                 const float x10 = __uint_as_float(v1 << 16), x11 = __uint_as_float(v1 & 0xffff0000u);
;                 ss += x00 * x00 + x01 * x01; ss += x10 * x10 + x11 * x11;
;                 const float wa = (k < 2 ? w0 : w1)[2 * (k & 1)], wb = (k < 2 ? w0 : w1)[2 * (k & 1) + 1];
;                 const float wc = (k < 2 ? w2 : w3)[2 * (k & 1)], wd = (k < 2 ? w2 : w3)[2 * (k & 1) + 1];
;                 acc0 = __builtin_amdgcn_mfma_f32_16x16x4f32(wa, x00, acc0, 0, 0, 0);
;                 acc1 = __builtin_amdgcn_mfma_f32_16x16x4f32(wc, x10, acc1, 0, 0, 0);
;                 acc0 = __builtin_amdgcn_mfma_f32_16x16x4f32(wb, x01, acc0, 0, 0, 0);
;                 acc1 = __builtin_amdgcn_mfma_f32_16x16x4f32(wd, x11, acc1, 0, 0, 0);
;             }
;             __builtin_amdgcn_sched_barrier(0);
;         }
	s_mov_b64 s[18:19], 0x600
	v_lshl_add_u64 v[84:85], v[108:109], 0, s[18:19]
	s_mov_b32 s16, m0
	s_mov_b32 m0, s75
	s_nop 0
	global_load_lds_dwordx4 v[84:85], off
	s_mov_b32 m0, s16
	v_lshl_add_u64 v[84:85], v[110:111], 0, s[18:19]
	s_mov_b32 s16, m0
	s_mov_b32 m0, s13
	s_nop 0
	global_load_lds_dwordx4 v[84:85], off
	s_mov_b32 m0, s16
	s_waitcnt vmcnt(4)
	ds_read_b128 v[100:103], v34 offset:40960
	ds_read_b128 v[88:91], v125 offset:2048
	ds_read_b128 v[84:87], v124 offset:2048
	ds_read_b128 v[104:107], v34 offset:41472
	s_waitcnt lgkmcnt(2)
	v_lshlrev_b32_e32 v113, 16, v88
	s_nop 1
	v_mfma_f32_16x16x4_f32 v[92:95], v100, v113, v[92:95]
	v_and_b32_e32 v115, 0xffff0000, v88
	v_lshlrev_b32_e32 v117, 16, v89
	s_waitcnt lgkmcnt(1)
	v_lshlrev_b32_e32 v114, 16, v84
	v_and_b32_e32 v119, 0xffff0000, v89
	v_and_b32_e32 v116, 0xffff0000, v84
	v_lshlrev_b32_e32 v118, 16, v85
	v_and_b32_e32 v120, 0xffff0000, v85
	v_mfma_f32_16x16x4_f32 v[92:95], v101, v115, v[92:95]
	v_lshlrev_b32_e32 v121, 16, v90
	v_mfma_f32_16x16x4_f32 v[92:95], v102, v117, v[92:95]
	v_mfma_f32_16x16x4_f32 v[92:95], v103, v119, v[92:95]
	ds_read_b128 v[100:103], v34 offset:41216
	s_waitcnt lgkmcnt(1)
	v_mfma_f32_16x16x4_f32 v[96:99], v104, v114, v[96:99]
	v_mfma_f32_16x16x4_f32 v[96:99], v105, v116, v[96:99]
	v_mfma_f32_16x16x4_f32 v[96:99], v106, v118, v[96:99]
	v_mfma_f32_16x16x4_f32 v[96:99], v107, v120, v[96:99]
	ds_read_b128 v[104:107], v34 offset:41728
	s_waitcnt lgkmcnt(1)
	v_mfma_f32_16x16x4_f32 v[92:95], v100, v121, v[92:95]
	v_lshlrev_b32_e32 v100, 16, v86
	s_waitcnt lgkmcnt(0)
	s_nop 0
	v_mfma_f32_16x16x4_f32 v[96:99], v104, v100, v[96:99]
	v_and_b32_e32 v104, 0xffff0000, v90
	s_nop 1
	v_mfma_f32_16x16x4_f32 v[92:95], v101, v104, v[92:95]
	v_and_b32_e32 v101, 0xffff0000, v86
	v_mul_f32_e32 v104, v104, v104
	v_fmac_f32_e32 v104, v121, v121
	v_mfma_f32_16x16x4_f32 v[96:99], v105, v101, v[96:99]
	v_mul_f32_e32 v105, v115, v115
	v_fmac_f32_e32 v105, v113, v113
	v_add_f32_e32 v105, v112, v105
	v_mul_f32_e32 v112, v116, v116
	v_fmac_f32_e32 v112, v114, v114
	v_add_f32_e32 v105, v112, v105
	v_lshlrev_b32_e32 v112, 16, v91
	v_mul_f32_e32 v101, v101, v101
	v_fmac_f32_e32 v101, v100, v100
	v_mfma_f32_16x16x4_f32 v[92:95], v102, v112, v[92:95]
	v_mul_f32_e32 v102, v119, v119
	v_fmac_f32_e32 v102, v117, v117
	v_add_f32_e32 v102, v102, v105
	v_mul_f32_e32 v105, v120, v120
	v_fmac_f32_e32 v105, v118, v118
	v_add_f32_e32 v102, v105, v102
	v_lshlrev_b32_e32 v105, 16, v87
	v_add_f32_e32 v102, v104, v102
	v_add_f32_e32 v104, v101, v102
	v_mfma_f32_16x16x4_f32 v[96:99], v106, v105, v[96:99]
	v_and_b32_e32 v106, 0xffff0000, v91
	s_nop 1
	v_mfma_f32_16x16x4_f32 v[100:103], v103, v106, v[92:95]
	v_and_b32_e32 v92, 0xffff0000, v87
	v_mul_f32_e32 v93, v106, v106
	v_fmac_f32_e32 v93, v112, v112
	v_mul_f32_e32 v94, v92, v92
	v_add_f32_e32 v93, v93, v104
	v_fmac_f32_e32 v94, v105, v105
	v_add_f32_e32 v120, v94, v93
	v_mfma_f32_16x16x4_f32 v[104:107], v107, v92, v[96:99]
	s_waitcnt lgkmcnt(0)
	s_mov_b64 s[18:19], 0x680
	v_lshl_add_u64 v[92:93], v[108:109], 0, s[18:19]
	s_mov_b32 s16, m0
	s_mov_b32 m0, s26
	s_nop 0
	global_load_lds_dwordx4 v[92:93], off
	s_mov_b32 m0, s16
	v_lshl_add_u64 v[92:93], v[110:111], 0, s[18:19]
	s_mov_b32 s16, m0
	s_mov_b32 m0, s27
	s_nop 0
	global_load_lds_dwordx4 v[92:93], off
	s_mov_b32 m0, s16
	s_waitcnt vmcnt(4)
	ds_read_b128 v[112:115], v34 offset:45056
	ds_read_b128 v[96:99], v125 offset:4096
	ds_read_b128 v[92:95], v124 offset:4096
	ds_read_b128 v[116:119], v34 offset:45568
	s_waitcnt lgkmcnt(2)
	v_lshlrev_b32_e32 v121, 16, v96
	s_nop 1
	v_mfma_f32_16x16x4_f32 v[100:103], v112, v121, v[100:103]
	v_and_b32_e32 v123, 0xffff0000, v96
	v_lshlrev_b32_e32 v127, 16, v97
	s_waitcnt lgkmcnt(1)
	v_lshlrev_b32_e32 v122, 16, v92
	v_and_b32_e32 v129, 0xffff0000, v97
	v_and_b32_e32 v126, 0xffff0000, v92
	v_lshlrev_b32_e32 v128, 16, v93
	v_and_b32_e32 v130, 0xffff0000, v93
	v_mfma_f32_16x16x4_f32 v[100:103], v113, v123, v[100:103]
	v_lshlrev_b32_e32 v131, 16, v98
	v_mfma_f32_16x16x4_f32 v[100:103], v114, v127, v[100:103]
	v_mfma_f32_16x16x4_f32 v[100:103], v115, v129, v[100:103]
	ds_read_b128 v[112:115], v34 offset:45312
	s_waitcnt lgkmcnt(1)
	v_mfma_f32_16x16x4_f32 v[104:107], v116, v122, v[104:107]
	v_mfma_f32_16x16x4_f32 v[104:107], v117, v126, v[104:107]
	v_mfma_f32_16x16x4_f32 v[104:107], v118, v128, v[104:107]
	v_mfma_f32_16x16x4_f32 v[104:107], v119, v130, v[104:107]
	ds_read_b128 v[116:119], v34 offset:45824
	s_waitcnt lgkmcnt(1)
	v_mfma_f32_16x16x4_f32 v[100:103], v112, v131, v[100:103]
	v_lshlrev_b32_e32 v112, 16, v94
	s_waitcnt lgkmcnt(0)
	s_nop 0
	v_mfma_f32_16x16x4_f32 v[104:107], v116, v112, v[104:107]
	v_and_b32_e32 v116, 0xffff0000, v98
	s_nop 1
	v_mfma_f32_16x16x4_f32 v[100:103], v113, v116, v[100:103]
	v_and_b32_e32 v113, 0xffff0000, v94
	v_mul_f32_e32 v116, v116, v116
	v_fmac_f32_e32 v116, v131, v131
	v_mfma_f32_16x16x4_f32 v[104:107], v117, v113, v[104:107]
	v_mul_f32_e32 v117, v123, v123
	v_fmac_f32_e32 v117, v121, v121
	v_add_f32_e32 v117, v120, v117
	v_mul_f32_e32 v120, v126, v126
	v_fmac_f32_e32 v120, v122, v122
	v_add_f32_e32 v117, v120, v117
	v_lshlrev_b32_e32 v120, 16, v99
	v_mul_f32_e32 v113, v113, v113
	v_fmac_f32_e32 v113, v112, v112
	v_mfma_f32_16x16x4_f32 v[100:103], v114, v120, v[100:103]
	v_mul_f32_e32 v114, v129, v129
	v_fmac_f32_e32 v114, v127, v127
	v_add_f32_e32 v114, v114, v117
	v_mul_f32_e32 v117, v130, v130
	v_fmac_f32_e32 v117, v128, v128
	v_add_f32_e32 v114, v117, v114
	v_lshlrev_b32_e32 v117, 16, v95
	v_add_f32_e32 v114, v116, v114
	v_add_f32_e32 v116, v113, v114
	v_mfma_f32_16x16x4_f32 v[104:107], v118, v117, v[104:107]
	v_and_b32_e32 v118, 0xffff0000, v99
	s_nop 1
	v_mfma_f32_16x16x4_f32 v[112:115], v115, v118, v[100:103]
	v_and_b32_e32 v100, 0xffff0000, v95
	v_mul_f32_e32 v101, v118, v118
	v_fmac_f32_e32 v101, v120, v120
	v_mul_f32_e32 v102, v100, v100
	v_add_f32_e32 v101, v101, v116
	v_fmac_f32_e32 v102, v117, v117
	v_add_f32_e32 v130, v102, v101
	v_mfma_f32_16x16x4_f32 v[116:119], v119, v100, v[104:107]
	s_waitcnt lgkmcnt(0)
; #define LAS __attribute__((address_space(3)))
; #define N2_DMA(c) do { const unsigned d_ = (unsigned)__builtin_amdgcn_readfirstlane(bufw + ((c) % 3) * 2048); n2_glds16(src0 + (c) * 64, d_); n2_glds16(src1 + (c) * 64, d_ + 1024); } while (0)
; __device__ __forceinline__ void n2_mfma(const Args& a, LAS unsigned char* lds, int layer) {
;     ...
;         for (int c = 0; c < 16; ++c) {
;             asm volatile("s_waitcnt lgkmcnt(0)" ::: "memory");
;             if (c + 2 < 16) { N2_DMA(c + 2); asm volatile("s_waitcnt vmcnt(4)" ::: "memory"); }
;             else if (c + 1 < 16) asm volatile("s_waitcnt vmcnt(2)" ::: "memory");
;             else asm volatile("s_waitcnt vmcnt(0)" ::: "memory");
;             const LAS unsigned char* cb = rdb + (c % 3) * 2048;
;             xs[2 * c] = *(const LAS u32x4*)(cb + sl0);
;             xs[2 * c + 1] = *(const LAS u32x4*)(cb + sl1);
;             const LAS f32x4* wq = (const LAS f32x4*)(WgL + ((c * 4) * 4 * 16) * 4) + (g * 4) * 16 + r;
;             f32x4 w0 = wq[0], w1 = wq[16], w2 = wq[32], w3 = wq[48];
; #pragma unroll
;             for (int k = 0; k < 4; ++k) {
;                 const unsigned v0 = xs[2 * c][k], v1 = xs[2 * c + 1][k];
;                 const float x00 = __uint_as_float(v0 << 16), x01 = __uint_as_float(v0 & 0xffff0000u);
;                 const float x10 = __uint_as_float(v1 << 16), x11 = __uint_as_float(v1 & 0xffff0000u);
;                 ss += x00 * x00 + x01 * x01; ss += x10 * x10 + x11 * x11;
;                 const float wa = (k < 2 ? w0 : w1)[2 * (k & 1)], wb = (k < 2 ? w0 : w1)[2 * (k & 1) + 1];
;                 const float wc = (k < 2 ? w2 : w3)[2 * (k & 1)], wd = (k < 2 ? w2 : w3)[2 * (k & 1) + 1];
;                 acc0 = __builtin_amdgcn_mfma_f32_16x16x4f32(wa, x00, acc0, 0, 0, 0);
;                 acc1 = __builtin_amdgcn_mfma_f32_16x16x4f32(wc, x10, acc1, 0, 0, 0);
;                 acc0 = __builtin_amdgcn_mfma_f32_16x16x4f32(wb, x01, acc0, 0, 0, 0);
;                 acc1 = __builtin_amdgcn_mfma_f32_16x16x4f32(wd, x11, acc1, 0, 0, 0);
;             }
;             __builtin_amdgcn_sched_barrier(0);
;         }
	s_mov_b64 s[18:19], 0x700
	v_lshl_add_u64 v[100:101], v[108:109], 0, s[18:19]
	s_mov_b32 s16, m0
	s_mov_b32 m0, s14
	s_nop 0
	global_load_lds_dwordx4 v[100:101], off
	s_mov_b32 m0, s16
	v_lshl_add_u64 v[100:101], v[110:111], 0, s[18:19]
	s_mov_b32 s14, m0
	s_mov_b32 m0, s15
	s_nop 0
	global_load_lds_dwordx4 v[100:101], off
	s_mov_b32 m0, s14
	s_waitcnt vmcnt(4)
	ds_read_b128 v[120:123], v34 offset:49152
	ds_read_b128 v[104:107], v125
	ds_read_b128 v[100:103], v124
	ds_read_b128 v[126:129], v34 offset:49664
	s_waitcnt lgkmcnt(2)
	v_lshlrev_b32_e32 v131, 16, v104
	s_nop 1
	v_mfma_f32_16x16x4_f32 v[112:115], v120, v131, v[112:115]
	v_and_b32_e32 v135, 0xffff0000, v104
	v_lshlrev_b32_e32 v143, 16, v105
	s_waitcnt lgkmcnt(1)
	v_lshlrev_b32_e32 v134, 16, v100
	v_and_b32_e32 v145, 0xffff0000, v105
	v_and_b32_e32 v142, 0xffff0000, v100
	v_lshlrev_b32_e32 v144, 16, v101
	v_and_b32_e32 v146, 0xffff0000, v101
	v_mfma_f32_16x16x4_f32 v[112:115], v121, v135, v[112:115]
	v_lshlrev_b32_e32 v147, 16, v106
	v_mfma_f32_16x16x4_f32 v[112:115], v122, v143, v[112:115]
	v_mfma_f32_16x16x4_f32 v[112:115], v123, v145, v[112:115]
	ds_read_b128 v[120:123], v34 offset:49408
	s_waitcnt lgkmcnt(1)
	v_mfma_f32_16x16x4_f32 v[116:119], v126, v134, v[116:119]
	v_mfma_f32_16x16x4_f32 v[116:119], v127, v142, v[116:119]
	v_mfma_f32_16x16x4_f32 v[116:119], v128, v144, v[116:119]
	v_mfma_f32_16x16x4_f32 v[116:119], v129, v146, v[116:119]
	ds_read_b128 v[126:129], v34 offset:49920
	s_waitcnt lgkmcnt(1)
	v_mfma_f32_16x16x4_f32 v[112:115], v120, v147, v[112:115]
	v_lshlrev_b32_e32 v120, 16, v102
	s_waitcnt lgkmcnt(0)
	s_nop 0
	v_mfma_f32_16x16x4_f32 v[116:119], v126, v120, v[116:119]
	v_and_b32_e32 v126, 0xffff0000, v106
	s_nop 1
	v_mfma_f32_16x16x4_f32 v[112:115], v121, v126, v[112:115]
	v_and_b32_e32 v121, 0xffff0000, v102
	v_mul_f32_e32 v126, v126, v126
	v_fmac_f32_e32 v126, v147, v147
	v_mfma_f32_16x16x4_f32 v[116:119], v127, v121, v[116:119]
	v_mul_f32_e32 v127, v135, v135
	v_fmac_f32_e32 v127, v131, v131
	v_add_f32_e32 v127, v130, v127
	v_mul_f32_e32 v130, v142, v142
	v_fmac_f32_e32 v130, v134, v134
	v_add_f32_e32 v127, v130, v127
	v_lshlrev_b32_e32 v130, 16, v107
	v_mul_f32_e32 v121, v121, v121
	v_fmac_f32_e32 v121, v120, v120
	v_mfma_f32_16x16x4_f32 v[112:115], v122, v130, v[112:115]
	v_mul_f32_e32 v122, v145, v145
	v_fmac_f32_e32 v122, v143, v143
	v_add_f32_e32 v122, v122, v127
	v_mul_f32_e32 v127, v146, v146
	v_fmac_f32_e32 v127, v144, v144
	v_add_f32_e32 v122, v127, v122
	v_lshlrev_b32_e32 v127, 16, v103
	v_add_f32_e32 v122, v126, v122
	v_add_f32_e32 v126, v121, v122
	v_mfma_f32_16x16x4_f32 v[116:119], v128, v127, v[116:119]
	v_and_b32_e32 v128, 0xffff0000, v107
	s_nop 1
	v_mfma_f32_16x16x4_f32 v[120:123], v123, v128, v[112:115]
	v_and_b32_e32 v112, 0xffff0000, v103
	v_mul_f32_e32 v113, v128, v128
	v_fmac_f32_e32 v113, v130, v130
	v_mul_f32_e32 v114, v112, v112
	v_add_f32_e32 v113, v113, v126
	v_fmac_f32_e32 v114, v127, v127
	v_add_f32_e32 v130, v114, v113
	v_mfma_f32_16x16x4_f32 v[116:119], v129, v112, v[116:119]
	s_waitcnt lgkmcnt(0)
	s_mov_b64 s[16:17], 0x780
	v_lshl_add_u64 v[108:109], v[108:109], 0, s[16:17]
	s_mov_b32 s14, m0
	s_mov_b32 m0, s75
	s_nop 0
	global_load_lds_dwordx4 v[108:109], off
	s_mov_b32 m0, s14
	v_lshl_add_u64 v[108:109], v[110:111], 0, s[16:17]
	s_mov_b32 s14, m0
	s_mov_b32 m0, s13
	s_nop 0
	global_load_lds_dwordx4 v[108:109], off
	s_mov_b32 m0, s14
	s_waitcnt vmcnt(4)
	ds_read_b128 v[126:129], v34 offset:53248
	ds_read_b128 v[112:115], v125 offset:2048
	ds_read_b128 v[108:111], v124 offset:2048
	ds_read_b128 v[142:145], v34 offset:53760
	s_waitcnt lgkmcnt(2)
	v_lshlrev_b32_e32 v131, 16, v112
	s_nop 1
	v_mfma_f32_16x16x4_f32 v[120:123], v126, v131, v[120:123]
	v_and_b32_e32 v135, 0xffff0000, v112
	v_lshlrev_b32_e32 v147, 16, v113
	s_waitcnt lgkmcnt(1)
	v_lshlrev_b32_e32 v134, 16, v108
	v_and_b32_e32 v149, 0xffff0000, v113
	v_and_b32_e32 v146, 0xffff0000, v108
	v_lshlrev_b32_e32 v148, 16, v109
	v_and_b32_e32 v150, 0xffff0000, v109
	v_mfma_f32_16x16x4_f32 v[120:123], v127, v135, v[120:123]
	v_lshlrev_b32_e32 v151, 16, v114
	v_mul_f32_e32 v135, v135, v135
	v_fmac_f32_e32 v135, v131, v131
	v_mul_f32_e32 v131, v146, v146
	v_add_f32_e32 v130, v130, v135
	v_fmac_f32_e32 v131, v134, v134
	v_add_f32_e32 v130, v131, v130
	v_mfma_f32_16x16x4_f32 v[120:123], v128, v147, v[120:123]
	v_lshlrev_b32_e32 v131, 16, v115
	v_and_b32_e32 v135, 0xffff0000, v115
	v_mfma_f32_16x16x4_f32 v[120:123], v129, v149, v[120:123]
	ds_read_b128 v[126:129], v34 offset:53504
	s_waitcnt lgkmcnt(1)
	v_mfma_f32_16x16x4_f32 v[116:119], v142, v134, v[116:119]
	v_mfma_f32_16x16x4_f32 v[116:119], v143, v146, v[116:119]
	v_mfma_f32_16x16x4_f32 v[116:119], v144, v148, v[116:119]
	v_mfma_f32_16x16x4_f32 v[116:119], v145, v150, v[116:119]
	ds_read_b128 v[142:145], v34 offset:54016
	s_waitcnt lgkmcnt(1)
	v_mfma_f32_16x16x4_f32 v[120:123], v126, v151, v[120:123]
	v_lshlrev_b32_e32 v126, 16, v110
	s_waitcnt lgkmcnt(0)
	s_nop 0
	v_mfma_f32_16x16x4_f32 v[116:119], v142, v126, v[116:119]
	v_and_b32_e32 v142, 0xffff0000, v114
	v_mul_f32_e32 v134, v142, v142
	v_fmac_f32_e32 v134, v151, v151
	v_mfma_f32_16x16x4_f32 v[120:123], v127, v142, v[120:123]
	v_and_b32_e32 v127, 0xffff0000, v110
	s_nop 1
	v_mfma_f32_16x16x4_f32 v[116:119], v143, v127, v[116:119]
	v_mul_f32_e32 v127, v127, v127
	v_fmac_f32_e32 v127, v126, v126
	v_mfma_f32_16x16x4_f32 v[120:123], v128, v131, v[120:123]
	v_mul_f32_e32 v128, v149, v149
	v_fmac_f32_e32 v128, v147, v147
	v_add_f32_e32 v128, v128, v130
	v_mul_f32_e32 v130, v150, v150
	v_fmac_f32_e32 v130, v148, v148
	v_add_f32_e32 v128, v130, v128
	v_lshlrev_b32_e32 v130, 16, v111
	v_add_f32_e32 v128, v134, v128
	v_add_f32_e32 v134, v127, v128
	v_mfma_f32_16x16x4_f32 v[116:119], v144, v130, v[116:119]
	v_mfma_f32_16x16x4_f32 v[126:129], v129, v135, v[120:123]
	v_and_b32_e32 v120, 0xffff0000, v111
	v_mul_f32_e32 v121, v135, v135
	v_fmac_f32_e32 v121, v131, v131
	v_mul_f32_e32 v122, v120, v120
	v_add_f32_e32 v121, v121, v134
	v_fmac_f32_e32 v122, v130, v130
	v_add_f32_e32 v130, v122, v121
	v_mfma_f32_16x16x4_f32 v[142:145], v145, v120, v[116:119]
	s_waitcnt lgkmcnt(0)
; #define LAS __attribute__((address_space(3)))
; #define N2_DMA(c) do { const unsigned d_ = (unsigned)__builtin_amdgcn_readfirstlane(bufw + ((c) % 3) * 2048); n2_glds16(src0 + (c) * 64, d_); n2_glds16(src1 + (c) * 64, d_ + 1024); } while (0)
; __device__ __forceinline__ void n2_mfma(const Args& a, LAS unsigned char* lds, int layer) {
;     ...
;         for (int c = 0; c < 16; ++c) {
;             asm volatile("s_waitcnt lgkmcnt(0)" ::: "memory");
;             if (c + 2 < 16) { N2_DMA(c + 2); asm volatile("s_waitcnt vmcnt(4)" ::: "memory"); }
;             else if (c + 1 < 16) asm volatile("s_waitcnt vmcnt(2)" ::: "memory");
;             else asm volatile("s_waitcnt vmcnt(0)" ::: "memory");
;             const LAS unsigned char* cb = rdb + (c % 3) * 2048;
;             xs[2 * c] = *(const LAS u32x4*)(cb + sl0);
;             xs[2 * c + 1] = *(const LAS u32x4*)(cb + sl1);
;             const LAS f32x4* wq = (const LAS f32x4*)(WgL + ((c * 4) * 4 * 16) * 4) + (g * 4) * 16 + r;
;             f32x4 w0 = wq[0], w1 = wq[16], w2 = wq[32], w3 = wq[48];
; #pragma unroll
;             for (int k = 0; k < 4; ++k) {
;                 const unsigned v0 = xs[2 * c][k], v1 = xs[2 * c + 1][k];
;                 const float x00 = __uint_as_float(v0 << 16), x01 = __uint_as_float(v0 & 0xffff0000u);
;                 const float x10 = __uint_as_float(v1 << 16), x11 = __uint_as_float(v1 & 0xffff0000u);
;                 ss += x00 * x00 + x01 * x01; ss += x10 * x10 + x11 * x11;
;                 const float wa = (k < 2 ? w0 : w1)[2 * (k & 1)], wb = (k < 2 ? w0 : w1)[2 * (k & 1) + 1];
;                 const float wc = (k < 2 ? w2 : w3)[2 * (k & 1)], wd = (k < 2 ? w2 : w3)[2 * (k & 1) + 1];
;                 acc0 = __builtin_amdgcn_mfma_f32_16x16x4f32(wa, x00, acc0, 0, 0, 0);
;                 acc1 = __builtin_amdgcn_mfma_f32_16x16x4f32(wc, x10, acc1, 0, 0, 0);
;                 acc0 = __builtin_amdgcn_mfma_f32_16x16x4f32(wb, x01, acc0, 0, 0, 0);
;                 acc1 = __builtin_amdgcn_mfma_f32_16x16x4f32(wd, x11, acc1, 0, 0, 0);
;             }
;             __builtin_amdgcn_sched_barrier(0);
;         }
;     ...
;         ss += __shfl_xor(ss, 16); ss += __shfl_xor(ss, 32);
	s_waitcnt vmcnt(2)
	ds_read_b128 v[146:149], v34 offset:57344
	ds_read_b128 v[120:123], v125 offset:4096
	ds_read_b128 v[116:119], v124 offset:4096
	ds_read_b128 v[150:153], v34 offset:57856
	s_waitcnt lgkmcnt(2)
	v_lshlrev_b32_e32 v131, 16, v120
	s_nop 1
	v_mfma_f32_16x16x4_f32 v[126:129], v146, v131, v[126:129]
	v_and_b32_e32 v135, 0xffff0000, v120
	v_lshlrev_b32_e32 v155, 16, v121
	s_waitcnt lgkmcnt(1)
	v_lshlrev_b32_e32 v134, 16, v116
	v_and_b32_e32 v157, 0xffff0000, v121
	v_and_b32_e32 v154, 0xffff0000, v116
	v_lshlrev_b32_e32 v156, 16, v117
	v_and_b32_e32 v158, 0xffff0000, v117
	v_mfma_f32_16x16x4_f32 v[126:129], v147, v135, v[126:129]
	v_lshlrev_b32_e32 v159, 16, v122
	v_mul_f32_e32 v135, v135, v135
	v_fmac_f32_e32 v135, v131, v131
	v_mul_f32_e32 v131, v154, v154
	v_add_f32_e32 v130, v130, v135
	v_fmac_f32_e32 v131, v134, v134
	v_add_f32_e32 v130, v131, v130
	v_mfma_f32_16x16x4_f32 v[126:129], v148, v155, v[126:129]
	v_lshlrev_b32_e32 v131, 16, v123
	v_mfma_f32_16x16x4_f32 v[126:129], v149, v157, v[126:129]
	ds_read_b128 v[146:149], v34 offset:57600
	s_waitcnt lgkmcnt(1)
	v_mfma_f32_16x16x4_f32 v[142:145], v150, v134, v[142:145]
	v_mul_f32_e32 v134, v157, v157
	v_fmac_f32_e32 v134, v155, v155
	v_add_f32_e32 v130, v134, v130
	v_mul_f32_e32 v134, v158, v158
	v_fmac_f32_e32 v134, v156, v156
	v_add_f32_e32 v130, v134, v130
	v_lshlrev_b32_e32 v134, 16, v119
	v_mfma_f32_16x16x4_f32 v[142:145], v151, v154, v[142:145]
	v_mfma_f32_16x16x4_f32 v[142:145], v152, v156, v[142:145]
	v_mfma_f32_16x16x4_f32 v[142:145], v153, v158, v[142:145]
	ds_read_b128 v[150:153], v34 offset:58112
	s_waitcnt lgkmcnt(1)
	v_mfma_f32_16x16x4_f32 v[126:129], v146, v159, v[126:129]
	v_lshlrev_b32_e32 v146, 16, v118
	s_waitcnt lgkmcnt(0)
	s_nop 0
	v_mfma_f32_16x16x4_f32 v[142:145], v150, v146, v[142:145]
	v_and_b32_e32 v150, 0xffff0000, v122
	v_mul_f32_e32 v135, v150, v150
	v_fmac_f32_e32 v135, v159, v159
	v_add_f32_e32 v130, v135, v130
	v_mfma_f32_16x16x4_f32 v[126:129], v147, v150, v[126:129]
	v_and_b32_e32 v147, 0xffff0000, v118
	v_mul_f32_e32 v135, v147, v147
	v_fmac_f32_e32 v135, v146, v146
	v_add_f32_e32 v130, v135, v130
	v_and_b32_e32 v135, 0xffff0000, v123
	v_mfma_f32_16x16x4_f32 v[142:145], v151, v147, v[142:145]
	v_mfma_f32_16x16x4_f32 v[126:129], v148, v131, v[126:129]
	v_mfma_f32_16x16x4_f32 v[142:145], v152, v134, v[142:145]
	v_mfma_f32_16x16x4_f32 v[146:149], v149, v135, v[126:129]
	s_nop 7
	v_and_b32_e32 v126, 0xffff0000, v119
	v_mul_f32_e32 v127, v135, v135
	v_fmac_f32_e32 v127, v131, v131
	v_mul_f32_e32 v128, v126, v126
	v_add_f32_e32 v127, v127, v130
	v_fmac_f32_e32 v128, v134, v134
	v_add_f32_e32 v168, v128, v127
	v_mfma_f32_16x16x4_f32 v[142:145], v153, v126, v[142:145]
	s_waitcnt lgkmcnt(0)
	s_waitcnt vmcnt(0)
	ds_read_b128 v[150:153], v34 offset:61440
	ds_read_b128 v[128:131], v125
	ds_read_b128 v[124:127], v124
	ds_read_b128 v[154:157], v34 offset:61696
	ds_read_b128 v[158:161], v34 offset:62208
	ds_read_b128 v[162:165], v34 offset:61952
	s_waitcnt lgkmcnt(4)
	v_lshlrev_b32_e32 v135, 16, v128
	v_and_b32_e32 v167, 0xffff0000, v128
	s_nop 0
	v_mfma_f32_16x16x4_f32 v[146:149], v150, v135, v[146:149]
	v_and_b32_e32 v169, 0xffff0000, v129
	s_waitcnt lgkmcnt(3)
	v_and_b32_e32 v166, 0xffff0000, v124
	v_lshlrev_b32_e32 v134, 16, v124
	v_lshlrev_b32_e32 v150, 16, v125
	v_and_b32_e32 v173, 0xffff0000, v131
	v_and_b32_e32 v172, 0xffff0000, v127
	v_pk_mul_f32 v[174:175], v[172:173], v[172:173]
	v_mfma_f32_16x16x4_f32 v[146:149], v151, v167, v[146:149]
	v_lshlrev_b32_e32 v151, 16, v129
	s_nop 1
	v_mfma_f32_16x16x4_f32 v[146:149], v152, v151, v[146:149]
	v_mfma_f32_16x16x4_f32 v[146:149], v153, v169, v[146:149]
	v_mul_f32_e64 v152, v166, v166
	v_mul_f32_e64 v153, v167, v167
	v_fma_f32 v152, v134, v134, v152
	v_fma_f32 v153, v135, v135, v153
	v_add_f32_e32 v34, v168, v153
	v_lshlrev_b32_e32 v153, 16, v130
	v_and_b32_e32 v168, 0xffff0000, v125
	v_pk_mul_f32 v[170:171], v[168:169], v[168:169]
	s_waitcnt lgkmcnt(2)
	v_mfma_f32_16x16x4_f32 v[146:149], v154, v153, v[146:149]
	v_add_f32_e32 v34, v152, v34
	v_fma_f32 v170, v150, v150, v170
	v_fma_f32 v171, v151, v151, v171
	v_lshlrev_b32_e32 v152, 16, v126
	v_add_f32_e32 v34, v171, v34
	v_and_b32_e32 v171, 0xffff0000, v130
	v_add_f32_e32 v34, v170, v34
	v_and_b32_e32 v170, 0xffff0000, v126
	v_mfma_f32_16x16x4_f32 v[146:149], v155, v171, v[146:149]
	v_mul_f32_e64 v154, v170, v170
	v_mul_f32_e64 v155, v171, v171
	v_fma_f32 v154, v152, v152, v154
	v_fma_f32 v155, v153, v153, v155
	v_add_f32_e32 v34, v155, v34
	v_lshlrev_b32_e32 v155, 16, v131
	v_add_f32_e32 v34, v154, v34
	v_lshlrev_b32_e32 v154, 16, v127
	v_mfma_f32_16x16x4_f32 v[146:149], v156, v155, v[146:149]
	v_fma_f32 v174, v154, v154, v174
	v_fma_f32 v175, v155, v155, v175
	v_add_f32_e32 v34, v175, v34
	v_add_f32_e32 v34, v174, v34
	v_mfma_f32_16x16x4_f32 v[146:149], v157, v173, v[146:149]
	s_waitcnt lgkmcnt(0)
	v_mfma_f32_16x16x4_f32 v[142:145], v162, v134, v[142:145]
	ds_bpermute_b32 v135, v250, v34
	s_waitcnt lgkmcnt(0)
	v_add_f32_e32 v34, v34, v135
	ds_bpermute_b32 v135, v251, v34
	v_mfma_f32_16x16x4_f32 v[142:145], v163, v166, v[142:145]
	s_waitcnt lgkmcnt(0)
; #define LAS __attribute__((address_space(3)))
; __device__ __forceinline__ unsigned pk2(float lo, float hi) { pk2_f32x2 v = {lo, hi}; pk2_bf16x2 b = __builtin_convertvector(v, pk2_bf16x2); return __builtin_bit_cast(unsigned, b); }
; __device__ __forceinline__ f32x4 bf4_lo(const u32x4& v) { return (f32x4){__uint_as_float(v.x << 16), __uint_as_float(v.x & 0xffff0000u), __uint_as_float(v.y << 16), __uint_as_float(v.y & 0xffff0000u)}; }
; __device__ __forceinline__ f32x4 bf4_hi(const u32x4& v) { return (f32x4){__uint_as_float(v.z << 16), __uint_as_float(v.z & 0xffff0000u), __uint_as_float(v.w << 16), __uint_as_float(v.w & 0xffff0000u)}; }
; __device__ __forceinline__ void n2_mfma(const Args& a, LAS unsigned char* lds, int layer) {
;     ...
;         ss += __shfl_xor(ss, 16); ss += __shfl_xor(ss, 32);
;         const float rstd = rsqrtf(ss * (1.f / D) + RMS_EPS);
; #pragma unroll
;         for (int i = 0; i < 32; ++i) asm volatile("" : "+v"(xs[i]));
;         int lane_b = tid & 63; asm volatile("" : "+v"(lane_b));
;         const int rb_ = lane_b & 15, gb_ = lane_b >> 4;
;         {
;             const f32x4 ce4 = *(const LAS f32x4*)(ceL + 4 * gb_);
;             *(LAS f32x4*)(lgw + (wave * 16 + rb_) * 16 + 4 * gb_) = (acc0 + acc1) * rstd + ce4;
;         }
;         bf16_t* arow = act + (size_t)(row0 + rb_) * D + 8 * gb_;
; #pragma unroll
;         for (int c = 0; c < 16; ++c)
; #pragma unroll
;             for (int i = 0; i < 2; ++i) {
;                 const int col0 = 64 * c + 32 * i;
;                 const LAS f32x4* gp = (const LAS f32x4*)(gaL + col0) + 2 * gb_; const LAS f32x4* sp = (const LAS f32x4*)(s0L + col0) + 2 * gb_;
;                 const f32x4 ga0 = gp[0] * rstd, ga1 = gp[1] * rstd, s00 = sp[0], s01 = sp[1];
;                 const u32x4 xv = xs[2 * c + i];
;                 const f32x4 h0 = bf4_lo(xv) * ga0 + s00, h1 = bf4_hi(xv) * ga1 + s01;
;                 u32x4 o; o.x = pk2(h0.x, h0.y); o.y = pk2(h0.z, h0.w); o.z = pk2(h1.x, h1.y); o.w = pk2(h1.z, h1.w);
;                 *(u32x4*)(arow + col0) = o;
;                 __builtin_amdgcn_sched_barrier(0);
;             }
	v_add_f32_e32 v34, v34, v135
	v_fmamk_f32 v34, v34, 0x3a800000, v198
	v_mul_f32_e32 v134, 0x4b800000, v34
	v_cmp_gt_f32_e32 vcc, s76, v34
	v_mfma_f32_16x16x4_f32 v[142:145], v164, v150, v[142:145]
	s_nop 0
	v_cndmask_b32_e32 v34, v34, v134, vcc
	v_rsq_f32_e32 v34, v34
	v_mfma_f32_16x16x4_f32 v[142:145], v165, v168, v[142:145]
	v_mul_f32_e32 v134, 0x45800000, v34
	v_cndmask_b32_e32 v34, v34, v134, vcc
	v_mov_b32_e32 v134, v1
	v_mfma_f32_16x16x4_f32 v[142:145], v158, v152, v[142:145]
	v_mfma_f32_16x16x4_f32 v[142:145], v159, v170, v[142:145]
	v_mfma_f32_16x16x4_f32 v[142:145], v160, v154, v[142:145]
	s_add_i32 s13, 0, 0x10000
	v_and_b32_e32 v154, -16, v134
	v_and_b32_e32 v155, 15, v134
	v_ashrrev_i32_e32 v156, 4, v134
	v_mfma_f32_16x16x4_f32 v[142:145], v161, v172, v[142:145]
	v_add_u32_e32 v134, 0, v154
	v_add_u32_e32 v134, 0x15000, v134
	ds_read_b128 v[150:153], v134
	v_or_b32_e32 v134, s66, v155
	v_lshlrev_b32_e32 v157, 6, v134
	v_lshlrev_b32_e32 v160, 16, v6
	v_and_b32_e32 v161, 0xffff0000, v6
	s_nop 2
	v_pk_add_f32 v[134:135], v[148:149], v[144:145]
	v_pk_add_f32 v[142:143], v[146:147], v[142:143]
	s_waitcnt lgkmcnt(0)
	v_pk_fma_f32 v[144:145], v[34:35], v[134:135], v[152:153] op_sel_hi:[0,1,1]
	v_pk_fma_f32 v[142:143], v[34:35], v[142:143], v[150:151] op_sel_hi:[0,1,1]
	v_add3_u32 v134, s13, v157, v154
	ds_write_b128 v134, v[142:145]
	v_lshl_add_u32 v142, v156, 5, 0
	v_add_u32_e32 v143, 0x13000, v142
	ds_read_b128 v[144:147], v143
	ds_read_b128 v[148:151], v143 offset:16
	v_or_b32_e32 v134, s12, v155
	v_ashrrev_i32_e32 v135, 31, v134
	v_lshlrev_b64 v[134:135], 11, v[134:135]
	v_lshlrev_b32_e32 v152, 3, v156
	v_lshl_add_u64 v[134:135], s[80:81], 0, v[134:135]
	v_ashrrev_i32_e32 v153, 31, v152
	v_add_u32_e32 v142, 0x14000, v142
	v_lshl_add_u64 v[134:135], v[152:153], 1, v[134:135]
	s_waitcnt lgkmcnt(1)
	v_pk_mul_f32 v[152:153], v[34:35], v[144:145] op_sel_hi:[0,1]
	v_pk_mul_f32 v[154:155], v[34:35], v[146:147] op_sel_hi:[0,1]
	s_waitcnt lgkmcnt(0)
	v_pk_mul_f32 v[156:157], v[34:35], v[148:149] op_sel_hi:[0,1]
	v_pk_mul_f32 v[158:159], v[34:35], v[150:151] op_sel_hi:[0,1]
	ds_read_b128 v[144:147], v142
	ds_read_b128 v[148:151], v142 offset:16
	v_lshlrev_b32_e32 v6, 16, v7
	v_and_b32_e32 v7, 0xffff0000, v7
	s_waitcnt lgkmcnt(1)
	v_pk_fma_f32 v[146:147], v[154:155], v[6:7], v[146:147]
	v_pk_fma_f32 v[6:7], v[152:153], v[160:161], v[144:145]
	v_lshlrev_b32_e32 v144, 16, v8
	v_and_b32_e32 v145, 0xffff0000, v8
	v_lshlrev_b32_e32 v8, 16, v9
	v_and_b32_e32 v9, 0xffff0000, v9
	s_waitcnt lgkmcnt(0)
	v_pk_fma_f32 v[150:151], v[158:159], v[8:9], v[150:151]
	v_pk_fma_f32 v[8:9], v[156:157], v[144:145], v[148:149]
	v_cvt_pk_bf16_f32 v6, v6, v7
	v_cvt_pk_bf16_f32 v7, v146, v147
	v_cvt_pk_bf16_f32 v8, v8, v9
	v_cvt_pk_bf16_f32 v9, v150, v151
	global_store_dwordx4 v[134:135], v[6:9], off sc1
	ds_read_b128 v[6:9], v143 offset:128
	ds_read_b128 v[144:147], v143 offset:144
	v_lshlrev_b32_e32 v156, 16, v2
	v_and_b32_e32 v157, 0xffff0000, v2
	v_lshlrev_b32_e32 v2, 16, v3
	s_waitcnt lgkmcnt(1)
	v_pk_mul_f32 v[148:149], v[34:35], v[6:7] op_sel_hi:[0,1]
	v_pk_mul_f32 v[150:151], v[34:35], v[8:9] op_sel_hi:[0,1]
	s_waitcnt lgkmcnt(0)
	v_pk_mul_f32 v[152:153], v[34:35], v[144:145] op_sel_hi:[0,1]
	v_pk_mul_f32 v[154:155], v[34:35], v[146:147] op_sel_hi:[0,1]
	ds_read_b128 v[6:9], v142 offset:128
	ds_read_b128 v[144:147], v142 offset:144
	v_and_b32_e32 v3, 0xffff0000, v3
	s_waitcnt lgkmcnt(1)
	v_pk_fma_f32 v[8:9], v[150:151], v[2:3], v[8:9]
	v_pk_fma_f32 v[2:3], v[148:149], v[156:157], v[6:7]
	v_lshlrev_b32_e32 v6, 16, v4
	v_and_b32_e32 v7, 0xffff0000, v4
	v_lshlrev_b32_e32 v4, 16, v5
	v_and_b32_e32 v5, 0xffff0000, v5
	s_waitcnt lgkmcnt(0)
	v_pk_fma_f32 v[146:147], v[154:155], v[4:5], v[146:147]
	v_pk_fma_f32 v[4:5], v[152:153], v[6:7], v[144:145]
	v_cvt_pk_bf16_f32 v2, v2, v3
	v_cvt_pk_bf16_f32 v3, v8, v9
	v_cvt_pk_bf16_f32 v4, v4, v5
	v_cvt_pk_bf16_f32 v5, v146, v147
	global_store_dwordx4 v[134:135], v[2:5], off offset:64 sc1
	ds_read_b128 v[2:5], v143 offset:256
	ds_read_b128 v[6:9], v143 offset:272
	v_lshlrev_b32_e32 v152, 16, v14
	v_and_b32_e32 v153, 0xffff0000, v14
	v_lshlrev_b32_e32 v14, 16, v15
	s_waitcnt lgkmcnt(1)
	v_pk_mul_f32 v[144:145], v[34:35], v[2:3] op_sel_hi:[0,1]
	v_pk_mul_f32 v[146:147], v[34:35], v[4:5] op_sel_hi:[0,1]
	s_waitcnt lgkmcnt(0)
	v_pk_mul_f32 v[148:149], v[34:35], v[6:7] op_sel_hi:[0,1]
	v_pk_mul_f32 v[150:151], v[34:35], v[8:9] op_sel_hi:[0,1]
	ds_read_b128 v[2:5], v142 offset:256
	ds_read_b128 v[6:9], v142 offset:272
	v_and_b32_e32 v15, 0xffff0000, v15
	s_waitcnt lgkmcnt(1)
	v_pk_fma_f32 v[4:5], v[146:147], v[14:15], v[4:5]
	v_lshlrev_b32_e32 v14, 16, v16
	v_and_b32_e32 v15, 0xffff0000, v16
	v_lshlrev_b32_e32 v16, 16, v17
	v_and_b32_e32 v17, 0xffff0000, v17
	v_pk_fma_f32 v[2:3], v[144:145], v[152:153], v[2:3]
	s_waitcnt lgkmcnt(0)
	v_pk_fma_f32 v[8:9], v[150:151], v[16:17], v[8:9]
	v_pk_fma_f32 v[6:7], v[148:149], v[14:15], v[6:7]
	v_cvt_pk_bf16_f32 v2, v2, v3
	v_cvt_pk_bf16_f32 v3, v4, v5
	v_cvt_pk_bf16_f32 v4, v6, v7
	v_cvt_pk_bf16_f32 v5, v8, v9
	global_store_dwordx4 v[134:135], v[2:5], off offset:128 sc1
	ds_read_b128 v[2:5], v143 offset:384
	ds_read_b128 v[6:9], v143 offset:400
	v_lshlrev_b32_e32 v148, 16, v10
	v_and_b32_e32 v149, 0xffff0000, v10
	v_lshlrev_b32_e32 v10, 16, v11
	s_waitcnt lgkmcnt(1)
	v_pk_mul_f32 v[14:15], v[34:35], v[2:3] op_sel_hi:[0,1]
	v_pk_mul_f32 v[16:17], v[34:35], v[4:5] op_sel_hi:[0,1]
	s_waitcnt lgkmcnt(0)
	v_pk_mul_f32 v[144:145], v[34:35], v[6:7] op_sel_hi:[0,1]
	v_pk_mul_f32 v[146:147], v[34:35], v[8:9] op_sel_hi:[0,1]
	ds_read_b128 v[2:5], v142 offset:384
	ds_read_b128 v[6:9], v142 offset:400
	v_and_b32_e32 v11, 0xffff0000, v11
	s_waitcnt lgkmcnt(1)
; #define LAS __attribute__((address_space(3)))
; __device__ __forceinline__ unsigned pk2(float lo, float hi) { pk2_f32x2 v = {lo, hi}; pk2_bf16x2 b = __builtin_convertvector(v, pk2_bf16x2); return __builtin_bit_cast(unsigned, b); }
; __device__ __forceinline__ f32x4 bf4_lo(const u32x4& v) { return (f32x4){__uint_as_float(v.x << 16), __uint_as_float(v.x & 0xffff0000u), __uint_as_float(v.y << 16), __uint_as_float(v.y & 0xffff0000u)}; }
; __device__ __forceinline__ f32x4 bf4_hi(const u32x4& v) { return (f32x4){__uint_as_float(v.z << 16), __uint_as_float(v.z & 0xffff0000u), __uint_as_float(v.w << 16), __uint_as_float(v.w & 0xffff0000u)}; }
; __device__ __forceinline__ void n2_mfma(const Args& a, LAS unsigned char* lds, int layer) {
;     ...
;         bf16_t* arow = act + (size_t)(row0 + rb_) * D + 8 * gb_;
; #pragma unroll
;         for (int c = 0; c < 16; ++c)
; #pragma unroll
;             for (int i = 0; i < 2; ++i) {
;                 const int col0 = 64 * c + 32 * i;
;                 const LAS f32x4* gp = (const LAS f32x4*)(gaL + col0) + 2 * gb_; const LAS f32x4* sp = (const LAS f32x4*)(s0L + col0) + 2 * gb_;
;                 const f32x4 ga0 = gp[0] * rstd, ga1 = gp[1] * rstd, s00 = sp[0], s01 = sp[1];
;                 const u32x4 xv = xs[2 * c + i];
;                 const f32x4 h0 = bf4_lo(xv) * ga0 + s00, h1 = bf4_hi(xv) * ga1 + s01;
;                 u32x4 o; o.x = pk2(h0.x, h0.y); o.y = pk2(h0.z, h0.w); o.z = pk2(h1.x, h1.y); o.w = pk2(h1.z, h1.w);
;                 *(u32x4*)(arow + col0) = o;
;                 __builtin_amdgcn_sched_barrier(0);
;             }
	v_pk_fma_f32 v[4:5], v[16:17], v[10:11], v[4:5]
	v_lshlrev_b32_e32 v10, 16, v12
	v_and_b32_e32 v11, 0xffff0000, v12
	v_lshlrev_b32_e32 v12, 16, v13
	v_and_b32_e32 v13, 0xffff0000, v13
	v_pk_fma_f32 v[2:3], v[14:15], v[148:149], v[2:3]
	s_waitcnt lgkmcnt(0)
	v_pk_fma_f32 v[8:9], v[146:147], v[12:13], v[8:9]
	v_pk_fma_f32 v[6:7], v[144:145], v[10:11], v[6:7]
	v_cvt_pk_bf16_f32 v2, v2, v3
	v_cvt_pk_bf16_f32 v3, v4, v5
	v_cvt_pk_bf16_f32 v4, v6, v7
	v_cvt_pk_bf16_f32 v5, v8, v9
	global_store_dwordx4 v[134:135], v[2:5], off offset:192 sc1
	ds_read_b128 v[2:5], v143 offset:512
	ds_read_b128 v[6:9], v143 offset:528
	v_lshlrev_b32_e32 v144, 16, v22
	v_and_b32_e32 v145, 0xffff0000, v22
	v_lshlrev_b32_e32 v22, 16, v23
	s_waitcnt lgkmcnt(1)
	v_pk_mul_f32 v[10:11], v[34:35], v[2:3] op_sel_hi:[0,1]
	v_pk_mul_f32 v[12:13], v[34:35], v[4:5] op_sel_hi:[0,1]
	s_waitcnt lgkmcnt(0)
	v_pk_mul_f32 v[14:15], v[34:35], v[6:7] op_sel_hi:[0,1]
	v_pk_mul_f32 v[16:17], v[34:35], v[8:9] op_sel_hi:[0,1]
	ds_read_b128 v[2:5], v142 offset:512
	ds_read_b128 v[6:9], v142 offset:528
	v_and_b32_e32 v23, 0xffff0000, v23
	s_waitcnt lgkmcnt(1)
	v_pk_fma_f32 v[4:5], v[12:13], v[22:23], v[4:5]
	v_pk_fma_f32 v[2:3], v[10:11], v[144:145], v[2:3]
	v_lshlrev_b32_e32 v10, 16, v24
	v_and_b32_e32 v11, 0xffff0000, v24
	v_lshlrev_b32_e32 v12, 16, v25
	v_and_b32_e32 v13, 0xffff0000, v25
	s_waitcnt lgkmcnt(0)
	v_pk_fma_f32 v[8:9], v[16:17], v[12:13], v[8:9]
	v_pk_fma_f32 v[6:7], v[14:15], v[10:11], v[6:7]
	v_cvt_pk_bf16_f32 v2, v2, v3
	v_cvt_pk_bf16_f32 v3, v4, v5
	v_cvt_pk_bf16_f32 v4, v6, v7
	v_cvt_pk_bf16_f32 v5, v8, v9
	global_store_dwordx4 v[134:135], v[2:5], off offset:256 sc1
	ds_read_b128 v[2:5], v143 offset:640
	ds_read_b128 v[6:9], v143 offset:656
	v_lshlrev_b32_e32 v22, 16, v18
	v_and_b32_e32 v23, 0xffff0000, v18
	v_lshlrev_b32_e32 v18, 16, v19
	s_waitcnt lgkmcnt(1)
	v_pk_mul_f32 v[10:11], v[34:35], v[2:3] op_sel_hi:[0,1]
	v_pk_mul_f32 v[12:13], v[34:35], v[4:5] op_sel_hi:[0,1]
	s_waitcnt lgkmcnt(0)
	v_pk_mul_f32 v[14:15], v[34:35], v[6:7] op_sel_hi:[0,1]
	v_pk_mul_f32 v[16:17], v[34:35], v[8:9] op_sel_hi:[0,1]
	ds_read_b128 v[2:5], v142 offset:640
	ds_read_b128 v[6:9], v142 offset:656
	v_and_b32_e32 v19, 0xffff0000, v19
	s_waitcnt lgkmcnt(1)
	v_pk_fma_f32 v[4:5], v[12:13], v[18:19], v[4:5]
	v_pk_fma_f32 v[2:3], v[10:11], v[22:23], v[2:3]
	v_lshlrev_b32_e32 v10, 16, v20
	v_and_b32_e32 v11, 0xffff0000, v20
	v_lshlrev_b32_e32 v12, 16, v21
	v_and_b32_e32 v13, 0xffff0000, v21
	s_waitcnt lgkmcnt(0)
	v_pk_fma_f32 v[8:9], v[16:17], v[12:13], v[8:9]
	v_pk_fma_f32 v[6:7], v[14:15], v[10:11], v[6:7]
	v_cvt_pk_bf16_f32 v2, v2, v3
	v_cvt_pk_bf16_f32 v3, v4, v5
	v_cvt_pk_bf16_f32 v4, v6, v7
	v_cvt_pk_bf16_f32 v5, v8, v9
	global_store_dwordx4 v[134:135], v[2:5], off offset:320 sc1
	ds_read_b128 v[2:5], v143 offset:768
	ds_read_b128 v[6:9], v143 offset:784
	v_lshlrev_b32_e32 v18, 16, v30
	v_and_b32_e32 v19, 0xffff0000, v30
	v_lshlrev_b32_e32 v20, 16, v31
	s_waitcnt lgkmcnt(1)
	v_pk_mul_f32 v[10:11], v[34:35], v[2:3] op_sel_hi:[0,1]
	v_pk_mul_f32 v[12:13], v[34:35], v[4:5] op_sel_hi:[0,1]
	s_waitcnt lgkmcnt(0)
	v_pk_mul_f32 v[14:15], v[34:35], v[6:7] op_sel_hi:[0,1]
	v_pk_mul_f32 v[16:17], v[34:35], v[8:9] op_sel_hi:[0,1]
	ds_read_b128 v[2:5], v142 offset:768
	ds_read_b128 v[6:9], v142 offset:784
	v_and_b32_e32 v21, 0xffff0000, v31
	s_waitcnt lgkmcnt(1)
	v_pk_fma_f32 v[4:5], v[12:13], v[20:21], v[4:5]
	v_pk_fma_f32 v[2:3], v[10:11], v[18:19], v[2:3]
	v_lshlrev_b32_e32 v10, 16, v32
	v_and_b32_e32 v11, 0xffff0000, v32
	v_lshlrev_b32_e32 v12, 16, v33
	v_and_b32_e32 v13, 0xffff0000, v33
	s_waitcnt lgkmcnt(0)
	v_pk_fma_f32 v[8:9], v[16:17], v[12:13], v[8:9]
	v_pk_fma_f32 v[6:7], v[14:15], v[10:11], v[6:7]
	v_cvt_pk_bf16_f32 v2, v2, v3
	v_cvt_pk_bf16_f32 v3, v4, v5
	v_cvt_pk_bf16_f32 v4, v6, v7
	v_cvt_pk_bf16_f32 v5, v8, v9
	global_store_dwordx4 v[134:135], v[2:5], off offset:384 sc1
	ds_read_b128 v[2:5], v143 offset:896
	ds_read_b128 v[6:9], v143 offset:912
	v_lshlrev_b32_e32 v18, 16, v26
	v_and_b32_e32 v19, 0xffff0000, v26
	v_lshlrev_b32_e32 v20, 16, v27
	s_waitcnt lgkmcnt(1)
	v_pk_mul_f32 v[10:11], v[34:35], v[2:3] op_sel_hi:[0,1]
	v_pk_mul_f32 v[12:13], v[34:35], v[4:5] op_sel_hi:[0,1]
	s_waitcnt lgkmcnt(0)
	v_pk_mul_f32 v[14:15], v[34:35], v[6:7] op_sel_hi:[0,1]
	v_pk_mul_f32 v[16:17], v[34:35], v[8:9] op_sel_hi:[0,1]
	ds_read_b128 v[2:5], v142 offset:896
	ds_read_b128 v[6:9], v142 offset:912
	v_and_b32_e32 v21, 0xffff0000, v27
	s_waitcnt lgkmcnt(1)
	v_pk_fma_f32 v[4:5], v[12:13], v[20:21], v[4:5]
	v_pk_fma_f32 v[2:3], v[10:11], v[18:19], v[2:3]
	v_lshlrev_b32_e32 v10, 16, v28
	v_and_b32_e32 v11, 0xffff0000, v28
	v_lshlrev_b32_e32 v12, 16, v29
	v_and_b32_e32 v13, 0xffff0000, v29
	s_waitcnt lgkmcnt(0)
	v_pk_fma_f32 v[8:9], v[16:17], v[12:13], v[8:9]
	v_pk_fma_f32 v[6:7], v[14:15], v[10:11], v[6:7]
	v_cvt_pk_bf16_f32 v2, v2, v3
	v_cvt_pk_bf16_f32 v3, v4, v5
	v_cvt_pk_bf16_f32 v4, v6, v7
	v_cvt_pk_bf16_f32 v5, v8, v9
	global_store_dwordx4 v[134:135], v[2:5], off offset:448 sc1
	ds_read_b128 v[2:5], v143 offset:1024
	ds_read_b128 v[6:9], v143 offset:1040
	v_lshlrev_b32_e32 v18, 16, v40
	v_and_b32_e32 v19, 0xffff0000, v40
	v_lshlrev_b32_e32 v20, 16, v41
	s_waitcnt lgkmcnt(1)
	v_pk_mul_f32 v[10:11], v[34:35], v[2:3] op_sel_hi:[0,1]
	v_pk_mul_f32 v[12:13], v[34:35], v[4:5] op_sel_hi:[0,1]
	s_waitcnt lgkmcnt(0)
	v_pk_mul_f32 v[14:15], v[34:35], v[6:7] op_sel_hi:[0,1]
	v_pk_mul_f32 v[16:17], v[34:35], v[8:9] op_sel_hi:[0,1]
	ds_read_b128 v[2:5], v142 offset:1024
	ds_read_b128 v[6:9], v142 offset:1040
	v_and_b32_e32 v21, 0xffff0000, v41
	s_waitcnt lgkmcnt(1)
; #define LAS __attribute__((address_space(3)))
; __device__ __forceinline__ unsigned pk2(float lo, float hi) { pk2_f32x2 v = {lo, hi}; pk2_bf16x2 b = __builtin_convertvector(v, pk2_bf16x2); return __builtin_bit_cast(unsigned, b); }
; __device__ __forceinline__ f32x4 bf4_lo(const u32x4& v) { return (f32x4){__uint_as_float(v.x << 16), __uint_as_float(v.x & 0xffff0000u), __uint_as_float(v.y << 16), __uint_as_float(v.y & 0xffff0000u)}; }
; __device__ __forceinline__ f32x4 bf4_hi(const u32x4& v) { return (f32x4){__uint_as_float(v.z << 16), __uint_as_float(v.z & 0xffff0000u), __uint_as_float(v.w << 16), __uint_as_float(v.w & 0xffff0000u)}; }
; __device__ __forceinline__ void n2_mfma(const Args& a, LAS unsigned char* lds, int layer) {
;     ...
;         bf16_t* arow = act + (size_t)(row0 + rb_) * D + 8 * gb_;
; #pragma unroll
;         for (int c = 0; c < 16; ++c)
; #pragma unroll
;             for (int i = 0; i < 2; ++i) {
;                 const int col0 = 64 * c + 32 * i;
;                 const LAS f32x4* gp = (const LAS f32x4*)(gaL + col0) + 2 * gb_; const LAS f32x4* sp = (const LAS f32x4*)(s0L + col0) + 2 * gb_;
;                 const f32x4 ga0 = gp[0] * rstd, ga1 = gp[1] * rstd, s00 = sp[0], s01 = sp[1];
;                 const u32x4 xv = xs[2 * c + i];
;                 const f32x4 h0 = bf4_lo(xv) * ga0 + s00, h1 = bf4_hi(xv) * ga1 + s01;
;                 u32x4 o; o.x = pk2(h0.x, h0.y); o.y = pk2(h0.z, h0.w); o.z = pk2(h1.x, h1.y); o.w = pk2(h1.z, h1.w);
;                 *(u32x4*)(arow + col0) = o;
;                 __builtin_amdgcn_sched_barrier(0);
;             }
	v_pk_fma_f32 v[4:5], v[12:13], v[20:21], v[4:5]
	v_pk_fma_f32 v[2:3], v[10:11], v[18:19], v[2:3]
	v_lshlrev_b32_e32 v10, 16, v42
	v_and_b32_e32 v11, 0xffff0000, v42
	v_lshlrev_b32_e32 v12, 16, v43
	v_and_b32_e32 v13, 0xffff0000, v43
	s_waitcnt lgkmcnt(0)
	v_pk_fma_f32 v[8:9], v[16:17], v[12:13], v[8:9]
	v_pk_fma_f32 v[6:7], v[14:15], v[10:11], v[6:7]
	v_cvt_pk_bf16_f32 v2, v2, v3
	v_cvt_pk_bf16_f32 v3, v4, v5
	v_cvt_pk_bf16_f32 v4, v6, v7
	v_cvt_pk_bf16_f32 v5, v8, v9
	global_store_dwordx4 v[134:135], v[2:5], off offset:512 sc1
	ds_read_b128 v[2:5], v143 offset:1152
	ds_read_b128 v[6:9], v143 offset:1168
	v_lshlrev_b32_e32 v18, 16, v36
	v_and_b32_e32 v19, 0xffff0000, v36
	v_lshlrev_b32_e32 v20, 16, v37
	s_waitcnt lgkmcnt(1)
	v_pk_mul_f32 v[10:11], v[34:35], v[2:3] op_sel_hi:[0,1]
	v_pk_mul_f32 v[12:13], v[34:35], v[4:5] op_sel_hi:[0,1]
	s_waitcnt lgkmcnt(0)
	v_pk_mul_f32 v[14:15], v[34:35], v[6:7] op_sel_hi:[0,1]
	v_pk_mul_f32 v[16:17], v[34:35], v[8:9] op_sel_hi:[0,1]
	ds_read_b128 v[2:5], v142 offset:1152
	ds_read_b128 v[6:9], v142 offset:1168
	v_and_b32_e32 v21, 0xffff0000, v37
	s_waitcnt lgkmcnt(1)
	v_pk_fma_f32 v[4:5], v[12:13], v[20:21], v[4:5]
	v_pk_fma_f32 v[2:3], v[10:11], v[18:19], v[2:3]
	v_lshlrev_b32_e32 v10, 16, v38
	v_and_b32_e32 v11, 0xffff0000, v38
	v_lshlrev_b32_e32 v12, 16, v39
	v_and_b32_e32 v13, 0xffff0000, v39
	s_waitcnt lgkmcnt(0)
	v_pk_fma_f32 v[8:9], v[16:17], v[12:13], v[8:9]
	v_pk_fma_f32 v[6:7], v[14:15], v[10:11], v[6:7]
	v_cvt_pk_bf16_f32 v2, v2, v3
	v_cvt_pk_bf16_f32 v3, v4, v5
	v_cvt_pk_bf16_f32 v4, v6, v7
	v_cvt_pk_bf16_f32 v5, v8, v9
	global_store_dwordx4 v[134:135], v[2:5], off offset:576 sc1
	ds_read_b128 v[2:5], v143 offset:1280
	ds_read_b128 v[6:9], v143 offset:1296
	v_lshlrev_b32_e32 v18, 16, v48
	v_and_b32_e32 v19, 0xffff0000, v48
	v_lshlrev_b32_e32 v20, 16, v49
	s_waitcnt lgkmcnt(1)
	v_pk_mul_f32 v[10:11], v[34:35], v[2:3] op_sel_hi:[0,1]
	v_pk_mul_f32 v[12:13], v[34:35], v[4:5] op_sel_hi:[0,1]
	s_waitcnt lgkmcnt(0)
	v_pk_mul_f32 v[14:15], v[34:35], v[6:7] op_sel_hi:[0,1]
	v_pk_mul_f32 v[16:17], v[34:35], v[8:9] op_sel_hi:[0,1]
	ds_read_b128 v[2:5], v142 offset:1280
	ds_read_b128 v[6:9], v142 offset:1296
	v_and_b32_e32 v21, 0xffff0000, v49
	s_waitcnt lgkmcnt(1)
	v_pk_fma_f32 v[4:5], v[12:13], v[20:21], v[4:5]
	v_pk_fma_f32 v[2:3], v[10:11], v[18:19], v[2:3]
	v_lshlrev_b32_e32 v10, 16, v50
	v_and_b32_e32 v11, 0xffff0000, v50
	v_lshlrev_b32_e32 v12, 16, v51
	v_and_b32_e32 v13, 0xffff0000, v51
	s_waitcnt lgkmcnt(0)
	v_pk_fma_f32 v[8:9], v[16:17], v[12:13], v[8:9]
	v_pk_fma_f32 v[6:7], v[14:15], v[10:11], v[6:7]
	v_cvt_pk_bf16_f32 v2, v2, v3
	v_cvt_pk_bf16_f32 v3, v4, v5
	v_cvt_pk_bf16_f32 v4, v6, v7
	v_cvt_pk_bf16_f32 v5, v8, v9
	global_store_dwordx4 v[134:135], v[2:5], off offset:640 sc1
	ds_read_b128 v[2:5], v143 offset:1408
	ds_read_b128 v[6:9], v143 offset:1424
	v_lshlrev_b32_e32 v18, 16, v44
	v_and_b32_e32 v19, 0xffff0000, v44
	v_lshlrev_b32_e32 v20, 16, v45
	s_waitcnt lgkmcnt(1)
	v_pk_mul_f32 v[10:11], v[34:35], v[2:3] op_sel_hi:[0,1]
	v_pk_mul_f32 v[12:13], v[34:35], v[4:5] op_sel_hi:[0,1]
	s_waitcnt lgkmcnt(0)
	v_pk_mul_f32 v[14:15], v[34:35], v[6:7] op_sel_hi:[0,1]
	v_pk_mul_f32 v[16:17], v[34:35], v[8:9] op_sel_hi:[0,1]
	ds_read_b128 v[2:5], v142 offset:1408
	ds_read_b128 v[6:9], v142 offset:1424
	v_and_b32_e32 v21, 0xffff0000, v45
	s_waitcnt lgkmcnt(1)
	v_pk_fma_f32 v[4:5], v[12:13], v[20:21], v[4:5]
	v_pk_fma_f32 v[2:3], v[10:11], v[18:19], v[2:3]
	v_lshlrev_b32_e32 v10, 16, v46
	v_and_b32_e32 v11, 0xffff0000, v46
	v_lshlrev_b32_e32 v12, 16, v47
	v_and_b32_e32 v13, 0xffff0000, v47
	s_waitcnt lgkmcnt(0)
	v_pk_fma_f32 v[8:9], v[16:17], v[12:13], v[8:9]
	v_pk_fma_f32 v[6:7], v[14:15], v[10:11], v[6:7]
	v_cvt_pk_bf16_f32 v2, v2, v3
	v_cvt_pk_bf16_f32 v3, v4, v5
	v_cvt_pk_bf16_f32 v4, v6, v7
	v_cvt_pk_bf16_f32 v5, v8, v9
	global_store_dwordx4 v[134:135], v[2:5], off offset:704 sc1
	ds_read_b128 v[2:5], v143 offset:1536
	ds_read_b128 v[6:9], v143 offset:1552
	v_lshlrev_b32_e32 v18, 16, v56
	v_and_b32_e32 v19, 0xffff0000, v56
	v_lshlrev_b32_e32 v20, 16, v57
	s_waitcnt lgkmcnt(1)
	v_pk_mul_f32 v[10:11], v[34:35], v[2:3] op_sel_hi:[0,1]
	v_pk_mul_f32 v[12:13], v[34:35], v[4:5] op_sel_hi:[0,1]
	s_waitcnt lgkmcnt(0)
	v_pk_mul_f32 v[14:15], v[34:35], v[6:7] op_sel_hi:[0,1]
	v_pk_mul_f32 v[16:17], v[34:35], v[8:9] op_sel_hi:[0,1]
	ds_read_b128 v[2:5], v142 offset:1536
	ds_read_b128 v[6:9], v142 offset:1552
	v_and_b32_e32 v21, 0xffff0000, v57
	s_waitcnt lgkmcnt(1)
	v_pk_fma_f32 v[4:5], v[12:13], v[20:21], v[4:5]
	v_pk_fma_f32 v[2:3], v[10:11], v[18:19], v[2:3]
	v_lshlrev_b32_e32 v10, 16, v58
	v_and_b32_e32 v11, 0xffff0000, v58
	v_lshlrev_b32_e32 v12, 16, v59
	v_and_b32_e32 v13, 0xffff0000, v59
	s_waitcnt lgkmcnt(0)
	v_pk_fma_f32 v[8:9], v[16:17], v[12:13], v[8:9]
	v_pk_fma_f32 v[6:7], v[14:15], v[10:11], v[6:7]
	v_cvt_pk_bf16_f32 v2, v2, v3
	v_cvt_pk_bf16_f32 v3, v4, v5
	v_cvt_pk_bf16_f32 v4, v6, v7
	v_cvt_pk_bf16_f32 v5, v8, v9
	global_store_dwordx4 v[134:135], v[2:5], off offset:768 sc1
	ds_read_b128 v[2:5], v143 offset:1664
	ds_read_b128 v[6:9], v143 offset:1680
	v_lshlrev_b32_e32 v18, 16, v52
	v_and_b32_e32 v19, 0xffff0000, v52
	v_lshlrev_b32_e32 v20, 16, v53
	s_waitcnt lgkmcnt(1)
	v_pk_mul_f32 v[10:11], v[34:35], v[2:3] op_sel_hi:[0,1]
	v_pk_mul_f32 v[12:13], v[34:35], v[4:5] op_sel_hi:[0,1]
	s_waitcnt lgkmcnt(0)
	v_pk_mul_f32 v[14:15], v[34:35], v[6:7] op_sel_hi:[0,1]
	v_pk_mul_f32 v[16:17], v[34:35], v[8:9] op_sel_hi:[0,1]
	ds_read_b128 v[2:5], v142 offset:1664
	ds_read_b128 v[6:9], v142 offset:1680
	v_and_b32_e32 v21, 0xffff0000, v53
	s_waitcnt lgkmcnt(1)
; #define LAS __attribute__((address_space(3)))
; __device__ __forceinline__ unsigned pk2(float lo, float hi) { pk2_f32x2 v = {lo, hi}; pk2_bf16x2 b = __builtin_convertvector(v, pk2_bf16x2); return __builtin_bit_cast(unsigned, b); }
; __device__ __forceinline__ f32x4 bf4_lo(const u32x4& v) { return (f32x4){__uint_as_float(v.x << 16), __uint_as_float(v.x & 0xffff0000u), __uint_as_float(v.y << 16), __uint_as_float(v.y & 0xffff0000u)}; }
; __device__ __forceinline__ f32x4 bf4_hi(const u32x4& v) { return (f32x4){__uint_as_float(v.z << 16), __uint_as_float(v.z & 0xffff0000u), __uint_as_float(v.w << 16), __uint_as_float(v.w & 0xffff0000u)}; }
; __device__ __forceinline__ void n2_mfma(const Args& a, LAS unsigned char* lds, int layer) {
;     ...
;         bf16_t* arow = act + (size_t)(row0 + rb_) * D + 8 * gb_;
; #pragma unroll
;         for (int c = 0; c < 16; ++c)
; #pragma unroll
;             for (int i = 0; i < 2; ++i) {
;                 const int col0 = 64 * c + 32 * i;
;                 const LAS f32x4* gp = (const LAS f32x4*)(gaL + col0) + 2 * gb_; const LAS f32x4* sp = (const LAS f32x4*)(s0L + col0) + 2 * gb_;
;                 const f32x4 ga0 = gp[0] * rstd, ga1 = gp[1] * rstd, s00 = sp[0], s01 = sp[1];
;                 const u32x4 xv = xs[2 * c + i];
;                 const f32x4 h0 = bf4_lo(xv) * ga0 + s00, h1 = bf4_hi(xv) * ga1 + s01;
;                 u32x4 o; o.x = pk2(h0.x, h0.y); o.y = pk2(h0.z, h0.w); o.z = pk2(h1.x, h1.y); o.w = pk2(h1.z, h1.w);
;                 *(u32x4*)(arow + col0) = o;
;                 __builtin_amdgcn_sched_barrier(0);
;             }
	v_pk_fma_f32 v[4:5], v[12:13], v[20:21], v[4:5]
	v_pk_fma_f32 v[2:3], v[10:11], v[18:19], v[2:3]
	v_lshlrev_b32_e32 v10, 16, v54
	v_and_b32_e32 v11, 0xffff0000, v54
	v_lshlrev_b32_e32 v12, 16, v55
	v_and_b32_e32 v13, 0xffff0000, v55
	s_waitcnt lgkmcnt(0)
	v_pk_fma_f32 v[8:9], v[16:17], v[12:13], v[8:9]
	v_pk_fma_f32 v[6:7], v[14:15], v[10:11], v[6:7]
	v_cvt_pk_bf16_f32 v2, v2, v3
	v_cvt_pk_bf16_f32 v3, v4, v5
	v_cvt_pk_bf16_f32 v4, v6, v7
	v_cvt_pk_bf16_f32 v5, v8, v9
	global_store_dwordx4 v[134:135], v[2:5], off offset:832 sc1
	ds_read_b128 v[2:5], v143 offset:1792
	ds_read_b128 v[6:9], v143 offset:1808
	v_lshlrev_b32_e32 v18, 16, v64
	v_and_b32_e32 v19, 0xffff0000, v64
	v_lshlrev_b32_e32 v20, 16, v65
	s_waitcnt lgkmcnt(1)
	v_pk_mul_f32 v[10:11], v[34:35], v[2:3] op_sel_hi:[0,1]
	v_pk_mul_f32 v[12:13], v[34:35], v[4:5] op_sel_hi:[0,1]
	s_waitcnt lgkmcnt(0)
	v_pk_mul_f32 v[14:15], v[34:35], v[6:7] op_sel_hi:[0,1]
	v_pk_mul_f32 v[16:17], v[34:35], v[8:9] op_sel_hi:[0,1]
	ds_read_b128 v[2:5], v142 offset:1792
	ds_read_b128 v[6:9], v142 offset:1808
	v_and_b32_e32 v21, 0xffff0000, v65
	s_waitcnt lgkmcnt(1)
	v_pk_fma_f32 v[4:5], v[12:13], v[20:21], v[4:5]
	v_pk_fma_f32 v[2:3], v[10:11], v[18:19], v[2:3]
	v_lshlrev_b32_e32 v10, 16, v66
	v_and_b32_e32 v11, 0xffff0000, v66
	v_lshlrev_b32_e32 v12, 16, v67
	v_and_b32_e32 v13, 0xffff0000, v67
	s_waitcnt lgkmcnt(0)
	v_pk_fma_f32 v[8:9], v[16:17], v[12:13], v[8:9]
	v_pk_fma_f32 v[6:7], v[14:15], v[10:11], v[6:7]
	v_cvt_pk_bf16_f32 v2, v2, v3
	v_cvt_pk_bf16_f32 v3, v4, v5
	v_cvt_pk_bf16_f32 v4, v6, v7
	v_cvt_pk_bf16_f32 v5, v8, v9
	global_store_dwordx4 v[134:135], v[2:5], off offset:896 sc1
	ds_read_b128 v[2:5], v143 offset:1920
	ds_read_b128 v[6:9], v143 offset:1936
	v_lshlrev_b32_e32 v18, 16, v60
	v_and_b32_e32 v19, 0xffff0000, v60
	v_lshlrev_b32_e32 v20, 16, v61
	s_waitcnt lgkmcnt(1)
	v_pk_mul_f32 v[10:11], v[34:35], v[2:3] op_sel_hi:[0,1]
	v_pk_mul_f32 v[12:13], v[34:35], v[4:5] op_sel_hi:[0,1]
	s_waitcnt lgkmcnt(0)
	v_pk_mul_f32 v[14:15], v[34:35], v[6:7] op_sel_hi:[0,1]
	v_pk_mul_f32 v[16:17], v[34:35], v[8:9] op_sel_hi:[0,1]
	ds_read_b128 v[2:5], v142 offset:1920
	ds_read_b128 v[6:9], v142 offset:1936
	v_and_b32_e32 v21, 0xffff0000, v61
	s_waitcnt lgkmcnt(1)
	v_pk_fma_f32 v[4:5], v[12:13], v[20:21], v[4:5]
	v_pk_fma_f32 v[2:3], v[10:11], v[18:19], v[2:3]
	v_lshlrev_b32_e32 v10, 16, v62
	v_and_b32_e32 v11, 0xffff0000, v62
	v_lshlrev_b32_e32 v12, 16, v63
	v_and_b32_e32 v13, 0xffff0000, v63
	s_waitcnt lgkmcnt(0)
	v_pk_fma_f32 v[8:9], v[16:17], v[12:13], v[8:9]
	v_pk_fma_f32 v[6:7], v[14:15], v[10:11], v[6:7]
	v_cvt_pk_bf16_f32 v2, v2, v3
	v_cvt_pk_bf16_f32 v3, v4, v5
	v_cvt_pk_bf16_f32 v4, v6, v7
	v_cvt_pk_bf16_f32 v5, v8, v9
	global_store_dwordx4 v[134:135], v[2:5], off offset:960 sc1
	ds_read_b128 v[2:5], v143 offset:2048
	ds_read_b128 v[6:9], v143 offset:2064
	v_lshlrev_b32_e32 v18, 16, v72
	v_and_b32_e32 v19, 0xffff0000, v72
	v_lshlrev_b32_e32 v20, 16, v73
	s_waitcnt lgkmcnt(1)
	v_pk_mul_f32 v[10:11], v[34:35], v[2:3] op_sel_hi:[0,1]
	v_pk_mul_f32 v[12:13], v[34:35], v[4:5] op_sel_hi:[0,1]
	s_waitcnt lgkmcnt(0)
	v_pk_mul_f32 v[14:15], v[34:35], v[6:7] op_sel_hi:[0,1]
	v_pk_mul_f32 v[16:17], v[34:35], v[8:9] op_sel_hi:[0,1]
	ds_read_b128 v[2:5], v142 offset:2048
	ds_read_b128 v[6:9], v142 offset:2064
	v_and_b32_e32 v21, 0xffff0000, v73
	s_waitcnt lgkmcnt(1)
	v_pk_fma_f32 v[4:5], v[12:13], v[20:21], v[4:5]
	v_pk_fma_f32 v[2:3], v[10:11], v[18:19], v[2:3]
	v_lshlrev_b32_e32 v10, 16, v74
	v_and_b32_e32 v11, 0xffff0000, v74
	v_lshlrev_b32_e32 v12, 16, v75
	v_and_b32_e32 v13, 0xffff0000, v75
	s_waitcnt lgkmcnt(0)
	v_pk_fma_f32 v[8:9], v[16:17], v[12:13], v[8:9]
	v_pk_fma_f32 v[6:7], v[14:15], v[10:11], v[6:7]
	v_cvt_pk_bf16_f32 v2, v2, v3
	v_cvt_pk_bf16_f32 v3, v4, v5
	v_cvt_pk_bf16_f32 v4, v6, v7
	v_cvt_pk_bf16_f32 v5, v8, v9
	global_store_dwordx4 v[134:135], v[2:5], off offset:1024 sc1
	ds_read_b128 v[2:5], v143 offset:2176
	ds_read_b128 v[6:9], v143 offset:2192
	v_lshlrev_b32_e32 v18, 16, v68
	v_and_b32_e32 v19, 0xffff0000, v68
	v_lshlrev_b32_e32 v20, 16, v69
	s_waitcnt lgkmcnt(1)
	v_pk_mul_f32 v[10:11], v[34:35], v[2:3] op_sel_hi:[0,1]
	v_pk_mul_f32 v[12:13], v[34:35], v[4:5] op_sel_hi:[0,1]
	s_waitcnt lgkmcnt(0)
	v_pk_mul_f32 v[14:15], v[34:35], v[6:7] op_sel_hi:[0,1]
	v_pk_mul_f32 v[16:17], v[34:35], v[8:9] op_sel_hi:[0,1]
	ds_read_b128 v[2:5], v142 offset:2176
	ds_read_b128 v[6:9], v142 offset:2192
	v_and_b32_e32 v21, 0xffff0000, v69
	s_waitcnt lgkmcnt(1)
	v_pk_fma_f32 v[4:5], v[12:13], v[20:21], v[4:5]
	v_pk_fma_f32 v[2:3], v[10:11], v[18:19], v[2:3]
	v_lshlrev_b32_e32 v10, 16, v70
	v_and_b32_e32 v11, 0xffff0000, v70
	v_lshlrev_b32_e32 v12, 16, v71
	v_and_b32_e32 v13, 0xffff0000, v71
	s_waitcnt lgkmcnt(0)
	v_pk_fma_f32 v[8:9], v[16:17], v[12:13], v[8:9]
	v_pk_fma_f32 v[6:7], v[14:15], v[10:11], v[6:7]
	v_cvt_pk_bf16_f32 v2, v2, v3
	v_cvt_pk_bf16_f32 v3, v4, v5
	v_cvt_pk_bf16_f32 v4, v6, v7
	v_cvt_pk_bf16_f32 v5, v8, v9
	global_store_dwordx4 v[134:135], v[2:5], off offset:1088 sc1
	ds_read_b128 v[2:5], v143 offset:2304
	ds_read_b128 v[6:9], v143 offset:2320
	v_lshlrev_b32_e32 v18, 16, v80
	v_and_b32_e32 v19, 0xffff0000, v80
	v_lshlrev_b32_e32 v20, 16, v81
	s_waitcnt lgkmcnt(1)
	v_pk_mul_f32 v[10:11], v[34:35], v[2:3] op_sel_hi:[0,1]
	v_pk_mul_f32 v[12:13], v[34:35], v[4:5] op_sel_hi:[0,1]
	s_waitcnt lgkmcnt(0)
	v_pk_mul_f32 v[14:15], v[34:35], v[6:7] op_sel_hi:[0,1]
	v_pk_mul_f32 v[16:17], v[34:35], v[8:9] op_sel_hi:[0,1]
	ds_read_b128 v[2:5], v142 offset:2304
	ds_read_b128 v[6:9], v142 offset:2320
	v_and_b32_e32 v21, 0xffff0000, v81
	s_waitcnt lgkmcnt(1)
; #define LAS __attribute__((address_space(3)))
; __device__ __forceinline__ unsigned pk2(float lo, float hi) { pk2_f32x2 v = {lo, hi}; pk2_bf16x2 b = __builtin_convertvector(v, pk2_bf16x2); return __builtin_bit_cast(unsigned, b); }
; __device__ __forceinline__ f32x4 bf4_lo(const u32x4& v) { return (f32x4){__uint_as_float(v.x << 16), __uint_as_float(v.x & 0xffff0000u), __uint_as_float(v.y << 16), __uint_as_float(v.y & 0xffff0000u)}; }
; __device__ __forceinline__ f32x4 bf4_hi(const u32x4& v) { return (f32x4){__uint_as_float(v.z << 16), __uint_as_float(v.z & 0xffff0000u), __uint_as_float(v.w << 16), __uint_as_float(v.w & 0xffff0000u)}; }
; __device__ __forceinline__ void n2_mfma(const Args& a, LAS unsigned char* lds, int layer) {
;     ...
;         bf16_t* arow = act + (size_t)(row0 + rb_) * D + 8 * gb_;
; #pragma unroll
;         for (int c = 0; c < 16; ++c)
; #pragma unroll
;             for (int i = 0; i < 2; ++i) {
;                 const int col0 = 64 * c + 32 * i;
;                 const LAS f32x4* gp = (const LAS f32x4*)(gaL + col0) + 2 * gb_; const LAS f32x4* sp = (const LAS f32x4*)(s0L + col0) + 2 * gb_;
;                 const f32x4 ga0 = gp[0] * rstd, ga1 = gp[1] * rstd, s00 = sp[0], s01 = sp[1];
;                 const u32x4 xv = xs[2 * c + i];
;                 const f32x4 h0 = bf4_lo(xv) * ga0 + s00, h1 = bf4_hi(xv) * ga1 + s01;
;                 u32x4 o; o.x = pk2(h0.x, h0.y); o.y = pk2(h0.z, h0.w); o.z = pk2(h1.x, h1.y); o.w = pk2(h1.z, h1.w);
;                 *(u32x4*)(arow + col0) = o;
;                 __builtin_amdgcn_sched_barrier(0);
;             }
	v_pk_fma_f32 v[4:5], v[12:13], v[20:21], v[4:5]
	v_pk_fma_f32 v[2:3], v[10:11], v[18:19], v[2:3]
	v_lshlrev_b32_e32 v10, 16, v82
	v_and_b32_e32 v11, 0xffff0000, v82
	v_lshlrev_b32_e32 v12, 16, v83
	v_and_b32_e32 v13, 0xffff0000, v83
	s_waitcnt lgkmcnt(0)
	v_pk_fma_f32 v[8:9], v[16:17], v[12:13], v[8:9]
	v_pk_fma_f32 v[6:7], v[14:15], v[10:11], v[6:7]
	v_cvt_pk_bf16_f32 v2, v2, v3
	v_cvt_pk_bf16_f32 v3, v4, v5
	v_cvt_pk_bf16_f32 v4, v6, v7
	v_cvt_pk_bf16_f32 v5, v8, v9
	global_store_dwordx4 v[134:135], v[2:5], off offset:1152 sc1
	ds_read_b128 v[2:5], v143 offset:2432
	ds_read_b128 v[6:9], v143 offset:2448
	v_lshlrev_b32_e32 v18, 16, v76
	v_and_b32_e32 v19, 0xffff0000, v76
	v_lshlrev_b32_e32 v20, 16, v77
	s_waitcnt lgkmcnt(1)
	v_pk_mul_f32 v[10:11], v[34:35], v[2:3] op_sel_hi:[0,1]
	v_pk_mul_f32 v[12:13], v[34:35], v[4:5] op_sel_hi:[0,1]
	s_waitcnt lgkmcnt(0)
	v_pk_mul_f32 v[14:15], v[34:35], v[6:7] op_sel_hi:[0,1]
	v_pk_mul_f32 v[16:17], v[34:35], v[8:9] op_sel_hi:[0,1]
	ds_read_b128 v[2:5], v142 offset:2432
	ds_read_b128 v[6:9], v142 offset:2448
	v_and_b32_e32 v21, 0xffff0000, v77
	s_waitcnt lgkmcnt(1)
	v_pk_fma_f32 v[4:5], v[12:13], v[20:21], v[4:5]
	v_pk_fma_f32 v[2:3], v[10:11], v[18:19], v[2:3]
	v_lshlrev_b32_e32 v10, 16, v78
	v_and_b32_e32 v11, 0xffff0000, v78
	v_lshlrev_b32_e32 v12, 16, v79
	v_and_b32_e32 v13, 0xffff0000, v79
	s_waitcnt lgkmcnt(0)
	v_pk_fma_f32 v[8:9], v[16:17], v[12:13], v[8:9]
	v_pk_fma_f32 v[6:7], v[14:15], v[10:11], v[6:7]
	v_cvt_pk_bf16_f32 v2, v2, v3
	v_cvt_pk_bf16_f32 v3, v4, v5
	v_cvt_pk_bf16_f32 v4, v6, v7
	v_cvt_pk_bf16_f32 v5, v8, v9
	global_store_dwordx4 v[134:135], v[2:5], off offset:1216 sc1
	ds_read_b128 v[2:5], v143 offset:2560
	ds_read_b128 v[6:9], v143 offset:2576
	v_lshlrev_b32_e32 v18, 16, v88
	v_and_b32_e32 v19, 0xffff0000, v88
	v_lshlrev_b32_e32 v20, 16, v89
	s_waitcnt lgkmcnt(1)
	v_pk_mul_f32 v[10:11], v[34:35], v[2:3] op_sel_hi:[0,1]
	v_pk_mul_f32 v[12:13], v[34:35], v[4:5] op_sel_hi:[0,1]
	s_waitcnt lgkmcnt(0)
	v_pk_mul_f32 v[14:15], v[34:35], v[6:7] op_sel_hi:[0,1]
	v_pk_mul_f32 v[16:17], v[34:35], v[8:9] op_sel_hi:[0,1]
	ds_read_b128 v[2:5], v142 offset:2560
	ds_read_b128 v[6:9], v142 offset:2576
	v_and_b32_e32 v21, 0xffff0000, v89
	s_waitcnt lgkmcnt(1)
	v_pk_fma_f32 v[4:5], v[12:13], v[20:21], v[4:5]
	v_pk_fma_f32 v[2:3], v[10:11], v[18:19], v[2:3]
	v_lshlrev_b32_e32 v10, 16, v90
	v_and_b32_e32 v11, 0xffff0000, v90
	v_lshlrev_b32_e32 v12, 16, v91
	v_and_b32_e32 v13, 0xffff0000, v91
	s_waitcnt lgkmcnt(0)
	v_pk_fma_f32 v[8:9], v[16:17], v[12:13], v[8:9]
	v_pk_fma_f32 v[6:7], v[14:15], v[10:11], v[6:7]
	v_cvt_pk_bf16_f32 v2, v2, v3
	v_cvt_pk_bf16_f32 v3, v4, v5
	v_cvt_pk_bf16_f32 v4, v6, v7
	v_cvt_pk_bf16_f32 v5, v8, v9
	global_store_dwordx4 v[134:135], v[2:5], off offset:1280 sc1
	ds_read_b128 v[2:5], v143 offset:2688
	ds_read_b128 v[6:9], v143 offset:2704
	v_lshlrev_b32_e32 v18, 16, v84
	v_and_b32_e32 v19, 0xffff0000, v84
	v_lshlrev_b32_e32 v20, 16, v85
	s_waitcnt lgkmcnt(1)
	v_pk_mul_f32 v[10:11], v[34:35], v[2:3] op_sel_hi:[0,1]
	v_pk_mul_f32 v[12:13], v[34:35], v[4:5] op_sel_hi:[0,1]
	s_waitcnt lgkmcnt(0)
	v_pk_mul_f32 v[14:15], v[34:35], v[6:7] op_sel_hi:[0,1]
	v_pk_mul_f32 v[16:17], v[34:35], v[8:9] op_sel_hi:[0,1]
	ds_read_b128 v[2:5], v142 offset:2688
	ds_read_b128 v[6:9], v142 offset:2704
	v_and_b32_e32 v21, 0xffff0000, v85
	s_waitcnt lgkmcnt(1)
	v_pk_fma_f32 v[4:5], v[12:13], v[20:21], v[4:5]
	v_pk_fma_f32 v[2:3], v[10:11], v[18:19], v[2:3]
	v_lshlrev_b32_e32 v10, 16, v86
	v_and_b32_e32 v11, 0xffff0000, v86
	v_lshlrev_b32_e32 v12, 16, v87
	v_and_b32_e32 v13, 0xffff0000, v87
	s_waitcnt lgkmcnt(0)
	v_pk_fma_f32 v[8:9], v[16:17], v[12:13], v[8:9]
	v_pk_fma_f32 v[6:7], v[14:15], v[10:11], v[6:7]
	v_cvt_pk_bf16_f32 v2, v2, v3
	v_cvt_pk_bf16_f32 v3, v4, v5
	v_cvt_pk_bf16_f32 v4, v6, v7
	v_cvt_pk_bf16_f32 v5, v8, v9
	global_store_dwordx4 v[134:135], v[2:5], off offset:1344 sc1
	ds_read_b128 v[2:5], v143 offset:2816
	ds_read_b128 v[6:9], v143 offset:2832
	v_lshlrev_b32_e32 v18, 16, v96
	v_and_b32_e32 v19, 0xffff0000, v96
	v_lshlrev_b32_e32 v20, 16, v97
	s_waitcnt lgkmcnt(1)
	v_pk_mul_f32 v[10:11], v[34:35], v[2:3] op_sel_hi:[0,1]
	v_pk_mul_f32 v[12:13], v[34:35], v[4:5] op_sel_hi:[0,1]
	s_waitcnt lgkmcnt(0)
	v_pk_mul_f32 v[14:15], v[34:35], v[6:7] op_sel_hi:[0,1]
	v_pk_mul_f32 v[16:17], v[34:35], v[8:9] op_sel_hi:[0,1]
	ds_read_b128 v[2:5], v142 offset:2816
	ds_read_b128 v[6:9], v142 offset:2832
	v_and_b32_e32 v21, 0xffff0000, v97
	s_waitcnt lgkmcnt(1)
	v_pk_fma_f32 v[4:5], v[12:13], v[20:21], v[4:5]
	v_pk_fma_f32 v[2:3], v[10:11], v[18:19], v[2:3]
	v_lshlrev_b32_e32 v10, 16, v98
	v_and_b32_e32 v11, 0xffff0000, v98
	v_lshlrev_b32_e32 v12, 16, v99
	v_and_b32_e32 v13, 0xffff0000, v99
	s_waitcnt lgkmcnt(0)
	v_pk_fma_f32 v[8:9], v[16:17], v[12:13], v[8:9]
	v_pk_fma_f32 v[6:7], v[14:15], v[10:11], v[6:7]
	v_cvt_pk_bf16_f32 v2, v2, v3
	v_cvt_pk_bf16_f32 v3, v4, v5
	v_cvt_pk_bf16_f32 v4, v6, v7
	v_cvt_pk_bf16_f32 v5, v8, v9
	global_store_dwordx4 v[134:135], v[2:5], off offset:1408 sc1
	ds_read_b128 v[2:5], v143 offset:2944
	ds_read_b128 v[6:9], v143 offset:2960
	v_lshlrev_b32_e32 v18, 16, v92
	v_and_b32_e32 v19, 0xffff0000, v92
	v_lshlrev_b32_e32 v20, 16, v93
	s_waitcnt lgkmcnt(1)
	v_pk_mul_f32 v[10:11], v[34:35], v[2:3] op_sel_hi:[0,1]
	v_pk_mul_f32 v[12:13], v[34:35], v[4:5] op_sel_hi:[0,1]
	s_waitcnt lgkmcnt(0)
	v_pk_mul_f32 v[14:15], v[34:35], v[6:7] op_sel_hi:[0,1]
	v_pk_mul_f32 v[16:17], v[34:35], v[8:9] op_sel_hi:[0,1]
	ds_read_b128 v[2:5], v142 offset:2944
	ds_read_b128 v[6:9], v142 offset:2960
	v_and_b32_e32 v21, 0xffff0000, v93
	s_waitcnt lgkmcnt(1)
; #define LAS __attribute__((address_space(3)))
; __device__ __forceinline__ unsigned pk2(float lo, float hi) { pk2_f32x2 v = {lo, hi}; pk2_bf16x2 b = __builtin_convertvector(v, pk2_bf16x2); return __builtin_bit_cast(unsigned, b); }
; __device__ __forceinline__ f32x4 bf4_lo(const u32x4& v) { return (f32x4){__uint_as_float(v.x << 16), __uint_as_float(v.x & 0xffff0000u), __uint_as_float(v.y << 16), __uint_as_float(v.y & 0xffff0000u)}; }
; __device__ __forceinline__ f32x4 bf4_hi(const u32x4& v) { return (f32x4){__uint_as_float(v.z << 16), __uint_as_float(v.z & 0xffff0000u), __uint_as_float(v.w << 16), __uint_as_float(v.w & 0xffff0000u)}; }
; __device__ __forceinline__ void n2_mfma(const Args& a, LAS unsigned char* lds, int layer) {
;     ...
;         bf16_t* arow = act + (size_t)(row0 + rb_) * D + 8 * gb_;
; #pragma unroll
;         for (int c = 0; c < 16; ++c)
; #pragma unroll
;             for (int i = 0; i < 2; ++i) {
;                 const int col0 = 64 * c + 32 * i;
;                 const LAS f32x4* gp = (const LAS f32x4*)(gaL + col0) + 2 * gb_; const LAS f32x4* sp = (const LAS f32x4*)(s0L + col0) + 2 * gb_;
;                 const f32x4 ga0 = gp[0] * rstd, ga1 = gp[1] * rstd, s00 = sp[0], s01 = sp[1];
;                 const u32x4 xv = xs[2 * c + i];
;                 const f32x4 h0 = bf4_lo(xv) * ga0 + s00, h1 = bf4_hi(xv) * ga1 + s01;
;                 u32x4 o; o.x = pk2(h0.x, h0.y); o.y = pk2(h0.z, h0.w); o.z = pk2(h1.x, h1.y); o.w = pk2(h1.z, h1.w);
;                 *(u32x4*)(arow + col0) = o;
;                 __builtin_amdgcn_sched_barrier(0);
;             }
	v_pk_fma_f32 v[4:5], v[12:13], v[20:21], v[4:5]
	v_pk_fma_f32 v[2:3], v[10:11], v[18:19], v[2:3]
	v_lshlrev_b32_e32 v10, 16, v94
	v_and_b32_e32 v11, 0xffff0000, v94
	v_lshlrev_b32_e32 v12, 16, v95
	v_and_b32_e32 v13, 0xffff0000, v95
	s_waitcnt lgkmcnt(0)
	v_pk_fma_f32 v[8:9], v[16:17], v[12:13], v[8:9]
	v_pk_fma_f32 v[6:7], v[14:15], v[10:11], v[6:7]
	v_cvt_pk_bf16_f32 v2, v2, v3
	v_cvt_pk_bf16_f32 v3, v4, v5
	v_cvt_pk_bf16_f32 v4, v6, v7
	v_cvt_pk_bf16_f32 v5, v8, v9
	global_store_dwordx4 v[134:135], v[2:5], off offset:1472 sc1
	ds_read_b128 v[2:5], v143 offset:3072
	ds_read_b128 v[6:9], v143 offset:3088
	v_lshlrev_b32_e32 v18, 16, v104
	v_and_b32_e32 v19, 0xffff0000, v104
	v_lshlrev_b32_e32 v20, 16, v105
	s_waitcnt lgkmcnt(1)
	v_pk_mul_f32 v[10:11], v[34:35], v[2:3] op_sel_hi:[0,1]
	v_pk_mul_f32 v[12:13], v[34:35], v[4:5] op_sel_hi:[0,1]
	s_waitcnt lgkmcnt(0)
	v_pk_mul_f32 v[14:15], v[34:35], v[6:7] op_sel_hi:[0,1]
	v_pk_mul_f32 v[16:17], v[34:35], v[8:9] op_sel_hi:[0,1]
	ds_read_b128 v[2:5], v142 offset:3072
	ds_read_b128 v[6:9], v142 offset:3088
	v_and_b32_e32 v21, 0xffff0000, v105
	s_waitcnt lgkmcnt(1)
	v_pk_fma_f32 v[4:5], v[12:13], v[20:21], v[4:5]
	v_pk_fma_f32 v[2:3], v[10:11], v[18:19], v[2:3]
	v_lshlrev_b32_e32 v10, 16, v106
	v_and_b32_e32 v11, 0xffff0000, v106
	v_lshlrev_b32_e32 v12, 16, v107
	v_and_b32_e32 v13, 0xffff0000, v107
	s_waitcnt lgkmcnt(0)
	v_pk_fma_f32 v[8:9], v[16:17], v[12:13], v[8:9]
	v_pk_fma_f32 v[6:7], v[14:15], v[10:11], v[6:7]
	v_cvt_pk_bf16_f32 v2, v2, v3
	v_cvt_pk_bf16_f32 v3, v4, v5
	v_cvt_pk_bf16_f32 v4, v6, v7
	v_cvt_pk_bf16_f32 v5, v8, v9
	global_store_dwordx4 v[134:135], v[2:5], off offset:1536 sc1
	ds_read_b128 v[2:5], v143 offset:3200
	ds_read_b128 v[6:9], v143 offset:3216
	v_lshlrev_b32_e32 v18, 16, v100
	v_and_b32_e32 v19, 0xffff0000, v100
	v_lshlrev_b32_e32 v20, 16, v101
	s_waitcnt lgkmcnt(1)
	v_pk_mul_f32 v[10:11], v[34:35], v[2:3] op_sel_hi:[0,1]
	v_pk_mul_f32 v[12:13], v[34:35], v[4:5] op_sel_hi:[0,1]
	s_waitcnt lgkmcnt(0)
	v_pk_mul_f32 v[14:15], v[34:35], v[6:7] op_sel_hi:[0,1]
	v_pk_mul_f32 v[16:17], v[34:35], v[8:9] op_sel_hi:[0,1]
	ds_read_b128 v[2:5], v142 offset:3200
	ds_read_b128 v[6:9], v142 offset:3216
	v_and_b32_e32 v21, 0xffff0000, v101
	s_waitcnt lgkmcnt(1)
	v_pk_fma_f32 v[4:5], v[12:13], v[20:21], v[4:5]
	v_pk_fma_f32 v[2:3], v[10:11], v[18:19], v[2:3]
	v_lshlrev_b32_e32 v10, 16, v102
	v_and_b32_e32 v11, 0xffff0000, v102
	v_lshlrev_b32_e32 v12, 16, v103
	v_and_b32_e32 v13, 0xffff0000, v103
	s_waitcnt lgkmcnt(0)
	v_pk_fma_f32 v[8:9], v[16:17], v[12:13], v[8:9]
	v_pk_fma_f32 v[6:7], v[14:15], v[10:11], v[6:7]
	v_cvt_pk_bf16_f32 v2, v2, v3
	v_cvt_pk_bf16_f32 v3, v4, v5
	v_cvt_pk_bf16_f32 v4, v6, v7
	v_cvt_pk_bf16_f32 v5, v8, v9
	global_store_dwordx4 v[134:135], v[2:5], off offset:1600 sc1
	ds_read_b128 v[2:5], v143 offset:3328
	ds_read_b128 v[6:9], v143 offset:3344
	v_lshlrev_b32_e32 v18, 16, v112
	v_and_b32_e32 v19, 0xffff0000, v112
	v_lshlrev_b32_e32 v20, 16, v113
	s_waitcnt lgkmcnt(1)
	v_pk_mul_f32 v[10:11], v[34:35], v[2:3] op_sel_hi:[0,1]
	v_pk_mul_f32 v[12:13], v[34:35], v[4:5] op_sel_hi:[0,1]
	s_waitcnt lgkmcnt(0)
	v_pk_mul_f32 v[14:15], v[34:35], v[6:7] op_sel_hi:[0,1]
	v_pk_mul_f32 v[16:17], v[34:35], v[8:9] op_sel_hi:[0,1]
	ds_read_b128 v[2:5], v142 offset:3328
	ds_read_b128 v[6:9], v142 offset:3344
	v_and_b32_e32 v21, 0xffff0000, v113
	s_waitcnt lgkmcnt(1)
	v_pk_fma_f32 v[4:5], v[12:13], v[20:21], v[4:5]
	v_pk_fma_f32 v[2:3], v[10:11], v[18:19], v[2:3]
	v_lshlrev_b32_e32 v10, 16, v114
	v_and_b32_e32 v11, 0xffff0000, v114
	v_lshlrev_b32_e32 v12, 16, v115
	v_and_b32_e32 v13, 0xffff0000, v115
	s_waitcnt lgkmcnt(0)
	v_pk_fma_f32 v[8:9], v[16:17], v[12:13], v[8:9]
	v_pk_fma_f32 v[6:7], v[14:15], v[10:11], v[6:7]
	v_cvt_pk_bf16_f32 v2, v2, v3
	v_cvt_pk_bf16_f32 v3, v4, v5
	v_cvt_pk_bf16_f32 v4, v6, v7
	v_cvt_pk_bf16_f32 v5, v8, v9
	global_store_dwordx4 v[134:135], v[2:5], off offset:1664 sc1
	ds_read_b128 v[2:5], v143 offset:3456
	ds_read_b128 v[6:9], v143 offset:3472
	v_lshlrev_b32_e32 v18, 16, v108
	v_and_b32_e32 v19, 0xffff0000, v108
	v_lshlrev_b32_e32 v20, 16, v109
	s_waitcnt lgkmcnt(1)
	v_pk_mul_f32 v[10:11], v[34:35], v[2:3] op_sel_hi:[0,1]
	v_pk_mul_f32 v[12:13], v[34:35], v[4:5] op_sel_hi:[0,1]
	s_waitcnt lgkmcnt(0)
	v_pk_mul_f32 v[14:15], v[34:35], v[6:7] op_sel_hi:[0,1]
	v_pk_mul_f32 v[16:17], v[34:35], v[8:9] op_sel_hi:[0,1]
	ds_read_b128 v[2:5], v142 offset:3456
	ds_read_b128 v[6:9], v142 offset:3472
	v_and_b32_e32 v21, 0xffff0000, v109
	s_waitcnt lgkmcnt(1)
	v_pk_fma_f32 v[4:5], v[12:13], v[20:21], v[4:5]
	v_pk_fma_f32 v[2:3], v[10:11], v[18:19], v[2:3]
	v_lshlrev_b32_e32 v10, 16, v110
	v_and_b32_e32 v11, 0xffff0000, v110
	v_lshlrev_b32_e32 v12, 16, v111
	v_and_b32_e32 v13, 0xffff0000, v111
	s_waitcnt lgkmcnt(0)
	v_pk_fma_f32 v[8:9], v[16:17], v[12:13], v[8:9]
	v_pk_fma_f32 v[6:7], v[14:15], v[10:11], v[6:7]
	v_cvt_pk_bf16_f32 v2, v2, v3
	v_cvt_pk_bf16_f32 v3, v4, v5
	v_cvt_pk_bf16_f32 v4, v6, v7
	v_cvt_pk_bf16_f32 v5, v8, v9
	global_store_dwordx4 v[134:135], v[2:5], off offset:1728 sc1
	ds_read_b128 v[2:5], v143 offset:3584
	ds_read_b128 v[6:9], v143 offset:3600
	v_lshlrev_b32_e32 v18, 16, v120
	v_and_b32_e32 v19, 0xffff0000, v120
	v_lshlrev_b32_e32 v20, 16, v121
	s_waitcnt lgkmcnt(1)
	v_pk_mul_f32 v[10:11], v[34:35], v[2:3] op_sel_hi:[0,1]
	v_pk_mul_f32 v[12:13], v[34:35], v[4:5] op_sel_hi:[0,1]
	s_waitcnt lgkmcnt(0)
	v_pk_mul_f32 v[14:15], v[34:35], v[6:7] op_sel_hi:[0,1]
	v_pk_mul_f32 v[16:17], v[34:35], v[8:9] op_sel_hi:[0,1]
	ds_read_b128 v[2:5], v142 offset:3584
	ds_read_b128 v[6:9], v142 offset:3600
	v_and_b32_e32 v21, 0xffff0000, v121
	s_waitcnt lgkmcnt(1)
; #define LAS __attribute__((address_space(3)))
; __device__ __forceinline__ unsigned pk2(float lo, float hi) { pk2_f32x2 v = {lo, hi}; pk2_bf16x2 b = __builtin_convertvector(v, pk2_bf16x2); return __builtin_bit_cast(unsigned, b); }
; __device__ __forceinline__ f32x4 bf4_lo(const u32x4& v) { return (f32x4){__uint_as_float(v.x << 16), __uint_as_float(v.x & 0xffff0000u), __uint_as_float(v.y << 16), __uint_as_float(v.y & 0xffff0000u)}; }
; __device__ __forceinline__ f32x4 bf4_hi(const u32x4& v) { return (f32x4){__uint_as_float(v.z << 16), __uint_as_float(v.z & 0xffff0000u), __uint_as_float(v.w << 16), __uint_as_float(v.w & 0xffff0000u)}; }
; __device__ __forceinline__ void n2_mfma(const Args& a, LAS unsigned char* lds, int layer) {
;     ...
; #pragma unroll
;         for (int c = 0; c < 16; ++c)
; #pragma unroll
;             for (int i = 0; i < 2; ++i) {
;                 const int col0 = 64 * c + 32 * i;
;                 const LAS f32x4* gp = (const LAS f32x4*)(gaL + col0) + 2 * gb_; const LAS f32x4* sp = (const LAS f32x4*)(s0L + col0) + 2 * gb_;
;                 const f32x4 ga0 = gp[0] * rstd, ga1 = gp[1] * rstd, s00 = sp[0], s01 = sp[1];
;                 const u32x4 xv = xs[2 * c + i];
;                 const f32x4 h0 = bf4_lo(xv) * ga0 + s00, h1 = bf4_hi(xv) * ga1 + s01;
;                 u32x4 o; o.x = pk2(h0.x, h0.y); o.y = pk2(h0.z, h0.w); o.z = pk2(h1.x, h1.y); o.w = pk2(h1.z, h1.w);
;                 *(u32x4*)(arow + col0) = o;
;                 __builtin_amdgcn_sched_barrier(0);
;             }
;     ...
;         if (lane_c < 16) {
;             const int lane = lane_c;
;             float lg[16];
; #pragma unroll
;             for (int q = 0; q < 4; ++q) { const f32x4 t4 = *(const LAS f32x4*)(lgw + (wave * 16 + lane) * 16 + 4 * q); const f32x4 rb4 = *(const f32x4*)(a.in[I_RB] + 4 * q);
;                 lg[4 * q] = t4.x + rb4.x; lg[4 * q + 1] = t4.y + rb4.y; lg[4 * q + 2] = t4.z + rb4.z; lg[4 * q + 3] = t4.w + rb4.w; }
;             float mx = lg[0];
; #pragma unroll
;             for (int e = 1; e < 16; ++e) mx = fmaxf(mx, lg[e]);
	v_pk_fma_f32 v[4:5], v[12:13], v[20:21], v[4:5]
	v_pk_fma_f32 v[2:3], v[10:11], v[18:19], v[2:3]
	v_lshlrev_b32_e32 v10, 16, v122
	v_and_b32_e32 v11, 0xffff0000, v122
	v_lshlrev_b32_e32 v12, 16, v123
	v_and_b32_e32 v13, 0xffff0000, v123
	s_waitcnt lgkmcnt(0)
	v_pk_fma_f32 v[8:9], v[16:17], v[12:13], v[8:9]
	v_pk_fma_f32 v[6:7], v[14:15], v[10:11], v[6:7]
	v_cvt_pk_bf16_f32 v2, v2, v3
	v_cvt_pk_bf16_f32 v3, v4, v5
	v_cvt_pk_bf16_f32 v4, v6, v7
	v_cvt_pk_bf16_f32 v5, v8, v9
	global_store_dwordx4 v[134:135], v[2:5], off offset:1792 sc1
	ds_read_b128 v[2:5], v143 offset:3712
	ds_read_b128 v[6:9], v143 offset:3728
	v_lshlrev_b32_e32 v18, 16, v116
	v_and_b32_e32 v19, 0xffff0000, v116
	v_lshlrev_b32_e32 v20, 16, v117
	s_waitcnt lgkmcnt(1)
	v_pk_mul_f32 v[10:11], v[34:35], v[2:3] op_sel_hi:[0,1]
	v_pk_mul_f32 v[12:13], v[34:35], v[4:5] op_sel_hi:[0,1]
	s_waitcnt lgkmcnt(0)
	v_pk_mul_f32 v[14:15], v[34:35], v[6:7] op_sel_hi:[0,1]
	v_pk_mul_f32 v[16:17], v[34:35], v[8:9] op_sel_hi:[0,1]
	ds_read_b128 v[2:5], v142 offset:3712
	ds_read_b128 v[6:9], v142 offset:3728
	v_and_b32_e32 v21, 0xffff0000, v117
	s_waitcnt lgkmcnt(1)
	v_pk_fma_f32 v[4:5], v[12:13], v[20:21], v[4:5]
	v_pk_fma_f32 v[2:3], v[10:11], v[18:19], v[2:3]
	v_lshlrev_b32_e32 v10, 16, v118
	v_and_b32_e32 v11, 0xffff0000, v118
	v_lshlrev_b32_e32 v12, 16, v119
	v_and_b32_e32 v13, 0xffff0000, v119
	s_waitcnt lgkmcnt(0)
	v_pk_fma_f32 v[8:9], v[16:17], v[12:13], v[8:9]
	v_pk_fma_f32 v[6:7], v[14:15], v[10:11], v[6:7]
	v_cvt_pk_bf16_f32 v2, v2, v3
	v_cvt_pk_bf16_f32 v3, v4, v5
	v_cvt_pk_bf16_f32 v4, v6, v7
	v_cvt_pk_bf16_f32 v5, v8, v9
	global_store_dwordx4 v[134:135], v[2:5], off offset:1856 sc1
	ds_read_b128 v[2:5], v143 offset:3840
	ds_read_b128 v[6:9], v143 offset:3856
	v_lshlrev_b32_e32 v18, 16, v128
	v_and_b32_e32 v19, 0xffff0000, v128
	v_lshlrev_b32_e32 v20, 16, v129
	s_waitcnt lgkmcnt(1)
	v_pk_mul_f32 v[10:11], v[34:35], v[2:3] op_sel_hi:[0,1]
	v_pk_mul_f32 v[12:13], v[34:35], v[4:5] op_sel_hi:[0,1]
	s_waitcnt lgkmcnt(0)
	v_pk_mul_f32 v[14:15], v[34:35], v[6:7] op_sel_hi:[0,1]
	v_pk_mul_f32 v[16:17], v[34:35], v[8:9] op_sel_hi:[0,1]
	ds_read_b128 v[2:5], v142 offset:3840
	ds_read_b128 v[6:9], v142 offset:3856
	v_and_b32_e32 v21, 0xffff0000, v129
	s_waitcnt lgkmcnt(1)
	v_pk_fma_f32 v[4:5], v[12:13], v[20:21], v[4:5]
	v_pk_fma_f32 v[2:3], v[10:11], v[18:19], v[2:3]
	v_lshlrev_b32_e32 v10, 16, v130
	v_and_b32_e32 v11, 0xffff0000, v130
	v_lshlrev_b32_e32 v12, 16, v131
	v_and_b32_e32 v13, 0xffff0000, v131
	s_waitcnt lgkmcnt(0)
	v_pk_fma_f32 v[8:9], v[16:17], v[12:13], v[8:9]
	v_pk_fma_f32 v[6:7], v[14:15], v[10:11], v[6:7]
	v_cvt_pk_bf16_f32 v2, v2, v3
	v_cvt_pk_bf16_f32 v3, v4, v5
	v_cvt_pk_bf16_f32 v4, v6, v7
	v_cvt_pk_bf16_f32 v5, v8, v9
	global_store_dwordx4 v[134:135], v[2:5], off offset:1920 sc1
	ds_read_b128 v[2:5], v143 offset:3968
	ds_read_b128 v[6:9], v143 offset:3984
	v_lshlrev_b32_e32 v18, 16, v124
	v_and_b32_e32 v19, 0xffff0000, v124
	v_lshlrev_b32_e32 v20, 16, v125
	s_waitcnt lgkmcnt(1)
	v_pk_mul_f32 v[10:11], v[34:35], v[2:3] op_sel_hi:[0,1]
	v_pk_mul_f32 v[12:13], v[34:35], v[4:5] op_sel_hi:[0,1]
	s_waitcnt lgkmcnt(0)
	v_pk_mul_f32 v[14:15], v[34:35], v[6:7] op_sel_hi:[0,1]
	v_pk_mul_f32 v[16:17], v[34:35], v[8:9] op_sel_hi:[0,1]
	ds_read_b128 v[2:5], v142 offset:3968
	ds_read_b128 v[6:9], v142 offset:3984
	v_and_b32_e32 v21, 0xffff0000, v125
	s_waitcnt lgkmcnt(1)
	v_pk_fma_f32 v[4:5], v[12:13], v[20:21], v[4:5]
	v_pk_fma_f32 v[2:3], v[10:11], v[18:19], v[2:3]
	v_lshlrev_b32_e32 v10, 16, v126
	v_and_b32_e32 v11, 0xffff0000, v126
	v_lshlrev_b32_e32 v12, 16, v127
	v_and_b32_e32 v13, 0xffff0000, v127
	s_waitcnt lgkmcnt(0)
	v_pk_fma_f32 v[8:9], v[16:17], v[12:13], v[8:9]
	v_pk_fma_f32 v[6:7], v[14:15], v[10:11], v[6:7]
	v_cvt_pk_bf16_f32 v2, v2, v3
	v_cvt_pk_bf16_f32 v3, v4, v5
	v_cvt_pk_bf16_f32 v4, v6, v7
	v_cvt_pk_bf16_f32 v5, v8, v9
	global_store_dwordx4 v[134:135], v[2:5], off offset:1984 sc1
	s_waitcnt lgkmcnt(0)
	s_nop 1
	v_mov_b32_e32 v2, v1
	s_nop 0
	v_cmp_gt_i32_e32 vcc, 16, v2
	s_and_saveexec_b64 s[20:21], vcc
	s_cbranch_execz .LBB0_813
	v_readlane_b32 s12, v252, 41
	v_readlane_b32 s18, v252, 47
	v_readlane_b32 s19, v252, 48
	s_nop 4
	global_load_dwordx4 v[4:7], v35, s[18:19]
	global_load_dwordx4 v[8:11], v35, s[18:19] offset:16
	global_load_dwordx4 v[16:19], v35, s[18:19] offset:32
	global_load_dwordx4 v[20:23], v35, s[18:19] offset:48
	v_add_u32_e32 v14, s66, v2
	v_lshl_add_u32 v2, v14, 6, 0
	v_add_u32_e32 v2, 0x10000, v2
	ds_read_b128 v[24:27], v2
	ds_read_b128 v[28:31], v2 offset:16
	ds_read_b128 v[36:39], v2 offset:32
	ds_read_b128 v[40:43], v2 offset:48
	v_readlane_b32 s13, v252, 42
	s_mov_b32 s12, 0x3fb8aa3b
	s_mov_b32 s13, 0x3f8147ae
	v_readlane_b32 s16, v252, 45
	v_readlane_b32 s17, v252, 46
	v_readlane_b32 s14, v252, 43
	v_readlane_b32 s15, v252, 44
	s_waitcnt vmcnt(3) lgkmcnt(3)
	v_add_f32_e32 v2, v24, v4
	v_add_f32_e32 v3, v25, v5
	v_add_f32_e32 v4, v26, v6
	v_add_f32_e32 v5, v27, v7
	s_waitcnt vmcnt(2) lgkmcnt(2)
	v_add_f32_e32 v6, v28, v8
	v_add_f32_e32 v8, v30, v10
	v_max_f32_e32 v10, v2, v3
	v_add_f32_e32 v7, v29, v9
	v_max3_f32 v10, v10, v4, v5
	v_add_f32_e32 v9, v31, v11
	v_max3_f32 v10, v10, v6, v7
	s_waitcnt vmcnt(1) lgkmcnt(1)
	v_add_f32_e32 v11, v36, v16
	v_add_f32_e32 v12, v37, v17
	v_max3_f32 v10, v10, v8, v9
	v_add_f32_e32 v13, v38, v18
	v_add_f32_e32 v15, v39, v19
	v_max3_f32 v10, v10, v11, v12
	s_waitcnt vmcnt(0) lgkmcnt(0)
; __device__ __forceinline__ void n2_mfma(const Args& a, LAS unsigned char* lds, int layer) {
;     ...
;             float p[16], sum = 0.f;
; #pragma unroll
;             for (int e = 0; e < 16; ++e) { p[e] = expf(lg[e] - mx); sum += p[e]; }
;             const float inv = 1.f / sum;
; #pragma unroll
;             for (int e = 0; e < 16; ++e) p[e] *= inv;
	v_add_f32_e32 v16, v40, v20
	v_add_f32_e32 v17, v41, v21
	v_max3_f32 v10, v10, v13, v15
	v_add_f32_e32 v20, v42, v22
	v_add_f32_e32 v21, v43, v23
	v_max3_f32 v10, v10, v16, v17
	v_max3_f32 v22, v10, v20, v21
	v_sub_f32_e32 v2, v2, v22
	v_sub_f32_e32 v3, v3, v22
	v_sub_f32_e32 v10, v4, v22
	v_mul_f32_e32 v4, 0x3fb8aa3b, v2
	v_sub_f32_e32 v18, v5, v22
	v_mul_f32_e32 v5, 0x3fb8aa3b, v3
	v_fma_f32 v25, v2, s12, -v4
	v_rndne_f32_e32 v26, v4
	v_mul_f32_e32 v19, 0x3fb8aa3b, v10
	v_fma_f32 v27, v3, s12, -v5
	v_rndne_f32_e32 v28, v5
	v_fmac_f32_e32 v25, 0x32a5705f, v2
	v_sub_f32_e32 v4, v4, v26
	v_mul_f32_e32 v23, 0x3fb8aa3b, v18
	v_fma_f32 v29, v10, s12, -v19
	v_rndne_f32_e32 v30, v19
	v_fmac_f32_e32 v27, 0x32a5705f, v3
	v_sub_f32_e32 v5, v5, v28
	v_add_f32_e32 v4, v4, v25
	v_fma_f32 v31, v18, s12, -v23
	v_rndne_f32_e32 v32, v23
	v_cvt_i32_f32_e32 v26, v26
	v_fmac_f32_e32 v29, 0x32a5705f, v10
	v_sub_f32_e32 v19, v19, v30
	v_add_f32_e32 v5, v5, v27
	v_exp_f32_e32 v4, v4
	v_cvt_i32_f32_e32 v28, v28
	v_fmac_f32_e32 v31, 0x32a5705f, v18
	v_sub_f32_e32 v23, v23, v32
	v_add_f32_e32 v19, v19, v29
	v_exp_f32_e32 v5, v5
	v_cvt_i32_f32_e32 v30, v30
	v_add_f32_e32 v23, v23, v31
	v_exp_f32_e32 v19, v19
	v_cvt_i32_f32_e32 v32, v32
	v_exp_f32_e32 v23, v23
	v_ldexp_f32 v4, v4, v26
	v_cmp_ngt_f32_e32 vcc, s65, v2
	v_ldexp_f32 v5, v5, v28
	v_ldexp_f32 v19, v19, v30
	v_cndmask_b32_e32 v4, 0, v4, vcc
	v_cmp_ngt_f32_e32 vcc, s65, v3
	v_sub_f32_e32 v6, v6, v22
	v_ldexp_f32 v23, v23, v32
	v_cndmask_b32_e32 v25, 0, v5, vcc
	v_cmp_ngt_f32_e32 vcc, s65, v10
	v_mul_f32_e32 v24, 0x3fb8aa3b, v6
	v_fma_f32 v33, v6, s12, -v24
	v_cndmask_b32_e32 v19, 0, v19, vcc
	v_cmp_ngt_f32_e32 vcc, s65, v18
	v_rndne_f32_e32 v34, v24
	v_sub_f32_e32 v7, v7, v22
	v_cndmask_b32_e32 v23, 0, v23, vcc
	v_cmp_nlt_f32_e32 vcc, s3, v2
	v_fmac_f32_e32 v33, 0x32a5705f, v6
	v_sub_f32_e32 v24, v24, v34
	v_cndmask_b32_e32 v5, v239, v4, vcc
	v_cmp_nlt_f32_e32 vcc, s3, v3
	v_add_f32_e32 v24, v24, v33
	v_cvt_i32_f32_e32 v34, v34
	v_cndmask_b32_e32 v4, v239, v25, vcc
	v_cmp_nlt_f32_e32 vcc, s3, v10
	v_mul_f32_e32 v10, 0x3fb8aa3b, v7
	v_exp_f32_e32 v24, v24
	v_cndmask_b32_e32 v25, v239, v19, vcc
	v_cmp_nlt_f32_e32 vcc, s3, v18
	v_fma_f32 v18, v7, s12, -v10
	v_rndne_f32_e32 v19, v10
	v_fmac_f32_e32 v18, 0x32a5705f, v7
	v_sub_f32_e32 v10, v10, v19
	v_add_f32_e32 v10, v10, v18
	v_exp_f32_e32 v10, v10
	v_cvt_i32_f32_e32 v18, v19
	v_ldexp_f32 v24, v24, v34
	v_cndmask_b32_e32 v26, v239, v23, vcc
	v_cmp_ngt_f32_e32 vcc, s65, v6
	v_sub_f32_e32 v8, v8, v22
	v_sub_f32_e32 v9, v9, v22
	v_cndmask_b32_e32 v3, 0, v24, vcc
	v_cmp_nlt_f32_e32 vcc, s3, v6
	v_add_f32_e32 v2, v5, v4
	v_add_f32_e32 v2, v25, v2
	v_cndmask_b32_e32 v6, v239, v3, vcc
	v_ldexp_f32 v3, v10, v18
	v_mul_f32_e32 v10, 0x3fb8aa3b, v8
	v_fma_f32 v18, v8, s12, -v10
	v_rndne_f32_e32 v19, v10
	v_fmac_f32_e32 v18, 0x32a5705f, v8
	v_sub_f32_e32 v10, v10, v19
	v_add_f32_e32 v10, v10, v18
	v_exp_f32_e32 v10, v10
	v_cvt_i32_f32_e32 v18, v19
	v_cmp_ngt_f32_e32 vcc, s65, v7
	v_add_f32_e32 v2, v26, v2
	v_add_f32_e32 v2, v6, v2
	v_cndmask_b32_e32 v3, 0, v3, vcc
	v_cmp_nlt_f32_e32 vcc, s3, v7
	s_nop 1
	v_cndmask_b32_e32 v7, v239, v3, vcc
	v_ldexp_f32 v3, v10, v18
	v_mul_f32_e32 v10, 0x3fb8aa3b, v9
	v_fma_f32 v18, v9, s12, -v10
	v_rndne_f32_e32 v19, v10
	v_fmac_f32_e32 v18, 0x32a5705f, v9
	v_sub_f32_e32 v10, v10, v19
	v_add_f32_e32 v10, v10, v18
	v_exp_f32_e32 v18, v10
	v_cvt_i32_f32_e32 v19, v19
	v_cmp_ngt_f32_e32 vcc, s65, v8
	v_add_f32_e32 v2, v7, v2
	s_nop 0
	v_cndmask_b32_e32 v3, 0, v3, vcc
	v_cmp_nlt_f32_e32 vcc, s3, v8
	v_sub_f32_e32 v8, v11, v22
	v_mul_f32_e32 v11, 0x3fb8aa3b, v8
	v_cndmask_b32_e32 v10, v239, v3, vcc
	v_ldexp_f32 v3, v18, v19
	v_fma_f32 v18, v8, s12, -v11
	v_rndne_f32_e32 v19, v11
	v_fmac_f32_e32 v18, 0x32a5705f, v8
	v_sub_f32_e32 v11, v11, v19
	v_add_f32_e32 v11, v11, v18
	v_exp_f32_e32 v18, v11
	v_cvt_i32_f32_e32 v19, v19
	v_cmp_ngt_f32_e32 vcc, s65, v9
	v_add_f32_e32 v2, v10, v2
	s_nop 0
	v_cndmask_b32_e32 v3, 0, v3, vcc
	v_cmp_nlt_f32_e32 vcc, s3, v9
	v_sub_f32_e32 v9, v12, v22
	v_mul_f32_e32 v12, 0x3fb8aa3b, v9
	v_cndmask_b32_e32 v11, v239, v3, vcc
	v_ldexp_f32 v3, v18, v19
	v_fma_f32 v18, v9, s12, -v12
	v_rndne_f32_e32 v19, v12
	v_fmac_f32_e32 v18, 0x32a5705f, v9
	v_sub_f32_e32 v12, v12, v19
	v_add_f32_e32 v12, v12, v18
	v_exp_f32_e32 v18, v12
	v_cvt_i32_f32_e32 v19, v19
	v_cmp_ngt_f32_e32 vcc, s65, v8
	v_add_f32_e32 v2, v11, v2
	s_nop 0
	v_cndmask_b32_e32 v3, 0, v3, vcc
	v_cmp_nlt_f32_e32 vcc, s3, v8
	v_sub_f32_e32 v8, v13, v22
	v_mul_f32_e32 v13, 0x3fb8aa3b, v8
	v_cndmask_b32_e32 v12, v239, v3, vcc
; __device__ __forceinline__ void n2_mfma(const Args& a, LAS unsigned char* lds, int layer) {
;     ...
;             for (int e = 0; e < 16; ++e) { p[e] = expf(lg[e] - mx); sum += p[e]; }
;             const float inv = 1.f / sum;
; #pragma unroll
;             for (int e = 0; e < 16; ++e) p[e] *= inv;
;             int bg = 0, bi0 = 0, bi1 = 1; float bscore = -1.f, bp0 = 0.f, bp1 = 0.f;
; #pragma unroll
;             for (int gq = 0; gq < 4; ++gq) {
;                 int i0 = 0; float p0 = p[4 * gq];
; #pragma unroll
;                 for (int k = 1; k < 4; ++k) if (p[4 * gq + k] > p0) { p0 = p[4 * gq + k]; i0 = k; }
;                 int i1 = -1; float p1 = -1.f;
; #pragma unroll
;                 for (int k = 0; k < 4; ++k) if (k != i0 && p[4 * gq + k] > p1) { p1 = p[4 * gq + k]; i1 = k; }
;                 const float sc2 = p0 + p1;
;                 if (sc2 > bscore) { bscore = sc2; bg = gq; bi0 = i0; bi1 = i1; bp0 = p0; bp1 = p1; }
;             }
;             const float gs = 1.f / (bp0 + bp1);
	v_ldexp_f32 v3, v18, v19
	v_fma_f32 v18, v8, s12, -v13
	v_rndne_f32_e32 v19, v13
	v_fmac_f32_e32 v18, 0x32a5705f, v8
	v_sub_f32_e32 v13, v13, v19
	v_add_f32_e32 v13, v13, v18
	v_exp_f32_e32 v18, v13
	v_cvt_i32_f32_e32 v19, v19
	v_cmp_ngt_f32_e32 vcc, s65, v9
	v_add_f32_e32 v2, v12, v2
	s_nop 0
	v_cndmask_b32_e32 v3, 0, v3, vcc
	v_cmp_nlt_f32_e32 vcc, s3, v9
	v_sub_f32_e32 v9, v15, v22
	v_mul_f32_e32 v15, 0x3fb8aa3b, v9
	v_cndmask_b32_e32 v13, v239, v3, vcc
	v_ldexp_f32 v3, v18, v19
	v_fma_f32 v18, v9, s12, -v15
	v_rndne_f32_e32 v19, v15
	v_fmac_f32_e32 v18, 0x32a5705f, v9
	v_sub_f32_e32 v15, v15, v19
	v_add_f32_e32 v15, v15, v18
	v_exp_f32_e32 v15, v15
	v_cvt_i32_f32_e32 v19, v19
	v_cmp_ngt_f32_e32 vcc, s65, v8
	v_add_f32_e32 v2, v13, v2
	s_nop 0
	v_cndmask_b32_e32 v3, 0, v3, vcc
	v_cmp_nlt_f32_e32 vcc, s3, v8
	v_sub_f32_e32 v8, v16, v22
	s_nop 0
	v_cndmask_b32_e32 v18, v239, v3, vcc
	v_ldexp_f32 v3, v15, v19
	v_mul_f32_e32 v15, 0x3fb8aa3b, v8
	v_fma_f32 v16, v8, s12, -v15
	v_rndne_f32_e32 v19, v15
	v_fmac_f32_e32 v16, 0x32a5705f, v8
	v_sub_f32_e32 v15, v15, v19
	v_add_f32_e32 v15, v15, v16
	v_exp_f32_e32 v15, v15
	v_cvt_i32_f32_e32 v16, v19
	v_cmp_ngt_f32_e32 vcc, s65, v9
	v_add_f32_e32 v2, v18, v2
	s_nop 0
	v_cndmask_b32_e32 v3, 0, v3, vcc
	v_cmp_nlt_f32_e32 vcc, s3, v9
	v_sub_f32_e32 v9, v17, v22
	s_nop 0
	v_cndmask_b32_e32 v19, v239, v3, vcc
	v_ldexp_f32 v3, v15, v16
	v_mul_f32_e32 v15, 0x3fb8aa3b, v9
	v_fma_f32 v16, v9, s12, -v15
	v_rndne_f32_e32 v17, v15
	v_fmac_f32_e32 v16, 0x32a5705f, v9
	v_sub_f32_e32 v15, v15, v17
	v_add_f32_e32 v15, v15, v16
	v_exp_f32_e32 v15, v15
	v_cvt_i32_f32_e32 v16, v17
	v_cmp_ngt_f32_e32 vcc, s65, v8
	v_add_f32_e32 v2, v19, v2
	s_nop 0
	v_cndmask_b32_e32 v3, 0, v3, vcc
	v_cmp_nlt_f32_e32 vcc, s3, v8
	v_ldexp_f32 v8, v15, v16
	v_sub_f32_e32 v16, v20, v22
	v_mul_f32_e32 v15, 0x3fb8aa3b, v16
	v_fma_f32 v17, v16, s12, -v15
	v_rndne_f32_e32 v20, v15
	v_fmac_f32_e32 v17, 0x32a5705f, v16
	v_sub_f32_e32 v15, v15, v20
	v_add_f32_e32 v15, v15, v17
	v_exp_f32_e32 v17, v15
	v_cvt_i32_f32_e32 v20, v20
	v_cndmask_b32_e32 v3, v239, v3, vcc
	v_cmp_ngt_f32_e32 vcc, s65, v9
	v_add_f32_e32 v2, v3, v2
	s_nop 0
	v_cndmask_b32_e32 v8, 0, v8, vcc
	v_cmp_nlt_f32_e32 vcc, s3, v9
	v_sub_f32_e32 v9, v21, v22
	s_nop 0
	v_cndmask_b32_e32 v15, v239, v8, vcc
	v_ldexp_f32 v8, v17, v20
	v_mul_f32_e32 v17, 0x3fb8aa3b, v9
	v_fma_f32 v20, v9, s12, -v17
	v_rndne_f32_e32 v21, v17
	v_fmac_f32_e32 v20, 0x32a5705f, v9
	v_sub_f32_e32 v17, v17, v21
	v_add_f32_e32 v17, v17, v20
	v_exp_f32_e32 v17, v17
	v_cvt_i32_f32_e32 v20, v21
	v_cmp_ngt_f32_e32 vcc, s65, v16
	v_add_f32_e32 v2, v15, v2
	s_nop 0
	v_cndmask_b32_e32 v8, 0, v8, vcc
	v_cmp_nlt_f32_e32 vcc, s3, v16
	s_nop 1
	v_cndmask_b32_e32 v16, v239, v8, vcc
	v_ldexp_f32 v8, v17, v20
	v_cmp_ngt_f32_e32 vcc, s65, v9
	v_add_f32_e32 v2, v16, v2
	s_nop 0
	v_cndmask_b32_e32 v8, 0, v8, vcc
	v_cmp_nlt_f32_e32 vcc, s3, v9
	s_nop 1
	v_cndmask_b32_e32 v17, v239, v8, vcc
	v_add_f32_e32 v2, v17, v2
	v_div_scale_f32 v8, s[12:13], v2, v2, 1.0
	v_rcp_f32_e32 v9, v8
	s_nop 0
	v_fma_f32 v20, -v8, v9, 1.0
	v_fmac_f32_e32 v9, v20, v9
	v_div_scale_f32 v20, vcc, 1.0, v2, 1.0
	v_mul_f32_e32 v21, v20, v9
	v_fma_f32 v22, -v8, v21, v20
	v_fmac_f32_e32 v21, v22, v9
	v_fma_f32 v8, -v8, v21, v20
	v_div_fmas_f32 v8, v8, v9, v21
	v_div_fixup_f32 v2, v8, v2, 1.0
	v_pk_mul_f32 v[22:23], v[4:5], v[2:3] op_sel_hi:[1,0]
	v_mul_f32_e32 v5, v25, v2
	v_cmp_gt_f32_e32 vcc, v22, v23
	v_mul_f32_e32 v8, v26, v2
	v_cmp_nlt_f32_e64 s[12:13], -1.0, v23
	v_cndmask_b32_e32 v9, v23, v22, vcc
	v_cndmask_b32_e64 v4, 0, 1, vcc
	v_cmp_ngt_f32_e32 vcc, v5, v9
	s_nop 1
	v_cndmask_b32_e32 v20, 2, v4, vcc
	v_cndmask_b32_e32 v4, v5, v9, vcc
	v_cmp_gt_f32_e64 s[16:17], v8, v4
	v_cmp_ngt_f32_e64 s[14:15], v8, v4
	s_nop 0
	v_cndmask_b32_e64 v21, v20, 3, s[16:17]
	v_cmp_eq_u32_e64 s[18:19], 0, v21
	s_or_b64 s[12:13], s[12:13], s[18:19]
	v_cndmask_b32_e64 v20, v23, -1.0, s[12:13]
	v_cndmask_b32_e64 v9, 0, -1, s[12:13]
	v_cmp_ne_u32_e64 s[12:13], 1, v21
	v_cmp_gt_f32_e64 s[18:19], v22, v20
	s_and_b64 s[12:13], s[12:13], s[18:19]
	v_cndmask_b32_e64 v20, v20, v22, s[12:13]
	v_cndmask_b32_e64 v9, v9, 1, s[12:13]
	s_or_b64 s[12:13], vcc, s[16:17]
	v_cmp_gt_f32_e32 vcc, v5, v20
	s_and_b64 vcc, s[12:13], vcc
	s_nop 0
	v_cndmask_b32_e64 v22, v9, 2, vcc
	v_cndmask_b32_e32 v9, v20, v5, vcc
	s_and_saveexec_b64 s[12:13], s[14:15]
	s_cbranch_execz .LBB0_792
	v_cmp_gt_f32_e32 vcc, v8, v9
	v_mov_b32_e32 v5, v9
	s_and_saveexec_b64 s[14:15], vcc
	v_mov_b32_e32 v5, v8
	v_mov_b32_e32 v22, 3
	s_or_b64 exec, exec, s[14:15]
	v_mov_b64_e32 v[8:9], v[4:5]

; __device__ __forceinline__ void n2_mfma(const Args& a, LAS unsigned char* lds, int layer) {
;     ...
;         if (tq < 16) {
;             const int c0 = wtot[tq], c1 = wtot[16 + tq], c2 = wtot[32 + tq], c3 = wtot[48 + tq], c = c0 + c1 + c2 + c3;
;             const int base = c ? (int)__hip_atomic_fetch_add(cnt + tq * 64, (unsigned)c, __ATOMIC_RELAXED, __HIP_MEMORY_SCOPE_AGENT) : 0;
;             sbase[tq] = base; sbase[16 + tq] = base + c0; sbase[32 + tq] = base + c0 + c1; sbase[48 + tq] = base + c0 + c1 + c2;
;         }
;         __syncthreads();
;         if (tq < 256) {
;             const int pos = sbase[(tq >> 6) * 16 + my_e] + my_rank;
;             list[my_e * NTOK + pos] = (rblk * 128 + (tq >> 1)) * 2 + (tq & 1); listw[my_e * NTOK + pos] = pg[tq];
;         }
.LBB0_851:
	s_or_b64 exec, exec, s[14:15]
	s_waitcnt lgkmcnt(0)
	s_barrier
	s_and_saveexec_b64 s[12:13], vcc
	s_cbranch_execz .LBB0_774
	v_and_b32_e32 v2, 0xffffffc0, v7
	s_add_i32 s14, 0, 0x12c00
	v_lshlrev_b32_e32 v3, 2, v8
	v_add3_u32 v2, s14, v2, v3
	ds_read_b32 v2, v2
	v_lshlrev_b32_e32 v3, 15, v8
	v_add_u32_e32 v4, 0x12400, v6
	ds_read_b32 v6, v4
	v_readlane_b32 s14, v253, 23
	s_waitcnt lgkmcnt(1)
	v_add3_u32 v2, v3, v9, v2
	v_ashrrev_i32_e32 v3, 31, v2
	v_lshlrev_b64 v[2:3], 2, v[2:3]
	v_readlane_b32 s15, v253, 24
	v_lshl_add_u32 v7, s2, 8, v7
	s_nop 0
	v_lshl_add_u64 v[4:5], s[14:15], 0, v[2:3]
	v_readlane_b32 s14, v253, 25
	v_readlane_b32 s15, v253, 26
	global_store_dword v[4:5], v7, off sc1
	s_nop 0
	v_lshl_add_u64 v[2:3], s[14:15], 0, v[2:3]
	s_waitcnt lgkmcnt(0)
	global_store_dword v[2:3], v6, off sc1
	s_branch .LBB0_774

; __device__ __forceinline__ unsigned cvt_pk_bf16(float lo, float hi) { unsigned r; asm volatile("v_cvt_pk_bf16_f32 %0, %1, %2" : "=v"(r) : "v"(lo), "v"(hi)); return r; }
;     __device__ __forceinline__ void operator()(const f32x4 (&acc)[2][2][4][2], const pg8::Unit& u, int wr, int wc, int fr, int fq) const {
;         bf16_t* base = hid + ((size_t)(seg[16 + u.e] + u.pm * 256 + wr * 64 + fr)) * DFF + u.pn * 128 + wc * 32 + 8 * fq;
; #pragma unroll
;         for (int ai = 0; ai < 2; ++ai)
; #pragma unroll
;             for (int m = 0; m < 4; ++m) {
;                 f32x4 h[2];
; #pragma unroll
;                 for (int n = 0; n < 2; ++n)
; #pragma unroll
;                     for (int j = 0; j < 4; ++j) { const float gte = acc[ai][0][m][n][j]; h[n][j] = gte * __builtin_amdgcn_rcpf(1.f + __expf(-gte)) * acc[ai][1][m][n][j]; }
;                 u32x4 w; w.x = pg8::cvt_pk_bf16(h[0][0], h[0][1]); w.y = pg8::cvt_pk_bf16(h[0][2], h[0][3]); w.z = pg8::cvt_pk_bf16(h[1][0], h[1][1]); w.w = pg8::cvt_pk_bf16(h[1][2], h[1][3]);
;                 *(u32x4*)(base + (size_t)(ai * 128 + m * 16) * DFF) = w;
;             }
;     }
.LBB0_1105:
	s_add_u32 s6, s54, 0xffffff00
	s_addc_u32 s7, s55, -1
	s_lshl_b32 s33, s10, 2
	s_add_i32 s33, s33, 0
	s_add_i32 s33, s33, 0x21e40
	v_mov_b32_e32 v34, s33
	ds_read_b32 v34, v34
	s_lshl_b32 s33, s44, 8
	v_mul_f32_e32 v138, 0xbfb8aa3b, v75
	v_mul_f32_e32 v139, 0xbfb8aa3b, v76
	v_mul_f32_e32 v140, 0xbfb8aa3b, v77
	s_waitcnt lgkmcnt(0)
	v_add_u32_e32 v34, s33, v34
	v_mul_f32_e32 v141, 0xbfb8aa3b, v130
	v_add_u32_e32 v36, v34, v247
	v_mul_f32_e32 v34, 0xbfb8aa3b, v74
	v_exp_f32_e32 v138, v138
	v_exp_f32_e32 v139, v139
	v_exp_f32_e32 v140, v140
	v_exp_f32_e32 v141, v141
	v_mul_f32_e32 v142, 0xbfb8aa3b, v131
	v_exp_f32_e32 v34, v34
	v_exp_f32_e32 v142, v142
	v_add_f32_e32 v138, 1.0, v138
	v_add_f32_e32 v139, 1.0, v139
	v_add_f32_e32 v140, 1.0, v140
	v_add_f32_e32 v141, 1.0, v141
	v_add_f32_e32 v34, 1.0, v34
	v_rcp_f32_e32 v138, v138
	v_rcp_f32_e32 v139, v139
	v_rcp_f32_e32 v140, v140
	v_rcp_f32_e32 v141, v141
	v_add_f32_e32 v142, 1.0, v142
	v_rcp_f32_e32 v34, v34
	v_rcp_f32_e32 v142, v142
	v_mul_f32_e32 v138, v75, v138
	v_mul_f32_e32 v139, v76, v139
	v_mul_f32_e32 v140, v77, v140
	v_mul_f32_e32 v141, v130, v141
	v_mul_f32_e32 v34, v74, v34
	v_mul_f32_e32 v138, v138, v103
	v_mul_f32_e32 v139, v139, v104
	v_mul_f32_e32 v140, v140, v105
	v_mul_f32_e32 v141, v141, v98
	v_mul_f32_e32 v143, 0xbfb8aa3b, v132
	v_mul_f32_e32 v144, 0xbfb8aa3b, v133
	v_mul_f32_e32 v142, v131, v142
	v_mul_f32_e32 v34, v34, v102
	v_exp_f32_e32 v143, v143
	v_exp_f32_e32 v144, v144
	v_mul_f32_e32 v142, v142, v99
	v_cvt_pk_bf16_f32 v138, v34, v138
	v_cvt_pk_bf16_f32 v139, v139, v140
	v_cvt_pk_bf16_f32 v140, v141, v142
	v_mul_f32_e32 v141, 0xbfb8aa3b, v127
	v_exp_f32_e32 v142, v141
	v_ashrrev_i32_e32 v37, 31, v36
	v_readlane_b32 s38, v253, 29
	v_add_f32_e32 v143, 1.0, v143
	v_add_f32_e32 v144, 1.0, v144
	s_lshl_b32 s36, s14, 7
	v_lshlrev_b64 v[36:37], 10, v[36:37]
	v_readlane_b32 s39, v253, 30
	v_rcp_f32_e32 v143, v143
	v_rcp_f32_e32 v144, v144
	v_add_f32_e32 v142, 1.0, v142
	s_ashr_i32 s37, s36, 31
	v_lshl_add_u64 v[36:37], s[38:39], 0, v[36:37]
	v_rcp_f32_e32 v142, v142
	v_lshl_add_u64 v[36:37], s[36:37], 1, v[36:37]
	v_lshl_add_u64 v[36:37], v[36:37], 0, s[66:67]
	v_mov_b32_e32 v209, v35
	v_lshl_add_u64 v[36:37], v[36:37], 0, v[208:209]
	v_mul_f32_e32 v143, v132, v143
	v_mul_f32_e32 v144, v133, v144
	v_mul_f32_e32 v143, v143, v100
	v_mul_f32_e32 v144, v144, v101
	v_cvt_pk_bf16_f32 v141, v143, v144
	global_store_dwordx4 v[36:37], v[138:141], off sc1
	v_mul_f32_e32 v34, 0xbfb8aa3b, v126
	v_mul_f32_e32 v144, 0xbfb8aa3b, v125
	v_mul_f32_e32 v138, v127, v142
	v_mul_f32_e32 v139, 0xbfb8aa3b, v128
	v_mul_f32_e32 v140, 0xbfb8aa3b, v129
	v_mul_f32_e32 v142, 0xbfb8aa3b, v123
	v_exp_f32_e32 v139, v139
	v_exp_f32_e32 v140, v140
	v_mul_f32_e32 v141, 0xbfb8aa3b, v122
	v_exp_f32_e32 v142, v142
	v_exp_f32_e32 v34, v34
	v_exp_f32_e32 v141, v141
	v_mul_f32_e32 v143, 0xbfb8aa3b, v124
	v_exp_f32_e32 v144, v144
	v_exp_f32_e32 v143, v143
	v_add_f32_e32 v139, 1.0, v139
	v_add_f32_e32 v140, 1.0, v140
	v_add_f32_e32 v142, 1.0, v142
	v_add_f32_e32 v34, 1.0, v34
	v_rcp_f32_e32 v139, v139
	v_rcp_f32_e32 v140, v140
	v_add_f32_e32 v141, 1.0, v141
	v_rcp_f32_e32 v142, v142
	v_add_f32_e32 v144, 1.0, v144
	v_rcp_f32_e32 v34, v34
	v_rcp_f32_e32 v141, v141
	v_add_f32_e32 v143, 1.0, v143
	v_rcp_f32_e32 v144, v144
	v_rcp_f32_e32 v143, v143
	v_mul_f32_e32 v139, v128, v139
	v_mul_f32_e32 v140, v129, v140
	v_mul_f32_e32 v142, v123, v142
	v_mul_f32_e32 v34, v126, v34
	v_mul_f32_e32 v138, v138, v95
	v_mul_f32_e32 v139, v139, v96
	v_mul_f32_e32 v140, v140, v97
	v_mul_f32_e32 v141, v122, v141
	v_mul_f32_e32 v142, v142, v91
	v_mul_f32_e32 v144, v125, v144
	v_mul_f32_e32 v34, v34, v94
	v_mul_f32_e32 v141, v141, v90
	v_mul_f32_e32 v143, v124, v143
	v_mul_f32_e32 v144, v144, v93
	v_cvt_pk_bf16_f32 v138, v34, v138
	v_cvt_pk_bf16_f32 v139, v139, v140
	v_cvt_pk_bf16_f32 v140, v141, v142
	v_mul_f32_e32 v142, 0xbfb8aa3b, v119
	v_mul_f32_e32 v143, v143, v92
	v_cvt_pk_bf16_f32 v141, v143, v144
	v_exp_f32_e32 v144, v142
	s_movk_i32 s33, 0x4000
	v_add_co_u32_e32 v142, vcc, s33, v36
	v_add_f32_e32 v144, 1.0, v144
	v_rcp_f32_e32 v144, v144
	v_addc_co_u32_e32 v143, vcc, 0, v37, vcc
	global_store_dwordx4 v[142:143], v[138:141], off sc1
	v_mul_f32_e32 v142, 0xbfb8aa3b, v115
	v_mul_f32_e32 v34, 0xbfb8aa3b, v118
	v_mul_f32_e32 v139, 0xbfb8aa3b, v120
	v_mul_f32_e32 v140, 0xbfb8aa3b, v121
	v_mul_f32_e32 v138, v119, v144
	v_exp_f32_e32 v139, v139
	v_exp_f32_e32 v140, v140
	v_mul_f32_e32 v141, 0xbfb8aa3b, v114
	v_exp_f32_e32 v142, v142
	v_mul_f32_e32 v144, 0xbfb8aa3b, v117
	v_exp_f32_e32 v34, v34
	v_exp_f32_e32 v141, v141
	v_mul_f32_e32 v143, 0xbfb8aa3b, v116
	v_exp_f32_e32 v144, v144
	v_exp_f32_e32 v143, v143
	v_add_f32_e32 v139, 1.0, v139
	v_add_f32_e32 v140, 1.0, v140
	v_add_f32_e32 v142, 1.0, v142
	v_add_f32_e32 v34, 1.0, v34
	v_rcp_f32_e32 v139, v139
	v_rcp_f32_e32 v140, v140
	v_add_f32_e32 v141, 1.0, v141
	v_rcp_f32_e32 v142, v142
	v_add_f32_e32 v144, 1.0, v144
	v_rcp_f32_e32 v34, v34
	v_rcp_f32_e32 v141, v141
	v_add_f32_e32 v143, 1.0, v143
	v_rcp_f32_e32 v144, v144
	v_rcp_f32_e32 v143, v143
	v_mul_f32_e32 v139, v120, v139
	v_mul_f32_e32 v140, v121, v140
	v_mul_f32_e32 v142, v115, v142
	v_mul_f32_e32 v34, v118, v34
	v_mul_f32_e32 v138, v138, v87
	v_mul_f32_e32 v139, v139, v88
	v_mul_f32_e32 v140, v140, v89
	v_mul_f32_e32 v141, v114, v141
	v_mul_f32_e32 v142, v142, v83
	v_mul_f32_e32 v144, v117, v144
	v_mul_f32_e32 v34, v34, v86
	v_mul_f32_e32 v141, v141, v82
	v_mul_f32_e32 v143, v116, v143
	v_mul_f32_e32 v144, v144, v85
	v_cvt_pk_bf16_f32 v138, v34, v138
	v_cvt_pk_bf16_f32 v139, v139, v140
	v_cvt_pk_bf16_f32 v140, v141, v142
; __device__ __forceinline__ unsigned cvt_pk_bf16(float lo, float hi) { unsigned r; asm volatile("v_cvt_pk_bf16_f32 %0, %1, %2" : "=v"(r) : "v"(lo), "v"(hi)); return r; }
;     __device__ __forceinline__ void operator()(const f32x4 (&acc)[2][2][4][2], const pg8::Unit& u, int wr, int wc, int fr, int fq) const {
;         bf16_t* base = hid + ((size_t)(seg[16 + u.e] + u.pm * 256 + wr * 64 + fr)) * DFF + u.pn * 128 + wc * 32 + 8 * fq;
; #pragma unroll
;         for (int ai = 0; ai < 2; ++ai)
; #pragma unroll
;             for (int m = 0; m < 4; ++m) {
;                 f32x4 h[2];
; #pragma unroll
;                 for (int n = 0; n < 2; ++n)
; #pragma unroll
;                     for (int j = 0; j < 4; ++j) { const float gte = acc[ai][0][m][n][j]; h[n][j] = gte * __builtin_amdgcn_rcpf(1.f + __expf(-gte)) * acc[ai][1][m][n][j]; }
;                 u32x4 w; w.x = pg8::cvt_pk_bf16(h[0][0], h[0][1]); w.y = pg8::cvt_pk_bf16(h[0][2], h[0][3]); w.z = pg8::cvt_pk_bf16(h[1][0], h[1][1]); w.w = pg8::cvt_pk_bf16(h[1][2], h[1][3]);
;                 *(u32x4*)(base + (size_t)(ai * 128 + m * 16) * DFF) = w;
;             }
;     }
	v_mul_f32_e32 v142, 0xbfb8aa3b, v111
	v_mul_f32_e32 v143, v143, v84
	v_cvt_pk_bf16_f32 v141, v143, v144
	v_exp_f32_e32 v144, v142
	s_mov_b32 s33, 0x8000
	v_add_co_u32_e32 v142, vcc, s33, v36
	v_add_f32_e32 v144, 1.0, v144
	v_rcp_f32_e32 v144, v144
	v_addc_co_u32_e32 v143, vcc, 0, v37, vcc
	global_store_dwordx4 v[142:143], v[138:141], off sc1
	v_mul_f32_e32 v142, 0xbfb8aa3b, v107
	v_mul_f32_e32 v34, 0xbfb8aa3b, v110
	v_mul_f32_e32 v139, 0xbfb8aa3b, v112
	v_mul_f32_e32 v140, 0xbfb8aa3b, v113
	v_mul_f32_e32 v138, v111, v144
	v_exp_f32_e32 v139, v139
	v_exp_f32_e32 v140, v140
	v_mul_f32_e32 v141, 0xbfb8aa3b, v106
	v_exp_f32_e32 v142, v142
	v_mul_f32_e32 v144, 0xbfb8aa3b, v109
	v_exp_f32_e32 v34, v34
	v_exp_f32_e32 v141, v141
	v_mul_f32_e32 v143, 0xbfb8aa3b, v108
	v_exp_f32_e32 v144, v144
	v_exp_f32_e32 v143, v143
	v_add_f32_e32 v139, 1.0, v139
	v_add_f32_e32 v140, 1.0, v140
	v_add_f32_e32 v142, 1.0, v142
	v_add_f32_e32 v34, 1.0, v34
	v_rcp_f32_e32 v139, v139
	v_rcp_f32_e32 v140, v140
	v_add_f32_e32 v141, 1.0, v141
	v_rcp_f32_e32 v142, v142
	v_add_f32_e32 v144, 1.0, v144
	v_rcp_f32_e32 v34, v34
	v_rcp_f32_e32 v141, v141
	v_add_f32_e32 v143, 1.0, v143
	v_rcp_f32_e32 v144, v144
	v_rcp_f32_e32 v143, v143
	v_mul_f32_e32 v139, v112, v139
	v_mul_f32_e32 v140, v113, v140
	v_mul_f32_e32 v142, v107, v142
	v_mul_f32_e32 v34, v110, v34
	v_mul_f32_e32 v138, v138, v79
	v_mul_f32_e32 v139, v139, v80
	v_mul_f32_e32 v140, v140, v81
	v_mul_f32_e32 v141, v106, v141
	v_mul_f32_e32 v142, v142, v71
	v_mul_f32_e32 v144, v109, v144
	v_mul_f32_e32 v34, v34, v78
	v_mul_f32_e32 v141, v141, v70
	v_mul_f32_e32 v143, v108, v143
	v_mul_f32_e32 v144, v144, v73
	v_cvt_pk_bf16_f32 v138, v34, v138
	v_cvt_pk_bf16_f32 v139, v139, v140
	v_cvt_pk_bf16_f32 v140, v141, v142
	v_mul_f32_e32 v142, 0xbfb8aa3b, v67
	v_mul_f32_e32 v143, v143, v72
	v_cvt_pk_bf16_f32 v141, v143, v144
	v_exp_f32_e32 v144, v142
	s_mov_b32 s33, 0xc000
	v_add_co_u32_e32 v142, vcc, s33, v36
	v_add_f32_e32 v144, 1.0, v144
	v_rcp_f32_e32 v144, v144
	v_addc_co_u32_e32 v143, vcc, 0, v37, vcc
	global_store_dwordx4 v[142:143], v[138:141], off sc1
	v_mul_f32_e32 v142, 0xbfb8aa3b, v63
	v_mul_f32_e32 v34, 0xbfb8aa3b, v66
	v_mul_f32_e32 v139, 0xbfb8aa3b, v68
	v_mul_f32_e32 v140, 0xbfb8aa3b, v69
	v_mul_f32_e32 v138, v67, v144
	v_exp_f32_e32 v139, v139
	v_exp_f32_e32 v140, v140
	v_mul_f32_e32 v141, 0xbfb8aa3b, v62
	v_exp_f32_e32 v142, v142
	v_mul_f32_e32 v144, 0xbfb8aa3b, v65
	v_exp_f32_e32 v34, v34
	v_exp_f32_e32 v141, v141
	v_mul_f32_e32 v143, 0xbfb8aa3b, v64
	v_exp_f32_e32 v144, v144
	v_exp_f32_e32 v143, v143
	v_add_f32_e32 v139, 1.0, v139
	v_add_f32_e32 v140, 1.0, v140
	v_add_f32_e32 v142, 1.0, v142
	v_add_f32_e32 v34, 1.0, v34
	v_rcp_f32_e32 v139, v139
	v_rcp_f32_e32 v140, v140
	v_add_f32_e32 v141, 1.0, v141
	v_rcp_f32_e32 v142, v142
	v_add_f32_e32 v144, 1.0, v144
	v_rcp_f32_e32 v34, v34
	v_rcp_f32_e32 v141, v141
	v_add_f32_e32 v143, 1.0, v143
	v_rcp_f32_e32 v144, v144
	v_rcp_f32_e32 v143, v143
	v_mul_f32_e32 v139, v68, v139
	v_mul_f32_e32 v140, v69, v140
	v_mul_f32_e32 v142, v63, v142
	v_mul_f32_e32 v34, v66, v34
	v_mul_f32_e32 v138, v31, v138
	v_mul_f32_e32 v139, v32, v139
	v_mul_f32_e32 v140, v33, v140
	v_mul_f32_e32 v141, v62, v141
	v_mul_f32_e32 v142, v27, v142
	v_mul_f32_e32 v144, v65, v144
	v_mul_f32_e32 v34, v30, v34
	v_mul_f32_e32 v141, v26, v141
	v_mul_f32_e32 v143, v64, v143
	v_mul_f32_e32 v144, v29, v144
	v_cvt_pk_bf16_f32 v138, v34, v138
	v_cvt_pk_bf16_f32 v139, v139, v140
	v_cvt_pk_bf16_f32 v140, v141, v142
	v_mul_f32_e32 v142, 0xbfb8aa3b, v59
	v_mul_f32_e32 v143, v28, v143
	v_cvt_pk_bf16_f32 v141, v143, v144
	v_exp_f32_e32 v144, v142
	s_mov_b32 s33, 0x20000
	v_add_co_u32_e32 v142, vcc, s33, v36
	v_add_f32_e32 v144, 1.0, v144
	v_rcp_f32_e32 v144, v144
	v_addc_co_u32_e32 v143, vcc, 0, v37, vcc
	global_store_dwordx4 v[142:143], v[138:141], off sc1
	v_mul_f32_e32 v142, 0xbfb8aa3b, v55
	v_mul_f32_e32 v34, 0xbfb8aa3b, v58
	v_mul_f32_e32 v139, 0xbfb8aa3b, v60
	v_mul_f32_e32 v140, 0xbfb8aa3b, v61
	v_mul_f32_e32 v138, v59, v144
	v_exp_f32_e32 v139, v139
	v_exp_f32_e32 v140, v140
	v_mul_f32_e32 v141, 0xbfb8aa3b, v54
	v_exp_f32_e32 v142, v142
	v_mul_f32_e32 v144, 0xbfb8aa3b, v57
	v_exp_f32_e32 v34, v34
	v_exp_f32_e32 v141, v141
	v_mul_f32_e32 v143, 0xbfb8aa3b, v56
	v_exp_f32_e32 v144, v144
	v_exp_f32_e32 v143, v143
	v_add_f32_e32 v139, 1.0, v139
	v_add_f32_e32 v140, 1.0, v140
	v_add_f32_e32 v142, 1.0, v142
	v_add_f32_e32 v34, 1.0, v34
	v_rcp_f32_e32 v139, v139
	v_rcp_f32_e32 v140, v140
	v_add_f32_e32 v141, 1.0, v141
	v_rcp_f32_e32 v142, v142
	v_add_f32_e32 v144, 1.0, v144
; __device__ __forceinline__ unsigned cvt_pk_bf16(float lo, float hi) { unsigned r; asm volatile("v_cvt_pk_bf16_f32 %0, %1, %2" : "=v"(r) : "v"(lo), "v"(hi)); return r; }
;     __device__ __forceinline__ void operator()(const f32x4 (&acc)[2][2][4][2], const pg8::Unit& u, int wr, int wc, int fr, int fq) const {
;         bf16_t* base = hid + ((size_t)(seg[16 + u.e] + u.pm * 256 + wr * 64 + fr)) * DFF + u.pn * 128 + wc * 32 + 8 * fq;
; #pragma unroll
;         for (int ai = 0; ai < 2; ++ai)
; #pragma unroll
;             for (int m = 0; m < 4; ++m) {
;                 f32x4 h[2];
; #pragma unroll
;                 for (int n = 0; n < 2; ++n)
; #pragma unroll
;                     for (int j = 0; j < 4; ++j) { const float gte = acc[ai][0][m][n][j]; h[n][j] = gte * __builtin_amdgcn_rcpf(1.f + __expf(-gte)) * acc[ai][1][m][n][j]; }
;                 u32x4 w; w.x = pg8::cvt_pk_bf16(h[0][0], h[0][1]); w.y = pg8::cvt_pk_bf16(h[0][2], h[0][3]); w.z = pg8::cvt_pk_bf16(h[1][0], h[1][1]); w.w = pg8::cvt_pk_bf16(h[1][2], h[1][3]);
;                 *(u32x4*)(base + (size_t)(ai * 128 + m * 16) * DFF) = w;
;             }
;     }
	v_rcp_f32_e32 v34, v34
	v_rcp_f32_e32 v141, v141
	v_add_f32_e32 v143, 1.0, v143
	v_rcp_f32_e32 v144, v144
	v_rcp_f32_e32 v143, v143
	v_mul_f32_e32 v139, v60, v139
	v_mul_f32_e32 v140, v61, v140
	v_mul_f32_e32 v142, v55, v142
	v_mul_f32_e32 v34, v58, v34
	v_mul_f32_e32 v138, v23, v138
	v_mul_f32_e32 v139, v24, v139
	v_mul_f32_e32 v140, v25, v140
	v_mul_f32_e32 v141, v54, v141
	v_mul_f32_e32 v142, v19, v142
	v_mul_f32_e32 v144, v57, v144
	v_mul_f32_e32 v34, v22, v34
	v_mul_f32_e32 v141, v18, v141
	v_mul_f32_e32 v143, v56, v143
	v_mul_f32_e32 v144, v21, v144
	v_cvt_pk_bf16_f32 v138, v34, v138
	v_cvt_pk_bf16_f32 v139, v139, v140
	v_cvt_pk_bf16_f32 v140, v141, v142
	v_mul_f32_e32 v142, 0xbfb8aa3b, v51
	v_mul_f32_e32 v143, v20, v143
	v_cvt_pk_bf16_f32 v141, v143, v144
	v_exp_f32_e32 v144, v142
	s_mov_b32 s33, 0x24000
	v_add_co_u32_e32 v142, vcc, s33, v36
	v_add_f32_e32 v144, 1.0, v144
	v_rcp_f32_e32 v144, v144
	v_addc_co_u32_e32 v143, vcc, 0, v37, vcc
	global_store_dwordx4 v[142:143], v[138:141], off sc1
	v_mul_f32_e32 v142, 0xbfb8aa3b, v47
	v_mul_f32_e32 v34, 0xbfb8aa3b, v50
	v_mul_f32_e32 v139, 0xbfb8aa3b, v52
	v_mul_f32_e32 v140, 0xbfb8aa3b, v53
	v_mul_f32_e32 v138, v51, v144
	v_exp_f32_e32 v139, v139
	v_exp_f32_e32 v140, v140
	v_mul_f32_e32 v141, 0xbfb8aa3b, v46
	v_exp_f32_e32 v142, v142
	v_mul_f32_e32 v144, 0xbfb8aa3b, v49
	v_exp_f32_e32 v34, v34
	v_exp_f32_e32 v141, v141
	v_mul_f32_e32 v143, 0xbfb8aa3b, v48
	v_exp_f32_e32 v144, v144
	v_exp_f32_e32 v143, v143
	v_add_f32_e32 v139, 1.0, v139
	v_add_f32_e32 v140, 1.0, v140
	v_add_f32_e32 v142, 1.0, v142
	v_add_f32_e32 v34, 1.0, v34
	v_rcp_f32_e32 v139, v139
	v_rcp_f32_e32 v140, v140
	v_add_f32_e32 v141, 1.0, v141
	v_rcp_f32_e32 v142, v142
	v_add_f32_e32 v144, 1.0, v144
	v_rcp_f32_e32 v34, v34
	v_rcp_f32_e32 v141, v141
	v_add_f32_e32 v143, 1.0, v143
	v_rcp_f32_e32 v144, v144
	v_rcp_f32_e32 v143, v143
	v_mul_f32_e32 v139, v52, v139
	v_mul_f32_e32 v140, v53, v140
	v_mul_f32_e32 v142, v47, v142
	v_mul_f32_e32 v34, v50, v34
	v_mul_f32_e32 v138, v15, v138
	v_mul_f32_e32 v139, v16, v139
	v_mul_f32_e32 v140, v17, v140
	v_mul_f32_e32 v141, v46, v141
	v_mul_f32_e32 v142, v11, v142
	v_mul_f32_e32 v144, v49, v144
	v_mul_f32_e32 v34, v14, v34
	v_mul_f32_e32 v141, v10, v141
	v_mul_f32_e32 v143, v48, v143
	v_mul_f32_e32 v144, v13, v144
	v_cvt_pk_bf16_f32 v138, v34, v138
	v_cvt_pk_bf16_f32 v139, v139, v140
	v_cvt_pk_bf16_f32 v140, v141, v142
	v_mul_f32_e32 v142, 0xbfb8aa3b, v43
	v_mul_f32_e32 v143, v12, v143
	v_cvt_pk_bf16_f32 v141, v143, v144
	v_exp_f32_e32 v144, v142
	s_mov_b32 s33, 0x28000
	v_add_co_u32_e32 v142, vcc, s33, v36
	v_add_f32_e32 v144, 1.0, v144
	v_rcp_f32_e32 v144, v144
	v_addc_co_u32_e32 v143, vcc, 0, v37, vcc
	global_store_dwordx4 v[142:143], v[138:141], off sc1
	v_mul_f32_e32 v34, 0xbfb8aa3b, v42
	v_mul_f32_e32 v142, 0xbfb8aa3b, v39
	v_mul_f32_e32 v139, 0xbfb8aa3b, v44
	v_mul_f32_e32 v140, 0xbfb8aa3b, v45
	v_mul_f32_e32 v141, 0xbfb8aa3b, v38
	v_mul_f32_e32 v138, v43, v144
	v_exp_f32_e32 v139, v139
	v_exp_f32_e32 v140, v140
	v_exp_f32_e32 v141, v141
	v_mul_f32_e32 v143, 0xbfb8aa3b, v40
	v_mul_f32_e32 v144, 0xbfb8aa3b, v41
	v_exp_f32_e32 v34, v34
	v_exp_f32_e32 v142, v142
	v_exp_f32_e32 v143, v143
	v_exp_f32_e32 v144, v144
	v_add_f32_e32 v139, 1.0, v139
	v_add_f32_e32 v140, 1.0, v140
	v_add_f32_e32 v141, 1.0, v141
	v_add_f32_e32 v34, 1.0, v34
	v_rcp_f32_e32 v139, v139
	v_rcp_f32_e32 v140, v140
	v_rcp_f32_e32 v141, v141
	v_add_f32_e32 v142, 1.0, v142
	v_add_f32_e32 v143, 1.0, v143
	v_add_f32_e32 v144, 1.0, v144
	v_rcp_f32_e32 v34, v34
	v_rcp_f32_e32 v142, v142
	v_rcp_f32_e32 v143, v143
	v_rcp_f32_e32 v144, v144
	v_add_co_u32_e32 v36, vcc, 0x2c000, v36
	v_mul_f32_e32 v139, v44, v139
	v_mul_f32_e32 v140, v45, v140
	v_mul_f32_e32 v141, v38, v141
	v_addc_co_u32_e32 v37, vcc, 0, v37, vcc
	v_mul_f32_e32 v34, v42, v34
	v_mul_f32_e32 v138, v7, v138
	v_mul_f32_e32 v139, v8, v139
	v_mul_f32_e32 v140, v9, v140
	v_mul_f32_e32 v141, v2, v141
	v_mul_f32_e32 v142, v39, v142
	v_mul_f32_e32 v143, v40, v143
	v_mul_f32_e32 v144, v41, v144
	s_andn2_b64 vcc, exec, s[20:21]
	v_mul_f32_e32 v34, v6, v34
	v_mul_f32_e32 v142, v3, v142
	v_mul_f32_e32 v143, v4, v143
	v_mul_f32_e32 v144, v5, v144
	v_cvt_pk_bf16_f32 v138, v34, v138
	v_cvt_pk_bf16_f32 v139, v139, v140
	v_cvt_pk_bf16_f32 v140, v141, v142
	v_cvt_pk_bf16_f32 v141, v143, v144
	global_store_dwordx4 v[36:37], v[138:141], off sc1
	s_cbranch_vccnz .LBB0_1110
	s_and_b64 vcc, exec, s[4:5]
	s_cbranch_vccnz .LBB0_1108
	v_mov_b32_e32 v250, v251
	s_mov_b32 s68, s29
	s_mov_b32 s69, s28
	s_mov_b32 s72, s73
	s_mov_b64 s[26:27], s[30:31]

; #define LAS __attribute__((address_space(3)))
; __device__ __forceinline__ void gu_mfma(const Args& a, LAS unsigned char* lds, int layer) {
;     seg_to_lds(a, lds, layer);
;     const LAS int* seg = (const LAS int*)(lds + SEG_OFF);
;     pg8::GroupedOrder So{(const char*)(a.ws + WS_HS), (const char*)(a.ws + WS_WGU + (size_t)layer * NE * 1024 * D * 2), seg, 4, (int)gridDim.x, (int)blockIdx.x, (size_t)D * 2, (size_t)1024 * D * 2, (size_t)256 * D * 2};
;     EpiGU E{(bf16_t*)(a.ws + WS_HID), seg};
;     pg8::gemm_phase_gather<EpiGU, pg8::GroupedOrder>(lds, D, So, E, (const char*)(a.ws + WS_ACT), (const int*)(a.ws + WS_LIST), seg);
; }
; __device__ __forceinline__ void dn_mfma(const Args& a, LAS unsigned char* lds, int layer) {
;     seg_to_lds(a, lds, layer);
;     const LAS int* seg = (const LAS int*)(lds + SEG_OFF);
;     pg8::GroupedOrder So{(const char*)(a.ws + WS_HID), (const char*)(a.ws + WS_WDN + (size_t)layer * NE * 1024 * DFF * 2), seg, 4, (int)gridDim.x, (int)blockIdx.x, (size_t)DFF * 2, (size_t)1024 * DFF * 2, (size_t)256 * DFF * 2};
;     EpiDown E{(bf16_t*)(a.ws + WS_YBUF), (const int*)(a.ws + WS_LIST), (const float*)(a.ws + WS_LISTW), seg, lds};
;     pg8::gemm_phase<EpiDown, pg8::GroupedOrder>(lds, DFF, So, E);
; }
.Ltail_signal:
	s_waitcnt vmcnt(0) lgkmcnt(0)
	s_barrier
	s_lshl_b32 vcc_hi, s77, 2
	s_sub_u32 s61, s61, vcc_hi
	v_readlane_b32 vcc_lo, v253, 31
	s_nop 1
	s_sub_u32 vcc_lo, vcc_lo, vcc_hi
	s_nop 1
	v_writelane_b32 v253, vcc_lo, 31
	s_nop 1
	s_mov_b32 vcc_lo, 0
	s_nop 1
	v_writelane_b32 v254, vcc_lo, 62
	s_nop 1
	v_cmp_eq_u32_e32 vcc, 0, v0
	s_and_saveexec_b64 s[4:5], vcc
	s_cbranch_execz .Ltail_sig_done
	s_waitcnt vmcnt(0)
	v_readlane_b32 s6, v254, 20
	s_nop 1
	s_lshl_b32 s6, s6, 2
	s_add_u32 s6, s6, 0x18000
	s_add_u32 s8, s92, s6
	s_addc_u32 s9, s93, 0
	v_mov_b32_e32 v1, 0
	v_mov_b32_e32 v2, 1
	global_atomic_add v1, v2, s[8:9]
	s_waitcnt vmcnt(0)

; #define LAS __attribute__((address_space(3)))
; __device__ __forceinline__ unsigned cvt_pk_bf16(float lo, float hi) { unsigned r; asm volatile("v_cvt_pk_bf16_f32 %0, %1, %2" : "=v"(r) : "v"(lo), "v"(hi)); return r; }
;     __device__ __forceinline__ void operator()(const f32x4 (&acc)[2][2][4][2], const pg8::Unit& u, int wr, int wc, int fr, int fq) const {
;         const int cnt = seg[u.e], col0 = u.pn * 256 + wc * 32 + 8 * fq;
;         const LAS int* sl_e = (const LAS int*)(ldsb + DNSL_OFF + u.par * 2048); const LAS float* sl_g = (const LAS float*)(ldsb + DNSL_OFF + u.par * 2048 + 1024);
; #pragma unroll
;         for (int ai = 0; ai < 2; ++ai)
; #pragma unroll
;             for (int m = 0; m < 4; ++m) {
;                 const int ll = ai * 128 + wr * 64 + m * 16 + fr, lr = u.pm * 256 + ll;
;                 if (lr < cnt) {
;                     const int ent = sl_e[ll]; const float gw = sl_g[ll];
;                     bf16_t* rowp = yb + ((size_t)(ent & 1) * NTOK + (size_t)(ent >> 1)) * D + col0;
; #pragma unroll
;                     for (int bj = 0; bj < 2; ++bj) {
;                         const f32x4 v0 = acc[ai][bj][m][0] * gw, v1 = acc[ai][bj][m][1] * gw;
;                         u32x4 w; w.x = pg8::cvt_pk_bf16(v0[0], v0[1]); w.y = pg8::cvt_pk_bf16(v0[2], v0[3]); w.z = pg8::cvt_pk_bf16(v1[0], v1[1]); w.w = pg8::cvt_pk_bf16(v1[2], v1[3]);
;                         *(u32x4*)(rowp + bj * 128) = w;
;                     }
;                 }
;             }
;     }
.LBB0_1300:
	s_lshl_b32 s6, s10, 2
	s_add_i32 s6, s6, 0
	s_add_i32 s6, s6, 0x21e00
	v_mov_b32_e32 v34, s6
	ds_read_b32 v134, v34
	v_lshl_or_b32 v36, s12, 8, v244
	s_add_i32 s54, s54, 0x22400
	v_add_u32_e32 v136, s22, v226
	v_ashrrev_i32_e32 v37, 31, v36
	s_waitcnt lgkmcnt(0)
	v_cmp_lt_i32_e32 vcc, v136, v134
	v_lshl_add_u32 v135, v226, 2, s54
	s_and_saveexec_b64 s[6:7], vcc
	s_cbranch_execz .LBB0_1302
	ds_read2st64_b32 v[138:139], v135 offset1:4
	s_waitcnt lgkmcnt(0)
	v_lshlrev_b32_e32 v34, 15, v138
	v_ashrrev_i32_e32 v138, 1, v138
	v_mov_b32_e32 v142, v139
	v_and_b32_e32 v34, 0x8000, v34
	v_ashrrev_i32_e32 v139, 31, v138
	v_lshl_add_u64 v[138:139], v[34:35], 0, v[138:139]
	v_lshlrev_b64 v[138:139], 11, v[138:139]
	v_lshl_add_u64 v[138:139], s[96:97], 0, v[138:139]
	v_pk_mul_f32 v[140:141], v[132:133], v[142:143] op_sel_hi:[1,0]
	v_lshl_add_u64 v[144:145], v[36:37], 1, v[138:139]
	v_pk_mul_f32 v[138:139], v[130:131], v[142:143] op_sel_hi:[1,0]
	v_pk_mul_f32 v[146:147], v[128:129], v[142:143] op_sel_hi:[1,0]
	v_pk_mul_f32 v[148:149], v[126:127], v[142:143] op_sel_hi:[1,0]
	v_cvt_pk_bf16_f32 v138, v138, v139
	v_cvt_pk_bf16_f32 v139, v140, v141
	s_nop 0
	v_cvt_pk_bf16_f32 v140, v148, v149
	v_cvt_pk_bf16_f32 v141, v146, v147
	global_store_dwordx4 v[144:145], v[138:141], off sc1
	v_pk_mul_f32 v[146:147], v[96:97], v[142:143] op_sel_hi:[1,0]
	s_nop 0
	v_pk_mul_f32 v[140:141], v[100:101], v[142:143] op_sel_hi:[1,0]
	v_pk_mul_f32 v[138:139], v[98:99], v[142:143] op_sel_hi:[1,0]
	v_pk_mul_f32 v[142:143], v[94:95], v[142:143] op_sel_hi:[1,0]
	v_cvt_pk_bf16_f32 v138, v138, v139
	v_cvt_pk_bf16_f32 v139, v140, v141
	s_nop 0
	v_cvt_pk_bf16_f32 v140, v142, v143
	v_cvt_pk_bf16_f32 v141, v146, v147
	global_store_dwordx4 v[144:145], v[138:141], off offset:256 sc1
.LBB0_1302:
	s_or_b64 exec, exec, s[6:7]
	v_add_u32_e32 v34, s22, v228
	v_cmp_lt_i32_e32 vcc, v34, v134
	s_and_saveexec_b64 s[6:7], vcc
	s_cbranch_execz .LBB0_1304
	v_add_u32_e32 v34, 64, v135
	ds_read2st64_b32 v[138:139], v34 offset1:4
	s_waitcnt lgkmcnt(0)
	v_lshlrev_b32_e32 v34, 15, v138
	v_ashrrev_i32_e32 v138, 1, v138
	v_mov_b32_e32 v142, v139
	v_and_b32_e32 v34, 0x8000, v34
	v_ashrrev_i32_e32 v139, 31, v138
	v_lshl_add_u64 v[138:139], v[34:35], 0, v[138:139]
	v_lshlrev_b64 v[138:139], 11, v[138:139]
	v_lshl_add_u64 v[138:139], s[96:97], 0, v[138:139]
	v_pk_mul_f32 v[140:141], v[124:125], v[142:143] op_sel_hi:[1,0]
	v_lshl_add_u64 v[144:145], v[36:37], 1, v[138:139]
	v_pk_mul_f32 v[138:139], v[122:123], v[142:143] op_sel_hi:[1,0]
	v_pk_mul_f32 v[146:147], v[120:121], v[142:143] op_sel_hi:[1,0]
	v_pk_mul_f32 v[148:149], v[118:119], v[142:143] op_sel_hi:[1,0]
	v_cvt_pk_bf16_f32 v138, v138, v139
	v_cvt_pk_bf16_f32 v139, v140, v141
	s_nop 0
	v_cvt_pk_bf16_f32 v140, v148, v149
	v_cvt_pk_bf16_f32 v141, v146, v147
	global_store_dwordx4 v[144:145], v[138:141], off sc1
	v_pk_mul_f32 v[146:147], v[88:89], v[142:143] op_sel_hi:[1,0]
	s_nop 0
	v_pk_mul_f32 v[140:141], v[92:93], v[142:143] op_sel_hi:[1,0]
	v_pk_mul_f32 v[138:139], v[90:91], v[142:143] op_sel_hi:[1,0]
	v_pk_mul_f32 v[142:143], v[86:87], v[142:143] op_sel_hi:[1,0]
	v_cvt_pk_bf16_f32 v138, v138, v139
	v_cvt_pk_bf16_f32 v139, v140, v141
	s_nop 0
	v_cvt_pk_bf16_f32 v140, v142, v143
	v_cvt_pk_bf16_f32 v141, v146, v147
	global_store_dwordx4 v[144:145], v[138:141], off offset:256 sc1
.LBB0_1304:
	s_or_b64 exec, exec, s[6:7]
	v_add_u32_e32 v34, s22, v229
	v_cmp_lt_i32_e32 vcc, v34, v134
	s_and_saveexec_b64 s[6:7], vcc
	s_cbranch_execz .LBB0_1306
	v_add_u32_e32 v34, 0x80, v135
	ds_read2st64_b32 v[138:139], v34 offset1:4
	s_waitcnt lgkmcnt(0)
	v_lshlrev_b32_e32 v34, 15, v138
	v_ashrrev_i32_e32 v138, 1, v138
	v_mov_b32_e32 v142, v139
	v_and_b32_e32 v34, 0x8000, v34
	v_ashrrev_i32_e32 v139, 31, v138
	v_lshl_add_u64 v[138:139], v[34:35], 0, v[138:139]
	v_lshlrev_b64 v[138:139], 11, v[138:139]
	v_lshl_add_u64 v[138:139], s[96:97], 0, v[138:139]
	v_pk_mul_f32 v[140:141], v[116:117], v[142:143] op_sel_hi:[1,0]
	v_lshl_add_u64 v[144:145], v[36:37], 1, v[138:139]
	v_pk_mul_f32 v[138:139], v[114:115], v[142:143] op_sel_hi:[1,0]
	v_pk_mul_f32 v[146:147], v[112:113], v[142:143] op_sel_hi:[1,0]
	v_pk_mul_f32 v[148:149], v[110:111], v[142:143] op_sel_hi:[1,0]
	v_cvt_pk_bf16_f32 v138, v138, v139
	v_cvt_pk_bf16_f32 v139, v140, v141
	s_nop 0
	v_cvt_pk_bf16_f32 v140, v148, v149
	v_cvt_pk_bf16_f32 v141, v146, v147
	global_store_dwordx4 v[144:145], v[138:141], off sc1
	v_pk_mul_f32 v[146:147], v[80:81], v[142:143] op_sel_hi:[1,0]
	s_nop 0
	v_pk_mul_f32 v[140:141], v[84:85], v[142:143] op_sel_hi:[1,0]
	v_pk_mul_f32 v[138:139], v[82:83], v[142:143] op_sel_hi:[1,0]
	v_pk_mul_f32 v[142:143], v[78:79], v[142:143] op_sel_hi:[1,0]
	v_cvt_pk_bf16_f32 v138, v138, v139
	v_cvt_pk_bf16_f32 v139, v140, v141
	s_nop 0
	v_cvt_pk_bf16_f32 v140, v142, v143
	v_cvt_pk_bf16_f32 v141, v146, v147
	global_store_dwordx4 v[144:145], v[138:141], off offset:256 sc1
; #define LAS __attribute__((address_space(3)))
; __device__ __forceinline__ unsigned cvt_pk_bf16(float lo, float hi) { unsigned r; asm volatile("v_cvt_pk_bf16_f32 %0, %1, %2" : "=v"(r) : "v"(lo), "v"(hi)); return r; }
;     __device__ __forceinline__ void operator()(const f32x4 (&acc)[2][2][4][2], const pg8::Unit& u, int wr, int wc, int fr, int fq) const {
;         const int cnt = seg[u.e], col0 = u.pn * 256 + wc * 32 + 8 * fq;
;         const LAS int* sl_e = (const LAS int*)(ldsb + DNSL_OFF + u.par * 2048); const LAS float* sl_g = (const LAS float*)(ldsb + DNSL_OFF + u.par * 2048 + 1024);
; #pragma unroll
;         for (int ai = 0; ai < 2; ++ai)
; #pragma unroll
;             for (int m = 0; m < 4; ++m) {
;                 const int ll = ai * 128 + wr * 64 + m * 16 + fr, lr = u.pm * 256 + ll;
;                 if (lr < cnt) {
;                     const int ent = sl_e[ll]; const float gw = sl_g[ll];
;                     bf16_t* rowp = yb + ((size_t)(ent & 1) * NTOK + (size_t)(ent >> 1)) * D + col0;
; #pragma unroll
;                     for (int bj = 0; bj < 2; ++bj) {
;                         const f32x4 v0 = acc[ai][bj][m][0] * gw, v1 = acc[ai][bj][m][1] * gw;
;                         u32x4 w; w.x = pg8::cvt_pk_bf16(v0[0], v0[1]); w.y = pg8::cvt_pk_bf16(v0[2], v0[3]); w.z = pg8::cvt_pk_bf16(v1[0], v1[1]); w.w = pg8::cvt_pk_bf16(v1[2], v1[3]);
;                         *(u32x4*)(rowp + bj * 128) = w;
;                     }
;                 }
;             }
;     }
.LBB0_1306:
	s_or_b64 exec, exec, s[6:7]
	v_add_u32_e32 v34, s22, v243
	v_cmp_lt_i32_e32 vcc, v34, v134
	s_and_saveexec_b64 s[6:7], vcc
	s_cbranch_execz .LBB0_1308
	v_add_u32_e32 v34, 0xc0, v135
	ds_read2st64_b32 v[138:139], v34 offset1:4
	s_waitcnt lgkmcnt(0)
	v_lshlrev_b32_e32 v34, 15, v138
	v_ashrrev_i32_e32 v138, 1, v138
	v_mov_b32_e32 v142, v139
	v_and_b32_e32 v34, 0x8000, v34
	v_ashrrev_i32_e32 v139, 31, v138
	v_lshl_add_u64 v[138:139], v[34:35], 0, v[138:139]
	v_lshlrev_b64 v[138:139], 11, v[138:139]
	v_lshl_add_u64 v[138:139], s[96:97], 0, v[138:139]
	v_pk_mul_f32 v[140:141], v[108:109], v[142:143] op_sel_hi:[1,0]
	v_lshl_add_u64 v[144:145], v[36:37], 1, v[138:139]
	v_pk_mul_f32 v[138:139], v[106:107], v[142:143] op_sel_hi:[1,0]
	v_pk_mul_f32 v[146:147], v[104:105], v[142:143] op_sel_hi:[1,0]
	v_pk_mul_f32 v[148:149], v[102:103], v[142:143] op_sel_hi:[1,0]
	v_cvt_pk_bf16_f32 v138, v138, v139
	v_cvt_pk_bf16_f32 v139, v140, v141
	s_nop 0
	v_cvt_pk_bf16_f32 v140, v148, v149
	v_cvt_pk_bf16_f32 v141, v146, v147
	global_store_dwordx4 v[144:145], v[138:141], off sc1
	v_pk_mul_f32 v[146:147], v[72:73], v[142:143] op_sel_hi:[1,0]
	s_nop 0
	v_pk_mul_f32 v[140:141], v[76:77], v[142:143] op_sel_hi:[1,0]
	v_pk_mul_f32 v[138:139], v[74:75], v[142:143] op_sel_hi:[1,0]
	v_pk_mul_f32 v[142:143], v[70:71], v[142:143] op_sel_hi:[1,0]
	v_cvt_pk_bf16_f32 v138, v138, v139
	v_cvt_pk_bf16_f32 v139, v140, v141
	s_nop 0
	v_cvt_pk_bf16_f32 v140, v142, v143
	v_cvt_pk_bf16_f32 v141, v146, v147
	global_store_dwordx4 v[144:145], v[138:141], off offset:256 sc1
.LBB0_1308:
	s_or_b64 exec, exec, s[6:7]
	v_add_u32_e32 v34, 0x80, v136
	v_cmp_lt_i32_e32 vcc, v34, v134
	s_and_saveexec_b64 s[6:7], vcc
	s_cbranch_execz .LBB0_1310
	ds_read2st64_b32 v[138:139], v135 offset0:2 offset1:6
	s_waitcnt lgkmcnt(0)
	v_lshlrev_b32_e32 v34, 15, v138
	v_ashrrev_i32_e32 v138, 1, v138
	v_mov_b32_e32 v142, v139
	v_and_b32_e32 v34, 0x8000, v34
	v_ashrrev_i32_e32 v139, 31, v138
	v_lshl_add_u64 v[138:139], v[34:35], 0, v[138:139]
	v_lshlrev_b64 v[138:139], 11, v[138:139]
	v_lshl_add_u64 v[138:139], s[96:97], 0, v[138:139]
	v_pk_mul_f32 v[140:141], v[68:69], v[142:143] op_sel_hi:[1,0]
	v_lshl_add_u64 v[144:145], v[36:37], 1, v[138:139]
	v_pk_mul_f32 v[138:139], v[66:67], v[142:143] op_sel_hi:[1,0]
	v_pk_mul_f32 v[146:147], v[64:65], v[142:143] op_sel_hi:[1,0]
	v_pk_mul_f32 v[148:149], v[62:63], v[142:143] op_sel_hi:[1,0]
	v_cvt_pk_bf16_f32 v138, v138, v139
	v_cvt_pk_bf16_f32 v139, v140, v141
	s_nop 0
	v_cvt_pk_bf16_f32 v140, v148, v149
	v_cvt_pk_bf16_f32 v141, v146, v147
	global_store_dwordx4 v[144:145], v[138:141], off sc1
	v_pk_mul_f32 v[146:147], v[28:29], v[142:143] op_sel_hi:[1,0]
	s_nop 0
	v_pk_mul_f32 v[140:141], v[32:33], v[142:143] op_sel_hi:[1,0]
	v_pk_mul_f32 v[138:139], v[30:31], v[142:143] op_sel_hi:[1,0]
	v_pk_mul_f32 v[142:143], v[26:27], v[142:143] op_sel_hi:[1,0]
	v_cvt_pk_bf16_f32 v138, v138, v139
	v_cvt_pk_bf16_f32 v139, v140, v141
	s_nop 0
	v_cvt_pk_bf16_f32 v140, v142, v143
	v_cvt_pk_bf16_f32 v141, v146, v147
	global_store_dwordx4 v[144:145], v[138:141], off offset:256 sc1
.LBB0_1310:
	s_or_b64 exec, exec, s[6:7]
	v_add_u32_e32 v34, 0x90, v136
	v_cmp_lt_i32_e32 vcc, v34, v134
	s_and_saveexec_b64 s[6:7], vcc
	s_cbranch_execz .LBB0_1312
	v_add_u32_e32 v34, 64, v135
	ds_read2st64_b32 v[138:139], v34 offset0:2 offset1:6
	s_waitcnt lgkmcnt(0)
	v_lshlrev_b32_e32 v34, 15, v138
	v_ashrrev_i32_e32 v138, 1, v138
	v_mov_b32_e32 v142, v139
	v_and_b32_e32 v34, 0x8000, v34
	v_ashrrev_i32_e32 v139, 31, v138
	v_lshl_add_u64 v[138:139], v[34:35], 0, v[138:139]
	v_lshlrev_b64 v[138:139], 11, v[138:139]
	v_lshl_add_u64 v[138:139], s[96:97], 0, v[138:139]
	v_pk_mul_f32 v[140:141], v[60:61], v[142:143] op_sel_hi:[1,0]
	v_lshl_add_u64 v[144:145], v[36:37], 1, v[138:139]
	v_pk_mul_f32 v[138:139], v[58:59], v[142:143] op_sel_hi:[1,0]
	v_pk_mul_f32 v[146:147], v[56:57], v[142:143] op_sel_hi:[1,0]
	v_pk_mul_f32 v[148:149], v[54:55], v[142:143] op_sel_hi:[1,0]
	v_cvt_pk_bf16_f32 v138, v138, v139
	v_cvt_pk_bf16_f32 v139, v140, v141
	s_nop 0
	v_cvt_pk_bf16_f32 v140, v148, v149
	v_cvt_pk_bf16_f32 v141, v146, v147
	global_store_dwordx4 v[144:145], v[138:141], off sc1
	v_pk_mul_f32 v[146:147], v[20:21], v[142:143] op_sel_hi:[1,0]
	s_nop 0
	v_pk_mul_f32 v[140:141], v[24:25], v[142:143] op_sel_hi:[1,0]
	v_pk_mul_f32 v[138:139], v[22:23], v[142:143] op_sel_hi:[1,0]
	v_pk_mul_f32 v[142:143], v[18:19], v[142:143] op_sel_hi:[1,0]
	v_cvt_pk_bf16_f32 v138, v138, v139
	v_cvt_pk_bf16_f32 v139, v140, v141
	s_nop 0
	v_cvt_pk_bf16_f32 v140, v142, v143
	v_cvt_pk_bf16_f32 v141, v146, v147
	global_store_dwordx4 v[144:145], v[138:141], off offset:256 sc1
; #define LAS __attribute__((address_space(3)))
; __device__ __forceinline__ unsigned cvt_pk_bf16(float lo, float hi) { unsigned r; asm volatile("v_cvt_pk_bf16_f32 %0, %1, %2" : "=v"(r) : "v"(lo), "v"(hi)); return r; }
;     __device__ __forceinline__ void operator()(const f32x4 (&acc)[2][2][4][2], const pg8::Unit& u, int wr, int wc, int fr, int fq) const {
;         const int cnt = seg[u.e], col0 = u.pn * 256 + wc * 32 + 8 * fq;
;         const LAS int* sl_e = (const LAS int*)(ldsb + DNSL_OFF + u.par * 2048); const LAS float* sl_g = (const LAS float*)(ldsb + DNSL_OFF + u.par * 2048 + 1024);
; #pragma unroll
;         for (int ai = 0; ai < 2; ++ai)
; #pragma unroll
;             for (int m = 0; m < 4; ++m) {
;                 const int ll = ai * 128 + wr * 64 + m * 16 + fr, lr = u.pm * 256 + ll;
;                 if (lr < cnt) {
;                     const int ent = sl_e[ll]; const float gw = sl_g[ll];
;                     bf16_t* rowp = yb + ((size_t)(ent & 1) * NTOK + (size_t)(ent >> 1)) * D + col0;
; #pragma unroll
;                     for (int bj = 0; bj < 2; ++bj) {
;                         const f32x4 v0 = acc[ai][bj][m][0] * gw, v1 = acc[ai][bj][m][1] * gw;
;                         u32x4 w; w.x = pg8::cvt_pk_bf16(v0[0], v0[1]); w.y = pg8::cvt_pk_bf16(v0[2], v0[3]); w.z = pg8::cvt_pk_bf16(v1[0], v1[1]); w.w = pg8::cvt_pk_bf16(v1[2], v1[3]);
;                         *(u32x4*)(rowp + bj * 128) = w;
;                     }
;                 }
;             }
;     }
.LBB0_1312:
	s_or_b64 exec, exec, s[6:7]
	v_add_u32_e32 v34, 0xa0, v136
	v_cmp_lt_i32_e32 vcc, v34, v134
	s_and_saveexec_b64 s[6:7], vcc
	s_cbranch_execz .LBB0_1314
	v_add_u32_e32 v34, 0x80, v135
	ds_read2st64_b32 v[138:139], v34 offset0:2 offset1:6
	s_waitcnt lgkmcnt(0)
	v_lshlrev_b32_e32 v34, 15, v138
	v_ashrrev_i32_e32 v138, 1, v138
	v_mov_b32_e32 v142, v139
	v_and_b32_e32 v34, 0x8000, v34
	v_ashrrev_i32_e32 v139, 31, v138
	v_lshl_add_u64 v[138:139], v[34:35], 0, v[138:139]
	v_lshlrev_b64 v[138:139], 11, v[138:139]
	v_lshl_add_u64 v[138:139], s[96:97], 0, v[138:139]
	v_pk_mul_f32 v[140:141], v[52:53], v[142:143] op_sel_hi:[1,0]
	v_lshl_add_u64 v[144:145], v[36:37], 1, v[138:139]
	v_pk_mul_f32 v[138:139], v[50:51], v[142:143] op_sel_hi:[1,0]
	v_pk_mul_f32 v[146:147], v[48:49], v[142:143] op_sel_hi:[1,0]
	v_pk_mul_f32 v[148:149], v[46:47], v[142:143] op_sel_hi:[1,0]
	v_cvt_pk_bf16_f32 v138, v138, v139
	v_cvt_pk_bf16_f32 v139, v140, v141
	s_nop 0
	v_cvt_pk_bf16_f32 v140, v148, v149
	v_cvt_pk_bf16_f32 v141, v146, v147
	global_store_dwordx4 v[144:145], v[138:141], off sc1
	v_pk_mul_f32 v[146:147], v[12:13], v[142:143] op_sel_hi:[1,0]
	s_nop 0
	v_pk_mul_f32 v[140:141], v[16:17], v[142:143] op_sel_hi:[1,0]
	v_pk_mul_f32 v[138:139], v[14:15], v[142:143] op_sel_hi:[1,0]
	v_pk_mul_f32 v[142:143], v[10:11], v[142:143] op_sel_hi:[1,0]
	v_cvt_pk_bf16_f32 v138, v138, v139
	v_cvt_pk_bf16_f32 v139, v140, v141
	s_nop 0
	v_cvt_pk_bf16_f32 v140, v142, v143
	v_cvt_pk_bf16_f32 v141, v146, v147
	global_store_dwordx4 v[144:145], v[138:141], off offset:256 sc1
.LBB0_1314:
	s_or_b64 exec, exec, s[6:7]
	v_add_u32_e32 v34, 0xb0, v136
	v_cmp_lt_i32_e32 vcc, v34, v134
	s_and_saveexec_b64 s[6:7], vcc
	s_cbranch_execz .LBB0_1316
	v_add_u32_e32 v34, 0xc0, v135
	ds_read2st64_b32 v[134:135], v34 offset0:2 offset1:6
	s_waitcnt lgkmcnt(0)
	v_lshlrev_b32_e32 v34, 15, v134
	v_ashrrev_i32_e32 v134, 1, v134
	v_mov_b32_e32 v138, v135
	v_and_b32_e32 v34, 0x8000, v34
	v_ashrrev_i32_e32 v135, 31, v134
	v_lshl_add_u64 v[134:135], v[34:35], 0, v[134:135]
	v_lshlrev_b64 v[134:135], 11, v[134:135]
	v_lshl_add_u64 v[134:135], s[96:97], 0, v[134:135]
	v_pk_mul_f32 v[136:137], v[44:45], v[138:139] op_sel_hi:[1,0]
	v_lshl_add_u64 v[36:37], v[36:37], 1, v[134:135]
	v_pk_mul_f32 v[134:135], v[42:43], v[138:139] op_sel_hi:[1,0]
	v_pk_mul_f32 v[140:141], v[40:41], v[138:139] op_sel_hi:[1,0]
	v_pk_mul_f32 v[142:143], v[38:39], v[138:139] op_sel_hi:[1,0]
	v_cvt_pk_bf16_f32 v134, v134, v135
	v_cvt_pk_bf16_f32 v135, v136, v137
	s_nop 0
	v_cvt_pk_bf16_f32 v136, v142, v143
	v_cvt_pk_bf16_f32 v137, v140, v141
	global_store_dwordx4 v[36:37], v[134:137], off sc1
	v_pk_mul_f32 v[140:141], v[4:5], v[138:139] op_sel_hi:[1,0]
	s_nop 0
	v_pk_mul_f32 v[136:137], v[8:9], v[138:139] op_sel_hi:[1,0]
	v_pk_mul_f32 v[134:135], v[6:7], v[138:139] op_sel_hi:[1,0]
	v_pk_mul_f32 v[138:139], v[2:3], v[138:139] op_sel_hi:[1,0]
	v_cvt_pk_bf16_f32 v134, v134, v135
	v_cvt_pk_bf16_f32 v135, v136, v137
	s_nop 0
	v_cvt_pk_bf16_f32 v136, v138, v139
	v_cvt_pk_bf16_f32 v137, v140, v141
	global_store_dwordx4 v[36:37], v[134:137], off offset:256 sc1

; __device__ __forceinline__ unsigned xb_ld(unsigned* p)              { return __hip_atomic_load(p, __ATOMIC_RELAXED, __HIP_MEMORY_SCOPE_AGENT); }
; __device__ __forceinline__ unsigned xb_add(unsigned* p, unsigned v) { return __hip_atomic_fetch_add(p, v, __ATOMIC_RELAXED, __HIP_MEMORY_SCOPE_AGENT); }
; #define XB_SPIN(cond, bar) do { unsigned _sp = 0; while (cond) { __builtin_amdgcn_s_sleep(1); \
;     if ((++_sp & 255u) == 0u) { if (xb_ld(&(bar)[XB_TMO])) break; if (_sp > XB_SPIN_CAP) { atomicAdd(&(bar)[XB_TMO], 1u); break; } } } } while (0)
; __device__ __forceinline__ void xcd_barrier(const XcdBarrier& b) {
;     ...
;         const unsigned old = xb_add(&bar[XB_XSUB(bx)], 1u);
;         const unsigned gen = old / nloc;
;         if (old + 1u == (gen + 1u) * nloc) {
;             __builtin_amdgcn_fence(__ATOMIC_RELEASE, "agent");
;             asm volatile("s_waitcnt vmcnt(0)" ::: "memory");
;             const unsigned og = xb_add(&bar[XB_TOP], 1u);
;             const unsigned tg = og / nx;
;             if (og + 1u == (tg + 1u) * nx) xb_add(&bar[XB_TOPGEN], 1u);
;             else XB_SPIN(xb_ld(&bar[XB_TOPGEN]) == tg, bar);
.LBB0_1350:
	v_mov_b32_e32 v1, s38
	v_add_co_u32_e32 v4, vcc, 0x3000, v1
	v_mov_b32_e32 v1, s39
	s_waitcnt vmcnt(0)
	v_addc_co_u32_e32 v5, vcc, 0, v1, vcc
	flat_atomic_add v3, v[4:5], v238 offset:1024 sc0
	v_cvt_f32_u32_e32 v1, v2
	v_sub_u32_e32 v4, 0, v2
	s_mov_b64 s[8:9], -1
	v_rcp_iflag_f32_e32 v1, v1
	s_nop 0
	v_mul_f32_e32 v1, 0x4f7ffffe, v1
	v_cvt_u32_f32_e32 v1, v1
	v_mul_lo_u32 v4, v4, v1
	v_mul_hi_u32 v4, v1, v4
	v_add_u32_e32 v1, v1, v4
	s_waitcnt vmcnt(0) lgkmcnt(0)
	v_mul_hi_u32 v1, v3, v1
	v_mul_lo_u32 v4, v1, v2
	v_sub_u32_e32 v4, v3, v4
	v_cmp_ge_u32_e32 vcc, v4, v2
	v_add_u32_e32 v5, 1, v1
	s_nop 0
	v_cndmask_b32_e32 v1, v1, v5, vcc
	v_sub_u32_e32 v5, v4, v2
	v_cndmask_b32_e32 v4, v4, v5, vcc
	v_cmp_ge_u32_e32 vcc, v4, v2
	v_add_u32_e32 v4, 1, v1
	s_nop 0
	v_cndmask_b32_e32 v1, v1, v4, vcc
	v_add_u32_e32 v4, 1, v3
	v_mad_u64_u32 v[2:3], s[4:5], v2, v1, v[2:3]
	s_add_u32 s4, s38, 0x3500
	s_addc_u32 s5, s39, 0
	v_cmp_ne_u32_e32 vcc, v4, v2
	v_mov_b64_e32 v[2:3], s[4:5]
	s_and_saveexec_b64 s[6:7], vcc
	s_cbranch_execz .LBB0_1362
	v_mov_b64_e32 v[2:3], s[4:5]
	flat_load_dword v2, v[2:3] sc1
	s_mov_b64 s[12:13], 0
	s_waitcnt vmcnt(0) lgkmcnt(0)
	v_cmp_eq_u32_e32 vcc, v2, v1
	s_and_saveexec_b64 s[10:11], vcc
	s_cbranch_execz .LBB0_1361
	s_add_u32 s8, s38, 0x200
	s_addc_u32 s9, s39, 0
	s_mov_b32 s24, 1
	s_branch .LBB0_1354
